# waitcnt thinning: consecutive pin ladders collapsed, provably redundant waits removed, gdn-chunk LDS pins merged per segment
# speedup vs baseline: 1.0024x; 1.0009x over previous
.LBB0_12:
	s_or_b64 exec, exec, s[24:25]
	v_add_u32_e32 v66, v189, v188
	s_waitcnt vmcnt(0)
	ds_write2_b32 v66, v6, v7 offset1:1
	ds_write2_b32 v66, v8, v9 offset0:2 offset1:3
	v_add_u32_e32 v6, 0x410, v66
	ds_write2_b32 v6, v2, v3 offset1:1
	v_add_u32_e32 v2, 0x418, v66
	ds_write2_b32 v2, v4, v5 offset1:1
	v_add_u32_e32 v2, 0x820, v66
	ds_write2_b32 v2, v14, v15 offset1:1
	v_add_u32_e32 v2, 0x828, v66
	ds_write2_b32 v2, v16, v17 offset1:1
	v_add_u32_e32 v2, 0xc30, v66
	ds_write2_b32 v2, v10, v11 offset1:1
	v_add_u32_e32 v2, 0xc38, v66
	ds_write2_b32 v2, v12, v13 offset1:1
	v_add_u32_e32 v2, 0x1040, v66
	ds_write2_b32 v2, v22, v23 offset1:1
	v_add_u32_e32 v2, 0x1048, v66
	ds_write2_b32 v2, v24, v25 offset1:1
	v_add_u32_e32 v2, 0x1450, v66
	ds_write2_b32 v2, v18, v19 offset1:1
	v_add_u32_e32 v2, 0x1458, v66
	ds_write2_b32 v2, v20, v21 offset1:1
	v_add_u32_e32 v2, 0x1860, v66
	ds_write2_b32 v2, v30, v31 offset1:1
	v_add_u32_e32 v2, 0x1868, v66
	ds_write2_b32 v2, v32, v33 offset1:1
	v_add_u32_e32 v2, 0x1c70, v66
	ds_write2_b32 v2, v26, v27 offset1:1
	v_add_u32_e32 v2, 0x1c78, v66
	ds_write2_b32 v2, v28, v29 offset1:1
	v_add_u32_e32 v2, 0x2080, v66
	ds_write2_b32 v2, v38, v39 offset1:1
	v_add_u32_e32 v2, 0x2088, v66
	ds_write2_b32 v2, v40, v41 offset1:1
	v_add_u32_e32 v2, 0x2490, v66
	ds_write2_b32 v2, v34, v35 offset1:1
	v_add_u32_e32 v2, 0x2498, v66
	ds_write2_b32 v2, v36, v37 offset1:1
	v_add_u32_e32 v2, 0x28a0, v66
	ds_write2_b32 v2, v46, v47 offset1:1
	v_add_u32_e32 v2, 0x28a8, v66
	ds_write2_b32 v2, v48, v49 offset1:1
	v_add_u32_e32 v2, 0x2cb0, v66
	ds_write2_b32 v2, v42, v43 offset1:1
	v_add_u32_e32 v2, 0x2cb8, v66
	ds_write2_b32 v2, v44, v45 offset1:1
	v_add_u32_e32 v2, 0x30c0, v66
	ds_write2_b32 v2, v54, v55 offset1:1
	v_add_u32_e32 v2, 0x30c8, v66
	ds_write2_b32 v2, v56, v57 offset1:1
	v_add_u32_e32 v2, 0x34d0, v66
	ds_write2_b32 v2, v50, v51 offset1:1
	v_add_u32_e32 v2, 0x34d8, v66
	ds_write2_b32 v2, v52, v53 offset1:1
	v_add_u32_e32 v2, 0x38e0, v66
	ds_write2_b32 v2, v62, v63 offset1:1
	v_add_u32_e32 v2, 0x38e8, v66
	ds_write2_b32 v2, v64, v65 offset1:1
	v_add_u32_e32 v2, 0x3cf0, v66
	s_mul_hi_i32 s2, s16, 0xe00000
	s_mul_i32 s16, s16, 0xe00000
	ds_write2_b32 v2, v58, v59 offset1:1
	v_add_u32_e32 v2, 0x3cf8, v66
	s_add_u32 s20, s42, s16
	ds_write2_b32 v2, v60, v61 offset1:1
	s_addc_u32 s2, s43, s2
	s_ashr_i32 s19, s18, 31
	s_waitcnt lgkmcnt(0)
	s_lshl_b64 s[16:17], s[18:19], 11
	v_add_u32_e32 v26, 0x400, v185
	s_add_u32 s18, s20, s16
	ds_read2_b32 v[6:7], v185 offset0:65 offset1:73
	ds_read2_b32 v[8:9], v185 offset1:8
	ds_read2_b32 v[10:11], v185 offset0:130 offset1:138
	ds_read2_b32 v[12:13], v185 offset0:195 offset1:203
	ds_read2_b32 v[14:15], v26 offset0:4 offset1:12
	ds_read2_b32 v[16:17], v26 offset0:69 offset1:77
	ds_read2_b32 v[18:19], v26 offset0:134 offset1:142
	ds_read2_b32 v[20:21], v26 offset0:199 offset1:207
	s_addc_u32 s2, s2, s17
	s_lshl_b64 s[16:17], s[22:23], 1
	s_add_u32 s16, s18, s16
	s_addc_u32 s17, s2, s17
	v_lshlrev_b32_e32 v66, 1, v70
	v_lshl_add_u64 v[22:23], s[16:17], 0, v[66:67]
	s_waitcnt lgkmcnt(6)
	v_cvt_pk_bf16_f32 v2, v8, v6
	s_waitcnt lgkmcnt(4)
	v_cvt_pk_bf16_f32 v3, v10, v12
	s_waitcnt lgkmcnt(2)
	v_cvt_pk_bf16_f32 v4, v14, v16
	s_waitcnt lgkmcnt(0)
	v_cvt_pk_bf16_f32 v5, v18, v20
	v_lshl_add_u64 v[24:25], v[22:23], 0, v[112:113]
	global_store_dwordx4 v[24:25], v[2:5], off
	s_nop 1
	v_cvt_pk_bf16_f32 v2, v9, v7
	v_cvt_pk_bf16_f32 v3, v11, v13
	v_cvt_pk_bf16_f32 v4, v15, v17
	v_cvt_pk_bf16_f32 v5, v19, v21
	ds_read2_b32 v[8:9], v185 offset0:81 offset1:89
	ds_read2_b32 v[10:11], v185 offset0:16 offset1:24
	ds_read2_b32 v[12:13], v185 offset0:146 offset1:154
	ds_read2_b32 v[14:15], v185 offset0:211 offset1:219
	ds_read2_b32 v[16:17], v26 offset0:20 offset1:28
	ds_read2_b32 v[18:19], v26 offset0:85 offset1:93
	ds_read2_b32 v[20:21], v26 offset0:150 offset1:158
	ds_read2_b32 v[24:25], v26 offset0:215 offset1:223
	v_lshl_add_u64 v[6:7], v[22:23], 0, v[74:75]
	global_store_dwordx4 v[6:7], v[2:5], off
	v_lshl_add_u64 v[6:7], v[22:23], 0, v[80:81]
	s_waitcnt lgkmcnt(6)
	v_cvt_pk_bf16_f32 v2, v10, v8
	s_waitcnt lgkmcnt(4)
	v_cvt_pk_bf16_f32 v3, v12, v14
	s_waitcnt lgkmcnt(2)
	v_cvt_pk_bf16_f32 v4, v16, v18
	s_waitcnt lgkmcnt(0)
	v_cvt_pk_bf16_f32 v5, v20, v24
	global_store_dwordx4 v[6:7], v[2:5], off
	v_lshl_add_u64 v[6:7], v[22:23], 0, v[86:87]
	s_nop 0
	v_cvt_pk_bf16_f32 v2, v11, v9
	v_cvt_pk_bf16_f32 v3, v13, v15
	v_cvt_pk_bf16_f32 v4, v17, v19
	v_cvt_pk_bf16_f32 v5, v21, v25
	ds_read2_b32 v[8:9], v185 offset0:32 offset1:40
	ds_read2_b32 v[10:11], v185 offset0:97 offset1:105
	ds_read2_b32 v[12:13], v185 offset0:162 offset1:170
	ds_read2_b32 v[14:15], v185 offset0:227 offset1:235
	ds_read2_b32 v[16:17], v26 offset0:36 offset1:44
	ds_read2_b32 v[18:19], v26 offset0:101 offset1:109
	ds_read2_b32 v[20:21], v26 offset0:166 offset1:174
	ds_read2_b32 v[24:25], v26 offset0:231 offset1:239
	global_store_dwordx4 v[6:7], v[2:5], off
	v_lshl_add_u64 v[6:7], v[22:23], 0, v[90:91]
	s_waitcnt lgkmcnt(6)
	v_cvt_pk_bf16_f32 v2, v8, v10
	s_waitcnt lgkmcnt(4)
	v_cvt_pk_bf16_f32 v3, v12, v14
	s_waitcnt lgkmcnt(2)
	v_cvt_pk_bf16_f32 v4, v16, v18
	s_waitcnt lgkmcnt(0)
	v_cvt_pk_bf16_f32 v5, v20, v24
	global_store_dwordx4 v[6:7], v[2:5], off
	v_lshl_add_u64 v[6:7], v[22:23], 0, v[94:95]
	s_nop 0
	v_cvt_pk_bf16_f32 v2, v9, v11
	v_cvt_pk_bf16_f32 v3, v13, v15
	v_cvt_pk_bf16_f32 v4, v17, v19
	v_cvt_pk_bf16_f32 v5, v21, v25
	ds_read2_b32 v[8:9], v185 offset0:48 offset1:56
	ds_read2_b32 v[10:11], v185 offset0:113 offset1:121
	ds_read2_b32 v[12:13], v185 offset0:178 offset1:186
	ds_read2_b32 v[14:15], v185 offset0:243 offset1:251
	ds_read2_b32 v[16:17], v26 offset0:52 offset1:60
	ds_read2_b32 v[18:19], v26 offset0:117 offset1:125
	ds_read2_b32 v[20:21], v26 offset0:182 offset1:190
	ds_read2_b32 v[24:25], v26 offset0:247 offset1:255
	global_store_dwordx4 v[6:7], v[2:5], off
	v_lshl_add_u64 v[6:7], v[22:23], 0, v[98:99]
	s_waitcnt lgkmcnt(6)
	v_cvt_pk_bf16_f32 v2, v8, v10
	s_waitcnt lgkmcnt(4)
	v_cvt_pk_bf16_f32 v3, v12, v14
	s_waitcnt lgkmcnt(2)
	v_cvt_pk_bf16_f32 v4, v16, v18
	s_waitcnt lgkmcnt(0)
	v_cvt_pk_bf16_f32 v5, v20, v24
	global_store_dwordx4 v[6:7], v[2:5], off
	v_lshl_add_u64 v[6:7], v[22:23], 0, v[102:103]
	s_nop 0
	v_cvt_pk_bf16_f32 v2, v9, v11
	v_cvt_pk_bf16_f32 v3, v13, v15
	v_cvt_pk_bf16_f32 v4, v17, v19
	v_cvt_pk_bf16_f32 v5, v21, v25
	global_store_dwordx4 v[6:7], v[2:5], off
.LBB0_13:
	s_add_i32 s2, s30, 0x800
	s_add_i32 s45, s45, 0x20000
	s_addk_i32 s46, 0x2000
	s_addk_i32 s47, 0x1000
	s_cmp_gt_i32 s30, 0xc9ff
	s_mov_b32 s30, s2
	s_cbranch_scc1 .LBB0_64
.LBB0_14:
	s_mul_hi_i32 s2, s30, 0x9c09c09d
	s_add_i32 s2, s2, s30
	s_lshr_b32 s16, s2, 31
	s_ashr_i32 s2, s2, 14
	s_add_i32 s16, s2, s16
	s_mul_i32 s2, s16, 0xffff9700
	s_add_i32 s20, s30, s2
	s_cmpk_gt_i32 s20, 0x6ff
	s_mov_b64 s[18:19], -1
	s_cbranch_scc0 .LBB0_28
	s_cmpk_gt_u32 s20, 0x7ff
	s_cbranch_scc0 .LBB0_25
	s_cmpk_gt_u32 s20, 0x8ff
	s_cbranch_scc0 .LBB0_22
	s_cmpk_gt_u32 s20, 0x48ff
	s_cbranch_scc0 .LBB0_19
	s_lshl_b32 s19, s30, 1
	s_add_i32 s2, s20, 0xffffb700
	s_and_b32 s18, s45, 0x3c0
	s_and_b32 s19, s19, 32
	s_lshr_b32 s2, s2, 8
	s_or_b32 s21, s19, s18
	s_lshl_b32 s18, s16, 5
	s_lshl_b32 s17, s30, 2
	s_add_i32 s18, s2, s18
	s_and_b32 s17, s17, 0x380
	s_ashr_i32 s19, s18, 31
	s_lshl_b64 s[22:23], s[18:19], 22
	s_lshl_b32 s2, s17, 12
	s_waitcnt lgkmcnt(0)
	s_add_u32 s22, s6, s22
	s_addc_u32 s23, s7, s23
	s_add_u32 s2, s22, s2
	s_addc_u32 s23, s23, 0
	s_lshl_b32 s22, s21, 2
	s_add_u32 s22, s2, s22
	s_addc_u32 s23, s23, 0
	v_lshl_add_u64 v[2:3], s[22:23], 0, v[106:107]
	v_lshlrev_b32_e32 v66, 2, v184
	v_lshl_add_u64 v[62:63], v[2:3], 0, v[66:67]
	v_add_co_u32_e32 v6, vcc, s48, v62
	s_lshl_b64 s[18:19], s[18:19], 20
	s_nop 0
	v_addc_co_u32_e32 v7, vcc, 0, v63, vcc
	v_add_co_u32_e32 v10, vcc, s49, v62
	global_load_dwordx4 v[2:5], v[62:63], off
	s_nop 0
	global_load_dwordx4 v[6:9], v[6:7], off
	v_addc_co_u32_e32 v11, vcc, 0, v63, vcc
	v_add_co_u32_e32 v14, vcc, s50, v62
	s_add_u32 s2, s31, s18
	s_nop 0
	v_addc_co_u32_e32 v15, vcc, 0, v63, vcc
	global_load_dwordx4 v[10:13], v[10:11], off
	s_nop 0
	global_load_dwordx4 v[14:17], v[14:15], off
	v_add_co_u32_e32 v18, vcc, s51, v62
	s_addc_u32 s18, s33, s19
	s_nop 0
	v_addc_co_u32_e32 v19, vcc, 0, v63, vcc
	v_add_co_u32_e32 v22, vcc, s52, v62
	s_lshl_b32 s19, s21, 10
	s_nop 0
	v_addc_co_u32_e32 v23, vcc, 0, v63, vcc
	global_load_dwordx4 v[18:21], v[18:19], off
	s_nop 0
	global_load_dwordx4 v[22:25], v[22:23], off
	v_add_co_u32_e32 v26, vcc, s53, v62
	s_add_u32 s2, s2, s19
	s_nop 0
	v_addc_co_u32_e32 v27, vcc, 0, v63, vcc
	v_add_co_u32_e32 v30, vcc, s54, v62
	s_addc_u32 s19, s18, 0
	s_nop 0
	v_addc_co_u32_e32 v31, vcc, 0, v63, vcc
	global_load_dwordx4 v[26:29], v[26:27], off
	s_nop 0
	global_load_dwordx4 v[30:33], v[30:31], off
	v_add_co_u32_e32 v34, vcc, s55, v62
	s_add_u32 s18, s2, s17
	s_nop 0
	v_addc_co_u32_e32 v35, vcc, 0, v63, vcc
	v_add_co_u32_e32 v38, vcc, s56, v62
	s_addc_u32 s19, s19, 0
	s_nop 0
	v_addc_co_u32_e32 v39, vcc, 0, v63, vcc
	global_load_dwordx4 v[34:37], v[34:35], off
	s_nop 0
	global_load_dwordx4 v[38:41], v[38:39], off
	v_add_co_u32_e32 v42, vcc, s57, v62
	s_nop 1
	v_addc_co_u32_e32 v43, vcc, 0, v63, vcc
	v_add_co_u32_e32 v46, vcc, s58, v62
	s_nop 1
	v_addc_co_u32_e32 v47, vcc, 0, v63, vcc
	global_load_dwordx4 v[42:45], v[42:43], off
	s_nop 0
	global_load_dwordx4 v[46:49], v[46:47], off
	v_add_co_u32_e32 v50, vcc, s59, v62
	s_nop 1
	v_addc_co_u32_e32 v51, vcc, 0, v63, vcc
	global_load_dwordx4 v[50:53], v[50:51], off
	v_add_co_u32_e32 v54, vcc, s60, v62
	s_nop 1
	v_addc_co_u32_e32 v55, vcc, 0, v63, vcc
	global_load_dwordx4 v[54:57], v[54:55], off
	v_add_co_u32_e32 v58, vcc, s61, v62
	s_nop 1
	v_addc_co_u32_e32 v59, vcc, 0, v63, vcc
	global_load_dwordx4 v[58:61], v[58:59], off
	v_add_co_u32_e32 v62, vcc, s62, v62
	s_nop 1
	v_addc_co_u32_e32 v63, vcc, 0, v63, vcc
	global_load_dwordx4 v[62:65], v[62:63], off
	s_waitcnt vmcnt(15)
	ds_write2_b32 v71, v2, v3 offset1:1
	ds_write2_b32 v71, v4, v5 offset0:2 offset1:3
	v_add_u32_e32 v2, 0x420, v71
	s_waitcnt vmcnt(14)
	ds_write2_b32 v2, v6, v7 offset1:1
	v_add_u32_e32 v2, 0x428, v71
	ds_write2_b32 v2, v8, v9 offset1:1
	v_add_u32_e32 v2, 0x840, v71
	s_waitcnt vmcnt(13)
	ds_write2_b32 v2, v10, v11 offset1:1
	v_add_u32_e32 v2, 0x848, v71
	ds_write2_b32 v2, v12, v13 offset1:1
	v_add_u32_e32 v2, 0xc60, v71
	s_waitcnt vmcnt(12)
	ds_write2_b32 v2, v14, v15 offset1:1
	v_add_u32_e32 v2, 0xc68, v71
	ds_write2_b32 v2, v16, v17 offset1:1
	v_add_u32_e32 v2, 0x1080, v71
	s_waitcnt vmcnt(11)
	ds_write2_b32 v2, v18, v19 offset1:1
	v_add_u32_e32 v2, 0x1088, v71
	ds_write2_b32 v2, v20, v21 offset1:1
	v_add_u32_e32 v2, 0x14a0, v71
	s_waitcnt vmcnt(10)
	ds_write2_b32 v2, v22, v23 offset1:1
	v_add_u32_e32 v2, 0x14a8, v71
	ds_write2_b32 v2, v24, v25 offset1:1
	v_add_u32_e32 v2, 0x18c0, v71
	s_waitcnt vmcnt(9)
	ds_write2_b32 v2, v26, v27 offset1:1
	v_add_u32_e32 v2, 0x18c8, v71
	ds_write2_b32 v2, v28, v29 offset1:1
	v_add_u32_e32 v2, 0x1ce0, v71
	s_waitcnt vmcnt(8)
	ds_write2_b32 v2, v30, v31 offset1:1
	v_add_u32_e32 v2, 0x1ce8, v71
	ds_write2_b32 v2, v32, v33 offset1:1
	v_add_u32_e32 v2, 0x2100, v71
	s_waitcnt vmcnt(7)
	ds_write2_b32 v2, v34, v35 offset1:1
	v_add_u32_e32 v2, 0x2108, v71
	ds_write2_b32 v2, v36, v37 offset1:1
	v_add_u32_e32 v2, 0x2520, v71
	s_waitcnt vmcnt(6)
	ds_write2_b32 v2, v38, v39 offset1:1
	v_add_u32_e32 v2, 0x2528, v71
	ds_write2_b32 v2, v40, v41 offset1:1
	v_add_u32_e32 v2, 0x2940, v71
	v_lshl_add_u64 v[38:39], s[18:19], 0, v[68:69]
	v_lshl_add_u64 v[40:41], v[38:39], 0, v[108:109]
	s_mov_b64 s[18:19], 0
	s_waitcnt vmcnt(5)
	ds_write2_b32 v2, v42, v43 offset1:1
	v_add_u32_e32 v2, 0x2948, v71
	ds_write2_b32 v2, v44, v45 offset1:1
	v_add_u32_e32 v2, 0x2d60, v71
	s_waitcnt vmcnt(4)
	ds_write2_b32 v2, v46, v47 offset1:1
	v_add_u32_e32 v2, 0x2d68, v71
	ds_write2_b32 v2, v48, v49 offset1:1
	v_add_u32_e32 v2, 0x3180, v71
	s_waitcnt vmcnt(3)
	ds_write2_b32 v2, v50, v51 offset1:1
	v_add_u32_e32 v2, 0x3188, v71
	ds_write2_b32 v2, v52, v53 offset1:1
	v_add_u32_e32 v2, 0x35a0, v71
	v_add_u32_e32 v42, 0x400, v119
	s_waitcnt vmcnt(2)
	ds_write2_b32 v2, v54, v55 offset1:1
	v_add_u32_e32 v2, 0x35a8, v71
	ds_write2_b32 v2, v56, v57 offset1:1
	v_add_u32_e32 v2, 0x39c0, v71
	s_waitcnt vmcnt(1)
	ds_write2_b32 v2, v58, v59 offset1:1
	v_add_u32_e32 v2, 0x39c8, v71
	ds_write2_b32 v2, v60, v61 offset1:1
	v_add_u32_e32 v2, 0x3de0, v71
	s_waitcnt vmcnt(0)
	ds_write2_b32 v2, v62, v63 offset1:1
	v_add_u32_e32 v2, 0x3de8, v71
	ds_write2_b32 v2, v64, v65 offset1:1
	s_waitcnt lgkmcnt(0)
	ds_read2_b32 v[6:7], v119 offset0:66 offset1:74
	ds_read2_b32 v[8:9], v119 offset0:99 offset1:107
	ds_read2_b32 v[10:11], v119 offset1:8
	ds_read2_b32 v[12:13], v119 offset0:33 offset1:41
	v_mov_b32_e32 v2, v67
	s_waitcnt lgkmcnt(3)
	v_mul_f32_e32 v3, 0x42000000, v6
	ds_read2_b32 v[14:15], v119 offset0:198 offset1:206
	ds_read2_b32 v[16:17], v119 offset0:231 offset1:239
	ds_read2_b32 v[18:19], v119 offset0:132 offset1:140
	ds_read2_b32 v[20:21], v119 offset0:165 offset1:173
	s_waitcnt lgkmcnt(5)
	v_mul_f32_e32 v5, 0x42000000, v10
	s_waitcnt lgkmcnt(4)
	v_mul_f32_e32 v6, 0x42000000, v12
	v_cvt_pk_fp8_f32 v2, v5, v6
	v_mul_f32_e32 v4, 0x42000000, v8
	s_waitcnt lgkmcnt(1)
	v_mul_f32_e32 v6, 0x42000000, v18
	s_waitcnt lgkmcnt(0)
	v_mul_f32_e32 v8, 0x42000000, v20
	v_cvt_pk_fp8_f32 v2, v3, v4 op_sel:[0,0,1]
	v_mov_b32_e32 v3, v67
	ds_read2_b32 v[22:23], v42 offset0:74 offset1:82
	ds_read2_b32 v[24:25], v42 offset0:107 offset1:115
	ds_read2_b32 v[26:27], v42 offset0:8 offset1:16
	ds_read2_b32 v[28:29], v42 offset0:41 offset1:49
	v_cvt_pk_fp8_f32 v3, v6, v8
	ds_read2_b32 v[30:31], v42 offset0:140 offset1:148
	ds_read2_b32 v[32:33], v42 offset0:173 offset1:181
	v_mul_f32_e32 v4, 0x42000000, v14
	v_mul_f32_e32 v5, 0x42000000, v16
	v_cvt_pk_fp8_f32 v3, v4, v5 op_sel:[0,0,1]
	s_waitcnt lgkmcnt(3)
	v_mul_f32_e32 v5, 0x42000000, v26
	s_waitcnt lgkmcnt(2)
	v_mul_f32_e32 v10, 0x42000000, v28
	v_mov_b32_e32 v4, v67
	ds_read2_b32 v[34:35], v42 offset0:206 offset1:214
	ds_read2_b32 v[36:37], v42 offset0:239 offset1:247
	v_cvt_pk_fp8_f32 v4, v5, v10
	s_waitcnt lgkmcnt(3)
	v_mul_f32_e32 v10, 0x42000000, v30
	s_waitcnt lgkmcnt(2)
	v_mul_f32_e32 v12, 0x42000000, v32
	v_mov_b32_e32 v5, v67
	v_cvt_pk_fp8_f32 v5, v10, v12
	v_mul_f32_e32 v6, 0x42000000, v22
	v_mul_f32_e32 v8, 0x42000000, v24
	v_cvt_pk_fp8_f32 v4, v6, v8 op_sel:[0,0,1]
	s_waitcnt lgkmcnt(1)
	v_mul_f32_e32 v6, 0x42000000, v34
	s_waitcnt lgkmcnt(0)
	v_mul_f32_e32 v8, 0x42000000, v36
	v_cvt_pk_fp8_f32 v5, v6, v8 op_sel:[0,0,1]
	v_mul_f32_e32 v6, 0x42000000, v13
	v_mul_f32_e32 v8, 0x42000000, v29
	global_store_dwordx4 v[40:41], v[2:5], off
	s_nop 1
	v_mul_f32_e32 v3, 0x42000000, v11
	v_mov_b32_e32 v2, v67
	v_mul_f32_e32 v4, 0x42000000, v7
	v_cvt_pk_fp8_f32 v2, v3, v6
	v_mul_f32_e32 v6, 0x42000000, v19
	v_mul_f32_e32 v7, 0x42000000, v21
	v_mov_b32_e32 v3, v67
	v_cvt_pk_fp8_f32 v3, v6, v7
	v_mul_f32_e32 v5, 0x42000000, v9
	v_cvt_pk_fp8_f32 v2, v4, v5 op_sel:[0,0,1]
	v_mul_f32_e32 v4, 0x42000000, v15
	v_mul_f32_e32 v5, 0x42000000, v17
	v_cvt_pk_fp8_f32 v3, v4, v5 op_sel:[0,0,1]
	v_mul_f32_e32 v5, 0x42000000, v27
	v_mov_b32_e32 v4, v67
	v_cvt_pk_fp8_f32 v4, v5, v8
	v_mul_f32_e32 v8, 0x42000000, v31
	v_mul_f32_e32 v9, 0x42000000, v33
	v_mov_b32_e32 v5, v67
	v_cvt_pk_fp8_f32 v5, v8, v9
	v_mul_f32_e32 v6, 0x42000000, v23
	v_mul_f32_e32 v7, 0x42000000, v25
	v_cvt_pk_fp8_f32 v4, v6, v7 op_sel:[0,0,1]
	v_mul_f32_e32 v6, 0x42000000, v35
	v_mul_f32_e32 v7, 0x42000000, v37
	ds_read2_b32 v[8:9], v119 offset0:82 offset1:90
	ds_read2_b32 v[10:11], v119 offset0:115 offset1:123
	ds_read2_b32 v[12:13], v119 offset0:16 offset1:24
	ds_read2_b32 v[14:15], v119 offset0:49 offset1:57
	v_cvt_pk_fp8_f32 v5, v6, v7 op_sel:[0,0,1]
	v_lshl_add_u64 v[6:7], v[38:39], 0, v[72:73]
	global_store_dwordx4 v[6:7], v[2:5], off
	s_waitcnt lgkmcnt(1)
	s_nop 0
	v_mul_f32_e32 v5, 0x42000000, v12
	s_waitcnt lgkmcnt(0)
	v_mul_f32_e32 v6, 0x42000000, v14
	v_mov_b32_e32 v2, v67
	v_cvt_pk_fp8_f32 v2, v5, v6
	ds_read2_b32 v[16:17], v119 offset0:214 offset1:222
	ds_read2_b32 v[18:19], v119 offset0:247 offset1:255
	ds_read2_b32 v[6:7], v119 offset0:148 offset1:156
	ds_read2_b32 v[20:21], v119 offset0:181 offset1:189
	v_mul_f32_e32 v3, 0x42000000, v8
	v_mul_f32_e32 v4, 0x42000000, v10
	v_cvt_pk_fp8_f32 v2, v3, v4 op_sel:[0,0,1]
	s_waitcnt lgkmcnt(1)
	v_mul_f32_e32 v6, 0x42000000, v6
	s_waitcnt lgkmcnt(0)
	v_mul_f32_e32 v8, 0x42000000, v20
	v_mov_b32_e32 v3, v67
	ds_read2_b32 v[22:23], v42 offset0:90 offset1:98
	ds_read2_b32 v[24:25], v42 offset0:123 offset1:131
	ds_read2_b32 v[26:27], v42 offset0:24 offset1:32
	ds_read2_b32 v[28:29], v42 offset0:57 offset1:65
	v_cvt_pk_fp8_f32 v3, v6, v8
	v_mul_f32_e32 v4, 0x42000000, v16
	v_mul_f32_e32 v5, 0x42000000, v18
	ds_read2_b32 v[30:31], v42 offset0:156 offset1:164
	ds_read2_b32 v[32:33], v42 offset0:189 offset1:197
	ds_read2_b32 v[34:35], v42 offset0:222 offset1:230
	v_cvt_pk_fp8_f32 v3, v4, v5 op_sel:[0,0,1]
	s_waitcnt lgkmcnt(4)
	v_mul_f32_e32 v5, 0x42000000, v26
	s_waitcnt lgkmcnt(3)
	v_mul_f32_e32 v10, 0x42000000, v28
	v_mov_b32_e32 v4, v67
	v_cvt_pk_fp8_f32 v4, v5, v10
	v_add_u32_e32 v5, 0x600, v119
	ds_read2_b32 v[36:37], v5 offset0:127 offset1:135
	s_waitcnt lgkmcnt(3)
	v_mul_f32_e32 v10, 0x42000000, v30
	s_waitcnt lgkmcnt(2)
	v_mul_f32_e32 v12, 0x42000000, v32
	v_mov_b32_e32 v5, v67
	v_cvt_pk_fp8_f32 v5, v10, v12
	v_mul_f32_e32 v6, 0x42000000, v22
	v_mul_f32_e32 v8, 0x42000000, v24
	v_cvt_pk_fp8_f32 v4, v6, v8 op_sel:[0,0,1]
	s_waitcnt lgkmcnt(1)
	v_mul_f32_e32 v6, 0x42000000, v34
	s_waitcnt lgkmcnt(0)
	v_mul_f32_e32 v8, 0x42000000, v36
	v_cvt_pk_fp8_f32 v5, v6, v8 op_sel:[0,0,1]
	v_mul_f32_e32 v8, 0x42000000, v9
	v_mul_f32_e32 v9, 0x42000000, v11
	v_mul_f32_e32 v10, 0x42000000, v13
	v_mul_f32_e32 v11, 0x42000000, v15
	v_mov_b32_e32 v6, v67
	v_cvt_pk_fp8_f32 v6, v10, v11
	v_mul_f32_e32 v10, 0x42000000, v7
	v_mul_f32_e32 v11, 0x42000000, v21
	v_mov_b32_e32 v7, v67
	v_cvt_pk_fp8_f32 v7, v10, v11
	v_cvt_pk_fp8_f32 v6, v8, v9 op_sel:[0,0,1]
	v_mul_f32_e32 v8, 0x42000000, v17
	v_mul_f32_e32 v9, 0x42000000, v19
	v_cvt_pk_fp8_f32 v7, v8, v9 op_sel:[0,0,1]
	v_mul_f32_e32 v9, 0x42000000, v27
	v_mul_f32_e32 v12, 0x42000000, v29
	v_mov_b32_e32 v8, v67
	v_cvt_pk_fp8_f32 v8, v9, v12
	v_mul_f32_e32 v12, 0x42000000, v31
	v_mul_f32_e32 v13, 0x42000000, v33
	v_mov_b32_e32 v9, v67
	v_cvt_pk_fp8_f32 v9, v12, v13
	v_mul_f32_e32 v10, 0x42000000, v23
	v_mul_f32_e32 v11, 0x42000000, v25
	v_cvt_pk_fp8_f32 v8, v10, v11 op_sel:[0,0,1]
	v_mul_f32_e32 v10, 0x42000000, v35
	v_mul_f32_e32 v11, 0x42000000, v37
	v_cvt_pk_fp8_f32 v9, v10, v11 op_sel:[0,0,1]
	v_lshl_add_u64 v[10:11], v[38:39], 0, v[78:79]
	global_store_dwordx4 v[10:11], v[2:5], off
	s_nop 1
	v_lshl_add_u64 v[2:3], v[38:39], 0, v[84:85]
	global_store_dwordx4 v[2:3], v[6:9], off
.LBB0_19:
	s_andn2_b64 vcc, exec, s[18:19]
	s_cbranch_vccnz .LBB0_21
	s_and_b32 s18, s45, 0x7c0
	s_and_b32 s19, s30, 32
	s_add_i32 s2, s20, 0xfffff700
	s_or_b32 s21, s18, s19
	s_lshr_b32 s19, s45, 1
	s_lshr_b32 s17, s2, 9
	s_lshl_b32 s2, s16, 9
	s_and_b32 s18, s21, 0xe0
	s_and_b32 s19, s19, 0x380
	s_sub_i32 s2, s47, s2
	s_or_b32 s22, s18, s19
	s_add_i32 s19, s19, s18
	s_and_b32 s2, s2, 0x380
	s_addk_i32 s19, 0x380
	s_cmpk_lt_u32 s18, 0x80
	s_cselect_b32 s24, s22, s19
	s_lshl_b32 s18, s16, 5
	s_add_i32 s18, s17, s18
	s_ashr_i32 s19, s18, 31
	s_lshl_b64 s[22:23], s[18:19], 23
	s_waitcnt lgkmcnt(0)
	s_add_u32 s17, s12, s22
	s_addc_u32 s22, s13, s23
	s_lshl_b32 s23, s2, 13
	s_add_u32 s17, s17, s23
	s_addc_u32 s23, s22, 0
	s_lshl_b32 s22, s24, 2
	s_add_u32 s22, s17, s22
	s_addc_u32 s23, s23, 0
	v_lshl_add_u64 v[2:3], s[22:23], 0, v[110:111]
	v_lshlrev_b32_e32 v66, 2, v184
	v_lshl_add_u64 v[62:63], v[2:3], 0, v[66:67]
	v_add_co_u32_e32 v6, vcc, s49, v62
	s_lshl_b64 s[18:19], s[18:19], 21
	s_nop 0
	v_addc_co_u32_e32 v7, vcc, 0, v63, vcc
	v_add_co_u32_e32 v10, vcc, s51, v62
	global_load_dwordx4 v[2:5], v[62:63], off
	s_nop 0
	global_load_dwordx4 v[6:9], v[6:7], off
	v_addc_co_u32_e32 v11, vcc, 0, v63, vcc
	v_add_co_u32_e32 v14, vcc, s53, v62
	s_add_u32 s17, s34, s18
	s_nop 0
	v_addc_co_u32_e32 v15, vcc, 0, v63, vcc
	global_load_dwordx4 v[10:13], v[10:11], off
	s_nop 0
	global_load_dwordx4 v[14:17], v[14:15], off
	v_add_co_u32_e32 v18, vcc, s55, v62
	s_addc_u32 s18, s35, s19
	s_nop 0
	v_addc_co_u32_e32 v19, vcc, 0, v63, vcc
	v_add_co_u32_e32 v22, vcc, s57, v62
	s_lshl_b32 s19, s21, 10
	s_nop 0
	v_addc_co_u32_e32 v23, vcc, 0, v63, vcc
	global_load_dwordx4 v[18:21], v[18:19], off
	s_nop 0
	global_load_dwordx4 v[22:25], v[22:23], off
	v_add_co_u32_e32 v26, vcc, s59, v62
	s_add_u32 s17, s17, s19
	s_nop 0
	v_addc_co_u32_e32 v27, vcc, 0, v63, vcc
	v_add_co_u32_e32 v30, vcc, s61, v62
	s_addc_u32 s19, s18, 0
	s_nop 0
	v_addc_co_u32_e32 v31, vcc, 0, v63, vcc
	global_load_dwordx4 v[26:29], v[26:27], off
	s_nop 0
	global_load_dwordx4 v[30:33], v[30:31], off
	v_add_co_u32_e32 v34, vcc, s63, v62
	s_add_u32 s18, s17, s2
	s_nop 0
	v_addc_co_u32_e32 v35, vcc, 0, v63, vcc
	v_add_co_u32_e32 v38, vcc, s64, v62
	s_addc_u32 s19, s19, 0
	s_nop 0
	v_addc_co_u32_e32 v39, vcc, 0, v63, vcc
	global_load_dwordx4 v[34:37], v[34:35], off
	s_nop 0
	global_load_dwordx4 v[38:41], v[38:39], off
	v_add_co_u32_e32 v42, vcc, s65, v62
	s_nop 1
	v_addc_co_u32_e32 v43, vcc, 0, v63, vcc
	v_add_co_u32_e32 v46, vcc, s66, v62
	s_nop 1
	v_addc_co_u32_e32 v47, vcc, 0, v63, vcc
	global_load_dwordx4 v[42:45], v[42:43], off
	s_nop 0
	global_load_dwordx4 v[46:49], v[46:47], off
	v_add_co_u32_e32 v50, vcc, s67, v62
	s_nop 1
	v_addc_co_u32_e32 v51, vcc, 0, v63, vcc
	global_load_dwordx4 v[50:53], v[50:51], off
	v_add_co_u32_e32 v54, vcc, s68, v62
	s_nop 1
	v_addc_co_u32_e32 v55, vcc, 0, v63, vcc
	global_load_dwordx4 v[54:57], v[54:55], off
	v_add_co_u32_e32 v58, vcc, s69, v62
	s_nop 1
	v_addc_co_u32_e32 v59, vcc, 0, v63, vcc
	global_load_dwordx4 v[58:61], v[58:59], off
	v_add_co_u32_e32 v62, vcc, s70, v62
	s_nop 1
	v_addc_co_u32_e32 v63, vcc, 0, v63, vcc
	global_load_dwordx4 v[62:65], v[62:63], off
	s_waitcnt vmcnt(15)
	ds_write2_b32 v71, v2, v3 offset1:1
	ds_write2_b32 v71, v4, v5 offset0:2 offset1:3
	v_add_u32_e32 v2, 0x420, v71
	s_waitcnt vmcnt(14)
	ds_write2_b32 v2, v6, v7 offset1:1
	v_add_u32_e32 v2, 0x428, v71
	ds_write2_b32 v2, v8, v9 offset1:1
	v_add_u32_e32 v2, 0x840, v71
	s_waitcnt vmcnt(13)
	ds_write2_b32 v2, v10, v11 offset1:1
	v_add_u32_e32 v2, 0x848, v71
	ds_write2_b32 v2, v12, v13 offset1:1
	v_add_u32_e32 v2, 0xc60, v71
	s_waitcnt vmcnt(12)
	ds_write2_b32 v2, v14, v15 offset1:1
	v_add_u32_e32 v2, 0xc68, v71
	ds_write2_b32 v2, v16, v17 offset1:1
	v_add_u32_e32 v2, 0x1080, v71
	s_waitcnt vmcnt(11)
	ds_write2_b32 v2, v18, v19 offset1:1
	v_add_u32_e32 v2, 0x1088, v71
	ds_write2_b32 v2, v20, v21 offset1:1
	v_add_u32_e32 v2, 0x14a0, v71
	s_waitcnt vmcnt(10)
	ds_write2_b32 v2, v22, v23 offset1:1
	v_add_u32_e32 v2, 0x14a8, v71
	ds_write2_b32 v2, v24, v25 offset1:1
	v_add_u32_e32 v2, 0x18c0, v71
	s_waitcnt vmcnt(9)
	ds_write2_b32 v2, v26, v27 offset1:1
	v_add_u32_e32 v2, 0x18c8, v71
	ds_write2_b32 v2, v28, v29 offset1:1
	v_add_u32_e32 v2, 0x1ce0, v71
	s_waitcnt vmcnt(8)
	ds_write2_b32 v2, v30, v31 offset1:1
	v_add_u32_e32 v2, 0x1ce8, v71
	ds_write2_b32 v2, v32, v33 offset1:1
	v_add_u32_e32 v2, 0x2100, v71
	s_waitcnt vmcnt(7)
	ds_write2_b32 v2, v34, v35 offset1:1
	v_add_u32_e32 v2, 0x2108, v71
	ds_write2_b32 v2, v36, v37 offset1:1
	v_add_u32_e32 v2, 0x2520, v71
	s_waitcnt vmcnt(6)
	ds_write2_b32 v2, v38, v39 offset1:1
	v_add_u32_e32 v2, 0x2528, v71
	ds_write2_b32 v2, v40, v41 offset1:1
	v_add_u32_e32 v2, 0x2940, v71
	v_lshl_add_u64 v[38:39], s[18:19], 0, v[68:69]
	v_lshl_add_u64 v[40:41], v[38:39], 0, v[108:109]
	s_waitcnt vmcnt(5)
	ds_write2_b32 v2, v42, v43 offset1:1
	v_add_u32_e32 v2, 0x2948, v71
	ds_write2_b32 v2, v44, v45 offset1:1
	v_add_u32_e32 v2, 0x2d60, v71
	s_waitcnt vmcnt(4)
	ds_write2_b32 v2, v46, v47 offset1:1
	v_add_u32_e32 v2, 0x2d68, v71
	ds_write2_b32 v2, v48, v49 offset1:1
	v_add_u32_e32 v2, 0x3180, v71
	s_waitcnt vmcnt(3)
	ds_write2_b32 v2, v50, v51 offset1:1
	v_add_u32_e32 v2, 0x3188, v71
	ds_write2_b32 v2, v52, v53 offset1:1
	v_add_u32_e32 v2, 0x35a0, v71
	v_add_u32_e32 v42, 0x400, v119
	s_waitcnt vmcnt(2)
	ds_write2_b32 v2, v54, v55 offset1:1
	v_add_u32_e32 v2, 0x35a8, v71
	ds_write2_b32 v2, v56, v57 offset1:1
	v_add_u32_e32 v2, 0x39c0, v71
	s_waitcnt vmcnt(1)
	ds_write2_b32 v2, v58, v59 offset1:1
	v_add_u32_e32 v2, 0x39c8, v71
	ds_write2_b32 v2, v60, v61 offset1:1
	v_add_u32_e32 v2, 0x3de0, v71
	s_waitcnt vmcnt(0)
	ds_write2_b32 v2, v62, v63 offset1:1
	v_add_u32_e32 v2, 0x3de8, v71
	ds_write2_b32 v2, v64, v65 offset1:1
	s_waitcnt lgkmcnt(0)
	ds_read2_b32 v[6:7], v119 offset0:66 offset1:74
	ds_read2_b32 v[8:9], v119 offset0:99 offset1:107
	ds_read2_b32 v[10:11], v119 offset1:8
	ds_read2_b32 v[12:13], v119 offset0:33 offset1:41
	v_mov_b32_e32 v2, v67
	s_waitcnt lgkmcnt(3)
	v_mul_f32_e32 v3, 0x42000000, v6
	ds_read2_b32 v[14:15], v119 offset0:198 offset1:206
	ds_read2_b32 v[16:17], v119 offset0:231 offset1:239
	ds_read2_b32 v[18:19], v119 offset0:132 offset1:140
	ds_read2_b32 v[20:21], v119 offset0:165 offset1:173
	s_waitcnt lgkmcnt(5)
	v_mul_f32_e32 v5, 0x42000000, v10
	s_waitcnt lgkmcnt(4)
	v_mul_f32_e32 v6, 0x42000000, v12
	v_cvt_pk_fp8_f32 v2, v5, v6
	v_mul_f32_e32 v4, 0x42000000, v8
	s_waitcnt lgkmcnt(1)
	v_mul_f32_e32 v6, 0x42000000, v18
	s_waitcnt lgkmcnt(0)
	v_mul_f32_e32 v8, 0x42000000, v20
	v_cvt_pk_fp8_f32 v2, v3, v4 op_sel:[0,0,1]
	v_mov_b32_e32 v3, v67
	ds_read2_b32 v[22:23], v42 offset0:74 offset1:82
	ds_read2_b32 v[24:25], v42 offset0:107 offset1:115
	ds_read2_b32 v[26:27], v42 offset0:8 offset1:16
	ds_read2_b32 v[28:29], v42 offset0:41 offset1:49
	v_cvt_pk_fp8_f32 v3, v6, v8
	ds_read2_b32 v[30:31], v42 offset0:140 offset1:148
	ds_read2_b32 v[32:33], v42 offset0:173 offset1:181
	v_mul_f32_e32 v4, 0x42000000, v14
	v_mul_f32_e32 v5, 0x42000000, v16
	v_cvt_pk_fp8_f32 v3, v4, v5 op_sel:[0,0,1]
	s_waitcnt lgkmcnt(3)
	v_mul_f32_e32 v5, 0x42000000, v26
	s_waitcnt lgkmcnt(2)
	v_mul_f32_e32 v10, 0x42000000, v28
	v_mov_b32_e32 v4, v67
	ds_read2_b32 v[34:35], v42 offset0:206 offset1:214
	ds_read2_b32 v[36:37], v42 offset0:239 offset1:247
	v_cvt_pk_fp8_f32 v4, v5, v10
	s_waitcnt lgkmcnt(3)
	v_mul_f32_e32 v10, 0x42000000, v30
	s_waitcnt lgkmcnt(2)
	v_mul_f32_e32 v12, 0x42000000, v32
	v_mov_b32_e32 v5, v67
	v_cvt_pk_fp8_f32 v5, v10, v12
	v_mul_f32_e32 v6, 0x42000000, v22
	v_mul_f32_e32 v8, 0x42000000, v24
	v_cvt_pk_fp8_f32 v4, v6, v8 op_sel:[0,0,1]
	s_waitcnt lgkmcnt(1)
	v_mul_f32_e32 v6, 0x42000000, v34
	s_waitcnt lgkmcnt(0)
	v_mul_f32_e32 v8, 0x42000000, v36
	v_cvt_pk_fp8_f32 v5, v6, v8 op_sel:[0,0,1]
	v_mul_f32_e32 v6, 0x42000000, v13
	v_mul_f32_e32 v8, 0x42000000, v29
	global_store_dwordx4 v[40:41], v[2:5], off
	s_nop 1
	v_mul_f32_e32 v3, 0x42000000, v11
	v_mov_b32_e32 v2, v67
	v_mul_f32_e32 v4, 0x42000000, v7
	v_cvt_pk_fp8_f32 v2, v3, v6
	v_mul_f32_e32 v6, 0x42000000, v19
	v_mul_f32_e32 v7, 0x42000000, v21
	v_mov_b32_e32 v3, v67
	v_cvt_pk_fp8_f32 v3, v6, v7
	v_mul_f32_e32 v5, 0x42000000, v9
	v_cvt_pk_fp8_f32 v2, v4, v5 op_sel:[0,0,1]
	v_mul_f32_e32 v4, 0x42000000, v15
	v_mul_f32_e32 v5, 0x42000000, v17
	v_cvt_pk_fp8_f32 v3, v4, v5 op_sel:[0,0,1]
	v_mul_f32_e32 v5, 0x42000000, v27
	v_mov_b32_e32 v4, v67
	v_cvt_pk_fp8_f32 v4, v5, v8
	v_mul_f32_e32 v8, 0x42000000, v31
	v_mul_f32_e32 v9, 0x42000000, v33
	v_mov_b32_e32 v5, v67
	v_cvt_pk_fp8_f32 v5, v8, v9
	v_mul_f32_e32 v6, 0x42000000, v23
	v_mul_f32_e32 v7, 0x42000000, v25
	v_cvt_pk_fp8_f32 v4, v6, v7 op_sel:[0,0,1]
	v_mul_f32_e32 v6, 0x42000000, v35
	v_mul_f32_e32 v7, 0x42000000, v37
	ds_read2_b32 v[8:9], v119 offset0:82 offset1:90
	ds_read2_b32 v[10:11], v119 offset0:115 offset1:123
	ds_read2_b32 v[12:13], v119 offset0:16 offset1:24
	ds_read2_b32 v[14:15], v119 offset0:49 offset1:57
	v_cvt_pk_fp8_f32 v5, v6, v7 op_sel:[0,0,1]
	v_lshl_add_u64 v[6:7], v[38:39], 0, v[72:73]
	global_store_dwordx4 v[6:7], v[2:5], off
	s_waitcnt lgkmcnt(1)
	s_nop 0
	v_mul_f32_e32 v5, 0x42000000, v12
	s_waitcnt lgkmcnt(0)
	v_mul_f32_e32 v6, 0x42000000, v14
	v_mov_b32_e32 v2, v67
	v_cvt_pk_fp8_f32 v2, v5, v6
	ds_read2_b32 v[16:17], v119 offset0:214 offset1:222
	ds_read2_b32 v[18:19], v119 offset0:247 offset1:255
	ds_read2_b32 v[6:7], v119 offset0:148 offset1:156
	ds_read2_b32 v[20:21], v119 offset0:181 offset1:189
	v_mul_f32_e32 v3, 0x42000000, v8
	v_mul_f32_e32 v4, 0x42000000, v10
	v_cvt_pk_fp8_f32 v2, v3, v4 op_sel:[0,0,1]
	s_waitcnt lgkmcnt(1)
	v_mul_f32_e32 v6, 0x42000000, v6
	s_waitcnt lgkmcnt(0)
	v_mul_f32_e32 v8, 0x42000000, v20
	v_mov_b32_e32 v3, v67
	ds_read2_b32 v[22:23], v42 offset0:90 offset1:98
	ds_read2_b32 v[24:25], v42 offset0:123 offset1:131
	ds_read2_b32 v[26:27], v42 offset0:24 offset1:32
	ds_read2_b32 v[28:29], v42 offset0:57 offset1:65
	v_cvt_pk_fp8_f32 v3, v6, v8
	v_mul_f32_e32 v4, 0x42000000, v16
	v_mul_f32_e32 v5, 0x42000000, v18
	ds_read2_b32 v[30:31], v42 offset0:156 offset1:164
	ds_read2_b32 v[32:33], v42 offset0:189 offset1:197
	ds_read2_b32 v[34:35], v42 offset0:222 offset1:230
	v_cvt_pk_fp8_f32 v3, v4, v5 op_sel:[0,0,1]
	s_waitcnt lgkmcnt(4)
	v_mul_f32_e32 v5, 0x42000000, v26
	s_waitcnt lgkmcnt(3)
	v_mul_f32_e32 v10, 0x42000000, v28
	v_mov_b32_e32 v4, v67
	v_cvt_pk_fp8_f32 v4, v5, v10
	v_add_u32_e32 v5, 0x600, v119
	ds_read2_b32 v[36:37], v5 offset0:127 offset1:135
	s_waitcnt lgkmcnt(3)
	v_mul_f32_e32 v10, 0x42000000, v30
	s_waitcnt lgkmcnt(2)
	v_mul_f32_e32 v12, 0x42000000, v32
	v_mov_b32_e32 v5, v67
	v_cvt_pk_fp8_f32 v5, v10, v12
	v_mul_f32_e32 v6, 0x42000000, v22
	v_mul_f32_e32 v8, 0x42000000, v24
	v_cvt_pk_fp8_f32 v4, v6, v8 op_sel:[0,0,1]
	s_waitcnt lgkmcnt(1)
	v_mul_f32_e32 v6, 0x42000000, v34
	s_waitcnt lgkmcnt(0)
	v_mul_f32_e32 v8, 0x42000000, v36
	v_cvt_pk_fp8_f32 v5, v6, v8 op_sel:[0,0,1]
	v_mul_f32_e32 v8, 0x42000000, v9
	v_mul_f32_e32 v9, 0x42000000, v11
	v_mul_f32_e32 v10, 0x42000000, v13
	v_mul_f32_e32 v11, 0x42000000, v15
	v_mov_b32_e32 v6, v67
	v_cvt_pk_fp8_f32 v6, v10, v11
	v_mul_f32_e32 v10, 0x42000000, v7
	v_mul_f32_e32 v11, 0x42000000, v21
	v_mov_b32_e32 v7, v67
	v_cvt_pk_fp8_f32 v7, v10, v11
	v_cvt_pk_fp8_f32 v6, v8, v9 op_sel:[0,0,1]
	v_mul_f32_e32 v8, 0x42000000, v17
	v_mul_f32_e32 v9, 0x42000000, v19
	v_cvt_pk_fp8_f32 v7, v8, v9 op_sel:[0,0,1]
	v_mul_f32_e32 v9, 0x42000000, v27
	v_mul_f32_e32 v12, 0x42000000, v29
	v_mov_b32_e32 v8, v67
	v_cvt_pk_fp8_f32 v8, v9, v12
	v_mul_f32_e32 v12, 0x42000000, v31
	v_mul_f32_e32 v13, 0x42000000, v33
	v_mov_b32_e32 v9, v67
	v_cvt_pk_fp8_f32 v9, v12, v13
	v_mul_f32_e32 v10, 0x42000000, v23
	v_mul_f32_e32 v11, 0x42000000, v25
	v_cvt_pk_fp8_f32 v8, v10, v11 op_sel:[0,0,1]
	v_mul_f32_e32 v10, 0x42000000, v35
	v_mul_f32_e32 v11, 0x42000000, v37
	v_cvt_pk_fp8_f32 v9, v10, v11 op_sel:[0,0,1]
	v_lshl_add_u64 v[10:11], v[38:39], 0, v[78:79]
	global_store_dwordx4 v[10:11], v[2:5], off
	s_nop 1
	v_lshl_add_u64 v[2:3], v[38:39], 0, v[84:85]
	global_store_dwordx4 v[2:3], v[6:9], off
.LBB0_21:
	s_mov_b64 s[18:19], 0
.LBB0_22:
	s_andn2_b64 vcc, exec, s[18:19]
	s_cbranch_vccnz .LBB0_24
	s_mul_i32 s2, s16, 0xfffe5c00
	s_add_i32 s2, s46, s2
	s_and_b32 s2, s2, 0x3fc0
	s_ashr_i32 s17, s16, 31
	s_addk_i32 s2, 0xe000
	s_lshl_b64 s[18:19], s[16:17], 22
	s_lshl_b64 s[22:23], s[2:3], 12
	s_waitcnt lgkmcnt(0)
	s_add_u32 s18, s10, s18
	s_addc_u32 s19, s11, s19
	s_add_u32 s18, s18, s22
	s_addc_u32 s19, s19, s23
	s_and_b32 s21, s45, 0x3c0
	s_lshl_b32 s22, s21, 2
	s_add_u32 s18, s18, s22
	s_addc_u32 s19, s19, 0
	v_lshlrev_b32_e32 v66, 2, v118
	v_lshl_add_u64 v[62:63], s[18:19], 0, v[66:67]
	v_lshl_add_u64 v[2:3], v[62:63], 0, v[120:121]
	global_load_dwordx4 v[2:5], v[2:3], off
	v_lshl_add_u64 v[34:35], v[62:63], 0, v[152:153]
	v_lshl_add_u64 v[38:39], v[62:63], 0, v[156:157]
	v_lshl_add_u64 v[6:7], v[62:63], 0, v[124:125]
	global_load_dwordx4 v[34:37], v[34:35], off
	v_lshl_add_u64 v[42:43], v[62:63], 0, v[160:161]
	global_load_dwordx4 v[38:41], v[38:39], off
	v_lshl_add_u64 v[10:11], v[62:63], 0, v[128:129]
	global_load_dwordx4 v[6:9], v[6:7], off
	v_lshl_add_u64 v[46:47], v[62:63], 0, v[164:165]
	global_load_dwordx4 v[42:45], v[42:43], off
	v_lshl_add_u64 v[14:15], v[62:63], 0, v[132:133]
	global_load_dwordx4 v[10:13], v[10:11], off
	v_lshl_add_u64 v[50:51], v[62:63], 0, v[168:169]
	global_load_dwordx4 v[46:49], v[46:47], off
	v_lshl_add_u64 v[18:19], v[62:63], 0, v[136:137]
	global_load_dwordx4 v[14:17], v[14:15], off
	v_lshl_add_u64 v[54:55], v[62:63], 0, v[172:173]
	global_load_dwordx4 v[50:53], v[50:51], off
	v_lshl_add_u64 v[22:23], v[62:63], 0, v[140:141]
	global_load_dwordx4 v[18:21], v[18:19], off
	v_lshl_add_u64 v[58:59], v[62:63], 0, v[176:177]
	global_load_dwordx4 v[54:57], v[54:55], off
	v_lshl_add_u64 v[26:27], v[62:63], 0, v[144:145]
	global_load_dwordx4 v[22:25], v[22:23], off
	v_lshl_add_u64 v[30:31], v[62:63], 0, v[148:149]
	global_load_dwordx4 v[58:61], v[58:59], off
	v_lshl_add_u64 v[62:63], v[62:63], 0, v[180:181]
	global_load_dwordx4 v[26:29], v[26:27], off
	v_add_u32_e32 v66, v189, v188
	global_load_dwordx4 v[62:65], v[62:63], off
	v_add_u32_e32 v186, 0x410, v66
	global_load_dwordx4 v[30:33], v[30:31], off
	v_add_u32_e32 v187, 0x418, v66
	v_add_u32_e32 v190, 0x820, v66
	v_add_u32_e32 v191, 0x828, v66
	v_add_u32_e32 v192, 0xc30, v66
	v_add_u32_e32 v193, 0xc38, v66
	v_add_u32_e32 v194, 0x1040, v66
	v_add_u32_e32 v195, 0x1048, v66
	v_add_u32_e32 v196, 0x1450, v66
	v_add_u32_e32 v197, 0x1458, v66
	v_add_u32_e32 v198, 0x1860, v66
	v_add_u32_e32 v199, 0x1868, v66
	v_add_u32_e32 v200, 0x1c70, v66
	v_add_u32_e32 v201, 0x1c78, v66
	v_add_u32_e32 v202, 0x2080, v66
	v_add_u32_e32 v203, 0x2088, v66
	v_add_u32_e32 v204, 0x2490, v66
	s_lshl_b64 s[18:19], s[16:17], 21
	s_add_u32 s17, s36, s18
	s_addc_u32 s18, s37, s19
	s_lshl_b32 s19, s21, 11
	s_add_u32 s17, s17, s19
	s_addc_u32 s21, s18, 0
	s_lshl_b64 s[18:19], s[2:3], 1
	s_add_u32 s18, s17, s18
	s_addc_u32 s19, s21, s19
	s_waitcnt vmcnt(15)
	ds_write2_b32 v66, v2, v3 offset1:1
	ds_write2_b32 v66, v4, v5 offset0:2 offset1:3
	s_waitcnt vmcnt(12)
	ds_write2_b32 v186, v6, v7 offset1:1
	ds_write2_b32 v187, v8, v9 offset1:1
	s_waitcnt vmcnt(10)
	ds_write2_b32 v190, v10, v11 offset1:1
	ds_write2_b32 v191, v12, v13 offset1:1
	s_waitcnt vmcnt(8)
	ds_write2_b32 v192, v14, v15 offset1:1
	ds_write2_b32 v193, v16, v17 offset1:1
	s_waitcnt vmcnt(6)
	ds_write2_b32 v194, v18, v19 offset1:1
	ds_write2_b32 v195, v20, v21 offset1:1
	s_waitcnt vmcnt(4)
	ds_write2_b32 v196, v22, v23 offset1:1
	ds_write2_b32 v197, v24, v25 offset1:1
	s_waitcnt vmcnt(2)
	ds_write2_b32 v198, v26, v27 offset1:1
	ds_write2_b32 v199, v28, v29 offset1:1
	s_waitcnt vmcnt(0)
	ds_write2_b32 v200, v30, v31 offset1:1
	ds_write2_b32 v201, v32, v33 offset1:1
	ds_write2_b32 v202, v34, v35 offset1:1
	ds_write2_b32 v203, v36, v37 offset1:1
	ds_write2_b32 v204, v38, v39 offset1:1
	v_add_u32_e32 v2, 0x2498, v66
	ds_write2_b32 v2, v40, v41 offset1:1
	v_add_u32_e32 v2, 0x28a0, v66
	ds_write2_b32 v2, v42, v43 offset1:1
	v_add_u32_e32 v2, 0x28a8, v66
	ds_write2_b32 v2, v44, v45 offset1:1
	v_add_u32_e32 v2, 0x2cb0, v66
	ds_write2_b32 v2, v46, v47 offset1:1
	v_add_u32_e32 v2, 0x2cb8, v66
	ds_write2_b32 v2, v48, v49 offset1:1
	v_add_u32_e32 v2, 0x30c0, v66
	ds_write2_b32 v2, v50, v51 offset1:1
	v_add_u32_e32 v2, 0x30c8, v66
	ds_write2_b32 v2, v52, v53 offset1:1
	v_add_u32_e32 v2, 0x34d0, v66
	ds_write2_b32 v2, v54, v55 offset1:1
	v_add_u32_e32 v2, 0x34d8, v66
	ds_write2_b32 v2, v56, v57 offset1:1
	v_add_u32_e32 v2, 0x38e0, v66
	ds_write2_b32 v2, v58, v59 offset1:1
	v_add_u32_e32 v2, 0x38e8, v66
	ds_write2_b32 v2, v60, v61 offset1:1
	v_add_u32_e32 v2, 0x3cf0, v66
	ds_write2_b32 v2, v62, v63 offset1:1
	v_add_u32_e32 v2, 0x3cf8, v66
	ds_write2_b32 v2, v64, v65 offset1:1
	s_waitcnt lgkmcnt(0)
	v_add_u32_e32 v26, 0x400, v185
	ds_read2_b32 v[6:7], v185 offset0:65 offset1:73
	ds_read2_b32 v[8:9], v185 offset1:8
	ds_read2_b32 v[10:11], v185 offset0:130 offset1:138
	ds_read2_b32 v[12:13], v185 offset0:195 offset1:203
	ds_read2_b32 v[14:15], v26 offset0:4 offset1:12
	ds_read2_b32 v[16:17], v26 offset0:69 offset1:77
	ds_read2_b32 v[18:19], v26 offset0:134 offset1:142
	ds_read2_b32 v[20:21], v26 offset0:199 offset1:207
	v_lshlrev_b32_e32 v66, 1, v70
	v_lshl_add_u64 v[22:23], s[18:19], 0, v[66:67]
	s_waitcnt lgkmcnt(6)
	v_cvt_pk_bf16_f32 v2, v8, v6
	s_waitcnt lgkmcnt(4)
	v_cvt_pk_bf16_f32 v3, v10, v12
	s_waitcnt lgkmcnt(2)
	v_cvt_pk_bf16_f32 v4, v14, v16
	s_waitcnt lgkmcnt(0)
	v_cvt_pk_bf16_f32 v5, v18, v20
	v_lshl_add_u64 v[24:25], v[22:23], 0, v[112:113]
	global_store_dwordx4 v[24:25], v[2:5], off
	s_nop 1
	v_cvt_pk_bf16_f32 v2, v9, v7
	v_cvt_pk_bf16_f32 v3, v11, v13
	v_cvt_pk_bf16_f32 v4, v15, v17
	v_cvt_pk_bf16_f32 v5, v19, v21
	ds_read2_b32 v[8:9], v185 offset0:81 offset1:89
	ds_read2_b32 v[10:11], v185 offset0:16 offset1:24
	ds_read2_b32 v[12:13], v185 offset0:146 offset1:154
	ds_read2_b32 v[14:15], v185 offset0:211 offset1:219
	ds_read2_b32 v[16:17], v26 offset0:20 offset1:28
	ds_read2_b32 v[18:19], v26 offset0:85 offset1:93
	ds_read2_b32 v[20:21], v26 offset0:150 offset1:158
	ds_read2_b32 v[24:25], v26 offset0:215 offset1:223
	v_lshl_add_u64 v[6:7], v[22:23], 0, v[74:75]
	global_store_dwordx4 v[6:7], v[2:5], off
	v_lshl_add_u64 v[6:7], v[22:23], 0, v[80:81]
	s_waitcnt lgkmcnt(6)
	v_cvt_pk_bf16_f32 v2, v10, v8
	s_waitcnt lgkmcnt(4)
	v_cvt_pk_bf16_f32 v3, v12, v14
	s_waitcnt lgkmcnt(2)
	v_cvt_pk_bf16_f32 v4, v16, v18
	s_waitcnt lgkmcnt(0)
	v_cvt_pk_bf16_f32 v5, v20, v24
	global_store_dwordx4 v[6:7], v[2:5], off
	v_lshl_add_u64 v[6:7], v[22:23], 0, v[86:87]
	s_nop 0
	v_cvt_pk_bf16_f32 v2, v11, v9
	v_cvt_pk_bf16_f32 v3, v13, v15
	v_cvt_pk_bf16_f32 v4, v17, v19
	v_cvt_pk_bf16_f32 v5, v21, v25
	ds_read2_b32 v[8:9], v185 offset0:32 offset1:40
	ds_read2_b32 v[10:11], v185 offset0:97 offset1:105
	ds_read2_b32 v[12:13], v185 offset0:162 offset1:170
	ds_read2_b32 v[14:15], v185 offset0:227 offset1:235
	ds_read2_b32 v[16:17], v26 offset0:36 offset1:44
	ds_read2_b32 v[18:19], v26 offset0:101 offset1:109
	ds_read2_b32 v[20:21], v26 offset0:166 offset1:174
	ds_read2_b32 v[24:25], v26 offset0:231 offset1:239
	global_store_dwordx4 v[6:7], v[2:5], off
	v_lshl_add_u64 v[6:7], v[22:23], 0, v[90:91]
	s_waitcnt lgkmcnt(6)
	v_cvt_pk_bf16_f32 v2, v8, v10
	s_waitcnt lgkmcnt(4)
	v_cvt_pk_bf16_f32 v3, v12, v14
	s_waitcnt lgkmcnt(2)
	v_cvt_pk_bf16_f32 v4, v16, v18
	s_waitcnt lgkmcnt(0)
	v_cvt_pk_bf16_f32 v5, v20, v24
	global_store_dwordx4 v[6:7], v[2:5], off
	v_lshl_add_u64 v[6:7], v[22:23], 0, v[94:95]
	s_nop 0
	v_cvt_pk_bf16_f32 v2, v9, v11
	v_cvt_pk_bf16_f32 v3, v13, v15
	v_cvt_pk_bf16_f32 v4, v17, v19
	v_cvt_pk_bf16_f32 v5, v21, v25
	ds_read2_b32 v[8:9], v185 offset0:48 offset1:56
	ds_read2_b32 v[10:11], v185 offset0:113 offset1:121
	ds_read2_b32 v[12:13], v185 offset0:178 offset1:186
	ds_read2_b32 v[14:15], v185 offset0:243 offset1:251
	ds_read2_b32 v[16:17], v26 offset0:52 offset1:60
	ds_read2_b32 v[18:19], v26 offset0:117 offset1:125
	ds_read2_b32 v[20:21], v26 offset0:182 offset1:190
	ds_read2_b32 v[24:25], v26 offset0:247 offset1:255
	global_store_dwordx4 v[6:7], v[2:5], off
	v_lshl_add_u64 v[6:7], v[22:23], 0, v[98:99]
	s_waitcnt lgkmcnt(6)
	v_cvt_pk_bf16_f32 v2, v8, v10
	s_waitcnt lgkmcnt(4)
	v_cvt_pk_bf16_f32 v3, v12, v14
	s_waitcnt lgkmcnt(2)
	v_cvt_pk_bf16_f32 v4, v16, v18
	s_waitcnt lgkmcnt(0)
	v_cvt_pk_bf16_f32 v5, v20, v24
	global_store_dwordx4 v[6:7], v[2:5], off
	v_lshl_add_u64 v[6:7], v[22:23], 0, v[102:103]
	s_nop 0
	v_cvt_pk_bf16_f32 v2, v9, v11
	v_cvt_pk_bf16_f32 v3, v13, v15
	v_cvt_pk_bf16_f32 v4, v17, v19
	v_cvt_pk_bf16_f32 v5, v21, v25
	global_store_dwordx4 v[6:7], v[2:5], off
.LBB0_24:
	s_mov_b64 s[18:19], 0
.LBB0_25:
	s_andn2_b64 vcc, exec, s[18:19]
	s_cbranch_vccnz .LBB0_27
	s_add_i32 s2, s20, 0xfffff900
	s_lshr_b32 s2, s2, 6
	s_lshl_b32 s17, s16, 2
	s_add_i32 s18, s2, s17
	s_ashr_i32 s19, s18, 31
	s_and_b32 s2, s46, 0xc0
	s_lshl_b64 s[22:23], s[18:19], 20
	s_waitcnt lgkmcnt(0)
	s_add_u32 s17, s8, s22
	s_addc_u32 s21, s9, s23
	s_lshl_b32 s22, s2, 12
	s_add_u32 s17, s17, s22
	s_addc_u32 s21, s21, 0
	s_and_b32 s24, s45, 0x3c0
	s_lshl_b32 s22, s24, 2
	s_add_u32 s22, s17, s22
	s_addc_u32 s23, s21, 0
	v_lshlrev_b32_e32 v66, 2, v118
	v_lshl_add_u64 v[62:63], s[22:23], 0, v[66:67]
	v_lshl_add_u64 v[2:3], v[62:63], 0, v[120:121]
	global_load_dwordx4 v[2:5], v[2:3], off
	v_lshl_add_u64 v[34:35], v[62:63], 0, v[152:153]
	v_lshl_add_u64 v[38:39], v[62:63], 0, v[156:157]
	v_lshl_add_u64 v[6:7], v[62:63], 0, v[124:125]
	global_load_dwordx4 v[34:37], v[34:35], off
	v_lshl_add_u64 v[42:43], v[62:63], 0, v[160:161]
	global_load_dwordx4 v[38:41], v[38:39], off
	v_lshl_add_u64 v[10:11], v[62:63], 0, v[128:129]
	global_load_dwordx4 v[6:9], v[6:7], off
	v_lshl_add_u64 v[46:47], v[62:63], 0, v[164:165]
	global_load_dwordx4 v[42:45], v[42:43], off
	v_lshl_add_u64 v[14:15], v[62:63], 0, v[132:133]
	global_load_dwordx4 v[10:13], v[10:11], off
	v_lshl_add_u64 v[50:51], v[62:63], 0, v[168:169]
	global_load_dwordx4 v[46:49], v[46:47], off
	v_lshl_add_u64 v[18:19], v[62:63], 0, v[136:137]
	global_load_dwordx4 v[14:17], v[14:15], off
	v_lshl_add_u64 v[54:55], v[62:63], 0, v[172:173]
	global_load_dwordx4 v[50:53], v[50:51], off
	v_lshl_add_u64 v[22:23], v[62:63], 0, v[140:141]
	global_load_dwordx4 v[18:21], v[18:19], off
	v_lshl_add_u64 v[58:59], v[62:63], 0, v[176:177]
	global_load_dwordx4 v[54:57], v[54:55], off
	v_lshl_add_u64 v[26:27], v[62:63], 0, v[144:145]
	global_load_dwordx4 v[22:25], v[22:23], off
	v_lshl_add_u64 v[30:31], v[62:63], 0, v[148:149]
	global_load_dwordx4 v[58:61], v[58:59], off
	v_lshl_add_u64 v[62:63], v[62:63], 0, v[180:181]
	global_load_dwordx4 v[26:29], v[26:27], off
	v_add_u32_e32 v66, v189, v188
	global_load_dwordx4 v[62:65], v[62:63], off
	v_add_u32_e32 v186, 0x410, v66
	global_load_dwordx4 v[30:33], v[30:31], off
	v_add_u32_e32 v187, 0x418, v66
	v_add_u32_e32 v190, 0x820, v66
	v_add_u32_e32 v191, 0x828, v66
	v_add_u32_e32 v192, 0xc30, v66
	v_add_u32_e32 v193, 0xc38, v66
	v_add_u32_e32 v194, 0x1040, v66
	v_add_u32_e32 v195, 0x1048, v66
	v_add_u32_e32 v196, 0x1450, v66
	v_add_u32_e32 v197, 0x1458, v66
	v_add_u32_e32 v198, 0x1860, v66
	v_add_u32_e32 v199, 0x1868, v66
	v_add_u32_e32 v200, 0x1c70, v66
	v_add_u32_e32 v201, 0x1c78, v66
	v_add_u32_e32 v202, 0x2080, v66
	v_add_u32_e32 v203, 0x2088, v66
	v_add_u32_e32 v204, 0x2490, v66
	s_lshl_b64 s[18:19], s[18:19], 19
	s_add_u32 s17, s38, s18
	s_addc_u32 s18, s39, s19
	s_lshl_b32 s19, s24, 9
	s_add_u32 s17, s17, s19
	s_addc_u32 s19, s18, 0
	s_lshl_b32 s2, s2, 1
	s_add_u32 s18, s17, s2
	s_addc_u32 s19, s19, 0
	s_waitcnt vmcnt(15)
	ds_write2_b32 v66, v2, v3 offset1:1
	ds_write2_b32 v66, v4, v5 offset0:2 offset1:3
	s_waitcnt vmcnt(12)
	ds_write2_b32 v186, v6, v7 offset1:1
	ds_write2_b32 v187, v8, v9 offset1:1
	s_waitcnt vmcnt(10)
	ds_write2_b32 v190, v10, v11 offset1:1
	ds_write2_b32 v191, v12, v13 offset1:1
	s_waitcnt vmcnt(8)
	ds_write2_b32 v192, v14, v15 offset1:1
	ds_write2_b32 v193, v16, v17 offset1:1
	s_waitcnt vmcnt(6)
	ds_write2_b32 v194, v18, v19 offset1:1
	ds_write2_b32 v195, v20, v21 offset1:1
	s_waitcnt vmcnt(4)
	ds_write2_b32 v196, v22, v23 offset1:1
	ds_write2_b32 v197, v24, v25 offset1:1
	s_waitcnt vmcnt(2)
	ds_write2_b32 v198, v26, v27 offset1:1
	ds_write2_b32 v199, v28, v29 offset1:1
	s_waitcnt vmcnt(0)
	ds_write2_b32 v200, v30, v31 offset1:1
	ds_write2_b32 v201, v32, v33 offset1:1
	ds_write2_b32 v202, v34, v35 offset1:1
	ds_write2_b32 v203, v36, v37 offset1:1
	ds_write2_b32 v204, v38, v39 offset1:1
	v_add_u32_e32 v2, 0x2498, v66
	ds_write2_b32 v2, v40, v41 offset1:1
	v_add_u32_e32 v2, 0x28a0, v66
	ds_write2_b32 v2, v42, v43 offset1:1
	v_add_u32_e32 v2, 0x28a8, v66
	ds_write2_b32 v2, v44, v45 offset1:1
	v_add_u32_e32 v2, 0x2cb0, v66
	ds_write2_b32 v2, v46, v47 offset1:1
	v_add_u32_e32 v2, 0x2cb8, v66
	ds_write2_b32 v2, v48, v49 offset1:1
	v_add_u32_e32 v2, 0x30c0, v66
	ds_write2_b32 v2, v50, v51 offset1:1
	v_add_u32_e32 v2, 0x30c8, v66
	ds_write2_b32 v2, v52, v53 offset1:1
	v_add_u32_e32 v2, 0x34d0, v66
	ds_write2_b32 v2, v54, v55 offset1:1
	v_add_u32_e32 v2, 0x34d8, v66
	ds_write2_b32 v2, v56, v57 offset1:1
	v_add_u32_e32 v2, 0x38e0, v66
	ds_write2_b32 v2, v58, v59 offset1:1
	v_add_u32_e32 v2, 0x38e8, v66
	ds_write2_b32 v2, v60, v61 offset1:1
	v_add_u32_e32 v2, 0x3cf0, v66
	ds_write2_b32 v2, v62, v63 offset1:1
	v_add_u32_e32 v2, 0x3cf8, v66
	ds_write2_b32 v2, v64, v65 offset1:1
	s_waitcnt lgkmcnt(0)
	v_add_u32_e32 v26, 0x400, v185
	ds_read2_b32 v[6:7], v185 offset0:65 offset1:73
	ds_read2_b32 v[8:9], v185 offset1:8
	ds_read2_b32 v[10:11], v185 offset0:130 offset1:138
	ds_read2_b32 v[12:13], v185 offset0:195 offset1:203
	ds_read2_b32 v[14:15], v26 offset0:4 offset1:12
	ds_read2_b32 v[16:17], v26 offset0:69 offset1:77
	ds_read2_b32 v[18:19], v26 offset0:134 offset1:142
	ds_read2_b32 v[20:21], v26 offset0:199 offset1:207
	v_lshlrev_b32_e32 v66, 1, v70
	v_lshl_add_u64 v[22:23], s[18:19], 0, v[66:67]
	s_waitcnt lgkmcnt(6)
	v_cvt_pk_bf16_f32 v2, v8, v6
	s_waitcnt lgkmcnt(4)
	v_cvt_pk_bf16_f32 v3, v10, v12
	s_waitcnt lgkmcnt(2)
	v_cvt_pk_bf16_f32 v4, v14, v16
	s_waitcnt lgkmcnt(0)
	v_cvt_pk_bf16_f32 v5, v18, v20
	v_lshl_add_u64 v[24:25], v[22:23], 0, v[114:115]
	global_store_dwordx4 v[24:25], v[2:5], off
	s_nop 1
	v_cvt_pk_bf16_f32 v2, v9, v7
	v_cvt_pk_bf16_f32 v3, v11, v13
	v_cvt_pk_bf16_f32 v4, v15, v17
	v_cvt_pk_bf16_f32 v5, v19, v21
	ds_read2_b32 v[8:9], v185 offset0:81 offset1:89
	ds_read2_b32 v[10:11], v185 offset0:16 offset1:24
	ds_read2_b32 v[12:13], v185 offset0:146 offset1:154
	ds_read2_b32 v[14:15], v185 offset0:211 offset1:219
	ds_read2_b32 v[16:17], v26 offset0:20 offset1:28
	ds_read2_b32 v[18:19], v26 offset0:85 offset1:93
	ds_read2_b32 v[20:21], v26 offset0:150 offset1:158
	ds_read2_b32 v[24:25], v26 offset0:215 offset1:223
	v_lshl_add_u64 v[6:7], v[22:23], 0, v[76:77]
	global_store_dwordx4 v[6:7], v[2:5], off
	v_lshl_add_u64 v[6:7], v[22:23], 0, v[82:83]
	s_waitcnt lgkmcnt(6)
	v_cvt_pk_bf16_f32 v2, v10, v8
	s_waitcnt lgkmcnt(4)
	v_cvt_pk_bf16_f32 v3, v12, v14
	s_waitcnt lgkmcnt(2)
	v_cvt_pk_bf16_f32 v4, v16, v18
	s_waitcnt lgkmcnt(0)
	v_cvt_pk_bf16_f32 v5, v20, v24
	global_store_dwordx4 v[6:7], v[2:5], off
	v_lshl_add_u64 v[6:7], v[22:23], 0, v[88:89]
	s_nop 0
	v_cvt_pk_bf16_f32 v2, v11, v9
	v_cvt_pk_bf16_f32 v3, v13, v15
	v_cvt_pk_bf16_f32 v4, v17, v19
	v_cvt_pk_bf16_f32 v5, v21, v25
	ds_read2_b32 v[8:9], v185 offset0:32 offset1:40
	ds_read2_b32 v[10:11], v185 offset0:97 offset1:105
	ds_read2_b32 v[12:13], v185 offset0:162 offset1:170
	ds_read2_b32 v[14:15], v185 offset0:227 offset1:235
	ds_read2_b32 v[16:17], v26 offset0:36 offset1:44
	ds_read2_b32 v[18:19], v26 offset0:101 offset1:109
	ds_read2_b32 v[20:21], v26 offset0:166 offset1:174
	ds_read2_b32 v[24:25], v26 offset0:231 offset1:239
	global_store_dwordx4 v[6:7], v[2:5], off
	v_lshl_add_u64 v[6:7], v[22:23], 0, v[92:93]
	s_waitcnt lgkmcnt(6)
	v_cvt_pk_bf16_f32 v2, v8, v10
	s_waitcnt lgkmcnt(4)
	v_cvt_pk_bf16_f32 v3, v12, v14
	s_waitcnt lgkmcnt(2)
	v_cvt_pk_bf16_f32 v4, v16, v18
	s_waitcnt lgkmcnt(0)
	v_cvt_pk_bf16_f32 v5, v20, v24
	global_store_dwordx4 v[6:7], v[2:5], off
	v_lshl_add_u64 v[6:7], v[22:23], 0, v[96:97]
	s_nop 0
	v_cvt_pk_bf16_f32 v2, v9, v11
	v_cvt_pk_bf16_f32 v3, v13, v15
	v_cvt_pk_bf16_f32 v4, v17, v19
	v_cvt_pk_bf16_f32 v5, v21, v25
	ds_read2_b32 v[8:9], v185 offset0:48 offset1:56
	ds_read2_b32 v[10:11], v185 offset0:113 offset1:121
	ds_read2_b32 v[12:13], v185 offset0:178 offset1:186
	ds_read2_b32 v[14:15], v185 offset0:243 offset1:251
	ds_read2_b32 v[16:17], v26 offset0:52 offset1:60
	ds_read2_b32 v[18:19], v26 offset0:117 offset1:125
	ds_read2_b32 v[20:21], v26 offset0:182 offset1:190
	ds_read2_b32 v[24:25], v26 offset0:247 offset1:255
	global_store_dwordx4 v[6:7], v[2:5], off
	v_lshl_add_u64 v[6:7], v[22:23], 0, v[100:101]
	s_waitcnt lgkmcnt(6)
	v_cvt_pk_bf16_f32 v2, v8, v10
	s_waitcnt lgkmcnt(4)
	v_cvt_pk_bf16_f32 v3, v12, v14
	s_waitcnt lgkmcnt(2)
	v_cvt_pk_bf16_f32 v4, v16, v18
	s_waitcnt lgkmcnt(0)
	v_cvt_pk_bf16_f32 v5, v20, v24
	global_store_dwordx4 v[6:7], v[2:5], off
	v_lshl_add_u64 v[6:7], v[22:23], 0, v[104:105]
	s_nop 0
	v_cvt_pk_bf16_f32 v2, v9, v11
	v_cvt_pk_bf16_f32 v3, v13, v15
	v_cvt_pk_bf16_f32 v4, v17, v19
	v_cvt_pk_bf16_f32 v5, v21, v25
	global_store_dwordx4 v[6:7], v[2:5], off
.LBB0_27:
	s_mov_b64 s[18:19], 0
.LBB0_28:
	s_andn2_b64 vcc, exec, s[18:19]
	s_cbranch_vccnz .LBB0_13
	s_mul_hi_i32 s2, s20, 0x92492493
	s_add_i32 s2, s2, s20
	s_lshr_b32 s17, s2, 31
	s_ashr_i32 s19, s2, 6
	s_add_i32 s19, s19, s17
	s_mul_i32 s2, s19, 0xffffff90
	s_mul_i32 s17, s16, 0x6900
	s_sub_i32 s2, s2, s17
	s_add_i32 s86, s30, s2
	s_lshl_b32 s18, s86, 6
	s_add_i32 s2, s18, 0xffffff10
	s_cmp_gt_u32 s86, 47
	s_cselect_b32 s2, s2, 0
	s_cmp_eq_u32 s86, 44
	s_cselect_b64 s[20:21], -1, 0
	s_and_b64 s[22:23], s[20:21], exec
	s_cselect_b32 s22, 0xb00, s2
	s_mov_b64 s[24:25], -1
	s_cmp_gt_i32 s86, 47
	s_mul_hi_i32 s87, s16, 0x1b10000
	s_mul_i32 s88, s16, 0x1b10000
	s_cbranch_scc0 .LBB0_31
	s_lshl_b32 s2, s19, 6
	s_and_b32 s25, s2, 0xffffff80
	s_lshl_b32 s2, s19, 5
	s_and_b32 s2, s2, 32
	s_ashr_i32 s17, s16, 31
	s_waitcnt lgkmcnt(0)
	s_add_u32 s23, s14, s88
	s_addc_u32 s89, s15, s87
	s_ashr_i32 s24, s25, 31
	s_mul_i32 s91, s25, 0x6c40
	s_mul_hi_i32 s90, s25, 0x6c40
	s_add_u32 s96, s23, s91
	s_addc_u32 s89, s89, s90
	s_ashr_i32 s23, s22, 31
	s_lshl_b64 s[90:91], s[22:23], 2
	s_add_u32 s23, s96, s90
	s_addc_u32 s89, s89, s91
	s_lshl_b32 s90, s2, 2
	s_add_u32 s90, s23, s90
	s_addc_u32 s91, s89, 0
	v_lshl_add_u64 v[2:3], s[90:91], 0, v[116:117]
	v_lshlrev_b32_e32 v66, 2, v184
	v_lshl_add_u64 v[62:63], v[2:3], 0, v[66:67]
	v_add_co_u32_e32 v6, vcc, s71, v62
	s_lshl_b64 s[90:91], s[16:17], 22
	s_nop 0
	v_addc_co_u32_e32 v7, vcc, 0, v63, vcc
	v_add_co_u32_e32 v10, vcc, s72, v62
	global_load_dwordx4 v[2:5], v[62:63], off
	s_nop 0
	global_load_dwordx4 v[6:9], v[6:7], off offset:512
	v_addc_co_u32_e32 v11, vcc, 0, v63, vcc
	v_add_co_u32_e32 v14, vcc, s73, v62
	s_add_u32 s17, s40, s90
	s_nop 0
	v_addc_co_u32_e32 v15, vcc, 0, v63, vcc
	global_load_dwordx4 v[10:13], v[10:11], off offset:1024
	s_nop 0
	global_load_dwordx4 v[14:17], v[14:15], off offset:1536
	v_add_co_u32_e32 v18, vcc, s74, v62
	s_addc_u32 s23, s41, s91
	s_nop 0
	v_addc_co_u32_e32 v19, vcc, 0, v63, vcc
	v_add_co_u32_e32 v22, vcc, s75, v62
	s_add_i32 s2, s18, s2
	s_nop 0
	v_addc_co_u32_e32 v23, vcc, 0, v63, vcc
	global_load_dwordx4 v[18:21], v[18:19], off offset:2048
	s_nop 0
	global_load_dwordx4 v[22:25], v[22:23], off offset:2560
	v_add_co_u32_e32 v26, vcc, s76, v62
	s_addk_i32 s2, 0xf400
	s_nop 0
	v_addc_co_u32_e32 v27, vcc, 0, v63, vcc
	v_add_co_u32_e32 v30, vcc, s77, v62
	s_lshl_b64 s[90:91], s[2:3], 10
	s_nop 0
	v_addc_co_u32_e32 v31, vcc, 0, v63, vcc
	global_load_dwordx4 v[26:29], v[26:27], off offset:3072
	s_nop 0
	global_load_dwordx4 v[30:33], v[30:31], off offset:3584
	v_add_co_u32_e32 v34, vcc, s78, v62
	s_add_u32 s2, s17, s90
	s_nop 0
	v_addc_co_u32_e32 v35, vcc, 0, v63, vcc
	v_add_co_u32_e32 v38, vcc, s79, v62
	s_addc_u32 s17, s23, s91
	s_nop 0
	v_addc_co_u32_e32 v39, vcc, 0, v63, vcc
	global_load_dwordx4 v[34:37], v[34:35], off
	s_nop 0
	global_load_dwordx4 v[38:41], v[38:39], off offset:512
	v_add_co_u32_e32 v42, vcc, s80, v62
	s_add_u32 s90, s2, s25
	s_nop 0
	v_addc_co_u32_e32 v43, vcc, 0, v63, vcc
	v_add_co_u32_e32 v46, vcc, s81, v62
	s_addc_u32 s91, s17, s24
	s_nop 0
	v_addc_co_u32_e32 v47, vcc, 0, v63, vcc
	global_load_dwordx4 v[42:45], v[42:43], off offset:1024
	s_nop 0
	global_load_dwordx4 v[46:49], v[46:47], off offset:1536
	v_add_co_u32_e32 v50, vcc, s82, v62
	s_mov_b64 s[24:25], 0
	s_nop 0
	v_addc_co_u32_e32 v51, vcc, 0, v63, vcc
	global_load_dwordx4 v[50:53], v[50:51], off offset:2048
	v_add_co_u32_e32 v54, vcc, s83, v62
	s_nop 1
	v_addc_co_u32_e32 v55, vcc, 0, v63, vcc
	global_load_dwordx4 v[54:57], v[54:55], off offset:2560
	v_add_co_u32_e32 v58, vcc, s84, v62
	s_nop 1
	v_addc_co_u32_e32 v59, vcc, 0, v63, vcc
	global_load_dwordx4 v[58:61], v[58:59], off offset:3072
	v_add_co_u32_e32 v62, vcc, s85, v62
	s_nop 1
	v_addc_co_u32_e32 v63, vcc, 0, v63, vcc
	global_load_dwordx4 v[62:65], v[62:63], off offset:3584
	s_waitcnt vmcnt(15)
	ds_write2_b32 v71, v2, v3 offset1:1
	ds_write2_b32 v71, v4, v5 offset0:2 offset1:3
	v_add_u32_e32 v2, 0x420, v71
	s_waitcnt vmcnt(14)
	ds_write2_b32 v2, v6, v7 offset1:1
	v_add_u32_e32 v2, 0x428, v71
	ds_write2_b32 v2, v8, v9 offset1:1
	v_add_u32_e32 v2, 0x840, v71
	s_waitcnt vmcnt(13)
	ds_write2_b32 v2, v10, v11 offset1:1
	v_add_u32_e32 v2, 0x848, v71
	ds_write2_b32 v2, v12, v13 offset1:1
	v_add_u32_e32 v2, 0xc60, v71
	s_waitcnt vmcnt(12)
	ds_write2_b32 v2, v14, v15 offset1:1
	v_add_u32_e32 v2, 0xc68, v71
	ds_write2_b32 v2, v16, v17 offset1:1
	v_add_u32_e32 v2, 0x1080, v71
	s_waitcnt vmcnt(11)
	ds_write2_b32 v2, v18, v19 offset1:1
	v_add_u32_e32 v2, 0x1088, v71
	ds_write2_b32 v2, v20, v21 offset1:1
	v_add_u32_e32 v2, 0x14a0, v71
	s_waitcnt vmcnt(10)
	ds_write2_b32 v2, v22, v23 offset1:1
	v_add_u32_e32 v2, 0x14a8, v71
	ds_write2_b32 v2, v24, v25 offset1:1
	v_add_u32_e32 v2, 0x18c0, v71
	s_waitcnt vmcnt(9)
	ds_write2_b32 v2, v26, v27 offset1:1
	v_add_u32_e32 v2, 0x18c8, v71
	ds_write2_b32 v2, v28, v29 offset1:1
	v_add_u32_e32 v2, 0x1ce0, v71
	s_waitcnt vmcnt(8)
	ds_write2_b32 v2, v30, v31 offset1:1
	v_add_u32_e32 v2, 0x1ce8, v71
	ds_write2_b32 v2, v32, v33 offset1:1
	v_add_u32_e32 v2, 0x2100, v71
	s_waitcnt vmcnt(7)
	ds_write2_b32 v2, v34, v35 offset1:1
	v_add_u32_e32 v2, 0x2108, v71
	ds_write2_b32 v2, v36, v37 offset1:1
	v_add_u32_e32 v2, 0x2520, v71
	s_waitcnt vmcnt(6)
	ds_write2_b32 v2, v38, v39 offset1:1
	v_add_u32_e32 v2, 0x2528, v71
	ds_write2_b32 v2, v40, v41 offset1:1
	v_add_u32_e32 v2, 0x2940, v71
	v_lshl_add_u64 v[38:39], s[90:91], 0, v[68:69]
	v_lshl_add_u64 v[40:41], v[38:39], 0, v[108:109]
	s_waitcnt vmcnt(5)
	ds_write2_b32 v2, v42, v43 offset1:1
	v_add_u32_e32 v2, 0x2948, v71
	ds_write2_b32 v2, v44, v45 offset1:1
	v_add_u32_e32 v2, 0x2d60, v71
	s_waitcnt vmcnt(4)
	ds_write2_b32 v2, v46, v47 offset1:1
	v_add_u32_e32 v2, 0x2d68, v71
	ds_write2_b32 v2, v48, v49 offset1:1
	v_add_u32_e32 v2, 0x3180, v71
	s_waitcnt vmcnt(3)
	ds_write2_b32 v2, v50, v51 offset1:1
	v_add_u32_e32 v2, 0x3188, v71
	ds_write2_b32 v2, v52, v53 offset1:1
	v_add_u32_e32 v2, 0x35a0, v71
	v_add_u32_e32 v42, 0x400, v119
	s_waitcnt vmcnt(2)
	ds_write2_b32 v2, v54, v55 offset1:1
	v_add_u32_e32 v2, 0x35a8, v71
	ds_write2_b32 v2, v56, v57 offset1:1
	v_add_u32_e32 v2, 0x39c0, v71
	s_waitcnt vmcnt(1)
	ds_write2_b32 v2, v58, v59 offset1:1
	v_add_u32_e32 v2, 0x39c8, v71
	ds_write2_b32 v2, v60, v61 offset1:1
	v_add_u32_e32 v2, 0x3de0, v71
	s_waitcnt vmcnt(0)
	ds_write2_b32 v2, v62, v63 offset1:1
	v_add_u32_e32 v2, 0x3de8, v71
	ds_write2_b32 v2, v64, v65 offset1:1
	s_waitcnt lgkmcnt(0)
	ds_read2_b32 v[6:7], v119 offset0:66 offset1:74
	ds_read2_b32 v[8:9], v119 offset0:99 offset1:107
	ds_read2_b32 v[10:11], v119 offset1:8
	ds_read2_b32 v[12:13], v119 offset0:33 offset1:41
	v_mov_b32_e32 v2, v67
	s_waitcnt lgkmcnt(3)
	v_mul_f32_e32 v3, 0x42000000, v6
	ds_read2_b32 v[14:15], v119 offset0:198 offset1:206
	ds_read2_b32 v[16:17], v119 offset0:231 offset1:239
	ds_read2_b32 v[18:19], v119 offset0:132 offset1:140
	ds_read2_b32 v[20:21], v119 offset0:165 offset1:173
	s_waitcnt lgkmcnt(5)
	v_mul_f32_e32 v5, 0x42000000, v10
	s_waitcnt lgkmcnt(4)
	v_mul_f32_e32 v6, 0x42000000, v12
	v_cvt_pk_fp8_f32 v2, v5, v6
	v_mul_f32_e32 v4, 0x42000000, v8
	s_waitcnt lgkmcnt(1)
	v_mul_f32_e32 v6, 0x42000000, v18
	s_waitcnt lgkmcnt(0)
	v_mul_f32_e32 v8, 0x42000000, v20
	v_cvt_pk_fp8_f32 v2, v3, v4 op_sel:[0,0,1]
	v_mov_b32_e32 v3, v67
	ds_read2_b32 v[22:23], v42 offset0:74 offset1:82
	ds_read2_b32 v[24:25], v42 offset0:107 offset1:115
	ds_read2_b32 v[26:27], v42 offset0:8 offset1:16
	ds_read2_b32 v[28:29], v42 offset0:41 offset1:49
	v_cvt_pk_fp8_f32 v3, v6, v8
	ds_read2_b32 v[30:31], v42 offset0:140 offset1:148
	ds_read2_b32 v[32:33], v42 offset0:173 offset1:181
	v_mul_f32_e32 v4, 0x42000000, v14
	v_mul_f32_e32 v5, 0x42000000, v16
	v_cvt_pk_fp8_f32 v3, v4, v5 op_sel:[0,0,1]
	s_waitcnt lgkmcnt(3)
	v_mul_f32_e32 v5, 0x42000000, v26
	s_waitcnt lgkmcnt(2)
	v_mul_f32_e32 v10, 0x42000000, v28
	v_mov_b32_e32 v4, v67
	ds_read2_b32 v[34:35], v42 offset0:206 offset1:214
	ds_read2_b32 v[36:37], v42 offset0:239 offset1:247
	v_cvt_pk_fp8_f32 v4, v5, v10
	s_waitcnt lgkmcnt(3)
	v_mul_f32_e32 v10, 0x42000000, v30
	s_waitcnt lgkmcnt(2)
	v_mul_f32_e32 v12, 0x42000000, v32
	v_mov_b32_e32 v5, v67
	v_cvt_pk_fp8_f32 v5, v10, v12
	v_mul_f32_e32 v6, 0x42000000, v22
	v_mul_f32_e32 v8, 0x42000000, v24
	v_cvt_pk_fp8_f32 v4, v6, v8 op_sel:[0,0,1]
	s_waitcnt lgkmcnt(1)
	v_mul_f32_e32 v6, 0x42000000, v34
	s_waitcnt lgkmcnt(0)
	v_mul_f32_e32 v8, 0x42000000, v36
	v_cvt_pk_fp8_f32 v5, v6, v8 op_sel:[0,0,1]
	v_mul_f32_e32 v6, 0x42000000, v13
	v_mul_f32_e32 v8, 0x42000000, v29
	global_store_dwordx4 v[40:41], v[2:5], off
	s_nop 1
	v_mul_f32_e32 v3, 0x42000000, v11
	v_mov_b32_e32 v2, v67
	v_mul_f32_e32 v4, 0x42000000, v7
	v_cvt_pk_fp8_f32 v2, v3, v6
	v_mul_f32_e32 v6, 0x42000000, v19
	v_mul_f32_e32 v7, 0x42000000, v21
	v_mov_b32_e32 v3, v67
	v_cvt_pk_fp8_f32 v3, v6, v7
	v_mul_f32_e32 v5, 0x42000000, v9
	v_cvt_pk_fp8_f32 v2, v4, v5 op_sel:[0,0,1]
	v_mul_f32_e32 v4, 0x42000000, v15
	v_mul_f32_e32 v5, 0x42000000, v17
	v_cvt_pk_fp8_f32 v3, v4, v5 op_sel:[0,0,1]
	v_mul_f32_e32 v5, 0x42000000, v27
	v_mov_b32_e32 v4, v67
	v_cvt_pk_fp8_f32 v4, v5, v8
	v_mul_f32_e32 v8, 0x42000000, v31
	v_mul_f32_e32 v9, 0x42000000, v33
	v_mov_b32_e32 v5, v67
	v_cvt_pk_fp8_f32 v5, v8, v9
	v_mul_f32_e32 v6, 0x42000000, v23
	v_mul_f32_e32 v7, 0x42000000, v25
	v_cvt_pk_fp8_f32 v4, v6, v7 op_sel:[0,0,1]
	v_mul_f32_e32 v6, 0x42000000, v35
	v_mul_f32_e32 v7, 0x42000000, v37
	ds_read2_b32 v[8:9], v119 offset0:82 offset1:90
	ds_read2_b32 v[10:11], v119 offset0:115 offset1:123
	ds_read2_b32 v[12:13], v119 offset0:16 offset1:24
	ds_read2_b32 v[14:15], v119 offset0:49 offset1:57
	v_cvt_pk_fp8_f32 v5, v6, v7 op_sel:[0,0,1]
	v_lshl_add_u64 v[6:7], v[38:39], 0, v[72:73]
	global_store_dwordx4 v[6:7], v[2:5], off
	s_waitcnt lgkmcnt(1)
	s_nop 0
	v_mul_f32_e32 v5, 0x42000000, v12
	s_waitcnt lgkmcnt(0)
	v_mul_f32_e32 v6, 0x42000000, v14
	v_mov_b32_e32 v2, v67
	v_cvt_pk_fp8_f32 v2, v5, v6
	ds_read2_b32 v[16:17], v119 offset0:214 offset1:222
	ds_read2_b32 v[18:19], v119 offset0:247 offset1:255
	ds_read2_b32 v[6:7], v119 offset0:148 offset1:156
	ds_read2_b32 v[20:21], v119 offset0:181 offset1:189
	v_mul_f32_e32 v3, 0x42000000, v8
	v_mul_f32_e32 v4, 0x42000000, v10
	v_cvt_pk_fp8_f32 v2, v3, v4 op_sel:[0,0,1]
	s_waitcnt lgkmcnt(1)
	v_mul_f32_e32 v6, 0x42000000, v6
	s_waitcnt lgkmcnt(0)
	v_mul_f32_e32 v8, 0x42000000, v20
	v_mov_b32_e32 v3, v67
	ds_read2_b32 v[22:23], v42 offset0:90 offset1:98
	ds_read2_b32 v[24:25], v42 offset0:123 offset1:131
	ds_read2_b32 v[26:27], v42 offset0:24 offset1:32
	ds_read2_b32 v[28:29], v42 offset0:57 offset1:65
	v_cvt_pk_fp8_f32 v3, v6, v8
	v_mul_f32_e32 v4, 0x42000000, v16
	v_mul_f32_e32 v5, 0x42000000, v18
	ds_read2_b32 v[30:31], v42 offset0:156 offset1:164
	ds_read2_b32 v[32:33], v42 offset0:189 offset1:197
	ds_read2_b32 v[34:35], v42 offset0:222 offset1:230
	v_cvt_pk_fp8_f32 v3, v4, v5 op_sel:[0,0,1]
	s_waitcnt lgkmcnt(4)
	v_mul_f32_e32 v5, 0x42000000, v26
	s_waitcnt lgkmcnt(3)
	v_mul_f32_e32 v10, 0x42000000, v28
	v_mov_b32_e32 v4, v67
	v_cvt_pk_fp8_f32 v4, v5, v10
	v_add_u32_e32 v5, 0x600, v119
	ds_read2_b32 v[36:37], v5 offset0:127 offset1:135
	s_waitcnt lgkmcnt(3)
	v_mul_f32_e32 v10, 0x42000000, v30
	s_waitcnt lgkmcnt(2)
	v_mul_f32_e32 v12, 0x42000000, v32
	v_mov_b32_e32 v5, v67
	v_cvt_pk_fp8_f32 v5, v10, v12
	v_mul_f32_e32 v6, 0x42000000, v22
	v_mul_f32_e32 v8, 0x42000000, v24
	v_cvt_pk_fp8_f32 v4, v6, v8 op_sel:[0,0,1]
	s_waitcnt lgkmcnt(1)
	v_mul_f32_e32 v6, 0x42000000, v34
	s_waitcnt lgkmcnt(0)
	v_mul_f32_e32 v8, 0x42000000, v36
	v_cvt_pk_fp8_f32 v5, v6, v8 op_sel:[0,0,1]
	v_mul_f32_e32 v8, 0x42000000, v9
	v_mul_f32_e32 v9, 0x42000000, v11
	v_mul_f32_e32 v10, 0x42000000, v13
	v_mul_f32_e32 v11, 0x42000000, v15
	v_mov_b32_e32 v6, v67
	v_cvt_pk_fp8_f32 v6, v10, v11
	v_mul_f32_e32 v10, 0x42000000, v7
	v_mul_f32_e32 v11, 0x42000000, v21
	v_mov_b32_e32 v7, v67
	v_cvt_pk_fp8_f32 v7, v10, v11
	v_cvt_pk_fp8_f32 v6, v8, v9 op_sel:[0,0,1]
	v_mul_f32_e32 v8, 0x42000000, v17
	v_mul_f32_e32 v9, 0x42000000, v19
	v_cvt_pk_fp8_f32 v7, v8, v9 op_sel:[0,0,1]
	v_mul_f32_e32 v9, 0x42000000, v27
	v_mul_f32_e32 v12, 0x42000000, v29
	v_mov_b32_e32 v8, v67
	v_cvt_pk_fp8_f32 v8, v9, v12
	v_mul_f32_e32 v12, 0x42000000, v31
	v_mul_f32_e32 v13, 0x42000000, v33
	v_mov_b32_e32 v9, v67
	v_cvt_pk_fp8_f32 v9, v12, v13
	v_mul_f32_e32 v10, 0x42000000, v23
	v_mul_f32_e32 v11, 0x42000000, v25
	v_cvt_pk_fp8_f32 v8, v10, v11 op_sel:[0,0,1]
	v_mul_f32_e32 v10, 0x42000000, v35
	v_mul_f32_e32 v11, 0x42000000, v37
	v_cvt_pk_fp8_f32 v9, v10, v11 op_sel:[0,0,1]
	v_lshl_add_u64 v[10:11], v[38:39], 0, v[78:79]
	global_store_dwordx4 v[10:11], v[2:5], off
	s_nop 1
	v_lshl_add_u64 v[2:3], v[38:39], 0, v[84:85]
	global_store_dwordx4 v[2:3], v[6:9], off
.LBB0_31:
	s_andn2_b64 vcc, exec, s[24:25]
	s_cbranch_vccnz .LBB0_13
	s_cmp_lt_i32 s86, 44
	s_cselect_b64 s[24:25], -1, 0
	s_and_b64 s[90:91], s[24:25], exec
	s_cselect_b32 s86, s18, s22
	s_waitcnt lgkmcnt(0)
	s_add_u32 s2, s14, s88
	s_addc_u32 s17, s15, s87
	s_lshl_b32 s22, s19, 6
	s_mul_i32 s19, s19, 0x1b1000
	s_mul_hi_i32 s23, s22, 0x6c40
	s_add_u32 s2, s2, s19
	s_addc_u32 s17, s17, s23
	s_ashr_i32 s87, s86, 31
	s_lshl_b64 s[86:87], s[86:87], 2
	s_add_u32 s86, s2, s86
	s_addc_u32 s87, s17, s87
	s_and_b64 s[20:21], s[20:21], s[4:5]
	v_lshlrev_b32_e32 v66, 2, v118
	s_or_b64 s[20:21], s[24:25], s[20:21]
	v_lshl_add_u64 v[186:187], s[86:87], 0, v[66:67]
	v_mov_b32_e32 v2, 0
	v_mov_b32_e32 v6, 0
	v_mov_b32_e32 v7, 0
	v_mov_b32_e32 v8, 0
	v_mov_b32_e32 v9, 0
	s_and_saveexec_b64 s[24:25], s[20:21]
	s_cbranch_execz .LBB0_34
	v_lshl_add_u64 v[4:5], v[186:187], 0, v[122:123]
	global_load_dwordx4 v[6:9], v[4:5], off

.LBB0_149:
	s_mov_b32 s25, s2
	s_add_i32 s2, s2, 2
	s_mul_hi_i32 s6, s2, 0x78787879
	s_lshr_b32 s7, s6, 31
	s_ashr_i32 s6, s6, 11
	s_add_i32 s6, s6, s7
	s_mul_i32 s7, s6, 0xffffef00
	s_add_i32 s28, s25, s7
	s_add_i32 s29, s28, 2
	s_cmpk_lt_i32 s29, 0x100
	s_cselect_b64 s[14:15], -1, 0
	s_and_b64 s[26:27], s[14:15], exec
	s_cselect_b32 s13, 16, s6
	s_ashr_i32 s7, s6, 31
	s_addk_i32 s28, 0xff02
	s_ashr_i32 s26, s29, 31
	s_and_b64 s[14:15], s[14:15], exec
	v_readlane_b32 s36, v252, 12
	v_readlane_b32 s40, v252, 14
	s_cselect_b32 s14, s29, s28
	v_readlane_b32 s37, v252, 13
	v_readlane_b32 s41, v252, 15
	s_cselect_b32 s28, 20, 24
	s_cselect_b32 s15, s26, 0
	s_cselect_b32 s26, s41, s37
	s_cselect_b32 s27, s40, s36
	s_lshl_b64 s[6:7], s[6:7], s28
	s_add_u32 s27, s27, s6
	s_addc_u32 s26, s26, s7
	s_lshl_b64 s[6:7], s[14:15], 12
	s_add_u32 s6, s27, s6
	s_addc_u32 s7, s26, s7
	v_lshlrev_b64 v[8:9], 2, v[60:61]
	v_lshl_add_u64 v[10:11], s[6:7], 0, v[8:9]
	s_add_i32 s6, s25, 3
	s_mul_hi_i32 s6, s6, 0x78787879
	s_lshr_b32 s7, s6, 31
	s_ashr_i32 s6, s6, 11
	s_add_i32 s6, s6, s7
	s_mul_i32 s7, s6, 0xffffef00
	s_add_i32 s14, s25, s7
	s_add_i32 s25, s14, 3
	s_cmpk_lt_i32 s25, 0x100
	s_cselect_b64 s[38:39], -1, 0
	s_ashr_i32 s7, s6, 31
	s_ashr_i32 s26, s25, 31
	s_add_i32 s27, s14, 0xffffff03
	s_and_b64 s[14:15], s[38:39], exec
	s_cselect_b32 s15, s26, 0
	s_cselect_b32 s26, 20, 24
	s_cselect_b32 s14, s25, s27
	s_cselect_b32 s25, s41, s37
	s_cselect_b32 s28, s40, s36
	s_lshl_b64 s[26:27], s[6:7], s26
	s_add_u32 s7, s28, s26
	s_addc_u32 s25, s25, s27
	s_lshl_b64 s[14:15], s[14:15], 12
	s_add_u32 s14, s7, s14
	s_addc_u32 s15, s25, s15
	v_lshl_add_u64 v[12:13], s[14:15], 0, v[8:9]
	global_load_dwordx4 v[40:43], v[10:11], off offset:16
	global_load_dwordx4 v[44:47], v[10:11], off
	global_load_dwordx4 v[32:35], v[10:11], off offset:2064
	global_load_dwordx4 v[36:39], v[10:11], off offset:2048
	global_load_dwordx4 v[16:19], v[12:13], off offset:16
	global_load_dwordx4 v[20:23], v[12:13], off
	s_nop 0
	global_load_dwordx4 v[8:11], v[12:13], off offset:2064
	s_nop 0
	global_load_dwordx4 v[12:15], v[12:13], off offset:2048
	s_cmp_eq_u32 s13, s4
	s_cbranch_scc1 .LBB0_151
	s_mul_i32 s7, s13, 0x6000
	s_mul_hi_i32 s4, s13, 0x6000
	s_add_u32 s14, s60, s7
	global_load_dwordx4 v[24:27], v[48:49], off offset:16
	global_load_dwordx4 v[28:31], v[48:49], off
	s_addc_u32 s15, s63, s4
	v_lshl_add_u64 v[84:85], v[60:61], 2, s[14:15]
	v_add_co_u32_e32 v0, vcc, 0x1000, v84
	v_lshl_add_u64 v[58:59], v[84:85], 0, s[84:85]
	s_nop 0
	v_addc_co_u32_e32 v1, vcc, 0, v85, vcc
	global_load_dwordx4 v[54:57], v[0:1], off
	global_load_dwordx4 v[62:65], v[58:59], off offset:16
	global_load_dwordx4 v[4:7], v[84:85], off offset:16
	s_nop 0
	global_load_dwordx4 v[0:3], v[84:85], off
	global_load_dwordx4 v[72:75], v[48:49], off offset:2048
	global_load_dwordx4 v[66:69], v[48:49], off offset:2064
	global_load_dwordx4 v[76:79], v[58:59], off offset:2064
	global_load_dwordx4 v[80:83], v[58:59], off offset:2048
	s_mov_b32 s4, s13
	s_waitcnt vmcnt(0)
	v_pk_add_f32 v[56:57], v[56:57], 1.0 op_sel_hi:[1,0]
	v_pk_add_f32 v[54:55], v[54:55], 1.0 op_sel_hi:[1,0]
	v_pk_add_f32 v[58:59], v[64:65], 1.0 op_sel_hi:[1,0]
	v_pk_add_f32 v[62:63], v[62:63], 1.0 op_sel_hi:[1,0]
	v_pk_mul_f32 v[56:57], v[30:31], v[56:57]
	v_pk_mul_f32 v[58:59], v[26:27], v[58:59]
	v_pk_mul_f32 v[54:55], v[28:29], v[54:55]
	v_pk_mul_f32 v[62:63], v[24:25], v[62:63]
	global_load_dwordx4 v[24:27], v[84:85], off offset:2064
	global_load_dwordx4 v[28:31], v[84:85], off offset:2048
	v_pk_add_f32 v[64:65], v[82:83], 1.0 op_sel_hi:[1,0]
	v_pk_add_f32 v[70:71], v[78:79], 1.0 op_sel_hi:[1,0]
	v_pk_add_f32 v[78:79], v[80:81], 1.0 op_sel_hi:[1,0]
	v_pk_add_f32 v[76:77], v[76:77], 1.0 op_sel_hi:[1,0]
	v_pk_mul_f32 v[68:69], v[68:69], v[70:71]
	v_pk_mul_f32 v[64:65], v[74:75], v[64:65]
	v_pk_mul_f32 v[70:71], v[66:67], v[76:77]
	v_pk_mul_f32 v[66:67], v[72:73], v[78:79]
.LBB0_151:
	s_waitcnt vmcnt(0)
	v_mul_f32_e32 v72, v45, v45
	v_mul_f32_e32 v73, v47, v47
	v_fmac_f32_e32 v72, v44, v44
	v_fmac_f32_e32 v73, v46, v46
	v_add_f32_e32 v72, v72, v73
	v_mul_f32_e32 v73, v41, v41
	v_mul_f32_e32 v74, v43, v43
	v_fmac_f32_e32 v73, v40, v40
	v_fmac_f32_e32 v74, v42, v42
	v_add_f32_e32 v73, v73, v74
	v_add_f32_e32 v72, v72, v73
	v_mul_f32_e32 v73, v37, v37
	v_mul_f32_e32 v74, v39, v39
	v_fmac_f32_e32 v73, v36, v36
	v_fmac_f32_e32 v74, v38, v38
	v_add_f32_e32 v73, v73, v74
	v_add_f32_e32 v72, v72, v73
	v_mul_f32_e32 v73, v33, v33
	v_mul_f32_e32 v74, v35, v35
	v_fmac_f32_e32 v73, v32, v32
	v_fmac_f32_e32 v74, v34, v34
	v_add_f32_e32 v73, v73, v74
	v_add_f32_e32 v72, v72, v73
	ds_swizzle_b32 v73, v72 offset:swizzle(SWAP,1)
	s_and_b64 s[14:15], s[38:39], exec
	s_mov_b32 s7, s4
	s_cselect_b32 s4, 16, s6
	s_mov_b32 s6, 0x17dd9000
	s_waitcnt lgkmcnt(0)
	v_add_f32_e32 v72, v72, v73
	ds_swizzle_b32 v73, v72 offset:swizzle(SWAP,2)
	s_cmp_eq_u32 s4, s7
	s_waitcnt lgkmcnt(0)
	v_add_f32_e32 v72, v72, v73
	ds_swizzle_b32 v73, v72 offset:swizzle(SWAP,4)
	s_waitcnt lgkmcnt(0)
	v_add_f32_e32 v72, v72, v73
	ds_swizzle_b32 v73, v72 offset:swizzle(SWAP,8)
	s_waitcnt lgkmcnt(0)
	v_add_f32_e32 v72, v72, v73
	ds_swizzle_b32 v73, v72 offset:swizzle(SWAP,16)
	s_waitcnt lgkmcnt(0)
	v_add_f32_e32 v72, v72, v73
	v_mov_b32_e32 v73, v72
	s_nop 1
	v_permlane32_swap_b32_e32 v72, v73
	v_add_f32_e32 v72, v72, v73
	v_fmamk_f32 v72, v72, 0x3a800000, v196
	v_cmp_gt_f32_e32 vcc, s35, v72
	v_mul_f32_e32 v73, 0x4b800000, v72
	s_nop 0
	v_cndmask_b32_e32 v72, v72, v73, vcc
	v_rsq_f32_e32 v72, v72
	s_nop 0
	v_mul_f32_e32 v73, 0x45800000, v72
	v_cndmask_b32_e32 v72, v72, v73, vcc
	v_pk_mul_f32 v[42:43], v[42:43], v[72:73] op_sel_hi:[1,0]
	v_pk_mul_f32 v[44:45], v[44:45], v[72:73] op_sel_hi:[1,0]
	v_pk_mul_f32 v[46:47], v[46:47], v[72:73] op_sel_hi:[1,0]
	v_pk_mul_f32 v[40:41], v[40:41], v[72:73] op_sel_hi:[1,0]
	v_pk_fma_f32 v[78:79], v[58:59], v[42:43], v[6:7]
	v_lshl_add_u64 v[42:43], s[94:95], 0, v[52:53]
	v_pk_fma_f32 v[74:75], v[56:57], v[46:47], v[2:3]
	v_pk_fma_f32 v[76:77], v[54:55], v[44:45], v[0:1]
	v_pk_fma_f32 v[40:41], v[62:63], v[40:41], v[4:5]
	v_add_co_u32_e32 v42, vcc, s6, v42
	v_cvt_pk_bf16_f32 v44, v76, v77
	v_cvt_pk_bf16_f32 v45, v74, v75
	v_cvt_pk_bf16_f32 v46, v40, v41
	v_cvt_pk_bf16_f32 v47, v78, v79
	v_addc_co_u32_e32 v43, vcc, 0, v43, vcc
	global_store_dwordx4 v[42:43], v[44:47], off
	s_mov_b32 s6, 0x711d9000
	v_pk_mul_f32 v[36:37], v[36:37], v[72:73] op_sel_hi:[1,0]
	v_mov_b32_e32 v44, v113
	v_mov_b32_e32 v45, v113
	v_cvt_pk_fp8_f32 v44, v76, v77
	v_cvt_pk_fp8_f32 v45, v40, v41
	v_lshl_add_u64 v[40:41], s[94:95], 0, v[50:51]
	v_add_co_u32_e32 v40, vcc, s6, v40
	v_cvt_pk_fp8_f32 v44, v74, v75 op_sel:[0,0,1]
	v_cvt_pk_fp8_f32 v45, v78, v79 op_sel:[0,0,1]
	v_addc_co_u32_e32 v41, vcc, 0, v41, vcc
	v_pk_mul_f32 v[38:39], v[38:39], v[72:73] op_sel_hi:[1,0]
	v_pk_mul_f32 v[32:33], v[32:33], v[72:73] op_sel_hi:[1,0]
	v_pk_mul_f32 v[34:35], v[34:35], v[72:73] op_sel_hi:[1,0]
	global_store_dwordx2 v[40:41], v[44:45], off
	v_pk_fma_f32 v[38:39], v[64:65], v[38:39], v[30:31]
	v_pk_fma_f32 v[36:37], v[66:67], v[36:37], v[28:29]
	v_pk_fma_f32 v[44:45], v[68:69], v[34:35], v[26:27]
	v_pk_fma_f32 v[46:47], v[70:71], v[32:33], v[24:25]
	v_cvt_pk_bf16_f32 v32, v36, v37
	v_cvt_pk_bf16_f32 v33, v38, v39
	v_cvt_pk_bf16_f32 v34, v46, v47
	v_cvt_pk_bf16_f32 v35, v44, v45
	global_store_dwordx4 v[42:43], v[32:35], off offset:1024
	s_nop 1
	v_mov_b32_e32 v32, v113
	v_mov_b32_e32 v33, v113
	v_cvt_pk_fp8_f32 v32, v36, v37
	v_cvt_pk_fp8_f32 v33, v46, v47
	v_cvt_pk_fp8_f32 v32, v38, v39 op_sel:[0,0,1]
	v_cvt_pk_fp8_f32 v33, v44, v45 op_sel:[0,0,1]
	global_store_dwordx2 v[40:41], v[32:33], off offset:512
	s_cbranch_scc1 .LBB0_148
	s_mul_i32 s6, s4, 0x6000
	s_mul_hi_i32 s7, s4, 0x6000
	s_add_u32 s6, s60, s6
	s_addc_u32 s7, s63, s7
	v_lshl_add_u64 v[44:45], v[60:61], 2, s[6:7]
	v_add_co_u32_e32 v24, vcc, 0x1000, v44
	global_load_dwordx4 v[0:3], v[48:49], off offset:16
	global_load_dwordx4 v[4:7], v[48:49], off
	v_addc_co_u32_e32 v25, vcc, 0, v45, vcc
	v_lshl_add_u64 v[36:37], v[44:45], 0, s[84:85]
	global_load_dwordx4 v[24:27], v[24:25], off
	s_nop 0
	global_load_dwordx4 v[28:31], v[36:37], off offset:16
	s_waitcnt vmcnt(1)
	v_pk_add_f32 v[26:27], v[26:27], 1.0 op_sel_hi:[1,0]
	v_pk_add_f32 v[24:25], v[24:25], 1.0 op_sel_hi:[1,0]
	v_pk_mul_f32 v[56:57], v[6:7], v[26:27]
	v_pk_mul_f32 v[54:55], v[4:5], v[24:25]
	s_waitcnt vmcnt(0)
	v_pk_add_f32 v[4:5], v[30:31], 1.0 op_sel_hi:[1,0]
	v_pk_add_f32 v[6:7], v[28:29], 1.0 op_sel_hi:[1,0]
	v_pk_mul_f32 v[58:59], v[2:3], v[4:5]
	v_pk_mul_f32 v[62:63], v[0:1], v[6:7]
	global_load_dwordx4 v[4:7], v[44:45], off offset:16
	global_load_dwordx4 v[0:3], v[44:45], off
	global_load_dwordx4 v[24:27], v[48:49], off offset:2064
	global_load_dwordx4 v[28:31], v[48:49], off offset:2048
	global_load_dwordx4 v[32:35], v[36:37], off offset:2064
	s_nop 0
	global_load_dwordx4 v[36:39], v[36:37], off offset:2048
	s_waitcnt vmcnt(0)
	v_pk_add_f32 v[38:39], v[38:39], 1.0 op_sel_hi:[1,0]
	v_pk_add_f32 v[36:37], v[36:37], 1.0 op_sel_hi:[1,0]
	v_pk_mul_f32 v[64:65], v[30:31], v[38:39]
	v_pk_mul_f32 v[66:67], v[28:29], v[36:37]
	v_pk_add_f32 v[28:29], v[34:35], 1.0 op_sel_hi:[1,0]
	v_pk_add_f32 v[30:31], v[32:33], 1.0 op_sel_hi:[1,0]
	v_pk_mul_f32 v[68:69], v[26:27], v[28:29]
	v_pk_mul_f32 v[70:71], v[24:25], v[30:31]
	global_load_dwordx4 v[24:27], v[44:45], off offset:2064
	global_load_dwordx4 v[28:31], v[44:45], off offset:2048
	s_branch .LBB0_148

.Lpeel_inproj:
	s_add_u32 s28, s76, 0xfffc0080
	s_addc_u32 s29, s77, -1
	s_add_i32 s30, 0, 0x10000
	s_cmp_eq_u32 s71, 12
	s_cselect_b32 s83, s36, s29
	s_cselect_b32 s82, s37, s28
	v_add_u32_e32 v112, s30, v153
	s_cselect_b32 s81, s43, s65
	s_cselect_b32 s80, s50, s51
	s_add_i32 s31, 0, 0x14000
	ds_read_b128 v[130:133], v112
	ds_read_b128 v[134:137], v112 offset:1024
	ds_read_b128 v[156:159], v112 offset:2048
	ds_read_b128 v[160:163], v112 offset:3072
	v_add_u32_e32 v112, s31, v153
	ds_read_b128 v[164:167], v112
	ds_read_b128 v[168:171], v112 offset:1024
	ds_read_b128 v[172:175], v112 offset:2048
	ds_read_b128 v[176:179], v112 offset:3072
	v_lshl_add_u64 v[150:151], s[76:77], 0, v[146:147]
	s_add_i32 m0, s26, 0xc000
	ds_read_b128 v[180:183], v154
	ds_read_b128 v[184:187], v154 offset:1024
	ds_read_b128 v[188:191], v154 offset:2048
	ds_read_b128 v[192:195], v154 offset:3072
	ds_read_b128 v[206:209], v154 offset:4096
	ds_read_b128 v[210:213], v154 offset:5120
	ds_read_b128 v[216:219], v154 offset:6144
	ds_read_b128 v[220:223], v154 offset:7168
	global_load_lds_dwordx4 v[150:151], off
	v_lshl_add_u64 v[150:151], s[76:77], 0, v[148:149]
	s_add_i32 m0, s26, 0xe000
	s_nop 0
	global_load_lds_dwordx4 v[150:151], off
	s_waitcnt vmcnt(8)
	s_waitcnt lgkmcnt(0)
	s_barrier
	s_setprio 1
	v_mfma_f32_16x16x32_bf16 v[126:129], v[130:133], v[180:183], 0
	v_mfma_f32_16x16x32_bf16 v[122:125], v[156:159], v[180:183], 0
	v_mfma_f32_16x16x32_bf16 v[118:121], v[130:133], v[188:191], 0
	v_mfma_f32_16x16x32_bf16 v[114:117], v[156:159], v[188:191], 0
	v_mfma_f32_16x16x32_bf16 v[100:103], v[130:133], v[206:209], 0
	v_mfma_f32_16x16x32_bf16 v[96:99], v[156:159], v[206:209], 0
	v_mfma_f32_16x16x32_bf16 v[84:87], v[130:133], v[216:219], 0
	v_mfma_f32_16x16x32_bf16 v[80:83], v[156:159], v[216:219], 0
	v_mfma_f32_16x16x32_bf16 v[126:129], v[134:137], v[184:187], v[126:129]
	v_mfma_f32_16x16x32_bf16 v[122:125], v[160:163], v[184:187], v[122:125]
	v_mfma_f32_16x16x32_bf16 v[118:121], v[134:137], v[192:195], v[118:121]
	v_mfma_f32_16x16x32_bf16 v[114:117], v[160:163], v[192:195], v[114:117]
	v_mfma_f32_16x16x32_bf16 v[100:103], v[134:137], v[210:213], v[100:103]
	v_mfma_f32_16x16x32_bf16 v[96:99], v[160:163], v[210:213], v[96:99]
	v_mfma_f32_16x16x32_bf16 v[84:87], v[134:137], v[220:223], v[84:87]
	v_mfma_f32_16x16x32_bf16 v[80:83], v[160:163], v[220:223], v[80:83]
	s_setprio 0
	s_setprio 1
	v_mfma_f32_16x16x32_bf16 v[108:111], v[164:167], v[180:183], 0
	v_mfma_f32_16x16x32_bf16 v[104:107], v[172:175], v[180:183], 0
	v_mfma_f32_16x16x32_bf16 v[92:95], v[164:167], v[188:191], 0
	v_mfma_f32_16x16x32_bf16 v[88:91], v[172:175], v[188:191], 0
	v_mfma_f32_16x16x32_bf16 v[76:79], v[164:167], v[206:209], 0
	v_mfma_f32_16x16x32_bf16 v[72:75], v[172:175], v[206:209], 0
	v_mfma_f32_16x16x32_bf16 v[68:71], v[164:167], v[216:219], 0
	v_mfma_f32_16x16x32_bf16 v[64:67], v[172:175], v[216:219], 0
	v_mfma_f32_16x16x32_bf16 v[108:111], v[168:171], v[184:187], v[108:111]
	v_mfma_f32_16x16x32_bf16 v[104:107], v[176:179], v[184:187], v[104:107]
	v_mfma_f32_16x16x32_bf16 v[92:95], v[168:171], v[192:195], v[92:95]
	v_mfma_f32_16x16x32_bf16 v[88:91], v[176:179], v[192:195], v[88:91]
	v_mfma_f32_16x16x32_bf16 v[76:79], v[168:171], v[210:213], v[76:79]
	v_mfma_f32_16x16x32_bf16 v[72:75], v[176:179], v[210:213], v[72:75]
	v_mfma_f32_16x16x32_bf16 v[68:71], v[168:171], v[220:223], v[68:71]
	v_mfma_f32_16x16x32_bf16 v[64:67], v[176:179], v[220:223], v[64:67]
	s_setprio 0
	s_barrier
	s_add_i32 s28, s30, s13
	v_lshl_add_u64 v[150:151], s[80:81], 0, v[140:141]
	s_mov_b32 m0, s28
	ds_read_b128 v[180:183], v154 offset:16384
	ds_read_b128 v[184:187], v154 offset:17408
	ds_read_b128 v[188:191], v154 offset:18432
	ds_read_b128 v[192:195], v154 offset:19456
	ds_read_b128 v[206:209], v154 offset:20480
	ds_read_b128 v[210:213], v154 offset:21504
	ds_read_b128 v[216:219], v154 offset:22528
	ds_read_b128 v[220:223], v154 offset:23552
	global_load_lds_dwordx4 v[150:151], off
	s_add_i32 m0, s28, 0x2000
	s_add_u32 s28, s80, 0x40000
	v_lshl_add_u64 v[224:225], s[80:81], 0, v[144:145]
	s_addc_u32 s29, s81, 0
	s_add_i32 s30, s31, s13
	global_load_lds_dwordx4 v[224:225], off
	v_lshl_add_u64 v[226:227], s[28:29], 0, v[140:141]
	s_mov_b32 m0, s30
	v_lshl_add_u64 v[228:229], s[82:83], 0, v[142:143]
	global_load_lds_dwordx4 v[226:227], off
	v_lshl_add_u64 v[226:227], s[28:29], 0, v[144:145]
	s_add_i32 m0, s30, 0x2000
	s_nop 0
	global_load_lds_dwordx4 v[226:227], off
	v_lshl_add_u64 v[226:227], s[82:83], 0, v[138:139]
	s_mov_b32 m0, s26
	s_nop 0
	global_load_lds_dwordx4 v[226:227], off
	s_mov_b32 m0, s27
	s_nop 0
	global_load_lds_dwordx4 v[228:229], off
	s_waitcnt vmcnt(8)
	s_waitcnt lgkmcnt(0)
	s_barrier
	s_setprio 1
	v_mfma_f32_16x16x32_bf16 v[60:63], v[130:133], v[180:183], 0
	v_mfma_f32_16x16x32_bf16 v[56:59], v[156:159], v[180:183], 0
	v_mfma_f32_16x16x32_bf16 v[52:55], v[130:133], v[188:191], 0
	v_mfma_f32_16x16x32_bf16 v[48:51], v[156:159], v[188:191], 0
	v_mfma_f32_16x16x32_bf16 v[36:39], v[130:133], v[206:209], 0
	v_mfma_f32_16x16x32_bf16 v[32:35], v[156:159], v[206:209], 0
	v_mfma_f32_16x16x32_bf16 v[20:23], v[130:133], v[216:219], 0
	v_mfma_f32_16x16x32_bf16 v[16:19], v[156:159], v[216:219], 0
	v_mfma_f32_16x16x32_bf16 v[60:63], v[134:137], v[184:187], v[60:63]
	v_mfma_f32_16x16x32_bf16 v[56:59], v[160:163], v[184:187], v[56:59]
	v_mfma_f32_16x16x32_bf16 v[52:55], v[134:137], v[192:195], v[52:55]
	v_mfma_f32_16x16x32_bf16 v[48:51], v[160:163], v[192:195], v[48:51]
	v_mfma_f32_16x16x32_bf16 v[36:39], v[134:137], v[210:213], v[36:39]
	v_mfma_f32_16x16x32_bf16 v[32:35], v[160:163], v[210:213], v[32:35]
	v_mfma_f32_16x16x32_bf16 v[20:23], v[134:137], v[220:223], v[20:23]
	v_mfma_f32_16x16x32_bf16 v[16:19], v[160:163], v[220:223], v[16:19]
	s_setprio 0
	s_setprio 1
	v_mfma_f32_16x16x32_bf16 v[44:47], v[164:167], v[180:183], 0
	v_mfma_f32_16x16x32_bf16 v[40:43], v[172:175], v[180:183], 0
	v_mfma_f32_16x16x32_bf16 v[28:31], v[164:167], v[188:191], 0
	v_mfma_f32_16x16x32_bf16 v[24:27], v[172:175], v[188:191], 0
	v_mfma_f32_16x16x32_bf16 v[12:15], v[164:167], v[206:209], 0
	v_mfma_f32_16x16x32_bf16 v[8:11], v[172:175], v[206:209], 0
	v_mfma_f32_16x16x32_bf16 v[4:7], v[164:167], v[216:219], 0
	v_mfma_f32_16x16x32_bf16 v[0:3], v[172:175], v[216:219], 0
	v_mfma_f32_16x16x32_bf16 v[44:47], v[168:171], v[184:187], v[44:47]
	v_mfma_f32_16x16x32_bf16 v[40:43], v[176:179], v[184:187], v[40:43]
	v_mfma_f32_16x16x32_bf16 v[28:31], v[168:171], v[192:195], v[28:31]
	v_mfma_f32_16x16x32_bf16 v[24:27], v[176:179], v[192:195], v[24:27]
	v_mfma_f32_16x16x32_bf16 v[12:15], v[168:171], v[210:213], v[12:15]
	v_mfma_f32_16x16x32_bf16 v[8:11], v[176:179], v[210:213], v[8:11]
	v_mfma_f32_16x16x32_bf16 v[4:7], v[168:171], v[220:223], v[4:7]
	v_mfma_f32_16x16x32_bf16 v[0:3], v[176:179], v[220:223], v[0:3]
	s_setprio 0
	s_barrier
	s_add_i32 s30, 0, 0x18000
	v_add_u32_e32 v112, s30, v153
	s_add_i32 s31, 0, 0x1c000
	ds_read_b128 v[130:133], v112
	ds_read_b128 v[134:137], v112 offset:1024
	ds_read_b128 v[156:159], v112 offset:2048
	ds_read_b128 v[160:163], v112 offset:3072
	v_add_u32_e32 v112, s31, v153
	ds_read_b128 v[164:167], v112
	ds_read_b128 v[168:171], v112 offset:1024
	ds_read_b128 v[172:175], v112 offset:2048
	ds_read_b128 v[176:179], v112 offset:3072
	s_add_u32 s28, s82, 0x40000
	s_addc_u32 s29, s83, 0
	s_mov_b32 m0, s34
	v_lshl_add_u64 v[230:231], s[28:29], 0, v[138:139]
	ds_read_b128 v[180:183], v154 offset:32768
	ds_read_b128 v[184:187], v154 offset:33792
	ds_read_b128 v[188:191], v154 offset:34816
	ds_read_b128 v[192:195], v154 offset:35840
	ds_read_b128 v[206:209], v154 offset:36864
	ds_read_b128 v[210:213], v154 offset:37888
	ds_read_b128 v[216:219], v154 offset:38912
	ds_read_b128 v[220:223], v154 offset:39936
	global_load_lds_dwordx4 v[230:231], off
	v_lshl_add_u64 v[230:231], s[28:29], 0, v[142:143]
	s_mov_b32 m0, s14
	s_nop 0
	global_load_lds_dwordx4 v[230:231], off
	s_waitcnt vmcnt(8)
	s_waitcnt lgkmcnt(0)
	s_barrier
	s_setprio 1
	v_mfma_f32_16x16x32_bf16 v[126:129], v[130:133], v[180:183], v[126:129]
	v_mfma_f32_16x16x32_bf16 v[122:125], v[156:159], v[180:183], v[122:125]
	v_mfma_f32_16x16x32_bf16 v[118:121], v[130:133], v[188:191], v[118:121]
	v_mfma_f32_16x16x32_bf16 v[114:117], v[156:159], v[188:191], v[114:117]
	v_mfma_f32_16x16x32_bf16 v[100:103], v[130:133], v[206:209], v[100:103]
	v_mfma_f32_16x16x32_bf16 v[96:99], v[156:159], v[206:209], v[96:99]
	v_mfma_f32_16x16x32_bf16 v[84:87], v[130:133], v[216:219], v[84:87]
	v_mfma_f32_16x16x32_bf16 v[80:83], v[156:159], v[216:219], v[80:83]
	v_mfma_f32_16x16x32_bf16 v[126:129], v[134:137], v[184:187], v[126:129]
	v_mfma_f32_16x16x32_bf16 v[122:125], v[160:163], v[184:187], v[122:125]
	v_mfma_f32_16x16x32_bf16 v[118:121], v[134:137], v[192:195], v[118:121]
	v_mfma_f32_16x16x32_bf16 v[114:117], v[160:163], v[192:195], v[114:117]
	v_mfma_f32_16x16x32_bf16 v[100:103], v[134:137], v[210:213], v[100:103]
	v_mfma_f32_16x16x32_bf16 v[96:99], v[160:163], v[210:213], v[96:99]
	v_mfma_f32_16x16x32_bf16 v[84:87], v[134:137], v[220:223], v[84:87]
	v_mfma_f32_16x16x32_bf16 v[80:83], v[160:163], v[220:223], v[80:83]
	s_setprio 0
	s_setprio 1
	v_mfma_f32_16x16x32_bf16 v[108:111], v[164:167], v[180:183], v[108:111]
	v_mfma_f32_16x16x32_bf16 v[104:107], v[172:175], v[180:183], v[104:107]
	v_mfma_f32_16x16x32_bf16 v[92:95], v[164:167], v[188:191], v[92:95]
	v_mfma_f32_16x16x32_bf16 v[88:91], v[172:175], v[188:191], v[88:91]
	v_mfma_f32_16x16x32_bf16 v[76:79], v[164:167], v[206:209], v[76:79]
	v_mfma_f32_16x16x32_bf16 v[72:75], v[172:175], v[206:209], v[72:75]
	v_mfma_f32_16x16x32_bf16 v[68:71], v[164:167], v[216:219], v[68:71]
	v_mfma_f32_16x16x32_bf16 v[64:67], v[172:175], v[216:219], v[64:67]
	v_mfma_f32_16x16x32_bf16 v[108:111], v[168:171], v[184:187], v[108:111]
	v_mfma_f32_16x16x32_bf16 v[104:107], v[176:179], v[184:187], v[104:107]
	v_mfma_f32_16x16x32_bf16 v[92:95], v[168:171], v[192:195], v[92:95]
	v_mfma_f32_16x16x32_bf16 v[88:91], v[176:179], v[192:195], v[88:91]
	v_mfma_f32_16x16x32_bf16 v[76:79], v[168:171], v[210:213], v[76:79]
	v_mfma_f32_16x16x32_bf16 v[72:75], v[176:179], v[210:213], v[72:75]
	v_mfma_f32_16x16x32_bf16 v[68:71], v[168:171], v[220:223], v[68:71]
	v_mfma_f32_16x16x32_bf16 v[64:67], v[176:179], v[220:223], v[64:67]
	s_setprio 0
	s_barrier
	s_add_i32 s28, s30, s13
	v_lshl_add_u64 v[150:151], v[150:151], 0, s[56:57]
	s_mov_b32 m0, s28
	ds_read_b128 v[180:183], v154 offset:49152
	ds_read_b128 v[184:187], v154 offset:50176
	ds_read_b128 v[188:191], v154 offset:51200
	ds_read_b128 v[192:195], v154 offset:52224
	ds_read_b128 v[206:209], v154 offset:53248
	ds_read_b128 v[210:213], v154 offset:54272
	ds_read_b128 v[216:219], v154 offset:55296
	ds_read_b128 v[220:223], v154 offset:56320
	global_load_lds_dwordx4 v[150:151], off
	s_add_i32 m0, s28, 0x2000
	s_add_u32 s28, s80, 0x40080
	v_lshl_add_u64 v[150:151], v[224:225], 0, s[56:57]
	s_addc_u32 s29, s81, 0
	s_add_i32 s30, s31, s13
	global_load_lds_dwordx4 v[150:151], off
	v_lshl_add_u64 v[150:151], s[28:29], 0, v[140:141]
	s_mov_b32 m0, s30
	s_nop 0
	global_load_lds_dwordx4 v[150:151], off
	v_lshl_add_u64 v[150:151], s[28:29], 0, v[144:145]
	s_add_i32 m0, s30, 0x2000
	s_nop 0
	global_load_lds_dwordx4 v[150:151], off
	v_lshl_add_u64 v[150:151], v[226:227], 0, s[56:57]
	s_mov_b32 m0, s33
	s_nop 0
	global_load_lds_dwordx4 v[150:151], off
	v_lshl_add_u64 v[150:151], v[228:229], 0, s[56:57]
	s_mov_b32 m0, s69
	s_nop 0
	global_load_lds_dwordx4 v[150:151], off
	s_waitcnt vmcnt(8)
	s_waitcnt lgkmcnt(0)
	s_barrier
	s_setprio 1
	v_mfma_f32_16x16x32_bf16 v[60:63], v[130:133], v[180:183], v[60:63]
	v_mfma_f32_16x16x32_bf16 v[56:59], v[156:159], v[180:183], v[56:59]
	v_mfma_f32_16x16x32_bf16 v[52:55], v[130:133], v[188:191], v[52:55]
	v_mfma_f32_16x16x32_bf16 v[48:51], v[156:159], v[188:191], v[48:51]
	v_mfma_f32_16x16x32_bf16 v[36:39], v[130:133], v[206:209], v[36:39]
	v_mfma_f32_16x16x32_bf16 v[32:35], v[156:159], v[206:209], v[32:35]
	v_mfma_f32_16x16x32_bf16 v[20:23], v[130:133], v[216:219], v[20:23]
	v_mfma_f32_16x16x32_bf16 v[16:19], v[156:159], v[216:219], v[16:19]
	v_mfma_f32_16x16x32_bf16 v[60:63], v[134:137], v[184:187], v[60:63]
	v_mfma_f32_16x16x32_bf16 v[56:59], v[160:163], v[184:187], v[56:59]
	v_mfma_f32_16x16x32_bf16 v[52:55], v[134:137], v[192:195], v[52:55]
	v_mfma_f32_16x16x32_bf16 v[48:51], v[160:163], v[192:195], v[48:51]
	v_mfma_f32_16x16x32_bf16 v[36:39], v[134:137], v[210:213], v[36:39]
	v_mfma_f32_16x16x32_bf16 v[32:35], v[160:163], v[210:213], v[32:35]
	v_mfma_f32_16x16x32_bf16 v[20:23], v[134:137], v[220:223], v[20:23]
	v_mfma_f32_16x16x32_bf16 v[16:19], v[160:163], v[220:223], v[16:19]
	s_setprio 0
	s_setprio 1
	v_mfma_f32_16x16x32_bf16 v[44:47], v[164:167], v[180:183], v[44:47]
	v_mfma_f32_16x16x32_bf16 v[40:43], v[172:175], v[180:183], v[40:43]
	v_mfma_f32_16x16x32_bf16 v[28:31], v[164:167], v[188:191], v[28:31]
	v_mfma_f32_16x16x32_bf16 v[24:27], v[172:175], v[188:191], v[24:27]
	v_mfma_f32_16x16x32_bf16 v[12:15], v[164:167], v[206:209], v[12:15]
	v_mfma_f32_16x16x32_bf16 v[8:11], v[172:175], v[206:209], v[8:11]
	v_mfma_f32_16x16x32_bf16 v[4:7], v[164:167], v[216:219], v[4:7]
	v_mfma_f32_16x16x32_bf16 v[0:3], v[172:175], v[216:219], v[0:3]
	v_mfma_f32_16x16x32_bf16 v[44:47], v[168:171], v[184:187], v[44:47]
	v_mfma_f32_16x16x32_bf16 v[40:43], v[176:179], v[184:187], v[40:43]
	v_mfma_f32_16x16x32_bf16 v[28:31], v[168:171], v[192:195], v[28:31]
	v_mfma_f32_16x16x32_bf16 v[24:27], v[176:179], v[192:195], v[24:27]
	v_mfma_f32_16x16x32_bf16 v[12:15], v[168:171], v[210:213], v[12:15]
	v_mfma_f32_16x16x32_bf16 v[8:11], v[176:179], v[210:213], v[8:11]
	v_mfma_f32_16x16x32_bf16 v[4:7], v[168:171], v[220:223], v[4:7]
	v_mfma_f32_16x16x32_bf16 v[0:3], v[176:179], v[220:223], v[0:3]
	s_setprio 0
	s_barrier
	s_add_i32 s71, s71, 2
	s_add_u32 s76, s76, 0x100
	s_addc_u32 s77, s77, 0
	s_add_u32 s51, s51, 0x100
	s_addc_u32 s65, s65, 0
	s_cmp_gt_u32 s71, 13
.LBB0_264:
	s_add_u32 s28, s76, 0xfffc0080
	s_addc_u32 s29, s77, -1
	s_add_i32 s30, 0, 0x10000
	s_cmp_eq_u32 s71, 12
	s_cselect_b32 s83, s36, s29
	s_cselect_b32 s82, s37, s28
	v_add_u32_e32 v112, s30, v153
	s_cselect_b32 s81, s43, s65
	s_cselect_b32 s80, s50, s51
	s_add_i32 s31, 0, 0x14000
	ds_read_b128 v[130:133], v112
	ds_read_b128 v[134:137], v112 offset:1024
	ds_read_b128 v[156:159], v112 offset:2048
	ds_read_b128 v[160:163], v112 offset:3072
	v_add_u32_e32 v112, s31, v153
	ds_read_b128 v[164:167], v112
	ds_read_b128 v[168:171], v112 offset:1024
	ds_read_b128 v[172:175], v112 offset:2048
	ds_read_b128 v[176:179], v112 offset:3072
	v_lshl_add_u64 v[150:151], s[76:77], 0, v[146:147]
	s_add_i32 m0, s26, 0xc000
	ds_read_b128 v[180:183], v154
	ds_read_b128 v[184:187], v154 offset:1024
	ds_read_b128 v[188:191], v154 offset:2048
	ds_read_b128 v[192:195], v154 offset:3072
	ds_read_b128 v[206:209], v154 offset:4096
	ds_read_b128 v[210:213], v154 offset:5120
	ds_read_b128 v[216:219], v154 offset:6144
	ds_read_b128 v[220:223], v154 offset:7168
	global_load_lds_dwordx4 v[150:151], off
	v_lshl_add_u64 v[150:151], s[76:77], 0, v[148:149]
	s_add_i32 m0, s26, 0xe000
	s_nop 0
	global_load_lds_dwordx4 v[150:151], off
	s_waitcnt vmcnt(8)
	s_waitcnt lgkmcnt(0)
	s_barrier
	s_setprio 1
	v_mfma_f32_16x16x32_bf16 v[126:129], v[130:133], v[180:183], v[126:129]
	v_mfma_f32_16x16x32_bf16 v[122:125], v[156:159], v[180:183], v[122:125]
	v_mfma_f32_16x16x32_bf16 v[118:121], v[130:133], v[188:191], v[118:121]
	v_mfma_f32_16x16x32_bf16 v[114:117], v[156:159], v[188:191], v[114:117]
	v_mfma_f32_16x16x32_bf16 v[100:103], v[130:133], v[206:209], v[100:103]
	v_mfma_f32_16x16x32_bf16 v[96:99], v[156:159], v[206:209], v[96:99]
	v_mfma_f32_16x16x32_bf16 v[84:87], v[130:133], v[216:219], v[84:87]
	v_mfma_f32_16x16x32_bf16 v[80:83], v[156:159], v[216:219], v[80:83]
	v_mfma_f32_16x16x32_bf16 v[126:129], v[134:137], v[184:187], v[126:129]
	v_mfma_f32_16x16x32_bf16 v[122:125], v[160:163], v[184:187], v[122:125]
	v_mfma_f32_16x16x32_bf16 v[118:121], v[134:137], v[192:195], v[118:121]
	v_mfma_f32_16x16x32_bf16 v[114:117], v[160:163], v[192:195], v[114:117]
	v_mfma_f32_16x16x32_bf16 v[100:103], v[134:137], v[210:213], v[100:103]
	v_mfma_f32_16x16x32_bf16 v[96:99], v[160:163], v[210:213], v[96:99]
	v_mfma_f32_16x16x32_bf16 v[84:87], v[134:137], v[220:223], v[84:87]
	v_mfma_f32_16x16x32_bf16 v[80:83], v[160:163], v[220:223], v[80:83]
	s_setprio 0
	s_setprio 1
	v_mfma_f32_16x16x32_bf16 v[108:111], v[164:167], v[180:183], v[108:111]
	v_mfma_f32_16x16x32_bf16 v[104:107], v[172:175], v[180:183], v[104:107]
	v_mfma_f32_16x16x32_bf16 v[92:95], v[164:167], v[188:191], v[92:95]
	v_mfma_f32_16x16x32_bf16 v[88:91], v[172:175], v[188:191], v[88:91]
	v_mfma_f32_16x16x32_bf16 v[76:79], v[164:167], v[206:209], v[76:79]
	v_mfma_f32_16x16x32_bf16 v[72:75], v[172:175], v[206:209], v[72:75]
	v_mfma_f32_16x16x32_bf16 v[68:71], v[164:167], v[216:219], v[68:71]
	v_mfma_f32_16x16x32_bf16 v[64:67], v[172:175], v[216:219], v[64:67]
	v_mfma_f32_16x16x32_bf16 v[108:111], v[168:171], v[184:187], v[108:111]
	v_mfma_f32_16x16x32_bf16 v[104:107], v[176:179], v[184:187], v[104:107]
	v_mfma_f32_16x16x32_bf16 v[92:95], v[168:171], v[192:195], v[92:95]
	v_mfma_f32_16x16x32_bf16 v[88:91], v[176:179], v[192:195], v[88:91]
	v_mfma_f32_16x16x32_bf16 v[76:79], v[168:171], v[210:213], v[76:79]
	v_mfma_f32_16x16x32_bf16 v[72:75], v[176:179], v[210:213], v[72:75]
	v_mfma_f32_16x16x32_bf16 v[68:71], v[168:171], v[220:223], v[68:71]
	v_mfma_f32_16x16x32_bf16 v[64:67], v[176:179], v[220:223], v[64:67]
	s_setprio 0
	s_barrier
	s_add_i32 s28, s30, s13
	v_lshl_add_u64 v[150:151], s[80:81], 0, v[140:141]
	s_mov_b32 m0, s28
	ds_read_b128 v[180:183], v154 offset:16384
	ds_read_b128 v[184:187], v154 offset:17408
	ds_read_b128 v[188:191], v154 offset:18432
	ds_read_b128 v[192:195], v154 offset:19456
	ds_read_b128 v[206:209], v154 offset:20480
	ds_read_b128 v[210:213], v154 offset:21504
	ds_read_b128 v[216:219], v154 offset:22528
	ds_read_b128 v[220:223], v154 offset:23552
	global_load_lds_dwordx4 v[150:151], off
	s_add_i32 m0, s28, 0x2000
	s_add_u32 s28, s80, 0x40000
	v_lshl_add_u64 v[224:225], s[80:81], 0, v[144:145]
	s_addc_u32 s29, s81, 0
	s_add_i32 s30, s31, s13
	global_load_lds_dwordx4 v[224:225], off
	v_lshl_add_u64 v[226:227], s[28:29], 0, v[140:141]
	s_mov_b32 m0, s30
	v_lshl_add_u64 v[228:229], s[82:83], 0, v[142:143]
	global_load_lds_dwordx4 v[226:227], off
	v_lshl_add_u64 v[226:227], s[28:29], 0, v[144:145]
	s_add_i32 m0, s30, 0x2000
	s_nop 0
	global_load_lds_dwordx4 v[226:227], off
	v_lshl_add_u64 v[226:227], s[82:83], 0, v[138:139]
	s_mov_b32 m0, s26
	s_nop 0
	global_load_lds_dwordx4 v[226:227], off
	s_mov_b32 m0, s27
	s_nop 0
	global_load_lds_dwordx4 v[228:229], off
	s_waitcnt vmcnt(8)
	s_waitcnt lgkmcnt(0)
	s_barrier
	s_setprio 1
	v_mfma_f32_16x16x32_bf16 v[60:63], v[130:133], v[180:183], v[60:63]
	v_mfma_f32_16x16x32_bf16 v[56:59], v[156:159], v[180:183], v[56:59]
	v_mfma_f32_16x16x32_bf16 v[52:55], v[130:133], v[188:191], v[52:55]
	v_mfma_f32_16x16x32_bf16 v[48:51], v[156:159], v[188:191], v[48:51]
	v_mfma_f32_16x16x32_bf16 v[36:39], v[130:133], v[206:209], v[36:39]
	v_mfma_f32_16x16x32_bf16 v[32:35], v[156:159], v[206:209], v[32:35]
	v_mfma_f32_16x16x32_bf16 v[20:23], v[130:133], v[216:219], v[20:23]
	v_mfma_f32_16x16x32_bf16 v[16:19], v[156:159], v[216:219], v[16:19]
	v_mfma_f32_16x16x32_bf16 v[60:63], v[134:137], v[184:187], v[60:63]
	v_mfma_f32_16x16x32_bf16 v[56:59], v[160:163], v[184:187], v[56:59]
	v_mfma_f32_16x16x32_bf16 v[52:55], v[134:137], v[192:195], v[52:55]
	v_mfma_f32_16x16x32_bf16 v[48:51], v[160:163], v[192:195], v[48:51]
	v_mfma_f32_16x16x32_bf16 v[36:39], v[134:137], v[210:213], v[36:39]
	v_mfma_f32_16x16x32_bf16 v[32:35], v[160:163], v[210:213], v[32:35]
	v_mfma_f32_16x16x32_bf16 v[20:23], v[134:137], v[220:223], v[20:23]
	v_mfma_f32_16x16x32_bf16 v[16:19], v[160:163], v[220:223], v[16:19]
	s_setprio 0
	s_setprio 1
	v_mfma_f32_16x16x32_bf16 v[44:47], v[164:167], v[180:183], v[44:47]
	v_mfma_f32_16x16x32_bf16 v[40:43], v[172:175], v[180:183], v[40:43]
	v_mfma_f32_16x16x32_bf16 v[28:31], v[164:167], v[188:191], v[28:31]
	v_mfma_f32_16x16x32_bf16 v[24:27], v[172:175], v[188:191], v[24:27]
	v_mfma_f32_16x16x32_bf16 v[12:15], v[164:167], v[206:209], v[12:15]
	v_mfma_f32_16x16x32_bf16 v[8:11], v[172:175], v[206:209], v[8:11]
	v_mfma_f32_16x16x32_bf16 v[4:7], v[164:167], v[216:219], v[4:7]
	v_mfma_f32_16x16x32_bf16 v[0:3], v[172:175], v[216:219], v[0:3]
	v_mfma_f32_16x16x32_bf16 v[44:47], v[168:171], v[184:187], v[44:47]
	v_mfma_f32_16x16x32_bf16 v[40:43], v[176:179], v[184:187], v[40:43]
	v_mfma_f32_16x16x32_bf16 v[28:31], v[168:171], v[192:195], v[28:31]
	v_mfma_f32_16x16x32_bf16 v[24:27], v[176:179], v[192:195], v[24:27]
	v_mfma_f32_16x16x32_bf16 v[12:15], v[168:171], v[210:213], v[12:15]
	v_mfma_f32_16x16x32_bf16 v[8:11], v[176:179], v[210:213], v[8:11]
	v_mfma_f32_16x16x32_bf16 v[4:7], v[168:171], v[220:223], v[4:7]
	v_mfma_f32_16x16x32_bf16 v[0:3], v[176:179], v[220:223], v[0:3]
	s_setprio 0
	s_barrier
	s_add_i32 s30, 0, 0x18000
	v_add_u32_e32 v112, s30, v153
	s_add_i32 s31, 0, 0x1c000
	ds_read_b128 v[130:133], v112
	ds_read_b128 v[134:137], v112 offset:1024
	ds_read_b128 v[156:159], v112 offset:2048
	ds_read_b128 v[160:163], v112 offset:3072
	v_add_u32_e32 v112, s31, v153
	ds_read_b128 v[164:167], v112
	ds_read_b128 v[168:171], v112 offset:1024
	ds_read_b128 v[172:175], v112 offset:2048
	ds_read_b128 v[176:179], v112 offset:3072
	s_add_u32 s28, s82, 0x40000
	s_addc_u32 s29, s83, 0
	s_mov_b32 m0, s34
	v_lshl_add_u64 v[230:231], s[28:29], 0, v[138:139]
	ds_read_b128 v[180:183], v154 offset:32768
	ds_read_b128 v[184:187], v154 offset:33792
	ds_read_b128 v[188:191], v154 offset:34816
	ds_read_b128 v[192:195], v154 offset:35840
	ds_read_b128 v[206:209], v154 offset:36864
	ds_read_b128 v[210:213], v154 offset:37888
	ds_read_b128 v[216:219], v154 offset:38912
	ds_read_b128 v[220:223], v154 offset:39936
	global_load_lds_dwordx4 v[230:231], off
	v_lshl_add_u64 v[230:231], s[28:29], 0, v[142:143]
	s_mov_b32 m0, s14
	s_nop 0
	global_load_lds_dwordx4 v[230:231], off
	s_waitcnt vmcnt(8)
	s_waitcnt lgkmcnt(0)
	s_barrier
	s_setprio 1
	v_mfma_f32_16x16x32_bf16 v[126:129], v[130:133], v[180:183], v[126:129]
	v_mfma_f32_16x16x32_bf16 v[122:125], v[156:159], v[180:183], v[122:125]
	v_mfma_f32_16x16x32_bf16 v[118:121], v[130:133], v[188:191], v[118:121]
	v_mfma_f32_16x16x32_bf16 v[114:117], v[156:159], v[188:191], v[114:117]
	v_mfma_f32_16x16x32_bf16 v[100:103], v[130:133], v[206:209], v[100:103]
	v_mfma_f32_16x16x32_bf16 v[96:99], v[156:159], v[206:209], v[96:99]
	v_mfma_f32_16x16x32_bf16 v[84:87], v[130:133], v[216:219], v[84:87]
	v_mfma_f32_16x16x32_bf16 v[80:83], v[156:159], v[216:219], v[80:83]
	v_mfma_f32_16x16x32_bf16 v[126:129], v[134:137], v[184:187], v[126:129]
	v_mfma_f32_16x16x32_bf16 v[122:125], v[160:163], v[184:187], v[122:125]
	v_mfma_f32_16x16x32_bf16 v[118:121], v[134:137], v[192:195], v[118:121]
	v_mfma_f32_16x16x32_bf16 v[114:117], v[160:163], v[192:195], v[114:117]
	v_mfma_f32_16x16x32_bf16 v[100:103], v[134:137], v[210:213], v[100:103]
	v_mfma_f32_16x16x32_bf16 v[96:99], v[160:163], v[210:213], v[96:99]
	v_mfma_f32_16x16x32_bf16 v[84:87], v[134:137], v[220:223], v[84:87]
	v_mfma_f32_16x16x32_bf16 v[80:83], v[160:163], v[220:223], v[80:83]
	s_setprio 0
	s_setprio 1
	v_mfma_f32_16x16x32_bf16 v[108:111], v[164:167], v[180:183], v[108:111]
	v_mfma_f32_16x16x32_bf16 v[104:107], v[172:175], v[180:183], v[104:107]
	v_mfma_f32_16x16x32_bf16 v[92:95], v[164:167], v[188:191], v[92:95]
	v_mfma_f32_16x16x32_bf16 v[88:91], v[172:175], v[188:191], v[88:91]
	v_mfma_f32_16x16x32_bf16 v[76:79], v[164:167], v[206:209], v[76:79]
	v_mfma_f32_16x16x32_bf16 v[72:75], v[172:175], v[206:209], v[72:75]
	v_mfma_f32_16x16x32_bf16 v[68:71], v[164:167], v[216:219], v[68:71]
	v_mfma_f32_16x16x32_bf16 v[64:67], v[172:175], v[216:219], v[64:67]
	v_mfma_f32_16x16x32_bf16 v[108:111], v[168:171], v[184:187], v[108:111]
	v_mfma_f32_16x16x32_bf16 v[104:107], v[176:179], v[184:187], v[104:107]
	v_mfma_f32_16x16x32_bf16 v[92:95], v[168:171], v[192:195], v[92:95]
	v_mfma_f32_16x16x32_bf16 v[88:91], v[176:179], v[192:195], v[88:91]
	v_mfma_f32_16x16x32_bf16 v[76:79], v[168:171], v[210:213], v[76:79]
	v_mfma_f32_16x16x32_bf16 v[72:75], v[176:179], v[210:213], v[72:75]
	v_mfma_f32_16x16x32_bf16 v[68:71], v[168:171], v[220:223], v[68:71]
	v_mfma_f32_16x16x32_bf16 v[64:67], v[176:179], v[220:223], v[64:67]
	s_setprio 0
	s_barrier
	s_add_i32 s28, s30, s13
	v_lshl_add_u64 v[150:151], v[150:151], 0, s[56:57]
	s_mov_b32 m0, s28
	ds_read_b128 v[180:183], v154 offset:49152
	ds_read_b128 v[184:187], v154 offset:50176
	ds_read_b128 v[188:191], v154 offset:51200
	ds_read_b128 v[192:195], v154 offset:52224
	ds_read_b128 v[206:209], v154 offset:53248
	ds_read_b128 v[210:213], v154 offset:54272
	ds_read_b128 v[216:219], v154 offset:55296
	ds_read_b128 v[220:223], v154 offset:56320
	global_load_lds_dwordx4 v[150:151], off
	s_add_i32 m0, s28, 0x2000
	s_add_u32 s28, s80, 0x40080
	v_lshl_add_u64 v[150:151], v[224:225], 0, s[56:57]
	s_addc_u32 s29, s81, 0
	s_add_i32 s30, s31, s13
	global_load_lds_dwordx4 v[150:151], off
	v_lshl_add_u64 v[150:151], s[28:29], 0, v[140:141]
	s_mov_b32 m0, s30
	s_nop 0
	global_load_lds_dwordx4 v[150:151], off
	v_lshl_add_u64 v[150:151], s[28:29], 0, v[144:145]
	s_add_i32 m0, s30, 0x2000
	s_nop 0
	global_load_lds_dwordx4 v[150:151], off
	v_lshl_add_u64 v[150:151], v[226:227], 0, s[56:57]
	s_mov_b32 m0, s33
	s_nop 0
	global_load_lds_dwordx4 v[150:151], off
	v_lshl_add_u64 v[150:151], v[228:229], 0, s[56:57]
	s_mov_b32 m0, s69
	s_nop 0
	global_load_lds_dwordx4 v[150:151], off
	s_waitcnt vmcnt(8)
	s_waitcnt lgkmcnt(0)
	s_barrier
	s_setprio 1
	v_mfma_f32_16x16x32_bf16 v[60:63], v[130:133], v[180:183], v[60:63]
	v_mfma_f32_16x16x32_bf16 v[56:59], v[156:159], v[180:183], v[56:59]
	v_mfma_f32_16x16x32_bf16 v[52:55], v[130:133], v[188:191], v[52:55]
	v_mfma_f32_16x16x32_bf16 v[48:51], v[156:159], v[188:191], v[48:51]
	v_mfma_f32_16x16x32_bf16 v[36:39], v[130:133], v[206:209], v[36:39]
	v_mfma_f32_16x16x32_bf16 v[32:35], v[156:159], v[206:209], v[32:35]
	v_mfma_f32_16x16x32_bf16 v[20:23], v[130:133], v[216:219], v[20:23]
	v_mfma_f32_16x16x32_bf16 v[16:19], v[156:159], v[216:219], v[16:19]
	v_mfma_f32_16x16x32_bf16 v[60:63], v[134:137], v[184:187], v[60:63]
	v_mfma_f32_16x16x32_bf16 v[56:59], v[160:163], v[184:187], v[56:59]
	v_mfma_f32_16x16x32_bf16 v[52:55], v[134:137], v[192:195], v[52:55]
	v_mfma_f32_16x16x32_bf16 v[48:51], v[160:163], v[192:195], v[48:51]
	v_mfma_f32_16x16x32_bf16 v[36:39], v[134:137], v[210:213], v[36:39]
	v_mfma_f32_16x16x32_bf16 v[32:35], v[160:163], v[210:213], v[32:35]
	v_mfma_f32_16x16x32_bf16 v[20:23], v[134:137], v[220:223], v[20:23]
	v_mfma_f32_16x16x32_bf16 v[16:19], v[160:163], v[220:223], v[16:19]
	s_setprio 0
	s_setprio 1
	v_mfma_f32_16x16x32_bf16 v[44:47], v[164:167], v[180:183], v[44:47]
	v_mfma_f32_16x16x32_bf16 v[40:43], v[172:175], v[180:183], v[40:43]
	v_mfma_f32_16x16x32_bf16 v[28:31], v[164:167], v[188:191], v[28:31]
	v_mfma_f32_16x16x32_bf16 v[24:27], v[172:175], v[188:191], v[24:27]
	v_mfma_f32_16x16x32_bf16 v[12:15], v[164:167], v[206:209], v[12:15]
	v_mfma_f32_16x16x32_bf16 v[8:11], v[172:175], v[206:209], v[8:11]
	v_mfma_f32_16x16x32_bf16 v[4:7], v[164:167], v[216:219], v[4:7]
	v_mfma_f32_16x16x32_bf16 v[0:3], v[172:175], v[216:219], v[0:3]
	v_mfma_f32_16x16x32_bf16 v[44:47], v[168:171], v[184:187], v[44:47]
	v_mfma_f32_16x16x32_bf16 v[40:43], v[176:179], v[184:187], v[40:43]
	v_mfma_f32_16x16x32_bf16 v[28:31], v[168:171], v[192:195], v[28:31]
	v_mfma_f32_16x16x32_bf16 v[24:27], v[176:179], v[192:195], v[24:27]
	v_mfma_f32_16x16x32_bf16 v[12:15], v[168:171], v[210:213], v[12:15]
	v_mfma_f32_16x16x32_bf16 v[8:11], v[176:179], v[210:213], v[8:11]
	v_mfma_f32_16x16x32_bf16 v[4:7], v[168:171], v[220:223], v[4:7]
	v_mfma_f32_16x16x32_bf16 v[0:3], v[176:179], v[220:223], v[0:3]
	s_setprio 0
	s_barrier
	s_add_i32 s71, s71, 2
	s_add_u32 s76, s76, 0x100
	s_addc_u32 s77, s77, 0
	s_add_u32 s51, s51, 0x100
	s_addc_u32 s65, s65, 0
	s_cmp_gt_u32 s71, 13
	s_cbranch_scc0 .LBB0_264
	s_and_b64 vcc, exec, s[46:47]
	s_cbranch_vccz .LBB0_267
	s_barrier

.LBB0_275:
	v_readlane_b32 s6, v255, 20
	v_readlane_b32 s7, v255, 21
	s_mul_i32 s2, s6, 11
	v_readlane_b32 s6, v252, 2
	s_add_i32 s2, s2, 3
	v_readlane_b32 s7, v252, 3
	s_cmp_ge_i32 s2, s7
	s_cbranch_scc1 .LBB0_325
	s_waitcnt vmcnt(0)
	s_barrier
	s_mov_b64 s[6:7], exec
	v_readlane_b32 s12, v252, 22
	v_readlane_b32 s13, v252, 23
	s_and_b64 s[12:13], s[6:7], s[12:13]
	s_mov_b64 exec, s[12:13]
	s_cbranch_execz .LBB0_324
	v_readlane_b32 s4, v254, 44
	s_waitcnt vmcnt(0) expcnt(0) lgkmcnt(0)
	s_nop 0
	v_mov_b32_e32 v0, s4
	ds_read_b32 v2, v0
	v_readlane_b32 s4, v254, 45
	s_waitcnt lgkmcnt(0)
	v_cmp_ne_u32_e32 vcc, 0, v2
	v_mov_b32_e32 v0, s4
	ds_read_b32 v0, v0
	s_cbranch_vccnz .LBB0_292
	v_readlane_b32 s14, v252, 24
	v_readlane_b32 s15, v252, 25
	s_load_dwordx2 s[12:13], s[14:15], 0x0
	s_load_dword s4, s[14:15], 0x8
	s_waitcnt lgkmcnt(0)
	s_mul_i32 s12, s13, s12
	s_mul_i32 s4, s12, s4
	s_mov_b32 s12, 1
	s_branch .LBB0_280

.LBB0_352:
	v_readlane_b32 s6, v255, 20
	v_readlane_b32 s7, v255, 21
	s_mul_i32 s2, s6, 11
	v_readlane_b32 s6, v252, 2
	s_add_i32 s2, s2, 4
	v_readlane_b32 s7, v252, 3
	s_cmp_ge_i32 s2, s7
	s_cbranch_scc1 .LBB0_402
	s_waitcnt vmcnt(0)
	s_barrier
	s_mov_b64 s[6:7], exec
	v_readlane_b32 s12, v252, 22
	v_readlane_b32 s13, v252, 23
	s_and_b64 s[12:13], s[6:7], s[12:13]
	s_mov_b64 exec, s[12:13]
	s_cbranch_execz .LBB0_401
	v_readlane_b32 s4, v254, 44
	s_waitcnt vmcnt(0) expcnt(0) lgkmcnt(0)
	s_nop 0
	v_mov_b32_e32 v0, s4
	ds_read_b32 v2, v0
	v_readlane_b32 s4, v254, 45
	s_waitcnt lgkmcnt(0)
	v_cmp_ne_u32_e32 vcc, 0, v2
	v_mov_b32_e32 v0, s4
	ds_read_b32 v0, v0
	s_cbranch_vccnz .LBB0_369
	v_readlane_b32 s14, v252, 24
	v_readlane_b32 s15, v252, 25
	s_load_dwordx2 s[12:13], s[14:15], 0x0
	s_load_dword s4, s[14:15], 0x8
	s_waitcnt lgkmcnt(0)
	s_mul_i32 s12, s13, s12
	s_mul_i32 s4, s12, s4
	s_mov_b32 s12, 1
	s_branch .LBB0_357

.LBB0_410:
	s_or_b64 exec, exec, s[6:7]
	s_waitcnt lgkmcnt(0)
	v_lshlrev_b32_e32 v25, 16, v25
	v_lshlrev_b32_e32 v4, 16, v4
	v_lshlrev_b32_e32 v156, 16, v156
	v_lshlrev_b32_e32 v130, 16, v130
	v_lshlrev_b32_e32 v118, 16, v118
	v_lshlrev_b32_e32 v116, 16, v116
	v_lshlrev_b32_e32 v114, 16, v114
	v_mul_f32_e32 v106, v106, v25
	v_mov_b32_e32 v25, s27
	v_mul_f32_e32 v4, v5, v4
	v_mul_f32_e32 v156, v157, v156
	v_mul_f32_e32 v157, v131, v130
	v_lshlrev_b32_e32 v127, 16, v127
	v_lshlrev_b32_e32 v125, 16, v125
	v_lshlrev_b32_e32 v123, 16, v123
	v_lshlrev_b32_e32 v121, 16, v121
	v_mul_f32_e32 v118, v119, v118
	v_mul_f32_e32 v119, v117, v116
	v_mul_f32_e32 v130, v115, v114
	v_lshlrev_b32_e32 v14, 16, v14
	s_barrier
	ds_read_b128 v[114:117], v25 offset:256
	v_mul_f32_e32 v4, v4, v9
	v_mul_f32_e32 v127, v128, v127
	v_mul_f32_e32 v126, v126, v125
	v_mul_f32_e32 v128, v124, v123
	v_mul_f32_e32 v121, v122, v121
	v_mul_f32_e32 v14, v15, v14
	ds_read_b128 v[122:125], v25 offset:512
	s_waitcnt lgkmcnt(1)
	v_lshlrev_b32_e32 v134, 16, v134
	v_mul_f32_e32 v5, v4, v114
	v_fma_f32 v5, v14, v7, -v5
	v_add_f32_e32 v5, 0, v5
	ds_read_b128 v[114:117], v25 offset:768
	s_waitcnt lgkmcnt(1)
	v_lshlrev_b32_e32 v132, 16, v132
	v_mul_f32_e32 v7, v4, v122
	v_fma_f32 v7, v106, v13, -v7
	v_fma_f32 v9, -v123, v5, 0
	v_add_f32_e32 v7, v7, v9
	ds_read_b128 v[122:125], v25 offset:1024
	s_waitcnt lgkmcnt(1)
	v_mul_f32_e32 v134, v135, v134
	v_mul_f32_e32 v9, v4, v114
	v_fma_f32 v9, v130, v11, -v9
	v_mul_f32_e32 v135, v133, v132
	v_fma_f32 v11, -v5, v115, 0
	v_fma_f32 v9, -v116, v7, v9
	ds_read_b128 v[114:117], v25 offset:1280
	ds_read_b128 v[130:133], v25 offset:1296
	v_add_f32_e32 v9, v11, v9
	s_waitcnt lgkmcnt(2)
	v_lshlrev_b32_e32 v153, 16, v153
	v_mul_f32_e32 v11, v4, v122
	v_fma_f32 v11, v119, v22, -v11
	v_fma_f32 v13, -v5, v123, 0
	v_lshlrev_b32_e32 v141, 16, v141
	v_lshlrev_b32_e32 v139, 16, v139
	v_lshlrev_b32_e32 v137, 16, v137
	v_fma_f32 v11, -v7, v124, v11
	v_fma_f32 v13, -v125, v9, v13
	v_mul_f32_e32 v153, v154, v153
	v_mul_f32_e32 v142, v142, v141
	v_mul_f32_e32 v154, v140, v139
	v_mul_f32_e32 v137, v138, v137
	v_add_f32_e32 v11, v11, v13
	ds_read_b128 v[122:125], v25 offset:1536
	ds_read_b128 v[138:141], v25 offset:1552
	s_waitcnt lgkmcnt(2)
	v_lshlrev_b32_e32 v151, 16, v151
	v_mul_f32_e32 v13, v4, v114
	v_fma_f32 v13, v118, v17, -v13
	v_fma_f32 v14, -v5, v115, 0
	v_fma_f32 v13, -v7, v116, v13
	v_fma_f32 v14, -v9, v117, v14
	v_fma_f32 v13, -v130, v11, v13
	v_add_f32_e32 v13, v14, v13
	ds_read_b128 v[114:117], v25 offset:1792
	ds_read_b128 v[130:133], v25 offset:1808
	s_waitcnt lgkmcnt(2)
	v_lshlrev_b32_e32 v148, 16, v148
	v_mul_f32_e32 v14, v4, v122
	v_fma_f32 v14, v121, v108, -v14
	v_fma_f32 v15, -v5, v123, 0
	v_fma_f32 v14, -v7, v124, v14
	v_fma_f32 v15, -v9, v125, v15
	v_fma_f32 v14, -v11, v138, v14
	v_fma_f32 v15, -v139, v13, v15
	v_add_f32_e32 v14, v14, v15
	ds_read_b128 v[122:125], v25 offset:2048
	ds_read_b128 v[138:141], v25 offset:2064
	s_waitcnt lgkmcnt(2)
	v_lshlrev_b32_e32 v146, 16, v146
	v_mul_f32_e32 v15, v4, v114
	v_fma_f32 v15, v128, v18, -v15
	v_fma_f32 v17, -v5, v115, 0
	v_fma_f32 v15, -v7, v116, v15
	v_fma_f32 v17, -v9, v117, v17
	v_fma_f32 v15, -v11, v130, v15
	v_lshlrev_b32_e32 v144, 16, v144
	v_fma_f32 v17, -v13, v131, v17
	v_fma_f32 v15, -v132, v14, v15
	v_mul_f32_e32 v151, v152, v151
	v_mul_f32_e32 v148, v149, v148
	v_mul_f32_e32 v149, v147, v146
	v_mul_f32_e32 v152, v145, v144
	v_add_f32_e32 v15, v17, v15
	ds_read_b128 v[114:117], v25 offset:2304
	ds_read_b128 v[130:133], v25 offset:2320
	ds_read_b128 v[144:147], v25 offset:2336
	s_waitcnt lgkmcnt(3)
	v_lshlrev_b32_e32 v150, 16, v150
	v_mul_f32_e32 v17, v4, v122
	v_fma_f32 v17, v126, v111, -v17
	v_fma_f32 v18, -v5, v123, 0
	v_fma_f32 v17, -v7, v124, v17
	v_fma_f32 v18, -v9, v125, v18
	v_fma_f32 v17, -v11, v138, v17
	v_fma_f32 v18, -v13, v139, v18
	v_lshlrev_b32_e32 v155, 16, v155
	v_lshlrev_b32_e32 v162, 16, v162
	v_lshlrev_b32_e32 v167, 16, v167
	v_fma_f32 v17, -v14, v140, v17
	v_fma_f32 v18, -v141, v15, v18
	v_mul_f32_e32 v150, v171, v150
	v_mul_f32_e32 v155, v170, v155
	v_mul_f32_e32 v162, v169, v162
	v_mul_f32_e32 v167, v168, v167
	v_add_f32_e32 v17, v17, v18
	ds_read_b128 v[122:125], v25 offset:2560
	ds_read_b128 v[138:141], v25 offset:2576
	ds_read_b128 v[168:171], v25 offset:2592
	s_waitcnt lgkmcnt(3)
	v_lshlrev_b32_e32 v120, 16, v120
	v_mul_f32_e32 v18, v4, v114
	v_fma_f32 v18, v127, v19, -v18
	v_fma_f32 v19, -v5, v115, 0
	v_fma_f32 v18, -v7, v116, v18
	v_fma_f32 v19, -v9, v117, v19
	v_fma_f32 v18, -v11, v130, v18
	v_fma_f32 v19, -v13, v131, v19
	v_fma_f32 v18, -v14, v132, v18
	v_fma_f32 v19, -v15, v133, v19
	v_fma_f32 v18, -v17, v144, v18
	v_add_f32_e32 v18, v19, v18
	ds_read_b128 v[114:117], v25 offset:2816
	ds_read_b128 v[130:133], v25 offset:2832
	ds_read_b128 v[144:147], v25 offset:2848
	s_waitcnt lgkmcnt(3)
	v_lshlrev_b32_e32 v129, 16, v129
	v_mul_f32_e32 v19, v4, v122
	v_fma_f32 v19, v157, v109, -v19
	v_fma_f32 v22, -v5, v123, 0
	v_fma_f32 v19, -v7, v124, v19
	v_fma_f32 v22, -v9, v125, v22
	v_fma_f32 v19, -v11, v138, v19
	v_fma_f32 v22, -v13, v139, v22
	v_fma_f32 v19, -v14, v140, v19
	v_fma_f32 v22, -v15, v141, v22
	v_fma_f32 v19, -v17, v168, v19
	v_fma_f32 v22, -v18, v169, v22
	v_add_f32_e32 v19, v19, v22
	ds_read_b128 v[122:125], v25 offset:3072
	ds_read_b128 v[138:141], v25 offset:3088
	ds_read_b128 v[168:171], v25 offset:3104
	s_waitcnt lgkmcnt(3)
	v_lshlrev_b32_e32 v136, 16, v136
	v_mul_f32_e32 v22, v4, v114
	v_fma_f32 v20, v135, v20, -v22
	v_fma_f32 v22, -v5, v115, 0
	v_fma_f32 v20, -v7, v116, v20
	v_fma_f32 v22, -v9, v117, v22
	v_fma_f32 v20, -v11, v130, v20
	v_fma_f32 v22, -v13, v131, v22
	v_fma_f32 v20, -v14, v132, v20
	v_fma_f32 v22, -v15, v133, v22
	v_fma_f32 v20, -v17, v144, v20
	v_lshlrev_b32_e32 v143, 16, v143
	v_fma_f32 v22, -v18, v145, v22
	v_fma_f32 v20, -v19, v146, v20
	v_mul_f32_e32 v120, v175, v120
	v_mul_f32_e32 v129, v174, v129
	v_mul_f32_e32 v136, v173, v136
	v_mul_f32_e32 v143, v172, v143
	v_add_f32_e32 v20, v22, v20
	ds_read_b128 v[114:117], v25 offset:3328
	ds_read_b128 v[130:133], v25 offset:3344
	ds_read_b128 v[144:147], v25 offset:3360
	ds_read_b128 v[172:175], v25 offset:3376
	s_waitcnt lgkmcnt(4)
	v_lshlrev_b32_e32 v103, 16, v103
	v_mul_f32_e32 v22, v4, v122
	v_fma_f32 v22, v134, v107, -v22
	v_fma_f32 v106, -v5, v123, 0
	v_fma_f32 v22, -v7, v124, v22
	v_fma_f32 v106, -v9, v125, v106
	v_fma_f32 v22, -v11, v138, v22
	v_fma_f32 v106, -v13, v139, v106
	v_fma_f32 v22, -v14, v140, v22
	v_fma_f32 v106, -v15, v141, v106
	v_fma_f32 v22, -v17, v168, v22
	v_fma_f32 v106, -v18, v169, v106
	v_fma_f32 v22, -v19, v170, v22
	v_fma_f32 v106, -v20, v171, v106
	v_add_f32_e32 v22, v22, v106
	ds_read_b128 v[106:109], v25 offset:3584
	ds_read_b128 v[122:125], v25 offset:3600
	ds_read_b128 v[138:141], v25 offset:3616
	ds_read_b128 v[168:171], v25 offset:3632
	s_waitcnt lgkmcnt(4)
	v_lshlrev_b32_e32 v104, 16, v104
	v_mul_f32_e32 v111, v4, v114
	v_fma_f32 v24, v137, v24, -v111
	v_fma_f32 v111, -v5, v115, 0
	v_fma_f32 v24, -v7, v116, v24
	v_fma_f32 v111, -v9, v117, v111
	v_fma_f32 v24, -v11, v130, v24
	v_fma_f32 v111, -v13, v131, v111
	v_fma_f32 v24, -v14, v132, v24
	v_fma_f32 v111, -v15, v133, v111
	v_fma_f32 v24, -v17, v144, v24
	v_fma_f32 v111, -v18, v145, v111
	v_fma_f32 v24, -v19, v146, v24
	v_fma_f32 v111, -v20, v147, v111
	v_fma_f32 v24, -v22, v172, v24
	ds_read_b128 v[114:117], v25 offset:3840
	ds_read_b128 v[130:133], v25 offset:3856
	ds_read_b128 v[144:147], v25 offset:3872
	ds_read_b128 v[172:175], v25 offset:3888
	s_waitcnt lgkmcnt(4)
	v_add_f32_e32 v24, v111, v24
	v_mul_f32_e32 v106, v4, v106
	v_fma_f32 v26, v154, v26, -v106
	v_fma_f32 v106, -v5, v107, 0
	v_fma_f32 v26, -v7, v108, v26
	v_fma_f32 v106, -v9, v109, v106
	v_fma_f32 v26, -v11, v122, v26
	v_fma_f32 v106, -v13, v123, v106
	v_fma_f32 v26, -v14, v124, v26
	v_fma_f32 v106, -v15, v125, v106
	v_fma_f32 v26, -v17, v138, v26
	v_fma_f32 v106, -v18, v139, v106
	v_fma_f32 v26, -v19, v140, v26
	v_fma_f32 v106, -v20, v141, v106
	v_lshlrev_b32_e32 v105, 16, v105
	v_fma_f32 v26, -v22, v168, v26
	v_fma_f32 v106, -v24, v169, v106
	v_add_f32_e32 v26, v26, v106
	ds_read_b128 v[106:109], v25 offset:4096
	ds_read_b128 v[122:125], v25 offset:4112
	ds_read_b128 v[138:141], v25 offset:4128
	ds_read_b128 v[168:171], v25 offset:4144
	s_waitcnt lgkmcnt(4)
	v_lshlrev_b32_e32 v110, 16, v110
	v_mul_f32_e32 v111, v4, v114
	v_fma_f32 v27, v142, v27, -v111
	v_fma_f32 v111, -v5, v115, 0
	v_fma_f32 v27, -v7, v116, v27
	v_fma_f32 v111, -v9, v117, v111
	v_fma_f32 v27, -v11, v130, v27
	v_fma_f32 v111, -v13, v131, v111
	v_fma_f32 v27, -v14, v132, v27
	v_fma_f32 v111, -v15, v133, v111
	v_fma_f32 v27, -v17, v144, v27
	v_fma_f32 v111, -v18, v145, v111
	v_fma_f32 v27, -v19, v146, v27
	v_fma_f32 v111, -v20, v147, v111
	v_fma_f32 v27, -v22, v172, v27
	v_mul_f32_e32 v103, v179, v103
	v_mul_f32_e32 v104, v178, v104
	v_mul_f32_e32 v105, v177, v105
	v_mul_f32_e32 v110, v176, v110
	v_fma_f32 v111, -v24, v173, v111
	v_fma_f32 v27, -v26, v174, v27
	ds_read_b128 v[114:117], v25 offset:4352
	ds_read_b128 v[130:133], v25 offset:4368
	ds_read_b128 v[144:147], v25 offset:4384
	ds_read_b128 v[172:175], v25 offset:4400
	ds_read_b128 v[176:179], v25 offset:4416
	s_waitcnt lgkmcnt(5)
	v_add_f32_e32 v27, v111, v27
	v_mul_f32_e32 v106, v4, v106
	v_fma_f32 v30, v152, v30, -v106
	v_fma_f32 v106, -v5, v107, 0
	v_fma_f32 v30, -v7, v108, v30
	v_fma_f32 v106, -v9, v109, v106
	v_fma_f32 v30, -v11, v122, v30
	v_fma_f32 v106, -v13, v123, v106
	v_fma_f32 v30, -v14, v124, v30
	v_fma_f32 v106, -v15, v125, v106
	v_fma_f32 v30, -v17, v138, v30
	v_fma_f32 v106, -v18, v139, v106
	v_fma_f32 v30, -v19, v140, v30
	v_fma_f32 v106, -v20, v141, v106
	v_lshlrev_b32_e32 v99, 16, v99
	v_fma_f32 v30, -v22, v168, v30
	v_fma_f32 v106, -v24, v169, v106
	v_lshlrev_b32_e32 v100, 16, v100
	v_lshlrev_b32_e32 v101, 16, v101
	v_lshlrev_b32_e32 v102, 16, v102
	v_fma_f32 v30, -v26, v170, v30
	v_fma_f32 v106, -v27, v171, v106
	v_mul_f32_e32 v99, v183, v99
	v_mul_f32_e32 v100, v182, v100
	v_mul_f32_e32 v101, v181, v101
	v_mul_f32_e32 v102, v180, v102
	v_add_f32_e32 v30, v30, v106
	ds_read_b128 v[106:109], v25 offset:4608
	ds_read_b128 v[122:125], v25 offset:4624
	ds_read_b128 v[138:141], v25 offset:4640
	ds_read_b128 v[168:171], v25 offset:4656
	ds_read_b128 v[180:183], v25 offset:4672
	s_waitcnt lgkmcnt(5)
	v_lshlrev_b32_e32 v95, 16, v95
	v_mul_f32_e32 v111, v4, v114
	v_fma_f32 v31, v149, v31, -v111
	v_fma_f32 v111, -v5, v115, 0
	v_fma_f32 v31, -v7, v116, v31
	v_fma_f32 v111, -v9, v117, v111
	v_fma_f32 v31, -v11, v130, v31
	v_fma_f32 v111, -v13, v131, v111
	v_fma_f32 v31, -v14, v132, v31
	v_fma_f32 v111, -v15, v133, v111
	v_fma_f32 v31, -v17, v144, v31
	v_fma_f32 v111, -v18, v145, v111
	v_fma_f32 v31, -v19, v146, v31
	v_fma_f32 v111, -v20, v147, v111
	v_fma_f32 v31, -v22, v172, v31
	v_fma_f32 v111, -v24, v173, v111
	v_fma_f32 v31, -v26, v174, v31
	v_fma_f32 v111, -v27, v175, v111
	v_fma_f32 v31, -v30, v176, v31
	ds_read_b128 v[114:117], v25 offset:4864
	ds_read_b128 v[130:133], v25 offset:4880
	ds_read_b128 v[144:147], v25 offset:4896
	ds_read_b128 v[172:175], v25 offset:4912
	ds_read_b128 v[176:179], v25 offset:4928
	s_waitcnt lgkmcnt(5)
	v_add_f32_e32 v31, v111, v31
	v_mul_f32_e32 v106, v4, v106
	v_fma_f32 v32, v148, v32, -v106
	v_fma_f32 v106, -v5, v107, 0
	v_fma_f32 v32, -v7, v108, v32
	v_fma_f32 v106, -v9, v109, v106
	v_fma_f32 v32, -v11, v122, v32
	v_fma_f32 v106, -v13, v123, v106
	v_fma_f32 v32, -v14, v124, v32
	v_fma_f32 v106, -v15, v125, v106
	v_fma_f32 v32, -v17, v138, v32
	v_fma_f32 v106, -v18, v139, v106
	v_fma_f32 v32, -v19, v140, v32
	v_fma_f32 v106, -v20, v141, v106
	v_fma_f32 v32, -v22, v168, v32
	v_fma_f32 v106, -v24, v169, v106
	v_fma_f32 v32, -v26, v170, v32
	v_fma_f32 v106, -v27, v171, v106
	v_lshlrev_b32_e32 v96, 16, v96
	v_fma_f32 v32, -v30, v180, v32
	v_fma_f32 v106, -v31, v181, v106
	v_add_f32_e32 v32, v32, v106
	ds_read_b128 v[106:109], v25 offset:5120
	ds_read_b128 v[122:125], v25 offset:5136
	ds_read_b128 v[138:141], v25 offset:5152
	ds_read_b128 v[168:171], v25 offset:5168
	ds_read_b128 v[180:183], v25 offset:5184
	s_waitcnt lgkmcnt(5)
	v_lshlrev_b32_e32 v97, 16, v97
	v_mul_f32_e32 v111, v4, v114
	v_fma_f32 v34, v151, v34, -v111
	v_fma_f32 v111, -v5, v115, 0
	v_fma_f32 v34, -v7, v116, v34
	v_fma_f32 v111, -v9, v117, v111
	v_fma_f32 v34, -v11, v130, v34
	v_fma_f32 v111, -v13, v131, v111
	v_fma_f32 v34, -v14, v132, v34
	v_fma_f32 v111, -v15, v133, v111
	v_fma_f32 v34, -v17, v144, v34
	v_fma_f32 v111, -v18, v145, v111
	v_fma_f32 v34, -v19, v146, v34
	v_fma_f32 v111, -v20, v147, v111
	v_fma_f32 v34, -v22, v172, v34
	v_fma_f32 v111, -v24, v173, v111
	v_fma_f32 v34, -v26, v174, v34
	v_lshlrev_b32_e32 v98, 16, v98
	v_fma_f32 v111, -v27, v175, v111
	v_fma_f32 v34, -v30, v176, v34
	v_mul_f32_e32 v95, v187, v95
	v_mul_f32_e32 v96, v186, v96
	v_mul_f32_e32 v97, v185, v97
	v_mul_f32_e32 v98, v184, v98
	v_fma_f32 v111, -v31, v177, v111
	v_fma_f32 v34, -v32, v178, v34
	ds_read_b128 v[114:117], v25 offset:5376
	ds_read_b128 v[130:133], v25 offset:5392
	ds_read_b128 v[144:147], v25 offset:5408
	ds_read_b128 v[172:175], v25 offset:5424
	ds_read_b128 v[176:179], v25 offset:5440
	ds_read_b128 v[184:187], v25 offset:5456
	s_waitcnt lgkmcnt(6)
	v_add_f32_e32 v34, v111, v34
	v_mul_f32_e32 v106, v4, v106
	v_fma_f32 v36, v153, v36, -v106
	v_fma_f32 v106, -v5, v107, 0
	v_fma_f32 v36, -v7, v108, v36
	v_fma_f32 v106, -v9, v109, v106
	v_fma_f32 v36, -v11, v122, v36
	v_fma_f32 v106, -v13, v123, v106
	v_fma_f32 v36, -v14, v124, v36
	v_fma_f32 v106, -v15, v125, v106
	v_fma_f32 v36, -v17, v138, v36
	v_fma_f32 v106, -v18, v139, v106
	v_fma_f32 v36, -v19, v140, v36
	v_fma_f32 v106, -v20, v141, v106
	v_fma_f32 v36, -v22, v168, v36
	v_fma_f32 v106, -v24, v169, v106
	v_fma_f32 v36, -v26, v170, v36
	v_fma_f32 v106, -v27, v171, v106
	v_lshlrev_b32_e32 v85, 16, v85
	v_fma_f32 v36, -v30, v180, v36
	v_fma_f32 v106, -v31, v181, v106
	v_lshlrev_b32_e32 v89, 16, v89
	v_lshlrev_b32_e32 v92, 16, v92
	v_lshlrev_b32_e32 v94, 16, v94
	v_fma_f32 v36, -v32, v182, v36
	v_fma_f32 v106, -v34, v183, v106
	v_mul_f32_e32 v85, v191, v85
	v_mul_f32_e32 v89, v190, v89
	v_mul_f32_e32 v92, v189, v92
	v_mul_f32_e32 v94, v188, v94
	v_add_f32_e32 v36, v36, v106
	ds_read_b128 v[106:109], v25 offset:5632
	ds_read_b128 v[122:125], v25 offset:5648
	ds_read_b128 v[138:141], v25 offset:5664
	ds_read_b128 v[168:171], v25 offset:5680
	ds_read_b128 v[180:183], v25 offset:5696
	ds_read_b128 v[188:191], v25 offset:5712
	s_waitcnt lgkmcnt(6)
	v_mul_f32_e32 v111, v4, v114
	v_fma_f32 v38, v156, v38, -v111
	v_fma_f32 v111, -v5, v115, 0
	v_fma_f32 v38, -v7, v116, v38
	v_fma_f32 v111, -v9, v117, v111
	v_fma_f32 v38, -v11, v130, v38
	v_fma_f32 v111, -v13, v131, v111
	v_fma_f32 v38, -v14, v132, v38
	v_fma_f32 v111, -v15, v133, v111
	v_fma_f32 v38, -v17, v144, v38
	v_fma_f32 v111, -v18, v145, v111
	v_fma_f32 v38, -v19, v146, v38
	v_fma_f32 v111, -v20, v147, v111
	v_fma_f32 v38, -v22, v172, v38
	v_fma_f32 v111, -v24, v173, v111
	v_fma_f32 v38, -v26, v174, v38
	v_fma_f32 v111, -v27, v175, v111
	v_fma_f32 v38, -v30, v176, v38
	v_fma_f32 v111, -v31, v177, v111
	v_fma_f32 v38, -v32, v178, v38
	v_lshlrev_b32_e32 v158, 16, v158
	v_fma_f32 v111, -v34, v179, v111
	v_fma_f32 v38, -v36, v184, v38
	ds_read_b128 v[114:117], v25 offset:5888
	ds_read_b128 v[130:133], v25 offset:5904
	ds_read_b128 v[144:147], v25 offset:5920
	ds_read_b128 v[172:175], v25 offset:5936
	ds_read_b128 v[176:179], v25 offset:5952
	ds_read_b128 v[184:187], v25 offset:5968
	s_waitcnt lgkmcnt(6)
	v_mul_f32_e32 v158, v159, v158
	v_mul_f32_e32 v106, v4, v106
	v_fma_f32 v40, v158, v40, -v106
	v_fma_f32 v106, -v5, v107, 0
	v_fma_f32 v40, -v7, v108, v40
	v_fma_f32 v106, -v9, v109, v106
	v_add_f32_e32 v38, v111, v38
	v_fma_f32 v40, -v11, v122, v40
	v_fma_f32 v106, -v13, v123, v106
	v_fma_f32 v40, -v14, v124, v40
	v_fma_f32 v106, -v15, v125, v106
	v_fma_f32 v40, -v17, v138, v40
	v_fma_f32 v106, -v18, v139, v106
	v_fma_f32 v40, -v19, v140, v40
	v_fma_f32 v106, -v20, v141, v106
	v_fma_f32 v40, -v22, v168, v40
	v_fma_f32 v106, -v24, v169, v106
	v_fma_f32 v40, -v26, v170, v40
	v_fma_f32 v106, -v27, v171, v106
	v_fma_f32 v40, -v30, v180, v40
	v_fma_f32 v106, -v31, v181, v106
	v_fma_f32 v40, -v32, v182, v40
	v_fma_f32 v106, -v34, v183, v106
	v_lshlrev_b32_e32 v160, 16, v160
	v_mul_f32_e32 v160, v161, v160
	v_fma_f32 v40, -v36, v188, v40
	v_fma_f32 v106, -v38, v189, v106
	v_add_f32_e32 v40, v40, v106
	ds_read_b128 v[106:109], v25 offset:6144
	ds_read_b128 v[122:125], v25 offset:6160
	ds_read_b128 v[138:141], v25 offset:6176
	ds_read_b128 v[156:159], v25 offset:6192
	ds_read_b128 v[168:171], v25 offset:6208
	ds_read_b128 v[180:183], v25 offset:6224
	s_waitcnt lgkmcnt(6)
	v_mul_f32_e32 v111, v4, v114
	v_fma_f32 v41, v160, v41, -v111
	v_fma_f32 v111, -v5, v115, 0
	v_fma_f32 v41, -v7, v116, v41
	v_fma_f32 v111, -v9, v117, v111
	v_fma_f32 v41, -v11, v130, v41
	v_fma_f32 v111, -v13, v131, v111
	v_fma_f32 v41, -v14, v132, v41
	v_fma_f32 v111, -v15, v133, v111
	v_fma_f32 v41, -v17, v144, v41
	v_fma_f32 v111, -v18, v145, v111
	v_fma_f32 v41, -v19, v146, v41
	v_fma_f32 v111, -v20, v147, v111
	v_fma_f32 v41, -v22, v172, v41
	v_fma_f32 v111, -v24, v173, v111
	v_fma_f32 v41, -v26, v174, v41
	v_fma_f32 v111, -v27, v175, v111
	v_fma_f32 v41, -v30, v176, v41
	v_fma_f32 v111, -v31, v177, v111
	v_fma_f32 v41, -v32, v178, v41
	v_fma_f32 v111, -v34, v179, v111
	v_fma_f32 v41, -v36, v184, v41
	v_lshlrev_b32_e32 v163, 16, v163
	v_fma_f32 v111, -v38, v185, v111
	v_fma_f32 v41, -v40, v186, v41
	ds_read_b128 v[114:117], v25 offset:6400
	ds_read_b128 v[130:133], v25 offset:6416
	ds_read_b128 v[144:147], v25 offset:6432
	ds_read_b128 v[172:175], v25 offset:6448
	ds_read_b128 v[176:179], v25 offset:6464
	ds_read_b128 v[184:187], v25 offset:6480
	ds_read_b128 v[188:191], v25 offset:6496
	s_waitcnt lgkmcnt(7)
	v_mul_f32_e32 v163, v164, v163
	v_mul_f32_e32 v106, v4, v106
	v_fma_f32 v43, v163, v43, -v106
	v_fma_f32 v106, -v5, v107, 0
	v_fma_f32 v43, -v7, v108, v43
	v_fma_f32 v106, -v9, v109, v106
	v_add_f32_e32 v41, v111, v41
	v_fma_f32 v43, -v11, v122, v43
	v_fma_f32 v106, -v13, v123, v106
	v_fma_f32 v43, -v14, v124, v43
	v_fma_f32 v106, -v15, v125, v106
	v_fma_f32 v43, -v17, v138, v43
	v_fma_f32 v106, -v18, v139, v106
	v_fma_f32 v43, -v19, v140, v43
	v_fma_f32 v106, -v20, v141, v106
	v_fma_f32 v43, -v22, v156, v43
	v_fma_f32 v106, -v24, v157, v106
	v_fma_f32 v43, -v26, v158, v43
	v_fma_f32 v106, -v27, v159, v106
	v_fma_f32 v43, -v30, v168, v43
	v_fma_f32 v106, -v31, v169, v106
	v_fma_f32 v43, -v32, v170, v43
	v_fma_f32 v106, -v34, v171, v106
	v_lshlrev_b32_e32 v69, 16, v69
	v_fma_f32 v43, -v36, v180, v43
	v_fma_f32 v106, -v38, v181, v106
	v_lshlrev_b32_e32 v73, 16, v73
	v_lshlrev_b32_e32 v77, 16, v77
	v_lshlrev_b32_e32 v80, 16, v80
	v_lshlrev_b32_e32 v165, 16, v165
	v_fma_f32 v43, -v40, v182, v43
	v_fma_f32 v106, -v41, v183, v106
	v_mul_f32_e32 v69, v195, v69
	v_mul_f32_e32 v73, v194, v73
	v_mul_f32_e32 v77, v193, v77
	v_mul_f32_e32 v80, v192, v80
	v_mul_f32_e32 v165, v166, v165
	v_add_f32_e32 v43, v43, v106
	ds_read_b128 v[106:109], v25 offset:6656
	ds_read_b128 v[122:125], v25 offset:6672
	ds_read_b128 v[138:141], v25 offset:6688
	ds_read_b128 v[156:159], v25 offset:6704
	ds_read_b128 v[168:171], v25 offset:6720
	ds_read_b128 v[180:183], v25 offset:6736
	ds_read_b128 v[192:195], v25 offset:6752
	s_waitcnt lgkmcnt(7)
	v_mul_f32_e32 v111, v4, v114
	v_fma_f32 v49, v165, v49, -v111
	v_fma_f32 v111, -v5, v115, 0
	v_fma_f32 v49, -v7, v116, v49
	v_fma_f32 v111, -v9, v117, v111
	v_fma_f32 v49, -v11, v130, v49
	v_fma_f32 v111, -v13, v131, v111
	v_fma_f32 v49, -v14, v132, v49
	v_fma_f32 v111, -v15, v133, v111
	v_fma_f32 v49, -v17, v144, v49
	v_fma_f32 v111, -v18, v145, v111
	v_fma_f32 v49, -v19, v146, v49
	v_fma_f32 v111, -v20, v147, v111
	v_fma_f32 v49, -v22, v172, v49
	v_fma_f32 v111, -v24, v173, v111
	v_fma_f32 v49, -v26, v174, v49
	v_fma_f32 v111, -v27, v175, v111
	v_fma_f32 v49, -v30, v176, v49
	v_fma_f32 v111, -v31, v177, v111
	v_fma_f32 v49, -v32, v178, v49
	v_fma_f32 v111, -v34, v179, v111
	v_fma_f32 v49, -v36, v184, v49
	v_fma_f32 v111, -v38, v185, v111
	v_fma_f32 v49, -v40, v186, v49
	v_fma_f32 v111, -v41, v187, v111
	v_fma_f32 v49, -v43, v188, v49
	ds_read_b128 v[114:117], v25 offset:6912
	ds_read_b128 v[130:133], v25 offset:6928
	ds_read_b128 v[144:147], v25 offset:6944
	ds_read_b128 v[172:175], v25 offset:6960
	ds_read_b128 v[176:179], v25 offset:6976
	ds_read_b128 v[184:187], v25 offset:6992
	ds_read_b128 v[188:191], v25 offset:7008
	s_waitcnt lgkmcnt(7)
	v_mul_f32_e32 v106, v4, v106
	v_fma_f32 v50, v167, v50, -v106
	v_fma_f32 v106, -v5, v107, 0
	v_fma_f32 v50, -v7, v108, v50
	v_fma_f32 v106, -v9, v109, v106
	v_fma_f32 v50, -v11, v122, v50
	v_fma_f32 v106, -v13, v123, v106
	v_fma_f32 v50, -v14, v124, v50
	v_fma_f32 v106, -v15, v125, v106
	v_fma_f32 v50, -v17, v138, v50
	v_fma_f32 v106, -v18, v139, v106
	v_fma_f32 v50, -v19, v140, v50
	v_fma_f32 v106, -v20, v141, v106
	v_fma_f32 v50, -v22, v156, v50
	v_fma_f32 v106, -v24, v157, v106
	v_fma_f32 v50, -v26, v158, v50
	v_fma_f32 v106, -v27, v159, v106
	v_fma_f32 v50, -v30, v168, v50
	v_fma_f32 v106, -v31, v169, v106
	v_fma_f32 v50, -v32, v170, v50
	v_fma_f32 v106, -v34, v171, v106
	v_fma_f32 v50, -v36, v180, v50
	v_fma_f32 v106, -v38, v181, v106
	v_add_f32_e32 v49, v111, v49
	v_fma_f32 v50, -v40, v182, v50
	v_fma_f32 v106, -v41, v183, v106
	v_lshlrev_b32_e32 v39, 16, v39
	v_fma_f32 v50, -v43, v192, v50
	v_fma_f32 v106, -v49, v193, v106
	v_add_f32_e32 v50, v50, v106
	ds_read_b128 v[106:109], v25 offset:7168
	ds_read_b128 v[122:125], v25 offset:7184
	ds_read_b128 v[138:141], v25 offset:7200
	ds_read_b128 v[156:159], v25 offset:7216
	ds_read_b128 v[164:167], v25 offset:7232
	ds_read_b128 v[168:171], v25 offset:7248
	ds_read_b128 v[180:183], v25 offset:7264
	s_waitcnt lgkmcnt(7)
	v_mul_f32_e32 v111, v4, v114
	v_fma_f32 v53, v162, v53, -v111
	v_fma_f32 v111, -v5, v115, 0
	v_fma_f32 v53, -v7, v116, v53
	v_fma_f32 v111, -v9, v117, v111
	v_fma_f32 v53, -v11, v130, v53
	v_fma_f32 v111, -v13, v131, v111
	v_fma_f32 v53, -v14, v132, v53
	v_fma_f32 v111, -v15, v133, v111
	v_fma_f32 v53, -v17, v144, v53
	v_fma_f32 v111, -v18, v145, v111
	v_fma_f32 v53, -v19, v146, v53
	v_fma_f32 v111, -v20, v147, v111
	v_fma_f32 v53, -v22, v172, v53
	v_fma_f32 v111, -v24, v173, v111
	v_fma_f32 v53, -v26, v174, v53
	v_fma_f32 v111, -v27, v175, v111
	v_fma_f32 v53, -v30, v176, v53
	v_fma_f32 v111, -v31, v177, v111
	v_fma_f32 v53, -v32, v178, v53
	v_fma_f32 v111, -v34, v179, v111
	v_fma_f32 v53, -v36, v184, v53
	v_fma_f32 v111, -v38, v185, v111
	v_fma_f32 v53, -v40, v186, v53
	v_fma_f32 v111, -v41, v187, v111
	v_fma_f32 v53, -v43, v188, v53
	v_fma_f32 v111, -v49, v189, v111
	v_fma_f32 v53, -v50, v190, v53
	ds_read_b128 v[114:117], v25 offset:7424
	ds_read_b128 v[130:133], v25 offset:7440
	ds_read_b128 v[144:147], v25 offset:7456
	ds_read_b128 v[160:163], v25 offset:7472
	ds_read_b128 v[172:175], v25 offset:7488
	ds_read_b128 v[176:179], v25 offset:7504
	ds_read_b128 v[184:187], v25 offset:7520
	ds_read_b128 v[188:191], v25 offset:7536
	s_waitcnt lgkmcnt(8)
	v_mul_f32_e32 v106, v4, v106
	v_fma_f32 v54, v155, v54, -v106
	v_fma_f32 v106, -v5, v107, 0
	v_fma_f32 v54, -v7, v108, v54
	v_fma_f32 v106, -v9, v109, v106
	v_fma_f32 v54, -v11, v122, v54
	v_fma_f32 v106, -v13, v123, v106
	v_fma_f32 v54, -v14, v124, v54
	v_fma_f32 v106, -v15, v125, v106
	v_fma_f32 v54, -v17, v138, v54
	v_fma_f32 v106, -v18, v139, v106
	v_fma_f32 v54, -v19, v140, v54
	v_fma_f32 v106, -v20, v141, v106
	v_fma_f32 v54, -v22, v156, v54
	v_fma_f32 v106, -v24, v157, v106
	v_fma_f32 v54, -v26, v158, v54
	v_fma_f32 v106, -v27, v159, v106
	v_fma_f32 v54, -v30, v164, v54
	v_fma_f32 v106, -v31, v165, v106
	v_fma_f32 v54, -v32, v166, v54
	v_fma_f32 v106, -v34, v167, v106
	v_fma_f32 v54, -v36, v168, v54
	v_fma_f32 v106, -v38, v169, v106
	v_fma_f32 v54, -v40, v170, v54
	v_fma_f32 v106, -v41, v171, v106
	v_add_f32_e32 v53, v111, v53
	v_lshlrev_b32_e32 v47, 16, v47
	v_fma_f32 v54, -v43, v180, v54
	v_fma_f32 v106, -v49, v181, v106
	v_fma_f32 v54, -v50, v182, v54
	v_fma_f32 v106, -v53, v183, v106
	v_add_f32_e32 v54, v54, v106
	ds_read_b128 v[106:109], v25 offset:7680
	ds_read_b128 v[122:125], v25 offset:7696
	ds_read_b128 v[138:141], v25 offset:7712
	ds_read_b128 v[152:155], v25 offset:7728
	ds_read_b128 v[156:159], v25 offset:7744
	ds_read_b128 v[164:167], v25 offset:7760
	ds_read_b128 v[168:171], v25 offset:7776
	ds_read_b128 v[180:183], v25 offset:7792
	s_waitcnt lgkmcnt(8)
	v_mul_f32_e32 v111, v4, v114
	v_fma_f32 v57, v150, v57, -v111
	v_fma_f32 v111, -v5, v115, 0
	v_fma_f32 v57, -v7, v116, v57
	v_fma_f32 v111, -v9, v117, v111
	v_fma_f32 v57, -v11, v130, v57
	v_fma_f32 v111, -v13, v131, v111
	v_fma_f32 v57, -v14, v132, v57
	v_fma_f32 v111, -v15, v133, v111
	v_fma_f32 v57, -v17, v144, v57
	v_fma_f32 v111, -v18, v145, v111
	v_fma_f32 v57, -v19, v146, v57
	v_fma_f32 v111, -v20, v147, v111
	v_fma_f32 v57, -v22, v160, v57
	v_fma_f32 v111, -v24, v161, v111
	v_fma_f32 v57, -v26, v162, v57
	v_fma_f32 v111, -v27, v163, v111
	v_fma_f32 v57, -v30, v172, v57
	v_fma_f32 v111, -v31, v173, v111
	v_fma_f32 v57, -v32, v174, v57
	v_fma_f32 v111, -v34, v175, v111
	v_fma_f32 v57, -v36, v176, v57
	v_fma_f32 v111, -v38, v177, v111
	v_fma_f32 v57, -v40, v178, v57
	v_fma_f32 v111, -v41, v179, v111
	v_lshlrev_b32_e32 v51, 16, v51
	v_fma_f32 v57, -v43, v184, v57
	v_fma_f32 v111, -v49, v185, v111
	v_fma_f32 v57, -v50, v186, v57
	v_fma_f32 v111, -v53, v187, v111
	ds_read_b128 v[114:117], v25 offset:7936
	ds_read_b128 v[130:133], v25 offset:7952
	ds_read_b128 v[144:147], v25 offset:7968
	ds_read_b128 v[148:151], v25 offset:7984
	ds_read_b128 v[160:163], v25 offset:8000
	ds_read_b128 v[172:175], v25 offset:8016
	ds_read_b128 v[176:179], v25 offset:8032
	ds_read_b128 v[184:187], v25 offset:8048
	s_waitcnt lgkmcnt(8)
	v_mul_f32_e32 v106, v4, v106
	v_fma_f32 v59, v143, v59, -v106
	v_fma_f32 v106, -v5, v107, 0
	v_fma_f32 v59, -v7, v108, v59
	v_fma_f32 v106, -v9, v109, v106
	v_fma_f32 v59, -v11, v122, v59
	v_fma_f32 v106, -v13, v123, v106
	v_fma_f32 v59, -v14, v124, v59
	v_fma_f32 v106, -v15, v125, v106
	v_fma_f32 v59, -v17, v138, v59
	v_fma_f32 v106, -v18, v139, v106
	v_fma_f32 v59, -v19, v140, v59
	v_fma_f32 v106, -v20, v141, v106
	v_fma_f32 v59, -v22, v152, v59
	v_fma_f32 v106, -v24, v153, v106
	v_fma_f32 v59, -v26, v154, v59
	v_fma_f32 v106, -v27, v155, v106
	v_fma_f32 v59, -v30, v156, v59
	v_fma_f32 v106, -v31, v157, v106
	v_fma_f32 v59, -v32, v158, v59
	v_fma_f32 v106, -v34, v159, v106
	v_fma_f32 v59, -v36, v164, v59
	v_fma_f32 v106, -v38, v165, v106
	v_fma_f32 v59, -v40, v166, v59
	v_fma_f32 v106, -v41, v167, v106
	v_fma_f32 v57, -v54, v188, v57
	v_add_f32_e32 v57, v111, v57
	v_fma_f32 v59, -v43, v168, v59
	v_fma_f32 v106, -v49, v169, v106
	v_fma_f32 v59, -v50, v170, v59
	v_fma_f32 v106, -v53, v171, v106
	v_lshlrev_b32_e32 v56, 16, v56
	v_fma_f32 v59, -v54, v180, v59
	v_fma_f32 v106, -v57, v181, v106
	v_add_f32_e32 v59, v59, v106
	ds_read_b128 v[106:109], v25 offset:8192
	ds_read_b128 v[122:125], v25 offset:8208
	ds_read_b128 v[138:141], v25 offset:8224
	ds_read_b128 v[152:155], v25 offset:8240
	ds_read_b128 v[156:159], v25 offset:8256
	ds_read_b128 v[164:167], v25 offset:8272
	ds_read_b128 v[168:171], v25 offset:8288
	ds_read_b128 v[180:183], v25 offset:8304
	s_waitcnt lgkmcnt(8)
	v_mul_f32_e32 v111, v4, v114
	v_fma_f32 v62, v136, v62, -v111
	v_fma_f32 v111, -v5, v115, 0
	v_fma_f32 v62, -v7, v116, v62
	v_fma_f32 v111, -v9, v117, v111
	v_fma_f32 v62, -v11, v130, v62
	v_fma_f32 v111, -v13, v131, v111
	v_fma_f32 v62, -v14, v132, v62
	v_fma_f32 v111, -v15, v133, v111
	v_fma_f32 v62, -v17, v144, v62
	v_fma_f32 v111, -v18, v145, v111
	v_fma_f32 v62, -v19, v146, v62
	v_fma_f32 v111, -v20, v147, v111
	v_fma_f32 v62, -v22, v148, v62
	v_fma_f32 v111, -v24, v149, v111
	v_fma_f32 v62, -v26, v150, v62
	v_fma_f32 v111, -v27, v151, v111
	v_fma_f32 v62, -v30, v160, v62
	v_fma_f32 v111, -v31, v161, v111
	v_fma_f32 v62, -v32, v162, v62
	v_fma_f32 v111, -v34, v163, v111
	v_fma_f32 v62, -v36, v172, v62
	v_fma_f32 v111, -v38, v173, v111
	v_fma_f32 v62, -v40, v174, v62
	v_fma_f32 v111, -v41, v175, v111
	v_fma_f32 v62, -v43, v176, v62
	v_fma_f32 v111, -v49, v177, v111
	v_fma_f32 v62, -v50, v178, v62
	v_fma_f32 v111, -v53, v179, v111
	v_fma_f32 v62, -v54, v184, v62
	v_fma_f32 v111, -v57, v185, v111
	v_fma_f32 v62, -v59, v186, v62
	ds_read_b128 v[114:117], v25 offset:8448
	ds_read_b128 v[130:133], v25 offset:8464
	ds_read_b128 v[134:137], v25 offset:8480
	ds_read_b128 v[142:145], v25 offset:8496
	ds_read_b128 v[146:149], v25 offset:8512
	ds_read_b128 v[160:163], v25 offset:8528
	ds_read_b128 v[172:175], v25 offset:8544
	ds_read_b128 v[176:179], v25 offset:8560
	ds_read_b128 v[184:187], v25 offset:8576
	s_waitcnt lgkmcnt(9)
	v_mul_f32_e32 v106, v4, v106
	v_fma_f32 v63, v129, v63, -v106
	v_fma_f32 v106, -v5, v107, 0
	v_fma_f32 v63, -v7, v108, v63
	v_fma_f32 v106, -v9, v109, v106
	v_fma_f32 v63, -v11, v122, v63
	v_fma_f32 v106, -v13, v123, v106
	v_fma_f32 v63, -v14, v124, v63
	v_fma_f32 v106, -v15, v125, v106
	v_fma_f32 v63, -v17, v138, v63
	v_fma_f32 v106, -v18, v139, v106
	v_fma_f32 v63, -v19, v140, v63
	v_fma_f32 v106, -v20, v141, v106
	v_fma_f32 v63, -v22, v152, v63
	v_fma_f32 v106, -v24, v153, v106
	v_fma_f32 v63, -v26, v154, v63
	v_fma_f32 v106, -v27, v155, v106
	v_fma_f32 v63, -v30, v156, v63
	v_fma_f32 v106, -v31, v157, v106
	v_fma_f32 v63, -v32, v158, v63
	v_fma_f32 v106, -v34, v159, v106
	v_fma_f32 v63, -v36, v164, v63
	v_fma_f32 v106, -v38, v165, v106
	v_fma_f32 v63, -v40, v166, v63
	v_fma_f32 v106, -v41, v167, v106
	v_add_f32_e32 v62, v111, v62
	v_fma_f32 v63, -v43, v168, v63
	v_fma_f32 v106, -v49, v169, v106
	v_fma_f32 v63, -v50, v170, v63
	v_fma_f32 v106, -v53, v171, v106
	v_mul_f32_e32 v39, v219, v39
	v_fma_f32 v63, -v54, v180, v63
	v_fma_f32 v106, -v57, v181, v106
	v_fma_f32 v63, -v59, v182, v63
	v_fma_f32 v106, -v62, v183, v106
	v_add_f32_e32 v63, v63, v106
	ds_read_b128 v[106:109], v25 offset:8704
	ds_read_b128 v[122:125], v25 offset:8720
	ds_read_b128 v[126:129], v25 offset:8736
	ds_read_b128 v[138:141], v25 offset:8752
	ds_read_b128 v[150:153], v25 offset:8768
	ds_read_b128 v[154:157], v25 offset:8784
	ds_read_b128 v[164:167], v25 offset:8800
	ds_read_b128 v[168:171], v25 offset:8816
	ds_read_b128 v[180:183], v25 offset:8832
	s_waitcnt lgkmcnt(9)
	v_mul_f32_e32 v111, v4, v114
	v_fma_f32 v71, v120, v71, -v111
	v_fma_f32 v111, -v5, v115, 0
	v_fma_f32 v71, -v7, v116, v71
	v_fma_f32 v111, -v9, v117, v111
	v_fma_f32 v71, -v11, v130, v71
	v_fma_f32 v111, -v13, v131, v111
	v_fma_f32 v71, -v14, v132, v71
	v_fma_f32 v111, -v15, v133, v111
	v_fma_f32 v71, -v17, v134, v71
	v_fma_f32 v111, -v18, v135, v111
	v_fma_f32 v71, -v19, v136, v71
	v_fma_f32 v111, -v20, v137, v111
	v_fma_f32 v71, -v22, v142, v71
	v_fma_f32 v111, -v24, v143, v111
	v_fma_f32 v71, -v26, v144, v71
	v_fma_f32 v111, -v27, v145, v111
	v_fma_f32 v71, -v30, v146, v71
	v_fma_f32 v111, -v31, v147, v111
	v_fma_f32 v71, -v32, v148, v71
	v_fma_f32 v111, -v34, v149, v111
	v_fma_f32 v71, -v36, v160, v71
	v_fma_f32 v111, -v38, v161, v111
	v_fma_f32 v71, -v40, v162, v71
	v_fma_f32 v111, -v41, v163, v111
	v_mul_f32_e32 v47, v218, v47
	v_fma_f32 v71, -v43, v172, v71
	v_fma_f32 v111, -v49, v173, v111
	v_fma_f32 v71, -v50, v174, v71
	v_fma_f32 v111, -v53, v175, v111
	v_fma_f32 v71, -v54, v176, v71
	v_fma_f32 v111, -v57, v177, v111
	v_fma_f32 v71, -v59, v178, v71
	v_fma_f32 v111, -v62, v179, v111
	ds_read_b128 v[114:117], v25 offset:8960
	ds_read_b128 v[118:121], v25 offset:8976
	ds_read_b128 v[130:133], v25 offset:8992
	ds_read_b128 v[134:137], v25 offset:9008
	ds_read_b128 v[142:145], v25 offset:9024
	ds_read_b128 v[146:149], v25 offset:9040
	ds_read_b128 v[158:161], v25 offset:9056
	ds_read_b128 v[172:175], v25 offset:9072
	ds_read_b128 v[176:179], v25 offset:9088
	s_waitcnt lgkmcnt(9)
	v_mul_f32_e32 v106, v4, v106
	v_fma_f32 v74, v110, v74, -v106
	v_fma_f32 v106, -v5, v107, 0
	v_fma_f32 v74, -v7, v108, v74
	v_fma_f32 v106, -v9, v109, v106
	v_fma_f32 v74, -v11, v122, v74
	v_fma_f32 v106, -v13, v123, v106
	v_fma_f32 v74, -v14, v124, v74
	v_fma_f32 v106, -v15, v125, v106
	v_fma_f32 v74, -v17, v126, v74
	v_fma_f32 v106, -v18, v127, v106
	v_fma_f32 v74, -v19, v128, v74
	v_fma_f32 v106, -v20, v129, v106
	v_fma_f32 v74, -v22, v138, v74
	v_fma_f32 v106, -v24, v139, v106
	v_fma_f32 v74, -v26, v140, v74
	v_fma_f32 v106, -v27, v141, v106
	v_fma_f32 v74, -v30, v150, v74
	v_fma_f32 v106, -v31, v151, v106
	v_fma_f32 v74, -v32, v152, v74
	v_fma_f32 v106, -v34, v153, v106
	v_fma_f32 v74, -v36, v154, v74
	v_fma_f32 v106, -v38, v155, v106
	v_fma_f32 v74, -v40, v156, v74
	v_fma_f32 v106, -v41, v157, v106
	v_fma_f32 v71, -v63, v184, v71
	v_fma_f32 v74, -v43, v164, v74
	v_fma_f32 v106, -v49, v165, v106
	v_fma_f32 v74, -v50, v166, v74
	v_fma_f32 v106, -v53, v167, v106
	v_add_f32_e32 v71, v111, v71
	v_fma_f32 v74, -v54, v168, v74
	v_fma_f32 v106, -v57, v169, v106
	v_fma_f32 v74, -v59, v170, v74
	v_fma_f32 v106, -v62, v171, v106
	v_mul_f32_e32 v51, v217, v51
	v_fma_f32 v74, -v63, v180, v74
	v_fma_f32 v106, -v71, v181, v106
	v_add_f32_e32 v74, v74, v106
	ds_read_b128 v[106:109], v25 offset:9216
	ds_read_b128 v[122:125], v25 offset:9232
	ds_read_b128 v[126:129], v25 offset:9248
	ds_read_b128 v[138:141], v25 offset:9264
	ds_read_b128 v[150:153], v25 offset:9280
	ds_read_b128 v[154:157], v25 offset:9296
	ds_read_b128 v[162:165], v25 offset:9312
	ds_read_b128 v[166:169], v25 offset:9328
	ds_read_b128 v[180:183], v25 offset:9344
	s_waitcnt lgkmcnt(9)
	v_mul_f32_e32 v110, v4, v114
	v_fma_f32 v76, v105, v76, -v110
	v_fma_f32 v105, -v5, v115, 0
	v_fma_f32 v76, -v7, v116, v76
	v_fma_f32 v105, -v9, v117, v105
	v_fma_f32 v76, -v11, v118, v76
	v_fma_f32 v105, -v13, v119, v105
	v_fma_f32 v76, -v14, v120, v76
	v_fma_f32 v105, -v15, v121, v105
	v_fma_f32 v76, -v17, v130, v76
	v_fma_f32 v105, -v18, v131, v105
	v_fma_f32 v76, -v19, v132, v76
	v_fma_f32 v105, -v20, v133, v105
	v_fma_f32 v76, -v22, v134, v76
	v_fma_f32 v105, -v24, v135, v105
	v_fma_f32 v76, -v26, v136, v76
	v_fma_f32 v105, -v27, v137, v105
	v_fma_f32 v76, -v30, v142, v76
	v_fma_f32 v105, -v31, v143, v105
	v_fma_f32 v76, -v32, v144, v76
	v_fma_f32 v105, -v34, v145, v105
	v_fma_f32 v76, -v36, v146, v76
	v_fma_f32 v105, -v38, v147, v105
	v_fma_f32 v76, -v40, v148, v76
	v_fma_f32 v105, -v41, v149, v105
	v_fma_f32 v76, -v43, v158, v76
	v_fma_f32 v105, -v49, v159, v105
	v_fma_f32 v76, -v50, v160, v76
	v_fma_f32 v105, -v53, v161, v105
	v_fma_f32 v76, -v54, v172, v76
	v_fma_f32 v105, -v57, v173, v105
	v_fma_f32 v76, -v59, v174, v76
	v_fma_f32 v105, -v62, v175, v105
	v_fma_f32 v76, -v63, v176, v76
	v_fma_f32 v105, -v71, v177, v105
	v_fma_f32 v76, -v74, v178, v76
	v_add_f32_e32 v76, v105, v76
	ds_read_b128 v[114:117], v25 offset:9472
	ds_read_b128 v[118:121], v25 offset:9488
	ds_read_b128 v[130:133], v25 offset:9504
	ds_read_b128 v[134:137], v25 offset:9520
	ds_read_b128 v[142:145], v25 offset:9536
	ds_read_b128 v[146:149], v25 offset:9552
	ds_read_b128 v[158:161], v25 offset:9568
	ds_read_b128 v[170:173], v25 offset:9584
	ds_read_b128 v[174:177], v25 offset:9600
	ds_read_b128 v[184:187], v25 offset:9616
	s_waitcnt lgkmcnt(10)
	v_mul_f32_e32 v105, v4, v106
	v_fma_f32 v79, v104, v79, -v105
	v_fma_f32 v104, -v5, v107, 0
	v_fma_f32 v79, -v7, v108, v79
	v_fma_f32 v104, -v9, v109, v104
	v_fma_f32 v79, -v11, v122, v79
	v_fma_f32 v104, -v13, v123, v104
	v_fma_f32 v79, -v14, v124, v79
	v_fma_f32 v104, -v15, v125, v104
	v_fma_f32 v79, -v17, v126, v79
	v_fma_f32 v104, -v18, v127, v104
	v_fma_f32 v79, -v19, v128, v79
	v_fma_f32 v104, -v20, v129, v104
	v_fma_f32 v79, -v22, v138, v79
	v_fma_f32 v104, -v24, v139, v104
	v_fma_f32 v79, -v26, v140, v79
	v_fma_f32 v104, -v27, v141, v104
	v_fma_f32 v79, -v30, v150, v79
	v_fma_f32 v104, -v31, v151, v104
	v_fma_f32 v79, -v32, v152, v79
	v_fma_f32 v104, -v34, v153, v104
	v_fma_f32 v79, -v36, v154, v79
	v_fma_f32 v104, -v38, v155, v104
	v_fma_f32 v79, -v40, v156, v79
	v_fma_f32 v104, -v41, v157, v104
	v_mul_f32_e32 v56, v216, v56
	v_fma_f32 v79, -v43, v162, v79
	v_fma_f32 v104, -v49, v163, v104
	v_fma_f32 v79, -v50, v164, v79
	v_fma_f32 v104, -v53, v165, v104
	v_fma_f32 v79, -v54, v166, v79
	v_fma_f32 v104, -v57, v167, v104
	v_fma_f32 v79, -v59, v168, v79
	v_fma_f32 v104, -v62, v169, v104
	v_fma_f32 v79, -v63, v180, v79
	v_fma_f32 v104, -v71, v181, v104
	v_fma_f32 v79, -v74, v182, v79
	v_fma_f32 v104, -v76, v183, v104
	v_add_f32_e32 v79, v79, v104
	ds_read_b128 v[104:107], v25 offset:9728
	ds_read_b128 v[108:111], v25 offset:9744
	ds_read_b128 v[122:125], v25 offset:9760
	ds_read_b128 v[126:129], v25 offset:9776
	ds_read_b128 v[138:141], v25 offset:9792
	ds_read_b128 v[150:153], v25 offset:9808
	ds_read_b128 v[154:157], v25 offset:9824
	ds_read_b128 v[162:165], v25 offset:9840
	ds_read_b128 v[166:169], v25 offset:9856
	ds_read_b128 v[178:181], v25 offset:9872
	s_waitcnt lgkmcnt(10)
	s_nop 0
	v_mul_f32_e32 v114, v4, v114
	v_fma_f32 v82, v103, v82, -v114
	v_fma_f32 v103, -v5, v115, 0
	v_fma_f32 v82, -v7, v116, v82
	v_fma_f32 v103, -v9, v117, v103
	v_fma_f32 v82, -v11, v118, v82
	v_fma_f32 v103, -v13, v119, v103
	v_fma_f32 v82, -v14, v120, v82
	v_fma_f32 v103, -v15, v121, v103
	v_fma_f32 v82, -v17, v130, v82
	v_fma_f32 v103, -v18, v131, v103
	v_fma_f32 v82, -v19, v132, v82
	v_fma_f32 v103, -v20, v133, v103
	v_fma_f32 v82, -v22, v134, v82
	v_fma_f32 v103, -v24, v135, v103
	v_fma_f32 v82, -v26, v136, v82
	v_fma_f32 v103, -v27, v137, v103
	v_fma_f32 v82, -v30, v142, v82
	v_fma_f32 v103, -v31, v143, v103
	v_fma_f32 v82, -v32, v144, v82
	v_fma_f32 v103, -v34, v145, v103
	v_fma_f32 v82, -v36, v146, v82
	v_fma_f32 v103, -v38, v147, v103
	v_fma_f32 v82, -v40, v148, v82
	v_fma_f32 v103, -v41, v149, v103
	v_fma_f32 v82, -v43, v158, v82
	v_fma_f32 v103, -v49, v159, v103
	v_fma_f32 v82, -v50, v160, v82
	v_fma_f32 v103, -v53, v161, v103
	v_fma_f32 v82, -v54, v170, v82
	v_fma_f32 v103, -v57, v171, v103
	v_fma_f32 v82, -v59, v172, v82
	v_fma_f32 v103, -v62, v173, v103
	v_fma_f32 v82, -v63, v174, v82
	v_fma_f32 v103, -v71, v175, v103
	v_fma_f32 v82, -v74, v176, v82
	v_fma_f32 v103, -v76, v177, v103
	v_fma_f32 v82, -v79, v184, v82
	v_add_f32_e32 v82, v103, v82
	ds_read_b128 v[114:117], v25 offset:9984
	ds_read_b128 v[118:121], v25 offset:10000
	ds_read_b128 v[130:133], v25 offset:10016
	ds_read_b128 v[134:137], v25 offset:10032
	ds_read_b128 v[142:145], v25 offset:10048
	ds_read_b128 v[146:149], v25 offset:10064
	ds_read_b128 v[158:161], v25 offset:10080
	ds_read_b128 v[170:173], v25 offset:10096
	ds_read_b128 v[174:177], v25 offset:10112
	ds_read_b128 v[182:185], v25 offset:10128
	s_waitcnt lgkmcnt(10)
	s_nop 0
	v_mul_f32_e32 v103, v4, v104
	v_fma_f32 v84, v102, v84, -v103
	v_fma_f32 v102, -v5, v105, 0
	v_fma_f32 v84, -v7, v106, v84
	v_fma_f32 v102, -v9, v107, v102
	v_fma_f32 v84, -v11, v108, v84
	v_fma_f32 v102, -v13, v109, v102
	v_fma_f32 v84, -v14, v110, v84
	v_fma_f32 v102, -v15, v111, v102
	v_fma_f32 v84, -v17, v122, v84
	v_fma_f32 v102, -v18, v123, v102
	v_fma_f32 v84, -v19, v124, v84
	v_fma_f32 v102, -v20, v125, v102
	v_fma_f32 v84, -v22, v126, v84
	v_fma_f32 v102, -v24, v127, v102
	v_fma_f32 v84, -v26, v128, v84
	v_fma_f32 v102, -v27, v129, v102
	v_fma_f32 v84, -v30, v138, v84
	v_fma_f32 v102, -v31, v139, v102
	v_fma_f32 v84, -v32, v140, v84
	v_fma_f32 v102, -v34, v141, v102
	v_fma_f32 v84, -v36, v150, v84
	v_fma_f32 v102, -v38, v151, v102
	v_fma_f32 v84, -v40, v152, v84
	v_fma_f32 v102, -v41, v153, v102
	v_lshlrev_b32_e32 v2, 16, v2
	v_fma_f32 v84, -v43, v154, v84
	v_fma_f32 v102, -v49, v155, v102
	v_fma_f32 v84, -v50, v156, v84
	v_fma_f32 v102, -v53, v157, v102
	v_fma_f32 v84, -v54, v162, v84
	v_fma_f32 v102, -v57, v163, v102
	v_fma_f32 v84, -v59, v164, v84
	v_fma_f32 v102, -v62, v165, v102
	v_fma_f32 v84, -v63, v166, v84
	v_fma_f32 v102, -v71, v167, v102
	v_fma_f32 v84, -v74, v168, v84
	v_fma_f32 v102, -v76, v169, v102
	v_fma_f32 v84, -v79, v178, v84
	v_fma_f32 v102, -v82, v179, v102
	v_add_f32_e32 v84, v84, v102
	ds_read_b128 v[102:105], v25 offset:10240
	ds_read_b128 v[106:109], v25 offset:10256
	ds_read_b128 v[122:125], v25 offset:10272
	ds_read_b128 v[126:129], v25 offset:10288
	ds_read_b128 v[138:141], v25 offset:10304
	ds_read_b128 v[150:153], v25 offset:10320
	ds_read_b128 v[154:157], v25 offset:10336
	ds_read_b128 v[162:165], v25 offset:10352
	ds_read_b128 v[166:169], v25 offset:10368
	ds_read_b128 v[178:181], v25 offset:10384
	s_waitcnt lgkmcnt(10)
	s_nop 0
	v_mul_f32_e32 v110, v4, v114
	v_fma_f32 v87, v101, v87, -v110
	v_fma_f32 v101, -v5, v115, 0
	v_fma_f32 v87, -v7, v116, v87
	v_fma_f32 v101, -v9, v117, v101
	v_fma_f32 v87, -v11, v118, v87
	v_fma_f32 v101, -v13, v119, v101
	v_fma_f32 v87, -v14, v120, v87
	v_fma_f32 v101, -v15, v121, v101
	v_fma_f32 v87, -v17, v130, v87
	v_fma_f32 v101, -v18, v131, v101
	v_fma_f32 v87, -v19, v132, v87
	v_fma_f32 v101, -v20, v133, v101
	v_fma_f32 v87, -v22, v134, v87
	v_fma_f32 v101, -v24, v135, v101
	v_fma_f32 v87, -v26, v136, v87
	v_fma_f32 v101, -v27, v137, v101
	v_fma_f32 v87, -v30, v142, v87
	v_fma_f32 v101, -v31, v143, v101
	v_fma_f32 v87, -v32, v144, v87
	v_fma_f32 v101, -v34, v145, v101
	v_fma_f32 v87, -v36, v146, v87
	v_fma_f32 v101, -v38, v147, v101
	v_fma_f32 v87, -v40, v148, v87
	v_fma_f32 v101, -v41, v149, v101
	v_fma_f32 v87, -v43, v158, v87
	v_fma_f32 v101, -v49, v159, v101
	v_fma_f32 v87, -v50, v160, v87
	v_fma_f32 v101, -v53, v161, v101
	v_fma_f32 v87, -v54, v170, v87
	v_fma_f32 v101, -v57, v171, v101
	v_fma_f32 v87, -v59, v172, v87
	v_fma_f32 v101, -v62, v173, v101
	v_fma_f32 v87, -v63, v174, v87
	v_fma_f32 v101, -v71, v175, v101
	v_fma_f32 v87, -v74, v176, v87
	v_fma_f32 v101, -v76, v177, v101
	v_fma_f32 v87, -v79, v182, v87
	v_fma_f32 v101, -v82, v183, v101
	v_fma_f32 v87, -v84, v184, v87
	v_add_f32_e32 v87, v101, v87
	ds_read_b128 v[114:117], v25 offset:10496
	ds_read_b128 v[118:121], v25 offset:10512
	ds_read_b128 v[130:133], v25 offset:10528
	ds_read_b128 v[134:137], v25 offset:10544
	ds_read_b128 v[142:145], v25 offset:10560
	ds_read_b128 v[146:149], v25 offset:10576
	ds_read_b128 v[158:161], v25 offset:10592
	ds_read_b128 v[170:173], v25 offset:10608
	ds_read_b128 v[174:177], v25 offset:10624
	ds_read_b128 v[182:185], v25 offset:10640
	ds_read_b128 v[186:189], v25 offset:10656
	s_waitcnt lgkmcnt(11)
	s_nop 0
	v_mul_f32_e32 v101, v4, v102
	v_fma_f32 v90, v100, v90, -v101
	v_fma_f32 v100, -v5, v103, 0
	v_fma_f32 v90, -v7, v104, v90
	v_fma_f32 v100, -v9, v105, v100
	v_fma_f32 v90, -v11, v106, v90
	v_fma_f32 v100, -v13, v107, v100
	v_fma_f32 v90, -v14, v108, v90
	v_fma_f32 v100, -v15, v109, v100
	v_fma_f32 v90, -v17, v122, v90
	v_fma_f32 v100, -v18, v123, v100
	v_fma_f32 v90, -v19, v124, v90
	v_fma_f32 v100, -v20, v125, v100
	v_fma_f32 v90, -v22, v126, v90
	v_fma_f32 v100, -v24, v127, v100
	v_fma_f32 v90, -v26, v128, v90
	v_fma_f32 v100, -v27, v129, v100
	v_fma_f32 v90, -v30, v138, v90
	v_fma_f32 v100, -v31, v139, v100
	v_fma_f32 v90, -v32, v140, v90
	v_fma_f32 v100, -v34, v141, v100
	v_fma_f32 v90, -v36, v150, v90
	v_fma_f32 v100, -v38, v151, v100
	v_fma_f32 v90, -v40, v152, v90
	v_fma_f32 v100, -v41, v153, v100
	v_lshlrev_b32_e32 v21, 16, v21
	v_fma_f32 v90, -v43, v154, v90
	v_fma_f32 v100, -v49, v155, v100
	v_fma_f32 v90, -v50, v156, v90
	v_fma_f32 v100, -v53, v157, v100
	v_fma_f32 v90, -v54, v162, v90
	v_fma_f32 v100, -v57, v163, v100
	v_fma_f32 v90, -v59, v164, v90
	v_fma_f32 v100, -v62, v165, v100
	v_fma_f32 v90, -v63, v166, v90
	v_fma_f32 v100, -v71, v167, v100
	v_fma_f32 v90, -v74, v168, v90
	v_fma_f32 v100, -v76, v169, v100
	v_fma_f32 v90, -v79, v178, v90
	v_fma_f32 v100, -v82, v179, v100
	v_fma_f32 v90, -v84, v180, v90
	v_fma_f32 v100, -v87, v181, v100
	v_add_f32_e32 v90, v90, v100
	ds_read_b128 v[100:103], v25 offset:10752
	ds_read_b128 v[104:107], v25 offset:10768
	ds_read_b128 v[108:111], v25 offset:10784
	ds_read_b128 v[122:125], v25 offset:10800
	ds_read_b128 v[126:129], v25 offset:10816
	ds_read_b128 v[138:141], v25 offset:10832
	ds_read_b128 v[150:153], v25 offset:10848
	ds_read_b128 v[154:157], v25 offset:10864
	ds_read_b128 v[162:165], v25 offset:10880
	ds_read_b128 v[166:169], v25 offset:10896
	ds_read_b128 v[178:181], v25 offset:10912
	s_waitcnt lgkmcnt(11)
	s_nop 0
	v_mul_f32_e32 v114, v4, v114
	v_fma_f32 v93, v99, v93, -v114
	v_fma_f32 v99, -v5, v115, 0
	v_fma_f32 v93, -v7, v116, v93
	v_fma_f32 v99, -v9, v117, v99
	v_fma_f32 v93, -v11, v118, v93
	v_fma_f32 v99, -v13, v119, v99
	v_fma_f32 v93, -v14, v120, v93
	v_fma_f32 v99, -v15, v121, v99
	v_fma_f32 v93, -v17, v130, v93
	v_fma_f32 v99, -v18, v131, v99
	v_fma_f32 v93, -v19, v132, v93
	v_fma_f32 v99, -v20, v133, v99
	v_fma_f32 v93, -v22, v134, v93
	v_fma_f32 v99, -v24, v135, v99
	v_fma_f32 v93, -v26, v136, v93
	v_fma_f32 v99, -v27, v137, v99
	v_fma_f32 v93, -v30, v142, v93
	v_fma_f32 v99, -v31, v143, v99
	v_fma_f32 v93, -v32, v144, v93
	v_fma_f32 v99, -v34, v145, v99
	v_fma_f32 v93, -v36, v146, v93
	v_fma_f32 v99, -v38, v147, v99
	v_fma_f32 v93, -v40, v148, v93
	v_fma_f32 v99, -v41, v149, v99
	v_fma_f32 v93, -v43, v158, v93
	v_fma_f32 v99, -v49, v159, v99
	v_fma_f32 v93, -v50, v160, v93
	v_fma_f32 v99, -v53, v161, v99
	v_fma_f32 v93, -v54, v170, v93
	v_fma_f32 v99, -v57, v171, v99
	v_fma_f32 v93, -v59, v172, v93
	v_fma_f32 v99, -v62, v173, v99
	v_fma_f32 v93, -v63, v174, v93
	v_fma_f32 v99, -v71, v175, v99
	v_fma_f32 v93, -v74, v176, v93
	v_fma_f32 v99, -v76, v177, v99
	v_fma_f32 v93, -v79, v182, v93
	v_fma_f32 v99, -v82, v183, v99
	v_fma_f32 v93, -v84, v184, v93
	v_fma_f32 v99, -v87, v185, v99
	v_fma_f32 v93, -v90, v186, v93
	v_add_f32_e32 v93, v99, v93
	ds_read_b128 v[114:117], v25 offset:11008
	ds_read_b128 v[118:121], v25 offset:11024
	ds_read_b128 v[130:133], v25 offset:11040
	ds_read_b128 v[134:137], v25 offset:11056
	ds_read_b128 v[142:145], v25 offset:11072
	ds_read_b128 v[146:149], v25 offset:11088
	ds_read_b128 v[158:161], v25 offset:11104
	ds_read_b128 v[170:173], v25 offset:11120
	ds_read_b128 v[174:177], v25 offset:11136
	ds_read_b128 v[182:185], v25 offset:11152
	ds_read_b128 v[186:189], v25 offset:11168
	s_waitcnt lgkmcnt(11)
	s_nop 0
	v_mul_f32_e32 v99, v4, v100
	v_fma_f32 v91, v98, v91, -v99
	v_fma_f32 v98, -v5, v101, 0
	v_fma_f32 v91, -v7, v102, v91
	v_fma_f32 v98, -v9, v103, v98
	v_fma_f32 v91, -v11, v104, v91
	v_fma_f32 v98, -v13, v105, v98
	v_fma_f32 v91, -v14, v106, v91
	v_fma_f32 v98, -v15, v107, v98
	v_fma_f32 v91, -v17, v108, v91
	v_fma_f32 v98, -v18, v109, v98
	v_fma_f32 v91, -v19, v110, v91
	v_fma_f32 v98, -v20, v111, v98
	v_fma_f32 v91, -v22, v122, v91
	v_fma_f32 v98, -v24, v123, v98
	v_fma_f32 v91, -v26, v124, v91
	v_fma_f32 v98, -v27, v125, v98
	v_fma_f32 v91, -v30, v126, v91
	v_fma_f32 v98, -v31, v127, v98
	v_fma_f32 v91, -v32, v128, v91
	v_fma_f32 v98, -v34, v129, v98
	v_fma_f32 v91, -v36, v138, v91
	v_fma_f32 v98, -v38, v139, v98
	v_fma_f32 v91, -v40, v140, v91
	v_fma_f32 v98, -v41, v141, v98
	v_lshlrev_b32_e32 v29, 16, v29
	v_fma_f32 v91, -v43, v150, v91
	v_fma_f32 v98, -v49, v151, v98
	v_fma_f32 v91, -v50, v152, v91
	v_fma_f32 v98, -v53, v153, v98
	v_fma_f32 v91, -v54, v154, v91
	v_fma_f32 v98, -v57, v155, v98
	v_fma_f32 v91, -v59, v156, v91
	v_fma_f32 v98, -v62, v157, v98
	v_fma_f32 v91, -v63, v162, v91
	v_fma_f32 v98, -v71, v163, v98
	v_fma_f32 v91, -v74, v164, v91
	v_fma_f32 v98, -v76, v165, v98
	v_fma_f32 v91, -v79, v166, v91
	v_fma_f32 v98, -v82, v167, v98
	v_fma_f32 v91, -v84, v168, v91
	v_fma_f32 v98, -v87, v169, v98
	v_fma_f32 v91, -v90, v178, v91
	v_fma_f32 v98, -v93, v179, v98
	v_add_f32_e32 v91, v91, v98
	ds_read_b128 v[98:101], v25 offset:11264
	ds_read_b128 v[102:105], v25 offset:11280
	ds_read_b128 v[106:109], v25 offset:11296
	ds_read_b128 v[122:125], v25 offset:11312
	ds_read_b128 v[126:129], v25 offset:11328
	ds_read_b128 v[138:141], v25 offset:11344
	ds_read_b128 v[150:153], v25 offset:11360
	ds_read_b128 v[154:157], v25 offset:11376
	ds_read_b128 v[162:165], v25 offset:11392
	ds_read_b128 v[166:169], v25 offset:11408
	ds_read_b128 v[178:181], v25 offset:11424
	s_waitcnt lgkmcnt(11)
	s_nop 0
	v_mul_f32_e32 v110, v4, v114
	v_fma_f32 v88, v97, v88, -v110
	v_fma_f32 v97, -v5, v115, 0
	v_fma_f32 v88, -v7, v116, v88
	v_fma_f32 v97, -v9, v117, v97
	v_fma_f32 v88, -v11, v118, v88
	v_fma_f32 v97, -v13, v119, v97
	v_fma_f32 v88, -v14, v120, v88
	v_fma_f32 v97, -v15, v121, v97
	v_fma_f32 v88, -v17, v130, v88
	v_fma_f32 v97, -v18, v131, v97
	v_fma_f32 v88, -v19, v132, v88
	v_fma_f32 v97, -v20, v133, v97
	v_fma_f32 v88, -v22, v134, v88
	v_fma_f32 v97, -v24, v135, v97
	v_fma_f32 v88, -v26, v136, v88
	v_fma_f32 v97, -v27, v137, v97
	v_fma_f32 v88, -v30, v142, v88
	v_fma_f32 v97, -v31, v143, v97
	v_fma_f32 v88, -v32, v144, v88
	v_fma_f32 v97, -v34, v145, v97
	v_fma_f32 v88, -v36, v146, v88
	v_fma_f32 v97, -v38, v147, v97
	v_fma_f32 v88, -v40, v148, v88
	v_fma_f32 v97, -v41, v149, v97
	v_fma_f32 v88, -v43, v158, v88
	v_fma_f32 v97, -v49, v159, v97
	v_fma_f32 v88, -v50, v160, v88
	v_fma_f32 v97, -v53, v161, v97
	v_fma_f32 v88, -v54, v170, v88
	v_fma_f32 v97, -v57, v171, v97
	v_fma_f32 v88, -v59, v172, v88
	v_fma_f32 v97, -v62, v173, v97
	v_fma_f32 v88, -v63, v174, v88
	v_fma_f32 v97, -v71, v175, v97
	v_fma_f32 v88, -v74, v176, v88
	v_fma_f32 v97, -v76, v177, v97
	v_fma_f32 v88, -v79, v182, v88
	v_fma_f32 v97, -v82, v183, v97
	v_fma_f32 v88, -v84, v184, v88
	v_fma_f32 v97, -v87, v185, v97
	v_fma_f32 v88, -v90, v186, v88
	v_fma_f32 v97, -v93, v187, v97
	v_fma_f32 v88, -v91, v188, v88
	v_add_f32_e32 v88, v97, v88
	ds_read_b128 v[114:117], v25 offset:11520
	ds_read_b128 v[118:121], v25 offset:11536
	ds_read_b128 v[130:133], v25 offset:11552
	ds_read_b128 v[134:137], v25 offset:11568
	ds_read_b128 v[142:145], v25 offset:11584
	ds_read_b128 v[146:149], v25 offset:11600
	ds_read_b128 v[158:161], v25 offset:11616
	ds_read_b128 v[170:173], v25 offset:11632
	ds_read_b128 v[174:177], v25 offset:11648
	ds_read_b128 v[182:185], v25 offset:11664
	ds_read_b128 v[186:189], v25 offset:11680
	ds_read_b128 v[190:193], v25 offset:11696
	s_waitcnt lgkmcnt(12)
	s_nop 0
	v_mul_f32_e32 v97, v4, v98
	v_fma_f32 v86, v96, v86, -v97
	v_fma_f32 v96, -v5, v99, 0
	v_fma_f32 v86, -v7, v100, v86
	v_fma_f32 v96, -v9, v101, v96
	v_fma_f32 v86, -v11, v102, v86
	v_fma_f32 v96, -v13, v103, v96
	v_fma_f32 v86, -v14, v104, v86
	v_fma_f32 v96, -v15, v105, v96
	v_fma_f32 v86, -v17, v106, v86
	v_fma_f32 v96, -v18, v107, v96
	v_fma_f32 v86, -v19, v108, v86
	v_fma_f32 v96, -v20, v109, v96
	v_fma_f32 v86, -v22, v122, v86
	v_fma_f32 v96, -v24, v123, v96
	v_fma_f32 v86, -v26, v124, v86
	v_fma_f32 v96, -v27, v125, v96
	v_fma_f32 v86, -v30, v126, v86
	v_fma_f32 v96, -v31, v127, v96
	v_fma_f32 v86, -v32, v128, v86
	v_fma_f32 v96, -v34, v129, v96
	v_fma_f32 v86, -v36, v138, v86
	v_fma_f32 v96, -v38, v139, v96
	v_fma_f32 v86, -v40, v140, v86
	v_fma_f32 v96, -v41, v141, v96
	v_lshlrev_b32_e32 v35, 16, v35
	v_fma_f32 v86, -v43, v150, v86
	v_fma_f32 v96, -v49, v151, v96
	v_fma_f32 v86, -v50, v152, v86
	v_fma_f32 v96, -v53, v153, v96
	v_fma_f32 v86, -v54, v154, v86
	v_fma_f32 v96, -v57, v155, v96
	v_fma_f32 v86, -v59, v156, v86
	v_fma_f32 v96, -v62, v157, v96
	v_fma_f32 v86, -v63, v162, v86
	v_fma_f32 v96, -v71, v163, v96
	v_fma_f32 v86, -v74, v164, v86
	v_fma_f32 v96, -v76, v165, v96
	v_fma_f32 v86, -v79, v166, v86
	v_fma_f32 v96, -v82, v167, v96
	v_fma_f32 v86, -v84, v168, v86
	v_fma_f32 v96, -v87, v169, v96
	v_fma_f32 v86, -v90, v178, v86
	v_fma_f32 v96, -v93, v179, v96
	v_fma_f32 v86, -v91, v180, v86
	v_fma_f32 v96, -v88, v181, v96
	v_add_f32_e32 v86, v86, v96
	ds_read_b128 v[96:99], v25 offset:11776
	ds_read_b128 v[100:103], v25 offset:11792
	ds_read_b128 v[104:107], v25 offset:11808
	ds_read_b128 v[108:111], v25 offset:11824
	ds_read_b128 v[122:125], v25 offset:11840
	ds_read_b128 v[126:129], v25 offset:11856
	ds_read_b128 v[138:141], v25 offset:11872
	ds_read_b128 v[150:153], v25 offset:11888
	ds_read_b128 v[154:157], v25 offset:11904
	ds_read_b128 v[162:165], v25 offset:11920
	ds_read_b128 v[166:169], v25 offset:11936
	ds_read_b128 v[178:181], v25 offset:11952
	s_waitcnt lgkmcnt(12)
	s_nop 0
	v_mul_f32_e32 v114, v4, v114
	v_fma_f32 v83, v95, v83, -v114
	v_fma_f32 v95, -v5, v115, 0
	v_fma_f32 v83, -v7, v116, v83
	v_fma_f32 v95, -v9, v117, v95
	v_fma_f32 v83, -v11, v118, v83
	v_fma_f32 v95, -v13, v119, v95
	v_fma_f32 v83, -v14, v120, v83
	v_fma_f32 v95, -v15, v121, v95
	v_fma_f32 v83, -v17, v130, v83
	v_fma_f32 v95, -v18, v131, v95
	v_fma_f32 v83, -v19, v132, v83
	v_fma_f32 v95, -v20, v133, v95
	v_fma_f32 v83, -v22, v134, v83
	v_fma_f32 v95, -v24, v135, v95
	v_fma_f32 v83, -v26, v136, v83
	v_fma_f32 v95, -v27, v137, v95
	v_fma_f32 v83, -v30, v142, v83
	v_fma_f32 v95, -v31, v143, v95
	v_fma_f32 v83, -v32, v144, v83
	v_fma_f32 v95, -v34, v145, v95
	v_fma_f32 v83, -v36, v146, v83
	v_fma_f32 v95, -v38, v147, v95
	v_fma_f32 v83, -v40, v148, v83
	v_fma_f32 v95, -v41, v149, v95
	v_fma_f32 v83, -v43, v158, v83
	v_fma_f32 v95, -v49, v159, v95
	v_fma_f32 v83, -v50, v160, v83
	v_fma_f32 v95, -v53, v161, v95
	v_fma_f32 v83, -v54, v170, v83
	v_fma_f32 v95, -v57, v171, v95
	v_fma_f32 v83, -v59, v172, v83
	v_fma_f32 v95, -v62, v173, v95
	v_fma_f32 v83, -v63, v174, v83
	v_fma_f32 v95, -v71, v175, v95
	v_fma_f32 v83, -v74, v176, v83
	v_fma_f32 v95, -v76, v177, v95
	v_fma_f32 v83, -v79, v182, v83
	v_fma_f32 v95, -v82, v183, v95
	v_fma_f32 v83, -v84, v184, v83
	v_fma_f32 v95, -v87, v185, v95
	v_fma_f32 v83, -v90, v186, v83
	v_fma_f32 v95, -v93, v187, v95
	v_fma_f32 v83, -v91, v188, v83
	v_fma_f32 v95, -v88, v189, v95
	v_fma_f32 v83, -v86, v190, v83
	v_add_f32_e32 v83, v95, v83
	ds_read_b128 v[114:117], v25 offset:12032
	ds_read_b128 v[118:121], v25 offset:12048
	ds_read_b128 v[130:133], v25 offset:12064
	ds_read_b128 v[134:137], v25 offset:12080
	ds_read_b128 v[142:145], v25 offset:12096
	ds_read_b128 v[146:149], v25 offset:12112
	ds_read_b128 v[158:161], v25 offset:12128
	ds_read_b128 v[170:173], v25 offset:12144
	ds_read_b128 v[174:177], v25 offset:12160
	ds_read_b128 v[182:185], v25 offset:12176
	ds_read_b128 v[186:189], v25 offset:12192
	ds_read_b128 v[190:193], v25 offset:12208
	s_waitcnt lgkmcnt(12)
	s_nop 0
	v_mul_f32_e32 v95, v4, v96
	v_fma_f32 v81, v94, v81, -v95
	v_fma_f32 v94, -v5, v97, 0
	v_fma_f32 v81, -v7, v98, v81
	v_fma_f32 v94, -v9, v99, v94
	v_fma_f32 v81, -v11, v100, v81
	v_fma_f32 v94, -v13, v101, v94
	v_fma_f32 v81, -v14, v102, v81
	v_fma_f32 v94, -v15, v103, v94
	v_fma_f32 v81, -v17, v104, v81
	v_fma_f32 v94, -v18, v105, v94
	v_fma_f32 v81, -v19, v106, v81
	v_fma_f32 v94, -v20, v107, v94
	v_fma_f32 v81, -v22, v108, v81
	v_fma_f32 v94, -v24, v109, v94
	v_fma_f32 v81, -v26, v110, v81
	v_fma_f32 v94, -v27, v111, v94
	v_fma_f32 v81, -v30, v122, v81
	v_fma_f32 v94, -v31, v123, v94
	v_fma_f32 v81, -v32, v124, v81
	v_fma_f32 v94, -v34, v125, v94
	v_fma_f32 v81, -v36, v126, v81
	v_fma_f32 v94, -v38, v127, v94
	v_fma_f32 v81, -v40, v128, v81
	v_fma_f32 v94, -v41, v129, v94
	v_fma_f32 v81, -v43, v138, v81
	v_fma_f32 v94, -v49, v139, v94
	v_fma_f32 v81, -v50, v140, v81
	v_fma_f32 v94, -v53, v141, v94
	v_fma_f32 v81, -v54, v150, v81
	v_fma_f32 v94, -v57, v151, v94
	v_fma_f32 v81, -v59, v152, v81
	v_fma_f32 v94, -v62, v153, v94
	v_fma_f32 v81, -v63, v154, v81
	v_fma_f32 v94, -v71, v155, v94
	v_fma_f32 v81, -v74, v156, v81
	v_fma_f32 v94, -v76, v157, v94
	v_fma_f32 v81, -v79, v162, v81
	v_fma_f32 v94, -v82, v163, v94
	v_fma_f32 v81, -v84, v164, v81
	v_fma_f32 v94, -v87, v165, v94
	v_fma_f32 v81, -v90, v166, v81
	v_fma_f32 v94, -v93, v167, v94
	v_fma_f32 v81, -v91, v168, v81
	v_fma_f32 v94, -v88, v169, v94
	v_fma_f32 v81, -v86, v178, v81
	v_fma_f32 v94, -v83, v179, v94
	v_add_f32_e32 v81, v81, v94
	ds_read_b128 v[94:97], v25 offset:12288
	ds_read_b128 v[98:101], v25 offset:12304
	ds_read_b128 v[102:105], v25 offset:12320
	ds_read_b128 v[106:109], v25 offset:12336
	ds_read_b128 v[122:125], v25 offset:12352
	ds_read_b128 v[126:129], v25 offset:12368
	ds_read_b128 v[138:141], v25 offset:12384
	ds_read_b128 v[150:153], v25 offset:12400
	ds_read_b128 v[154:157], v25 offset:12416
	ds_read_b128 v[162:165], v25 offset:12432
	ds_read_b128 v[166:169], v25 offset:12448
	ds_read_b128 v[178:181], v25 offset:12464
	s_waitcnt lgkmcnt(12)
	s_nop 0
	v_mul_f32_e32 v110, v4, v114
	v_fma_f32 v78, v92, v78, -v110
	v_fma_f32 v92, -v5, v115, 0
	v_fma_f32 v78, -v7, v116, v78
	v_fma_f32 v92, -v9, v117, v92
	v_fma_f32 v78, -v11, v118, v78
	v_fma_f32 v92, -v13, v119, v92
	v_fma_f32 v78, -v14, v120, v78
	v_fma_f32 v92, -v15, v121, v92
	v_fma_f32 v78, -v17, v130, v78
	v_fma_f32 v92, -v18, v131, v92
	v_fma_f32 v78, -v19, v132, v78
	v_fma_f32 v92, -v20, v133, v92
	v_fma_f32 v78, -v22, v134, v78
	v_fma_f32 v92, -v24, v135, v92
	v_fma_f32 v78, -v26, v136, v78
	v_fma_f32 v92, -v27, v137, v92
	v_fma_f32 v78, -v30, v142, v78
	v_fma_f32 v92, -v31, v143, v92
	v_fma_f32 v78, -v32, v144, v78
	v_fma_f32 v92, -v34, v145, v92
	v_fma_f32 v78, -v36, v146, v78
	v_fma_f32 v92, -v38, v147, v92
	v_fma_f32 v78, -v40, v148, v78
	v_fma_f32 v92, -v41, v149, v92
	v_fma_f32 v78, -v43, v158, v78
	v_fma_f32 v92, -v49, v159, v92
	v_fma_f32 v78, -v50, v160, v78
	v_fma_f32 v92, -v53, v161, v92
	v_fma_f32 v78, -v54, v170, v78
	v_fma_f32 v92, -v57, v171, v92
	v_fma_f32 v78, -v59, v172, v78
	v_fma_f32 v92, -v62, v173, v92
	v_fma_f32 v78, -v63, v174, v78
	v_fma_f32 v92, -v71, v175, v92
	v_fma_f32 v78, -v74, v176, v78
	v_fma_f32 v92, -v76, v177, v92
	v_fma_f32 v78, -v79, v182, v78
	v_fma_f32 v92, -v82, v183, v92
	v_fma_f32 v78, -v84, v184, v78
	v_fma_f32 v92, -v87, v185, v92
	v_fma_f32 v78, -v90, v186, v78
	v_fma_f32 v92, -v93, v187, v92
	v_fma_f32 v78, -v91, v188, v78
	v_fma_f32 v92, -v88, v189, v92
	v_fma_f32 v78, -v86, v190, v78
	v_fma_f32 v92, -v83, v191, v92
	v_fma_f32 v78, -v81, v192, v78
	v_add_f32_e32 v78, v92, v78
	ds_read_b128 v[114:117], v25 offset:12544
	ds_read_b128 v[118:121], v25 offset:12560
	ds_read_b128 v[130:133], v25 offset:12576
	ds_read_b128 v[134:137], v25 offset:12592
	ds_read_b128 v[142:145], v25 offset:12608
	ds_read_b128 v[146:149], v25 offset:12624
	ds_read_b128 v[158:161], v25 offset:12640
	ds_read_b128 v[170:173], v25 offset:12656
	ds_read_b128 v[174:177], v25 offset:12672
	ds_read_b128 v[182:185], v25 offset:12688
	ds_read_b128 v[186:189], v25 offset:12704
	ds_read_b128 v[190:193], v25 offset:12720
	ds_read_b128 v[206:209], v25 offset:12736
	s_waitcnt lgkmcnt(13)
	s_nop 0
	v_mul_f32_e32 v92, v4, v94
	v_fma_f32 v75, v89, v75, -v92
	v_fma_f32 v89, -v5, v95, 0
	v_fma_f32 v75, -v7, v96, v75
	v_fma_f32 v89, -v9, v97, v89
	v_fma_f32 v75, -v11, v98, v75
	v_fma_f32 v89, -v13, v99, v89
	v_fma_f32 v75, -v14, v100, v75
	v_fma_f32 v89, -v15, v101, v89
	v_fma_f32 v75, -v17, v102, v75
	v_fma_f32 v89, -v18, v103, v89
	v_fma_f32 v75, -v19, v104, v75
	v_fma_f32 v89, -v20, v105, v89
	v_fma_f32 v75, -v22, v106, v75
	v_fma_f32 v89, -v24, v107, v89
	v_fma_f32 v75, -v26, v108, v75
	v_fma_f32 v89, -v27, v109, v89
	v_fma_f32 v75, -v30, v122, v75
	v_fma_f32 v89, -v31, v123, v89
	v_fma_f32 v75, -v32, v124, v75
	v_fma_f32 v89, -v34, v125, v89
	v_fma_f32 v75, -v36, v126, v75
	v_fma_f32 v89, -v38, v127, v89
	v_fma_f32 v75, -v40, v128, v75
	v_fma_f32 v89, -v41, v129, v89
	v_fma_f32 v75, -v43, v138, v75
	v_fma_f32 v89, -v49, v139, v89
	v_fma_f32 v75, -v50, v140, v75
	v_fma_f32 v89, -v53, v141, v89
	v_fma_f32 v75, -v54, v150, v75
	v_fma_f32 v89, -v57, v151, v89
	v_fma_f32 v75, -v59, v152, v75
	v_fma_f32 v89, -v62, v153, v89
	v_fma_f32 v75, -v63, v154, v75
	v_fma_f32 v89, -v71, v155, v89
	v_fma_f32 v75, -v74, v156, v75
	v_fma_f32 v89, -v76, v157, v89
	v_fma_f32 v75, -v79, v162, v75
	v_fma_f32 v89, -v82, v163, v89
	v_fma_f32 v75, -v84, v164, v75
	v_fma_f32 v89, -v87, v165, v89
	v_fma_f32 v75, -v90, v166, v75
	v_fma_f32 v89, -v93, v167, v89
	v_fma_f32 v75, -v91, v168, v75
	v_fma_f32 v89, -v88, v169, v89
	v_fma_f32 v75, -v86, v178, v75
	v_fma_f32 v89, -v83, v179, v89
	v_fma_f32 v75, -v81, v180, v75
	v_fma_f32 v89, -v78, v181, v89
	v_add_f32_e32 v75, v75, v89
	ds_read_b128 v[94:97], v25 offset:12800
	ds_read_b128 v[98:101], v25 offset:12816
	ds_read_b128 v[102:105], v25 offset:12832
	ds_read_b128 v[106:109], v25 offset:12848
	ds_read_b128 v[122:125], v25 offset:12864
	ds_read_b128 v[126:129], v25 offset:12880
	ds_read_b128 v[138:141], v25 offset:12896
	ds_read_b128 v[150:153], v25 offset:12912
	ds_read_b128 v[154:157], v25 offset:12928
	ds_read_b128 v[162:165], v25 offset:12944
	ds_read_b128 v[166:169], v25 offset:12960
	ds_read_b128 v[178:181], v25 offset:12976
	ds_read_b128 v[210:213], v25 offset:12992
	s_waitcnt lgkmcnt(13)
	s_nop 0
	v_mul_f32_e32 v89, v4, v114
	v_fma_f32 v72, v85, v72, -v89
	v_fma_f32 v85, -v5, v115, 0
	v_fma_f32 v72, -v7, v116, v72
	v_fma_f32 v85, -v9, v117, v85
	v_fma_f32 v72, -v11, v118, v72
	v_fma_f32 v85, -v13, v119, v85
	v_fma_f32 v72, -v14, v120, v72
	v_fma_f32 v85, -v15, v121, v85
	v_fma_f32 v72, -v17, v130, v72
	v_fma_f32 v85, -v18, v131, v85
	v_fma_f32 v72, -v19, v132, v72
	v_fma_f32 v85, -v20, v133, v85
	v_fma_f32 v72, -v22, v134, v72
	v_fma_f32 v85, -v24, v135, v85
	v_fma_f32 v72, -v26, v136, v72
	v_fma_f32 v85, -v27, v137, v85
	v_fma_f32 v72, -v30, v142, v72
	v_fma_f32 v85, -v31, v143, v85
	v_fma_f32 v72, -v32, v144, v72
	v_fma_f32 v85, -v34, v145, v85
	v_fma_f32 v72, -v36, v146, v72
	v_fma_f32 v85, -v38, v147, v85
	v_fma_f32 v72, -v40, v148, v72
	v_fma_f32 v85, -v41, v149, v85
	v_fma_f32 v72, -v43, v158, v72
	v_fma_f32 v85, -v49, v159, v85
	v_fma_f32 v72, -v50, v160, v72
	v_fma_f32 v85, -v53, v161, v85
	v_fma_f32 v72, -v54, v170, v72
	v_fma_f32 v85, -v57, v171, v85
	v_fma_f32 v72, -v59, v172, v72
	v_fma_f32 v85, -v62, v173, v85
	v_fma_f32 v72, -v63, v174, v72
	v_fma_f32 v85, -v71, v175, v85
	v_fma_f32 v72, -v74, v176, v72
	v_fma_f32 v85, -v76, v177, v85
	v_fma_f32 v72, -v79, v182, v72
	v_fma_f32 v85, -v82, v183, v85
	v_fma_f32 v72, -v84, v184, v72
	v_fma_f32 v85, -v87, v185, v85
	v_fma_f32 v72, -v90, v186, v72
	v_fma_f32 v85, -v93, v187, v85
	v_fma_f32 v72, -v91, v188, v72
	v_fma_f32 v85, -v88, v189, v85
	v_fma_f32 v72, -v86, v190, v72
	v_fma_f32 v85, -v83, v191, v85
	v_fma_f32 v72, -v81, v192, v72
	v_fma_f32 v85, -v78, v193, v85
	v_fma_f32 v72, -v75, v206, v72
	v_add_f32_e32 v72, v85, v72
	ds_read_b128 v[114:117], v25 offset:13056
	ds_read_b128 v[118:121], v25 offset:13072
	ds_read_b128 v[130:133], v25 offset:13088
	ds_read_b128 v[134:137], v25 offset:13104
	ds_read_b128 v[142:145], v25 offset:13120
	ds_read_b128 v[146:149], v25 offset:13136
	ds_read_b128 v[158:161], v25 offset:13152
	ds_read_b128 v[170:173], v25 offset:13168
	ds_read_b128 v[174:177], v25 offset:13184
	ds_read_b128 v[182:185], v25 offset:13200
	ds_read_b128 v[186:189], v25 offset:13216
	ds_read_b128 v[190:193], v25 offset:13232
	ds_read_b128 v[206:209], v25 offset:13248
	s_waitcnt lgkmcnt(13)
	s_nop 0
	v_mul_f32_e32 v85, v4, v94
	v_fma_f32 v70, v80, v70, -v85
	v_fma_f32 v80, -v5, v95, 0
	v_fma_f32 v70, -v7, v96, v70
	v_fma_f32 v80, -v9, v97, v80
	v_fma_f32 v70, -v11, v98, v70
	v_fma_f32 v80, -v13, v99, v80
	v_fma_f32 v70, -v14, v100, v70
	v_fma_f32 v80, -v15, v101, v80
	v_fma_f32 v70, -v17, v102, v70
	v_fma_f32 v80, -v18, v103, v80
	v_fma_f32 v70, -v19, v104, v70
	v_fma_f32 v80, -v20, v105, v80
	v_fma_f32 v70, -v22, v106, v70
	v_fma_f32 v80, -v24, v107, v80
	v_fma_f32 v70, -v26, v108, v70
	v_fma_f32 v80, -v27, v109, v80
	v_fma_f32 v70, -v30, v122, v70
	v_fma_f32 v80, -v31, v123, v80
	v_fma_f32 v70, -v32, v124, v70
	v_fma_f32 v80, -v34, v125, v80
	v_fma_f32 v70, -v36, v126, v70
	v_fma_f32 v80, -v38, v127, v80
	v_fma_f32 v70, -v40, v128, v70
	v_fma_f32 v80, -v41, v129, v80
	s_nop 0
	v_fma_f32 v70, -v43, v138, v70
	v_fma_f32 v80, -v49, v139, v80
	v_fma_f32 v70, -v50, v140, v70
	v_fma_f32 v80, -v53, v141, v80
	v_fma_f32 v70, -v54, v150, v70
	v_fma_f32 v80, -v57, v151, v80
	v_fma_f32 v70, -v59, v152, v70
	v_fma_f32 v80, -v62, v153, v80
	v_fma_f32 v70, -v63, v154, v70
	v_fma_f32 v80, -v71, v155, v80
	v_fma_f32 v70, -v74, v156, v70
	v_fma_f32 v80, -v76, v157, v80
	v_fma_f32 v70, -v79, v162, v70
	v_fma_f32 v80, -v82, v163, v80
	v_fma_f32 v70, -v84, v164, v70
	v_fma_f32 v80, -v87, v165, v80
	v_fma_f32 v70, -v90, v166, v70
	v_fma_f32 v80, -v93, v167, v80
	v_fma_f32 v70, -v91, v168, v70
	v_fma_f32 v80, -v88, v169, v80
	v_fma_f32 v70, -v86, v178, v70
	v_fma_f32 v80, -v83, v179, v80
	v_fma_f32 v70, -v81, v180, v70
	v_fma_f32 v80, -v78, v181, v80
	v_mul_f32_e32 v12, v12, v2
	v_fma_f32 v70, -v75, v210, v70
	v_fma_f32 v80, -v72, v211, v80
	v_add_f32_e32 v70, v70, v80
	ds_read_b128 v[94:97], v25 offset:13312
	ds_read_b128 v[98:101], v25 offset:13328
	ds_read_b128 v[102:105], v25 offset:13344
	ds_read_b128 v[106:109], v25 offset:13360
	ds_read_b128 v[122:125], v25 offset:13376
	ds_read_b128 v[126:129], v25 offset:13392
	ds_read_b128 v[138:141], v25 offset:13408
	ds_read_b128 v[150:153], v25 offset:13424
	ds_read_b128 v[154:157], v25 offset:13440
	ds_read_b128 v[162:165], v25 offset:13456
	ds_read_b128 v[166:169], v25 offset:13472
	ds_read_b128 v[178:181], v25 offset:13488
	ds_read_b128 v[210:213], v25 offset:13504
	s_waitcnt lgkmcnt(13)
	s_nop 0
	v_mul_f32_e32 v80, v4, v114
	v_fma_f32 v61, v77, v61, -v80
	v_fma_f32 v77, -v5, v115, 0
	v_fma_f32 v61, -v7, v116, v61
	v_fma_f32 v77, -v9, v117, v77
	v_fma_f32 v61, -v11, v118, v61
	v_fma_f32 v77, -v13, v119, v77
	v_fma_f32 v61, -v14, v120, v61
	v_fma_f32 v77, -v15, v121, v77
	v_fma_f32 v61, -v17, v130, v61
	v_fma_f32 v77, -v18, v131, v77
	v_fma_f32 v61, -v19, v132, v61
	v_fma_f32 v77, -v20, v133, v77
	v_fma_f32 v61, -v22, v134, v61
	v_fma_f32 v77, -v24, v135, v77
	v_fma_f32 v61, -v26, v136, v61
	v_fma_f32 v77, -v27, v137, v77
	v_fma_f32 v61, -v30, v142, v61
	v_fma_f32 v77, -v31, v143, v77
	v_fma_f32 v61, -v32, v144, v61
	v_fma_f32 v77, -v34, v145, v77
	v_fma_f32 v61, -v36, v146, v61
	v_fma_f32 v77, -v38, v147, v77
	v_fma_f32 v61, -v40, v148, v61
	v_fma_f32 v77, -v41, v149, v77
	v_fma_f32 v61, -v43, v158, v61
	v_fma_f32 v77, -v49, v159, v77
	v_fma_f32 v61, -v50, v160, v61
	v_fma_f32 v77, -v53, v161, v77
	v_fma_f32 v61, -v54, v170, v61
	v_fma_f32 v77, -v57, v171, v77
	v_fma_f32 v61, -v59, v172, v61
	v_fma_f32 v77, -v62, v173, v77
	v_fma_f32 v61, -v63, v174, v61
	v_fma_f32 v77, -v71, v175, v77
	v_fma_f32 v61, -v74, v176, v61
	v_fma_f32 v77, -v76, v177, v77
	v_fma_f32 v61, -v79, v182, v61
	v_fma_f32 v77, -v82, v183, v77
	v_fma_f32 v61, -v84, v184, v61
	v_fma_f32 v77, -v87, v185, v77
	v_fma_f32 v61, -v90, v186, v61
	v_fma_f32 v77, -v93, v187, v77
	v_fma_f32 v61, -v91, v188, v61
	v_fma_f32 v77, -v88, v189, v77
	v_fma_f32 v61, -v86, v190, v61
	v_fma_f32 v77, -v83, v191, v77
	v_fma_f32 v61, -v81, v192, v61
	v_fma_f32 v77, -v78, v193, v77
	v_fma_f32 v61, -v75, v206, v61
	v_fma_f32 v77, -v72, v207, v77
	v_fma_f32 v61, -v70, v208, v61
	v_add_f32_e32 v61, v77, v61
	ds_read_b128 v[114:117], v25 offset:13568
	ds_read_b128 v[118:121], v25 offset:13584
	ds_read_b128 v[130:133], v25 offset:13600
	ds_read_b128 v[134:137], v25 offset:13616
	ds_read_b128 v[142:145], v25 offset:13632
	ds_read_b128 v[146:149], v25 offset:13648
	ds_read_b128 v[158:161], v25 offset:13664
	ds_read_b128 v[170:173], v25 offset:13680
	ds_read_b128 v[174:177], v25 offset:13696
	ds_read_b128 v[182:185], v25 offset:13712
	ds_read_b128 v[186:189], v25 offset:13728
	ds_read_b128 v[190:193], v25 offset:13744
	ds_read_b128 v[206:209], v25 offset:13760
	ds_read_b128 v[216:219], v25 offset:13776
	s_waitcnt lgkmcnt(14)
	s_nop 0
	v_mul_f32_e32 v77, v4, v94
	v_fma_f32 v58, v73, v58, -v77
	v_fma_f32 v73, -v5, v95, 0
	v_fma_f32 v58, -v7, v96, v58
	v_fma_f32 v73, -v9, v97, v73
	v_fma_f32 v58, -v11, v98, v58
	v_fma_f32 v73, -v13, v99, v73
	v_fma_f32 v58, -v14, v100, v58
	v_fma_f32 v73, -v15, v101, v73
	v_fma_f32 v58, -v17, v102, v58
	v_fma_f32 v73, -v18, v103, v73
	v_fma_f32 v58, -v19, v104, v58
	v_fma_f32 v73, -v20, v105, v73
	v_fma_f32 v58, -v22, v106, v58
	v_fma_f32 v73, -v24, v107, v73
	v_fma_f32 v58, -v26, v108, v58
	v_fma_f32 v73, -v27, v109, v73
	v_fma_f32 v58, -v30, v122, v58
	v_fma_f32 v73, -v31, v123, v73
	v_fma_f32 v58, -v32, v124, v58
	v_fma_f32 v73, -v34, v125, v73
	v_fma_f32 v58, -v36, v126, v58
	v_fma_f32 v73, -v38, v127, v73
	v_fma_f32 v58, -v40, v128, v58
	v_fma_f32 v73, -v41, v129, v73
	s_nop 0
	v_fma_f32 v58, -v43, v138, v58
	v_fma_f32 v73, -v49, v139, v73
	v_fma_f32 v58, -v50, v140, v58
	v_fma_f32 v73, -v53, v141, v73
	v_fma_f32 v58, -v54, v150, v58
	v_fma_f32 v73, -v57, v151, v73
	v_fma_f32 v58, -v59, v152, v58
	v_fma_f32 v73, -v62, v153, v73
	v_fma_f32 v58, -v63, v154, v58
	v_fma_f32 v73, -v71, v155, v73
	v_fma_f32 v58, -v74, v156, v58
	v_fma_f32 v73, -v76, v157, v73
	v_fma_f32 v58, -v79, v162, v58
	v_fma_f32 v73, -v82, v163, v73
	v_fma_f32 v58, -v84, v164, v58
	v_fma_f32 v73, -v87, v165, v73
	v_fma_f32 v58, -v90, v166, v58
	v_fma_f32 v73, -v93, v167, v73
	v_fma_f32 v58, -v91, v168, v58
	v_fma_f32 v73, -v88, v169, v73
	v_fma_f32 v58, -v86, v178, v58
	v_fma_f32 v73, -v83, v179, v73
	v_fma_f32 v58, -v81, v180, v58
	v_fma_f32 v73, -v78, v181, v73
	v_lshlrev_b32_e32 v2, 16, v223
	v_fma_f32 v58, -v75, v210, v58
	v_fma_f32 v73, -v72, v211, v73
	v_fma_f32 v58, -v70, v212, v58
	v_fma_f32 v73, -v61, v213, v73
	v_mul_f32_e32 v21, v222, v21
	v_mul_f32_e32 v29, v221, v29
	v_mul_f32_e32 v35, v220, v35
	v_add_f32_e32 v58, v58, v73
	ds_read_b128 v[94:97], v25 offset:13824
	ds_read_b128 v[98:101], v25 offset:13840
	ds_read_b128 v[102:105], v25 offset:13856
	ds_read_b128 v[106:109], v25 offset:13872
	ds_read_b128 v[122:125], v25 offset:13888
	ds_read_b128 v[126:129], v25 offset:13904
	ds_read_b128 v[138:141], v25 offset:13920
	ds_read_b128 v[150:153], v25 offset:13936
	ds_read_b128 v[154:157], v25 offset:13952
	ds_read_b128 v[162:165], v25 offset:13968
	ds_read_b128 v[166:169], v25 offset:13984
	ds_read_b128 v[178:181], v25 offset:14000
	ds_read_b128 v[210:213], v25 offset:14016
	ds_read_b128 v[220:223], v25 offset:14032
	s_waitcnt lgkmcnt(14)
	s_nop 0
	v_mul_f32_e32 v73, v4, v114
	v_fma_f32 v55, v69, v55, -v73
	v_fma_f32 v69, -v5, v115, 0
	v_fma_f32 v55, -v7, v116, v55
	v_fma_f32 v69, -v9, v117, v69
	v_fma_f32 v55, -v11, v118, v55
	v_fma_f32 v69, -v13, v119, v69
	v_fma_f32 v55, -v14, v120, v55
	v_fma_f32 v69, -v15, v121, v69
	v_fma_f32 v55, -v17, v130, v55
	v_fma_f32 v69, -v18, v131, v69
	v_fma_f32 v55, -v19, v132, v55
	v_fma_f32 v69, -v20, v133, v69
	v_fma_f32 v55, -v22, v134, v55
	v_fma_f32 v69, -v24, v135, v69
	v_fma_f32 v55, -v26, v136, v55
	v_fma_f32 v69, -v27, v137, v69
	v_fma_f32 v55, -v30, v142, v55
	v_fma_f32 v69, -v31, v143, v69
	v_fma_f32 v55, -v32, v144, v55
	v_fma_f32 v69, -v34, v145, v69
	v_fma_f32 v55, -v36, v146, v55
	v_fma_f32 v69, -v38, v147, v69
	v_fma_f32 v55, -v40, v148, v55
	v_fma_f32 v69, -v41, v149, v69
	v_fma_f32 v55, -v43, v158, v55
	v_fma_f32 v69, -v49, v159, v69
	v_fma_f32 v55, -v50, v160, v55
	v_fma_f32 v69, -v53, v161, v69
	v_fma_f32 v55, -v54, v170, v55
	v_fma_f32 v69, -v57, v171, v69
	v_fma_f32 v55, -v59, v172, v55
	v_fma_f32 v69, -v62, v173, v69
	v_fma_f32 v55, -v63, v174, v55
	v_fma_f32 v69, -v71, v175, v69
	v_fma_f32 v55, -v74, v176, v55
	v_fma_f32 v69, -v76, v177, v69
	v_fma_f32 v55, -v79, v182, v55
	v_fma_f32 v69, -v82, v183, v69
	v_fma_f32 v55, -v84, v184, v55
	v_fma_f32 v69, -v87, v185, v69
	v_fma_f32 v55, -v90, v186, v55
	v_fma_f32 v69, -v93, v187, v69
	v_fma_f32 v55, -v91, v188, v55
	v_fma_f32 v69, -v88, v189, v69
	v_fma_f32 v55, -v86, v190, v55
	v_fma_f32 v69, -v83, v191, v69
	v_fma_f32 v55, -v81, v192, v55
	v_fma_f32 v69, -v78, v193, v69
	v_fma_f32 v55, -v75, v206, v55
	v_fma_f32 v69, -v72, v207, v69
	v_fma_f32 v55, -v70, v208, v55
	v_lshlrev_b32_e32 v60, 16, v60
	v_fma_f32 v69, -v61, v209, v69
	v_fma_f32 v55, -v58, v216, v55
	v_mul_f32_e32 v60, v215, v60
	v_add_f32_e32 v55, v69, v55
	ds_read_b128 v[114:117], v25 offset:14080
	ds_read_b128 v[118:121], v25 offset:14096
	ds_read_b128 v[130:133], v25 offset:14112
	ds_read_b128 v[134:137], v25 offset:14128
	ds_read_b128 v[142:145], v25 offset:14144
	ds_read_b128 v[146:149], v25 offset:14160
	ds_read_b128 v[158:161], v25 offset:14176
	ds_read_b128 v[170:173], v25 offset:14192
	ds_read_b128 v[174:177], v25 offset:14208
	ds_read_b128 v[182:185], v25 offset:14224
	ds_read_b128 v[186:189], v25 offset:14240
	ds_read_b128 v[190:193], v25 offset:14256
	ds_read_b128 v[206:209], v25 offset:14272
	ds_read_b128 v[216:219], v25 offset:14288
	s_waitcnt lgkmcnt(14)
	s_nop 0
	v_mul_f32_e32 v69, v4, v94
	v_fma_f32 v52, v60, v52, -v69
	v_fma_f32 v60, -v5, v95, 0
	v_fma_f32 v52, -v7, v96, v52
	v_fma_f32 v60, -v9, v97, v60
	v_fma_f32 v52, -v11, v98, v52
	v_fma_f32 v60, -v13, v99, v60
	v_fma_f32 v52, -v14, v100, v52
	v_fma_f32 v60, -v15, v101, v60
	v_fma_f32 v52, -v17, v102, v52
	v_fma_f32 v60, -v18, v103, v60
	v_fma_f32 v52, -v19, v104, v52
	v_fma_f32 v60, -v20, v105, v60
	v_fma_f32 v52, -v22, v106, v52
	v_fma_f32 v60, -v24, v107, v60
	v_fma_f32 v52, -v26, v108, v52
	v_fma_f32 v60, -v27, v109, v60
	v_fma_f32 v52, -v30, v122, v52
	v_fma_f32 v60, -v31, v123, v60
	v_fma_f32 v52, -v32, v124, v52
	v_fma_f32 v60, -v34, v125, v60
	v_fma_f32 v52, -v36, v126, v52
	v_fma_f32 v60, -v38, v127, v60
	v_fma_f32 v52, -v40, v128, v52
	v_fma_f32 v60, -v41, v129, v60
	s_nop 0
	v_fma_f32 v52, -v43, v138, v52
	v_fma_f32 v60, -v49, v139, v60
	v_fma_f32 v52, -v50, v140, v52
	v_fma_f32 v60, -v53, v141, v60
	v_fma_f32 v52, -v54, v150, v52
	v_fma_f32 v60, -v57, v151, v60
	v_fma_f32 v52, -v59, v152, v52
	v_fma_f32 v60, -v62, v153, v60
	v_fma_f32 v52, -v63, v154, v52
	v_fma_f32 v60, -v71, v155, v60
	v_fma_f32 v52, -v74, v156, v52
	v_fma_f32 v60, -v76, v157, v60
	v_fma_f32 v52, -v79, v162, v52
	v_fma_f32 v60, -v82, v163, v60
	v_fma_f32 v52, -v84, v164, v52
	v_fma_f32 v60, -v87, v165, v60
	v_fma_f32 v52, -v90, v166, v52
	v_fma_f32 v60, -v93, v167, v60
	v_fma_f32 v52, -v91, v168, v52
	v_fma_f32 v60, -v88, v169, v60
	v_fma_f32 v52, -v86, v178, v52
	v_fma_f32 v60, -v83, v179, v60
	v_fma_f32 v52, -v81, v180, v52
	v_fma_f32 v60, -v78, v181, v60
	v_mul_f32_e32 v2, v224, v2
	v_fma_f32 v52, -v75, v210, v52
	v_fma_f32 v60, -v72, v211, v60
	v_fma_f32 v52, -v70, v212, v52
	v_fma_f32 v60, -v61, v213, v60
	v_fma_f32 v52, -v58, v220, v52
	v_fma_f32 v60, -v55, v221, v60
	v_add_f32_e32 v52, v52, v60
	ds_read_b128 v[94:97], v25 offset:14336
	ds_read_b128 v[98:101], v25 offset:14352
	ds_read_b128 v[102:105], v25 offset:14368
	ds_read_b128 v[106:109], v25 offset:14384
	ds_read_b128 v[122:125], v25 offset:14400
	ds_read_b128 v[126:129], v25 offset:14416
	ds_read_b128 v[138:141], v25 offset:14432
	ds_read_b128 v[150:153], v25 offset:14448
	ds_read_b128 v[154:157], v25 offset:14464
	ds_read_b128 v[162:165], v25 offset:14480
	ds_read_b128 v[166:169], v25 offset:14496
	ds_read_b128 v[178:181], v25 offset:14512
	ds_read_b128 v[210:213], v25 offset:14528
	ds_read_b128 v[220:223], v25 offset:14544
	s_waitcnt lgkmcnt(14)
	s_nop 0
	v_mul_f32_e32 v60, v4, v114
	v_fma_f32 v48, v56, v48, -v60
	v_fma_f32 v56, -v5, v115, 0
	v_fma_f32 v48, -v7, v116, v48
	v_fma_f32 v56, -v9, v117, v56
	v_fma_f32 v48, -v11, v118, v48
	v_fma_f32 v56, -v13, v119, v56
	v_fma_f32 v48, -v14, v120, v48
	v_fma_f32 v56, -v15, v121, v56
	v_fma_f32 v48, -v17, v130, v48
	v_fma_f32 v56, -v18, v131, v56
	v_fma_f32 v48, -v19, v132, v48
	v_fma_f32 v56, -v20, v133, v56
	v_fma_f32 v48, -v22, v134, v48
	v_fma_f32 v56, -v24, v135, v56
	v_fma_f32 v48, -v26, v136, v48
	v_fma_f32 v56, -v27, v137, v56
	v_fma_f32 v48, -v30, v142, v48
	v_fma_f32 v56, -v31, v143, v56
	v_fma_f32 v48, -v32, v144, v48
	v_fma_f32 v56, -v34, v145, v56
	v_fma_f32 v48, -v36, v146, v48
	v_fma_f32 v56, -v38, v147, v56
	v_fma_f32 v48, -v40, v148, v48
	v_fma_f32 v56, -v41, v149, v56
	v_fma_f32 v48, -v43, v158, v48
	v_fma_f32 v56, -v49, v159, v56
	v_fma_f32 v48, -v50, v160, v48
	v_fma_f32 v56, -v53, v161, v56
	v_fma_f32 v48, -v54, v170, v48
	v_fma_f32 v56, -v57, v171, v56
	v_fma_f32 v48, -v59, v172, v48
	v_fma_f32 v56, -v62, v173, v56
	v_fma_f32 v48, -v63, v174, v48
	v_fma_f32 v56, -v71, v175, v56
	v_fma_f32 v48, -v74, v176, v48
	v_fma_f32 v56, -v76, v177, v56
	v_fma_f32 v48, -v79, v182, v48
	v_fma_f32 v56, -v82, v183, v56
	v_fma_f32 v48, -v84, v184, v48
	v_fma_f32 v56, -v87, v185, v56
	v_fma_f32 v48, -v90, v186, v48
	v_fma_f32 v56, -v93, v187, v56
	v_fma_f32 v48, -v91, v188, v48
	v_fma_f32 v56, -v88, v189, v56
	v_fma_f32 v48, -v86, v190, v48
	v_fma_f32 v56, -v83, v191, v56
	v_fma_f32 v48, -v81, v192, v48
	v_fma_f32 v56, -v78, v193, v56
	v_fma_f32 v48, -v75, v206, v48
	v_fma_f32 v56, -v72, v207, v56
	v_fma_f32 v48, -v70, v208, v48
	v_fma_f32 v56, -v61, v209, v56
	v_fma_f32 v48, -v58, v216, v48
	v_fma_f32 v56, -v55, v217, v56
	v_fma_f32 v48, -v52, v218, v48
	v_add_f32_e32 v48, v56, v48
	ds_read_b128 v[114:117], v25 offset:14592
	ds_read_b128 v[118:121], v25 offset:14608
	ds_read_b128 v[130:133], v25 offset:14624
	ds_read_b128 v[134:137], v25 offset:14640
	ds_read_b128 v[142:145], v25 offset:14656
	ds_read_b128 v[146:149], v25 offset:14672
	ds_read_b128 v[158:161], v25 offset:14688
	ds_read_b128 v[170:173], v25 offset:14704
	ds_read_b128 v[174:177], v25 offset:14720
	ds_read_b128 v[182:185], v25 offset:14736
	ds_read_b128 v[186:189], v25 offset:14752
	ds_read_b128 v[190:193], v25 offset:14768
	ds_read_b128 v[206:209], v25 offset:14784
	ds_read_b128 v[216:219], v25 offset:14800
	ds_read_b128 v[224:227], v25 offset:14816
	s_waitcnt lgkmcnt(14)
	s_nop 0
	v_mul_f32_e32 v56, v4, v94
	v_fma_f32 v42, v51, v42, -v56
	v_fma_f32 v51, -v5, v95, 0
	v_fma_f32 v42, -v7, v96, v42
	v_fma_f32 v51, -v9, v97, v51
	v_fma_f32 v42, -v11, v98, v42
	v_fma_f32 v51, -v13, v99, v51
	v_fma_f32 v42, -v14, v100, v42
	v_fma_f32 v51, -v15, v101, v51
	v_fma_f32 v42, -v17, v102, v42
	v_fma_f32 v51, -v18, v103, v51
	v_fma_f32 v42, -v19, v104, v42
	v_fma_f32 v51, -v20, v105, v51
	v_fma_f32 v42, -v22, v106, v42
	v_fma_f32 v51, -v24, v107, v51
	v_fma_f32 v42, -v26, v108, v42
	v_fma_f32 v51, -v27, v109, v51
	v_fma_f32 v42, -v30, v122, v42
	v_fma_f32 v51, -v31, v123, v51
	v_fma_f32 v42, -v32, v124, v42
	v_fma_f32 v51, -v34, v125, v51
	v_fma_f32 v42, -v36, v126, v42
	v_fma_f32 v51, -v38, v127, v51
	v_fma_f32 v42, -v40, v128, v42
	v_fma_f32 v51, -v41, v129, v51
	s_nop 0
	v_fma_f32 v42, -v43, v138, v42
	v_fma_f32 v51, -v49, v139, v51
	v_fma_f32 v42, -v50, v140, v42
	v_fma_f32 v51, -v53, v141, v51
	v_fma_f32 v42, -v54, v150, v42
	v_fma_f32 v51, -v57, v151, v51
	v_fma_f32 v42, -v59, v152, v42
	v_fma_f32 v51, -v62, v153, v51
	v_fma_f32 v42, -v63, v154, v42
	v_fma_f32 v51, -v71, v155, v51
	v_fma_f32 v42, -v74, v156, v42
	v_fma_f32 v51, -v76, v157, v51
	v_fma_f32 v42, -v79, v162, v42
	v_fma_f32 v51, -v82, v163, v51
	v_fma_f32 v42, -v84, v164, v42
	v_fma_f32 v51, -v87, v165, v51
	v_fma_f32 v42, -v90, v166, v42
	v_fma_f32 v51, -v93, v167, v51
	v_fma_f32 v42, -v91, v168, v42
	v_fma_f32 v51, -v88, v169, v51
	v_fma_f32 v42, -v86, v178, v42
	v_fma_f32 v51, -v83, v179, v51
	v_fma_f32 v42, -v81, v180, v42
	v_fma_f32 v51, -v78, v181, v51
	s_add_u32 s6, s40, 0x8000
	v_fma_f32 v42, -v75, v210, v42
	v_fma_f32 v51, -v72, v211, v51
	v_fma_f32 v42, -v70, v212, v42
	v_fma_f32 v51, -v61, v213, v51
	v_fma_f32 v42, -v58, v220, v42
	v_fma_f32 v51, -v55, v221, v51
	v_fma_f32 v42, -v52, v222, v42
	v_fma_f32 v51, -v48, v223, v51
	v_add_f32_e32 v42, v42, v51
	ds_read_b128 v[94:97], v25 offset:14848
	ds_read_b128 v[98:101], v25 offset:14864
	ds_read_b128 v[102:105], v25 offset:14880
	ds_read_b128 v[106:109], v25 offset:14896
	ds_read_b128 v[122:125], v25 offset:14912
	ds_read_b128 v[126:129], v25 offset:14928
	ds_read_b128 v[138:141], v25 offset:14944
	ds_read_b128 v[150:153], v25 offset:14960
	ds_read_b128 v[154:157], v25 offset:14976
	ds_read_b128 v[162:165], v25 offset:14992
	ds_read_b128 v[166:169], v25 offset:15008
	ds_read_b128 v[178:181], v25 offset:15024
	ds_read_b128 v[210:213], v25 offset:15040
	ds_read_b128 v[220:223], v25 offset:15056
	ds_read_b128 v[228:231], v25 offset:15072
	s_waitcnt lgkmcnt(14)
	v_mul_f32_e32 v51, v4, v114
	v_fma_f32 v37, v47, v37, -v51
	v_fma_f32 v47, -v5, v115, 0
	v_fma_f32 v37, -v7, v116, v37
	v_fma_f32 v47, -v9, v117, v47
	v_fma_f32 v37, -v11, v118, v37
	v_fma_f32 v47, -v13, v119, v47
	v_fma_f32 v37, -v14, v120, v37
	v_fma_f32 v47, -v15, v121, v47
	v_fma_f32 v37, -v17, v130, v37
	v_fma_f32 v47, -v18, v131, v47
	v_fma_f32 v37, -v19, v132, v37
	v_fma_f32 v47, -v20, v133, v47
	v_fma_f32 v37, -v22, v134, v37
	v_fma_f32 v47, -v24, v135, v47
	v_fma_f32 v37, -v26, v136, v37
	v_fma_f32 v47, -v27, v137, v47
	v_fma_f32 v37, -v30, v142, v37
	v_fma_f32 v47, -v31, v143, v47
	v_fma_f32 v37, -v32, v144, v37
	v_fma_f32 v47, -v34, v145, v47
	v_fma_f32 v37, -v36, v146, v37
	v_fma_f32 v47, -v38, v147, v47
	v_fma_f32 v37, -v40, v148, v37
	v_fma_f32 v47, -v41, v149, v47
	v_fma_f32 v37, -v43, v158, v37
	v_fma_f32 v47, -v49, v159, v47
	v_fma_f32 v37, -v50, v160, v37
	v_fma_f32 v47, -v53, v161, v47
	v_fma_f32 v37, -v54, v170, v37
	v_fma_f32 v47, -v57, v171, v47
	v_fma_f32 v37, -v59, v172, v37
	v_fma_f32 v47, -v62, v173, v47
	v_fma_f32 v37, -v63, v174, v37
	v_fma_f32 v47, -v71, v175, v47
	v_fma_f32 v37, -v74, v176, v37
	v_fma_f32 v47, -v76, v177, v47
	v_fma_f32 v37, -v79, v182, v37
	v_fma_f32 v47, -v82, v183, v47
	v_fma_f32 v37, -v84, v184, v37
	v_fma_f32 v47, -v87, v185, v47
	v_fma_f32 v37, -v90, v186, v37
	v_fma_f32 v47, -v93, v187, v47
	v_fma_f32 v37, -v91, v188, v37
	v_fma_f32 v47, -v88, v189, v47
	v_fma_f32 v37, -v86, v190, v37
	v_fma_f32 v47, -v83, v191, v47
	v_fma_f32 v37, -v81, v192, v37
	v_fma_f32 v47, -v78, v193, v47
	v_fma_f32 v37, -v75, v206, v37
	v_fma_f32 v47, -v72, v207, v47
	v_fma_f32 v37, -v70, v208, v37
	v_fma_f32 v47, -v61, v209, v47
	v_fma_f32 v37, -v58, v216, v37
	v_fma_f32 v47, -v55, v217, v47
	v_fma_f32 v37, -v52, v218, v37
	v_fma_f32 v47, -v48, v219, v47
	v_fma_f32 v37, -v42, v224, v37
	v_add_f32_e32 v37, v47, v37
	ds_read_b128 v[114:117], v25 offset:15104
	ds_read_b128 v[118:121], v25 offset:15120
	ds_read_b128 v[130:133], v25 offset:15136
	ds_read_b128 v[134:137], v25 offset:15152
	ds_read_b128 v[142:145], v25 offset:15168
	ds_read_b128 v[146:149], v25 offset:15184
	ds_read_b128 v[158:161], v25 offset:15200
	ds_read_b128 v[170:173], v25 offset:15216
	ds_read_b128 v[174:177], v25 offset:15232
	ds_read_b128 v[182:185], v25 offset:15248
	ds_read_b128 v[186:189], v25 offset:15264
	ds_read_b128 v[190:193], v25 offset:15280
	ds_read_b128 v[206:209], v25 offset:15296
	ds_read_b128 v[216:219], v25 offset:15312
	ds_read_b128 v[224:227], v25 offset:15328
	s_waitcnt lgkmcnt(14)
	v_mul_f32_e32 v47, v4, v94
	v_fma_f32 v33, v39, v33, -v47
	v_fma_f32 v39, -v5, v95, 0
	v_fma_f32 v33, -v7, v96, v33
	v_fma_f32 v39, -v9, v97, v39
	v_fma_f32 v33, -v11, v98, v33
	v_fma_f32 v39, -v13, v99, v39
	v_fma_f32 v33, -v14, v100, v33
	v_fma_f32 v39, -v15, v101, v39
	v_fma_f32 v33, -v17, v102, v33
	v_fma_f32 v39, -v18, v103, v39
	v_fma_f32 v33, -v19, v104, v33
	v_fma_f32 v39, -v20, v105, v39
	v_fma_f32 v33, -v22, v106, v33
	v_fma_f32 v39, -v24, v107, v39
	v_fma_f32 v33, -v26, v108, v33
	v_fma_f32 v39, -v27, v109, v39
	v_fma_f32 v33, -v30, v122, v33
	v_fma_f32 v39, -v31, v123, v39
	v_fma_f32 v33, -v32, v124, v33
	v_fma_f32 v39, -v34, v125, v39
	v_fma_f32 v33, -v36, v126, v33
	v_fma_f32 v39, -v38, v127, v39
	v_fma_f32 v33, -v40, v128, v33
	v_fma_f32 v39, -v41, v129, v39
	s_nop 0
	v_fma_f32 v33, -v43, v138, v33
	v_fma_f32 v39, -v49, v139, v39
	v_fma_f32 v33, -v50, v140, v33
	v_fma_f32 v39, -v53, v141, v39
	v_fma_f32 v33, -v54, v150, v33
	v_fma_f32 v39, -v57, v151, v39
	v_fma_f32 v33, -v59, v152, v33
	v_fma_f32 v39, -v62, v153, v39
	v_fma_f32 v33, -v63, v154, v33
	v_fma_f32 v39, -v71, v155, v39
	v_fma_f32 v33, -v74, v156, v33
	v_fma_f32 v39, -v76, v157, v39
	v_fma_f32 v33, -v79, v162, v33
	v_fma_f32 v39, -v82, v163, v39
	v_fma_f32 v33, -v84, v164, v33
	v_fma_f32 v39, -v87, v165, v39
	v_fma_f32 v33, -v90, v166, v33
	v_fma_f32 v39, -v93, v167, v39
	v_fma_f32 v33, -v91, v168, v33
	v_fma_f32 v39, -v88, v169, v39
	v_fma_f32 v33, -v86, v178, v33
	v_fma_f32 v39, -v83, v179, v39
	v_fma_f32 v33, -v81, v180, v33
	v_fma_f32 v39, -v78, v181, v39
	s_addc_u32 s7, s41, 0
	v_fma_f32 v33, -v75, v210, v33
	v_fma_f32 v39, -v72, v211, v39
	v_fma_f32 v33, -v70, v212, v33
	v_fma_f32 v39, -v61, v213, v39
	v_fma_f32 v33, -v58, v220, v33
	v_fma_f32 v39, -v55, v221, v39
	v_fma_f32 v33, -v52, v222, v33
	v_fma_f32 v39, -v48, v223, v39
	v_fma_f32 v33, -v42, v228, v33
	v_fma_f32 v39, -v37, v229, v39
	v_add_f32_e32 v33, v33, v39
	ds_read_b128 v[94:97], v25 offset:15360
	ds_read_b128 v[98:101], v25 offset:15376
	ds_read_b128 v[102:105], v25 offset:15392
	ds_read_b128 v[106:109], v25 offset:15408
	ds_read_b128 v[122:125], v25 offset:15424
	ds_read_b128 v[126:129], v25 offset:15440
	ds_read_b128 v[138:141], v25 offset:15456
	ds_read_b128 v[150:153], v25 offset:15472
	ds_read_b128 v[154:157], v25 offset:15488
	ds_read_b128 v[162:165], v25 offset:15504
	ds_read_b128 v[166:169], v25 offset:15520
	ds_read_b128 v[178:181], v25 offset:15536
	ds_read_b128 v[210:213], v25 offset:15552
	ds_read_b128 v[220:223], v25 offset:15568
	ds_read_b128 v[228:231], v25 offset:15584
	s_waitcnt lgkmcnt(14)
	v_mul_f32_e32 v39, v4, v114
	v_fma_f32 v28, v35, v28, -v39
	v_fma_f32 v35, -v5, v115, 0
	v_fma_f32 v28, -v7, v116, v28
	v_fma_f32 v35, -v9, v117, v35
	v_fma_f32 v28, -v11, v118, v28
	v_fma_f32 v35, -v13, v119, v35
	v_fma_f32 v28, -v14, v120, v28
	v_fma_f32 v35, -v15, v121, v35
	v_fma_f32 v28, -v17, v130, v28
	v_fma_f32 v35, -v18, v131, v35
	v_fma_f32 v28, -v19, v132, v28
	v_fma_f32 v35, -v20, v133, v35
	v_fma_f32 v28, -v22, v134, v28
	v_fma_f32 v35, -v24, v135, v35
	v_fma_f32 v28, -v26, v136, v28
	v_fma_f32 v35, -v27, v137, v35
	v_fma_f32 v28, -v30, v142, v28
	v_fma_f32 v35, -v31, v143, v35
	v_fma_f32 v28, -v32, v144, v28
	v_fma_f32 v35, -v34, v145, v35
	v_fma_f32 v28, -v36, v146, v28
	v_fma_f32 v35, -v38, v147, v35
	v_fma_f32 v28, -v40, v148, v28
	v_fma_f32 v35, -v41, v149, v35
	v_fma_f32 v28, -v43, v158, v28
	v_fma_f32 v35, -v49, v159, v35
	v_fma_f32 v28, -v50, v160, v28
	v_fma_f32 v35, -v53, v161, v35
	v_fma_f32 v28, -v54, v170, v28
	v_fma_f32 v35, -v57, v171, v35
	v_fma_f32 v28, -v59, v172, v28
	v_fma_f32 v35, -v62, v173, v35
	v_fma_f32 v28, -v63, v174, v28
	v_fma_f32 v35, -v71, v175, v35
	v_fma_f32 v28, -v74, v176, v28
	v_fma_f32 v35, -v76, v177, v35
	v_fma_f32 v28, -v79, v182, v28
	v_fma_f32 v35, -v82, v183, v35
	v_fma_f32 v28, -v84, v184, v28
	v_fma_f32 v35, -v87, v185, v35
	v_fma_f32 v28, -v90, v186, v28
	v_fma_f32 v35, -v93, v187, v35
	v_fma_f32 v28, -v91, v188, v28
	v_fma_f32 v35, -v88, v189, v35
	v_fma_f32 v28, -v86, v190, v28
	v_fma_f32 v35, -v83, v191, v35
	v_fma_f32 v28, -v81, v192, v28
	v_fma_f32 v35, -v78, v193, v35
	v_fma_f32 v28, -v75, v206, v28
	v_fma_f32 v35, -v72, v207, v35
	v_fma_f32 v28, -v70, v208, v28
	v_fma_f32 v35, -v61, v209, v35
	v_fma_f32 v28, -v58, v216, v28
	v_fma_f32 v35, -v55, v217, v35
	v_fma_f32 v28, -v52, v218, v28
	v_fma_f32 v35, -v48, v219, v35
	v_fma_f32 v28, -v42, v224, v28
	v_fma_f32 v35, -v37, v225, v35
	v_fma_f32 v28, -v33, v226, v28
	v_add_f32_e32 v28, v35, v28
	ds_read_b128 v[114:117], v25 offset:15616
	ds_read_b128 v[118:121], v25 offset:15632
	ds_read_b128 v[130:133], v25 offset:15648
	ds_read_b128 v[134:137], v25 offset:15664
	ds_read_b128 v[142:145], v25 offset:15680
	ds_read_b128 v[146:149], v25 offset:15696
	ds_read_b128 v[158:161], v25 offset:15712
	ds_read_b128 v[170:173], v25 offset:15728
	ds_read_b128 v[174:177], v25 offset:15744
	ds_read_b128 v[182:185], v25 offset:15760
	ds_read_b128 v[186:189], v25 offset:15776
	ds_read_b128 v[190:193], v25 offset:15792
	ds_read_b128 v[206:209], v25 offset:15808
	ds_read_b128 v[216:219], v25 offset:15824
	ds_read_b128 v[224:227], v25 offset:15840
	ds_read_b128 v[232:235], v25 offset:15856
	s_waitcnt lgkmcnt(14)
	v_mul_f32_e32 v35, v4, v94
	v_fma_f32 v23, v29, v23, -v35
	v_fma_f32 v29, -v5, v95, 0
	v_fma_f32 v23, -v7, v96, v23
	v_fma_f32 v29, -v9, v97, v29
	v_fma_f32 v23, -v11, v98, v23
	v_fma_f32 v29, -v13, v99, v29
	v_fma_f32 v23, -v14, v100, v23
	v_fma_f32 v29, -v15, v101, v29
	v_fma_f32 v23, -v17, v102, v23
	v_fma_f32 v29, -v18, v103, v29
	v_fma_f32 v23, -v19, v104, v23
	v_fma_f32 v29, -v20, v105, v29
	v_fma_f32 v23, -v22, v106, v23
	v_fma_f32 v29, -v24, v107, v29
	v_fma_f32 v23, -v26, v108, v23
	v_fma_f32 v29, -v27, v109, v29
	v_fma_f32 v23, -v30, v122, v23
	v_fma_f32 v29, -v31, v123, v29
	v_fma_f32 v23, -v32, v124, v23
	v_fma_f32 v29, -v34, v125, v29
	v_fma_f32 v23, -v36, v126, v23
	v_fma_f32 v29, -v38, v127, v29
	v_fma_f32 v23, -v40, v128, v23
	v_fma_f32 v29, -v41, v129, v29
	s_nop 0
	v_fma_f32 v23, -v43, v138, v23
	v_fma_f32 v29, -v49, v139, v29
	v_fma_f32 v23, -v50, v140, v23
	v_fma_f32 v29, -v53, v141, v29
	v_fma_f32 v23, -v54, v150, v23
	v_fma_f32 v29, -v57, v151, v29
	v_fma_f32 v23, -v59, v152, v23
	v_fma_f32 v29, -v62, v153, v29
	v_fma_f32 v23, -v63, v154, v23
	v_fma_f32 v29, -v71, v155, v29
	v_fma_f32 v23, -v74, v156, v23
	v_fma_f32 v29, -v76, v157, v29
	v_fma_f32 v23, -v79, v162, v23
	v_fma_f32 v29, -v82, v163, v29
	v_fma_f32 v23, -v84, v164, v23
	v_fma_f32 v29, -v87, v165, v29
	v_fma_f32 v23, -v90, v166, v23
	v_fma_f32 v29, -v93, v167, v29
	v_fma_f32 v23, -v91, v168, v23
	v_fma_f32 v29, -v88, v169, v29
	v_fma_f32 v23, -v86, v178, v23
	v_fma_f32 v29, -v83, v179, v29
	v_fma_f32 v23, -v81, v180, v23
	v_fma_f32 v29, -v78, v181, v29
	s_add_i32 s2, s50, 0x400
	v_fma_f32 v23, -v75, v210, v23
	v_fma_f32 v29, -v72, v211, v29
	v_fma_f32 v23, -v70, v212, v23
	v_fma_f32 v29, -v61, v213, v29
	v_fma_f32 v23, -v58, v220, v23
	v_fma_f32 v29, -v55, v221, v29
	v_fma_f32 v23, -v52, v222, v23
	v_fma_f32 v29, -v48, v223, v29
	v_fma_f32 v23, -v42, v228, v23
	v_fma_f32 v29, -v37, v229, v29
	v_fma_f32 v23, -v33, v230, v23
	v_fma_f32 v29, -v28, v231, v29
	v_add_f32_e32 v23, v23, v29
	ds_read_b128 v[94:97], v25 offset:15872
	ds_read_b128 v[98:101], v25 offset:15888
	ds_read_b128 v[102:105], v25 offset:15904
	ds_read_b128 v[106:109], v25 offset:15920
	ds_read_b128 v[122:125], v25 offset:15936
	ds_read_b128 v[126:129], v25 offset:15952
	ds_read_b128 v[138:141], v25 offset:15968
	ds_read_b128 v[150:153], v25 offset:15984
	ds_read_b128 v[154:157], v25 offset:16000
	ds_read_b128 v[162:165], v25 offset:16016
	ds_read_b128 v[166:169], v25 offset:16032
	ds_read_b128 v[178:181], v25 offset:16048
	ds_read_b128 v[210:213], v25 offset:16064
	ds_read_b128 v[220:223], v25 offset:16080
	ds_read_b128 v[228:231], v25 offset:16096
	ds_read_b128 v[236:239], v25 offset:16112
	s_waitcnt lgkmcnt(14)
	v_mul_f32_e32 v29, v4, v114
	v_fma_f32 v16, v21, v16, -v29
	v_fma_f32 v21, -v5, v115, 0
	v_fma_f32 v16, -v7, v116, v16
	v_fma_f32 v21, -v9, v117, v21
	v_fma_f32 v16, -v11, v118, v16
	v_fma_f32 v21, -v13, v119, v21
	v_fma_f32 v16, -v14, v120, v16
	v_fma_f32 v21, -v15, v121, v21
	v_fma_f32 v16, -v17, v130, v16
	v_fma_f32 v21, -v18, v131, v21
	v_fma_f32 v16, -v19, v132, v16
	v_fma_f32 v21, -v20, v133, v21
	v_fma_f32 v16, -v22, v134, v16
	v_fma_f32 v21, -v24, v135, v21
	v_fma_f32 v16, -v26, v136, v16
	v_fma_f32 v21, -v27, v137, v21
	v_fma_f32 v16, -v30, v142, v16
	v_fma_f32 v21, -v31, v143, v21
	v_fma_f32 v16, -v32, v144, v16
	v_fma_f32 v21, -v34, v145, v21
	v_fma_f32 v16, -v36, v146, v16
	v_fma_f32 v21, -v38, v147, v21
	v_fma_f32 v16, -v40, v148, v16
	v_fma_f32 v21, -v41, v149, v21
	v_fma_f32 v16, -v43, v158, v16
	v_fma_f32 v21, -v49, v159, v21
	v_fma_f32 v16, -v50, v160, v16
	v_fma_f32 v21, -v53, v161, v21
	v_fma_f32 v16, -v54, v170, v16
	v_fma_f32 v21, -v57, v171, v21
	v_fma_f32 v16, -v59, v172, v16
	v_fma_f32 v21, -v62, v173, v21
	v_fma_f32 v16, -v63, v174, v16
	v_fma_f32 v21, -v71, v175, v21
	v_fma_f32 v16, -v74, v176, v16
	v_fma_f32 v21, -v76, v177, v21
	v_fma_f32 v16, -v79, v182, v16
	v_fma_f32 v21, -v82, v183, v21
	v_fma_f32 v16, -v84, v184, v16
	v_fma_f32 v21, -v87, v185, v21
	v_fma_f32 v16, -v90, v186, v16
	v_fma_f32 v21, -v93, v187, v21
	v_fma_f32 v16, -v91, v188, v16
	v_fma_f32 v21, -v88, v189, v21
	v_fma_f32 v16, -v86, v190, v16
	v_fma_f32 v21, -v83, v191, v21
	v_fma_f32 v16, -v81, v192, v16
	v_fma_f32 v21, -v78, v193, v21
	v_fma_f32 v16, -v75, v206, v16
	v_fma_f32 v21, -v72, v207, v21
	v_fma_f32 v16, -v70, v208, v16
	v_fma_f32 v21, -v61, v209, v21
	v_fma_f32 v16, -v58, v216, v16
	v_fma_f32 v21, -v55, v217, v21
	v_fma_f32 v16, -v52, v218, v16
	v_fma_f32 v21, -v48, v219, v21
	v_fma_f32 v16, -v42, v224, v16
	v_fma_f32 v21, -v37, v225, v21
	v_fma_f32 v16, -v33, v226, v16
	v_fma_f32 v21, -v28, v227, v21
	v_fma_f32 v16, -v23, v232, v16
	v_add_f32_e32 v16, v21, v16
	ds_read_b128 v[114:117], v25 offset:16128
	ds_read_b128 v[118:121], v25 offset:16144
	ds_read_b128 v[130:133], v25 offset:16160
	ds_read_b128 v[134:137], v25 offset:16176
	ds_read_b128 v[142:145], v25 offset:16192
	ds_read_b128 v[146:149], v25 offset:16208
	ds_read_b128 v[158:161], v25 offset:16224
	ds_read_b128 v[170:173], v25 offset:16240
	ds_read_b128 v[174:177], v25 offset:16256
	ds_read_b128 v[182:185], v25 offset:16272
	ds_read_b128 v[186:189], v25 offset:16288
	ds_read_b128 v[190:193], v25 offset:16304
	ds_read_b128 v[206:209], v25 offset:16320
	ds_read_b128 v[216:219], v25 offset:16336
	ds_read_b128 v[224:227], v25 offset:16352
	ds_read_b128 v[232:235], v25 offset:16368
	s_waitcnt lgkmcnt(0)
	v_mul_f32_e32 v21, v4, v94
	v_fma_f32 v3, v12, v3, -v21
	v_fma_f32 v12, -v5, v95, 0
	v_fma_f32 v3, -v7, v96, v3
	v_fma_f32 v12, -v9, v97, v12
	v_fma_f32 v3, -v11, v98, v3
	v_fma_f32 v12, -v13, v99, v12
	v_fma_f32 v3, -v14, v100, v3
	v_fma_f32 v12, -v15, v101, v12
	v_fma_f32 v3, -v17, v102, v3
	v_fma_f32 v12, -v18, v103, v12
	v_fma_f32 v3, -v19, v104, v3
	v_fma_f32 v12, -v20, v105, v12
	v_fma_f32 v3, -v22, v106, v3
	v_fma_f32 v12, -v24, v107, v12
	v_fma_f32 v3, -v26, v108, v3
	v_fma_f32 v12, -v27, v109, v12
	v_fma_f32 v3, -v30, v122, v3
	v_fma_f32 v12, -v31, v123, v12
	v_fma_f32 v3, -v32, v124, v3
	v_fma_f32 v12, -v34, v125, v12
	v_fma_f32 v3, -v36, v126, v3
	v_fma_f32 v12, -v38, v127, v12
	v_fma_f32 v3, -v40, v128, v3
	v_fma_f32 v12, -v41, v129, v12
	s_nop 0
	v_fma_f32 v3, -v43, v138, v3
	v_fma_f32 v12, -v49, v139, v12
	v_fma_f32 v3, -v50, v140, v3
	v_fma_f32 v12, -v53, v141, v12
	v_fma_f32 v3, -v54, v150, v3
	v_fma_f32 v12, -v57, v151, v12
	v_fma_f32 v3, -v59, v152, v3
	v_fma_f32 v12, -v62, v153, v12
	v_fma_f32 v3, -v63, v154, v3
	v_fma_f32 v12, -v71, v155, v12
	v_fma_f32 v3, -v74, v156, v3
	v_fma_f32 v12, -v76, v157, v12
	v_fma_f32 v3, -v79, v162, v3
	v_fma_f32 v12, -v82, v163, v12
	v_fma_f32 v3, -v84, v164, v3
	v_fma_f32 v12, -v87, v165, v12
	v_fma_f32 v3, -v90, v166, v3
	v_fma_f32 v12, -v93, v167, v12
	v_fma_f32 v3, -v91, v168, v3
	v_fma_f32 v12, -v88, v169, v12
	v_fma_f32 v3, -v86, v178, v3
	v_fma_f32 v12, -v83, v179, v12
	v_fma_f32 v3, -v81, v180, v3
	v_fma_f32 v12, -v78, v181, v12
	s_nop 0
	v_fma_f32 v3, -v75, v210, v3
	v_fma_f32 v12, -v72, v211, v12
	v_fma_f32 v3, -v70, v212, v3
	v_fma_f32 v12, -v61, v213, v12
	v_fma_f32 v3, -v58, v220, v3
	v_fma_f32 v12, -v55, v221, v12
	v_fma_f32 v3, -v52, v222, v3
	v_fma_f32 v12, -v48, v223, v12
	v_fma_f32 v3, -v42, v228, v3
	v_fma_f32 v12, -v37, v229, v12
	v_fma_f32 v3, -v33, v230, v3
	v_fma_f32 v12, -v28, v231, v12
	v_fma_f32 v3, -v23, v236, v3
	v_fma_f32 v12, -v16, v237, v12
	v_add_f32_e32 v3, v3, v12
	v_mul_f32_e32 v12, v4, v114
	v_fma_f32 v1, v2, v1, -v12
	v_fma_f32 v2, -v5, v115, 0
	v_fma_f32 v1, -v7, v116, v1
	v_fma_f32 v2, -v9, v117, v2
	v_fma_f32 v1, -v11, v118, v1
	v_fma_f32 v2, -v13, v119, v2
	v_fma_f32 v1, -v14, v120, v1
	v_fma_f32 v2, -v15, v121, v2
	v_fma_f32 v1, -v17, v130, v1
	v_fma_f32 v2, -v18, v131, v2
	v_fma_f32 v1, -v19, v132, v1
	v_fma_f32 v2, -v20, v133, v2
	v_fma_f32 v1, -v22, v134, v1
	v_fma_f32 v2, -v24, v135, v2
	v_fma_f32 v1, -v26, v136, v1
	v_fma_f32 v2, -v27, v137, v2
	v_fma_f32 v1, -v30, v142, v1
	v_fma_f32 v2, -v31, v143, v2
	v_fma_f32 v1, -v32, v144, v1
	v_fma_f32 v2, -v34, v145, v2
	v_fma_f32 v1, -v36, v146, v1
	v_fma_f32 v2, -v38, v147, v2
	v_fma_f32 v1, -v40, v148, v1
	v_fma_f32 v2, -v41, v149, v2
	v_fma_f32 v1, -v43, v158, v1
	v_fma_f32 v2, -v49, v159, v2
	v_fma_f32 v1, -v50, v160, v1
	v_fma_f32 v2, -v53, v161, v2
	v_fma_f32 v1, -v54, v170, v1
	v_fma_f32 v2, -v57, v171, v2
	v_fma_f32 v1, -v59, v172, v1
	v_fma_f32 v2, -v62, v173, v2
	v_fma_f32 v1, -v63, v174, v1
	v_fma_f32 v2, -v71, v175, v2
	v_fma_f32 v1, -v74, v176, v1
	v_fma_f32 v2, -v76, v177, v2
	v_fma_f32 v1, -v79, v182, v1
	v_fma_f32 v2, -v82, v183, v2
	v_fma_f32 v1, -v84, v184, v1
	v_fma_f32 v2, -v87, v185, v2
	v_fma_f32 v1, -v90, v186, v1
	v_fma_f32 v2, -v93, v187, v2
	v_fma_f32 v1, -v91, v188, v1
	v_fma_f32 v2, -v88, v189, v2
	v_fma_f32 v1, -v86, v190, v1
	v_fma_f32 v2, -v83, v191, v2
	v_fma_f32 v1, -v81, v192, v1
	v_fma_f32 v2, -v78, v193, v2
	v_fma_f32 v1, -v75, v206, v1
	v_fma_f32 v2, -v72, v207, v2
	v_fma_f32 v1, -v70, v208, v1
	v_fma_f32 v2, -v61, v209, v2
	v_fma_f32 v1, -v58, v216, v1
	v_fma_f32 v2, -v55, v217, v2
	v_fma_f32 v1, -v52, v218, v1
	v_fma_f32 v2, -v48, v219, v2
	v_fma_f32 v1, -v42, v224, v1
	v_fma_f32 v2, -v37, v225, v2
	v_fma_f32 v1, -v33, v226, v1
	v_fma_f32 v2, -v28, v227, v2
	v_fma_f32 v1, -v23, v232, v1
	v_fma_f32 v2, -v16, v233, v2
	v_fma_f32 v1, -v234, v3, v1
	v_add_f32_e32 v1, v2, v1
	v_cvt_pk_bf16_f32 v2, v4, s0
	ds_write_b16 v0, v2 offset:17408
	v_cvt_pk_bf16_f32 v2, v5, s0
	ds_write_b16 v0, v2 offset:17664
	v_cvt_pk_bf16_f32 v2, v7, s0
	ds_write_b16 v0, v2 offset:17920
	v_cvt_pk_bf16_f32 v2, v9, s0
	ds_write_b16 v0, v2 offset:18176
	v_cvt_pk_bf16_f32 v2, v11, s0
	ds_write_b16 v0, v2 offset:18432
	v_cvt_pk_bf16_f32 v2, v13, s0
	ds_write_b16 v0, v2 offset:18688
	v_cvt_pk_bf16_f32 v2, v14, s0
	ds_write_b16 v0, v2 offset:18944
	v_cvt_pk_bf16_f32 v2, v15, s0
	ds_write_b16 v0, v2 offset:19200
	v_cvt_pk_bf16_f32 v2, v17, s0
	ds_write_b16 v0, v2 offset:19456
	v_cvt_pk_bf16_f32 v2, v18, s0
	ds_write_b16 v0, v2 offset:19712
	v_cvt_pk_bf16_f32 v2, v19, s0
	ds_write_b16 v0, v2 offset:19968
	v_cvt_pk_bf16_f32 v2, v20, s0
	ds_write_b16 v0, v2 offset:20224
	v_cvt_pk_bf16_f32 v2, v22, s0
	ds_write_b16 v0, v2 offset:20480
	v_cvt_pk_bf16_f32 v2, v24, s0
	ds_write_b16 v0, v2 offset:20736
	v_cvt_pk_bf16_f32 v2, v26, s0
	ds_write_b16 v0, v2 offset:20992
	v_cvt_pk_bf16_f32 v2, v27, s0
	ds_write_b16 v0, v2 offset:21248
	v_cvt_pk_bf16_f32 v2, v30, s0
	ds_write_b16 v0, v2 offset:21504
	v_cvt_pk_bf16_f32 v2, v31, s0
	ds_write_b16 v0, v2 offset:21760
	v_cvt_pk_bf16_f32 v2, v32, s0
	ds_write_b16 v0, v2 offset:22016
	v_cvt_pk_bf16_f32 v2, v34, s0
	ds_write_b16 v0, v2 offset:22272
	v_cvt_pk_bf16_f32 v2, v36, s0
	ds_write_b16 v0, v2 offset:22528
	v_cvt_pk_bf16_f32 v2, v38, s0
	ds_write_b16 v0, v2 offset:22784
	v_cvt_pk_bf16_f32 v2, v40, s0
	ds_write_b16 v0, v2 offset:23040
	v_cvt_pk_bf16_f32 v2, v41, s0
	ds_write_b16 v0, v2 offset:23296
	v_cvt_pk_bf16_f32 v2, v43, s0
	ds_write_b16 v0, v2 offset:23552
	v_cvt_pk_bf16_f32 v2, v49, s0
	ds_write_b16 v0, v2 offset:23808
	v_cvt_pk_bf16_f32 v2, v50, s0
	ds_write_b16 v0, v2 offset:24064
	v_cvt_pk_bf16_f32 v2, v53, s0
	ds_write_b16 v0, v2 offset:24320
	v_cvt_pk_bf16_f32 v2, v54, s0
	ds_write_b16 v0, v2 offset:24576
	v_cvt_pk_bf16_f32 v2, v57, s0
	ds_write_b16 v0, v2 offset:24832
	v_cvt_pk_bf16_f32 v2, v59, s0
	ds_write_b16 v0, v2 offset:25088
	v_cvt_pk_bf16_f32 v2, v62, s0
	ds_write_b16 v0, v2 offset:25344
	v_cvt_pk_bf16_f32 v2, v63, s0
	ds_write_b16 v0, v2 offset:25600
	v_cvt_pk_bf16_f32 v2, v71, s0
	ds_write_b16 v0, v2 offset:25856
	v_cvt_pk_bf16_f32 v2, v74, s0
	ds_write_b16 v0, v2 offset:26112
	v_cvt_pk_bf16_f32 v2, v76, s0
	ds_write_b16 v0, v2 offset:26368
	v_cvt_pk_bf16_f32 v2, v79, s0
	ds_write_b16 v0, v2 offset:26624
	v_cvt_pk_bf16_f32 v2, v82, s0
	ds_write_b16 v0, v2 offset:26880
	v_cvt_pk_bf16_f32 v2, v84, s0
	ds_write_b16 v0, v2 offset:27136
	v_cvt_pk_bf16_f32 v2, v87, s0
	ds_write_b16 v0, v2 offset:27392
	v_cvt_pk_bf16_f32 v2, v90, s0
	ds_write_b16 v0, v2 offset:27648
	v_cvt_pk_bf16_f32 v2, v93, s0
	ds_write_b16 v0, v2 offset:27904
	v_cvt_pk_bf16_f32 v2, v91, s0
	ds_write_b16 v0, v2 offset:28160
	v_cvt_pk_bf16_f32 v2, v88, s0
	ds_write_b16 v0, v2 offset:28416
	v_cvt_pk_bf16_f32 v2, v86, s0
	ds_write_b16 v0, v2 offset:28672
	v_cvt_pk_bf16_f32 v2, v83, s0
	ds_write_b16 v0, v2 offset:28928
	v_cvt_pk_bf16_f32 v2, v81, s0
	ds_write_b16 v0, v2 offset:29184
	v_cvt_pk_bf16_f32 v2, v78, s0
	ds_write_b16 v0, v2 offset:29440
	v_cvt_pk_bf16_f32 v2, v75, s0
	ds_write_b16 v0, v2 offset:29696
	v_cvt_pk_bf16_f32 v2, v72, s0
	ds_write_b16 v0, v2 offset:29952
	v_cvt_pk_bf16_f32 v2, v70, s0
	ds_write_b16 v0, v2 offset:30208
	v_cvt_pk_bf16_f32 v2, v61, s0
	ds_write_b16 v0, v2 offset:30464
	v_cvt_pk_bf16_f32 v2, v58, s0
	ds_write_b16 v0, v2 offset:30720
	v_cvt_pk_bf16_f32 v2, v55, s0
	ds_write_b16 v0, v2 offset:30976
	v_cvt_pk_bf16_f32 v2, v52, s0
	ds_write_b16 v0, v2 offset:31232
	v_cvt_pk_bf16_f32 v2, v48, s0
	ds_write_b16 v0, v2 offset:31488
	v_cvt_pk_bf16_f32 v2, v42, s0
	ds_write_b16 v0, v2 offset:31744
	v_cvt_pk_bf16_f32 v2, v37, s0
	ds_write_b16 v0, v2 offset:32000
	v_cvt_pk_bf16_f32 v2, v33, s0
	ds_write_b16 v0, v2 offset:32256
	v_cvt_pk_bf16_f32 v2, v28, s0
	ds_write_b16 v0, v2 offset:32512
	v_cvt_pk_bf16_f32 v2, v23, s0
	ds_write_b16 v0, v2 offset:32768
	v_cvt_pk_bf16_f32 v2, v16, s0
	ds_write_b16 v0, v2 offset:33024
	v_cvt_pk_bf16_f32 v2, v3, s0
	v_cvt_pk_bf16_f32 v1, v1, s0
	ds_write_b16 v0, v2 offset:33280
	ds_write_b16 v0, v1 offset:33536
	v_lshlrev_b32_e32 v0, 8, v67
	v_and_b32_e32 v0, 0xf00, v0
	v_add_u32_e32 v0, s27, v0
	v_add3_u32 v11, v0, v44, v46
	v_add_u32_e32 v0, 0x4000, v11
	s_waitcnt lgkmcnt(0)
	s_barrier
	ds_read2_b64 v[0:3], v0 offset0:128 offset1:132
	v_add_u32_e32 v4, 0x5000, v11
	ds_read2_b64 v[12:15], v4 offset0:128 offset1:132
	v_lshl_add_u64 v[4:5], s[40:41], 0, v[112:113]
	v_mov_b32_e32 v7, v113
	s_waitcnt lgkmcnt(0)
	v_xor_b32_e32 v0, 0x80008000, v0
	v_xor_b32_e32 v1, 0x80008000, v1
	v_xor_b32_e32 v2, 0x80008000, v2
	v_xor_b32_e32 v3, 0x80008000, v3
	global_store_dwordx4 v[4:5], v[0:3], off
	v_mov_b32_e32 v9, v113
	s_cmpk_gt_i32 s50, 0x1dff
	v_add_u32_e32 v1, 0x6000, v11
	v_xor_b32_e32 v0, 0x80008000, v12
	ds_read2_b64 v[16:19], v1 offset0:128 offset1:132
	v_xor_b32_e32 v1, 0x80008000, v13
	v_xor_b32_e32 v2, 0x80008000, v14
	v_xor_b32_e32 v3, 0x80008000, v15
	global_store_dwordx4 v[4:5], v[0:3], off offset:2048
	v_lshl_add_u64 v[4:5], s[40:41], 0, v[6:7]
	s_mov_b32 s50, s2
	v_add_u32_e32 v2, 0x7000, v11
	ds_read2_b64 v[12:15], v2 offset0:128 offset1:132
	s_waitcnt lgkmcnt(0)
	v_xor_b32_e32 v0, 0x80008000, v16
	v_xor_b32_e32 v1, 0x80008000, v17
	v_xor_b32_e32 v2, 0x80008000, v18
	v_xor_b32_e32 v3, 0x80008000, v19
	global_store_dwordx4 v[4:5], v[0:3], off
	v_lshl_add_u64 v[4:5], s[40:41], 0, v[8:9]
	v_lshlrev_b32_e32 v8, 8, v68
	v_xor_b32_e32 v0, 0x80008000, v12
	v_xor_b32_e32 v1, 0x80008000, v13
	v_xor_b32_e32 v2, 0x80008000, v14
	v_xor_b32_e32 v3, 0x80008000, v15
	global_store_dwordx4 v[4:5], v[0:3], off
	s_nop 1
	v_and_b32_e32 v0, 16, v45
	v_lshlrev_b32_e32 v0, 1, v0
	v_add3_u32 v3, v10, v0, v8
	ds_read_u16 v0, v3 offset:17536
	ds_read_u16 v1, v3 offset:17792
	ds_read_u16 v2, v3 offset:18048
	ds_read_u16 v4, v3 offset:18304
	ds_read_u16 v5, v3 offset:21632
	ds_read_u16 v6, v3 offset:21888
	ds_read_u16 v7, v3 offset:22144
	ds_read_u16 v9, v3 offset:22400
	s_waitcnt lgkmcnt(2)
	v_lshl_or_b32 v0, v1, 16, v0
	v_lshl_or_b32 v1, v4, 16, v2
	v_lshl_or_b32 v2, v6, 16, v5
	ds_read_u16 v4, v3 offset:25728
	ds_read_u16 v5, v3 offset:25984
	ds_read_u16 v6, v3 offset:26240
	ds_read_u16 v11, v3 offset:26496
	ds_read_u16 v12, v3 offset:29824
	ds_read_u16 v13, v3 offset:30080
	ds_read_u16 v14, v3 offset:30336
	ds_read_u16 v15, v3 offset:30592
	s_waitcnt lgkmcnt(0)
	v_lshl_or_b32 v3, v9, 16, v7
	v_lshlrev_b32_e32 v9, 5, v65
	v_lshl_or_b32 v4, v5, 16, v4
	v_lshl_or_b32 v5, v11, 16, v6
	v_lshl_or_b32 v6, v13, 16, v12
	v_lshl_or_b32 v7, v15, 16, v14
	global_store_dwordx4 v9, v[0:3], s[6:7]
	global_store_dwordx4 v9, v[4:7], s[6:7] offset:16
	s_nop 0
	v_lshrrev_b32_e32 v0, 1, v66
	v_and_b32_e32 v0, 0x60, v0
	v_add3_u32 v3, v10, v0, v8
	ds_read_u16 v0, v3 offset:17536
	ds_read_u16 v1, v3 offset:17792
	ds_read_u16 v2, v3 offset:18048
	ds_read_u16 v4, v3 offset:18304
	ds_read_u16 v5, v3 offset:21632
	ds_read_u16 v6, v3 offset:21888
	ds_read_u16 v7, v3 offset:22144
	ds_read_u16 v8, v3 offset:22400
	s_waitcnt lgkmcnt(2)
	v_lshl_or_b32 v0, v1, 16, v0
	v_lshl_or_b32 v1, v4, 16, v2
	v_lshl_or_b32 v2, v6, 16, v5
	ds_read_u16 v4, v3 offset:25728
	ds_read_u16 v5, v3 offset:25984
	ds_read_u16 v6, v3 offset:26240
	ds_read_u16 v9, v3 offset:26496
	ds_read_u16 v10, v3 offset:29824
	ds_read_u16 v11, v3 offset:30080
	ds_read_u16 v12, v3 offset:30336
	ds_read_u16 v13, v3 offset:30592
	s_waitcnt lgkmcnt(0)
	v_lshl_or_b32 v3, v8, 16, v7
	v_lshlrev_b32_e32 v8, 5, v66
	v_lshl_or_b32 v4, v5, 16, v4
	v_lshl_or_b32 v5, v9, 16, v6
	v_lshl_or_b32 v6, v11, 16, v10
	v_lshl_or_b32 v7, v13, 16, v12
	global_store_dwordx4 v8, v[0:3], s[6:7]
	global_store_dwordx4 v8, v[4:7], s[6:7] offset:16
	s_cbranch_scc1 .LBB0_547

.LBB0_415:
	v_and_b32_e32 v69, 15, v67
	v_lshrrev_b32_e32 v4, 1, v67
	v_or_b32_e32 v10, s12, v69
	v_and_b32_e32 v70, 32, v4
	v_lshlrev_b32_e32 v44, 1, v70
	v_mov_b32_e32 v45, v113
	v_sub_u32_e32 v6, s2, v10
	v_or_b32_e32 v8, 16, v10
	v_lshl_add_u64 v[4:5], s[70:71], 0, v[44:45]
	v_lshrrev_b32_e32 v45, 2, v67
	v_cndmask_b32_e64 v6, v6, v10, s[38:39]
	v_sub_u32_e32 v9, s2, v8
	v_and_b32_e32 v68, 12, v45
	v_ashrrev_i32_e32 v7, 31, v6
	v_cndmask_b32_e64 v8, v9, v8, s[38:39]
	v_lshlrev_b32_e32 v46, 1, v68
	v_mov_b32_e32 v47, v113
	v_lshl_add_u64 v[6:7], s[64:65], 0, v[6:7]
	v_ashrrev_i32_e32 v9, 31, v8
	v_lshl_add_u64 v[4:5], v[4:5], 0, v[46:47]
	v_lshlrev_b64 v[6:7], 9, v[6:7]
	v_lshl_add_u64 v[8:9], s[64:65], 0, v[8:9]
	v_lshl_add_u64 v[6:7], v[4:5], 0, v[6:7]
	v_lshlrev_b64 v[8:9], 9, v[8:9]
	s_waitcnt lgkmcnt(0)
	s_barrier
	v_lshl_add_u64 v[8:9], v[4:5], 0, v[8:9]
	global_load_dwordx2 v[62:63], v[6:7], off
	global_load_dwordx2 v[60:61], v[6:7], off offset:32
	global_load_dwordx2 v[58:59], v[8:9], off
	global_load_dwordx2 v[56:57], v[8:9], off offset:32
	v_or_b32_e32 v6, 32, v10
	v_sub_u32_e32 v7, s2, v6
	v_or_b32_e32 v8, 48, v10
	v_cndmask_b32_e64 v6, v7, v6, s[38:39]
	v_sub_u32_e32 v9, s2, v8
	v_ashrrev_i32_e32 v7, 31, v6
	v_cndmask_b32_e64 v8, v9, v8, s[38:39]
	v_lshl_add_u64 v[6:7], s[64:65], 0, v[6:7]
	v_ashrrev_i32_e32 v9, 31, v8
	v_lshlrev_b64 v[6:7], 9, v[6:7]
	v_lshl_add_u64 v[8:9], s[64:65], 0, v[8:9]
	v_lshl_add_u64 v[6:7], v[4:5], 0, v[6:7]
	v_lshlrev_b64 v[8:9], 9, v[8:9]
	v_lshl_add_u64 v[4:5], v[4:5], 0, v[8:9]
	global_load_dwordx2 v[54:55], v[6:7], off
	global_load_dwordx2 v[52:53], v[6:7], off offset:32
	global_load_dwordx2 v[50:51], v[4:5], off
	global_load_dwordx2 v[48:49], v[4:5], off offset:32
	v_lshl_add_u32 v72, v73, 2, s27
	ds_read_b32 v74, v72 offset:16384
	s_mul_i32 s4, s6, 0xa000
	s_mul_hi_i32 s2, s6, 0xa000
	s_add_u32 s40, s10, s4
	s_addc_u32 s41, s11, s2
	s_mov_b64 s[6:7], -1
	s_andn2_b64 vcc, exec, s[46:47]
	v_lshlrev_b32_e32 v47, 2, v75
	v_or_b32_e32 v71, 32, v73
	s_cbranch_vccnz .LBB0_417
	v_lshl_add_u32 v102, v73, 8, s27
	v_add_u32_e32 v103, v102, v112
	ds_read_b128 v[4:7], v103 offset:17408
	ds_read_b128 v[78:81], v103 offset:17440
	v_or_b32_e32 v77, v112, v69
	s_movk_i32 s2, 0x80
	v_add_u32_e32 v76, s27, v112
	s_waitcnt vmcnt(15) lgkmcnt(1)
	v_mfma_f32_32x32x16_bf16 v[0:15], v[4:7], v[0:3], 0
	v_add_u32_e32 v82, 0x4000, v76
	v_sub_u32_e32 v86, v73, v47
	v_cmp_lt_i32_e32 vcc, -1, v86
	s_mov_b32 s12, 0x5040100
	s_add_u32 s64, s40, 0x4000
	s_addc_u32 s65, s41, 0
	s_mov_b32 s4, s5
	s_waitcnt vmcnt(14) lgkmcnt(0)
	v_mfma_f32_32x32x16_bf16 v[0:15], v[78:81], v[40:43], v[0:15]
	ds_read_b128 v[40:43], v103 offset:17472
	v_add_u32_e32 v78, 0x4004, v76
	s_mov_b32 s6, s5
	s_mov_b32 s7, s5
	s_waitcnt vmcnt(13) lgkmcnt(0)
	v_mfma_f32_32x32x16_bf16 v[0:15], v[40:43], v[36:39], v[0:15]
	ds_read_b128 v[36:39], v103 offset:17504
	ds_read2_b32 v[42:43], v82 offset0:3 offset1:8
	s_waitcnt vmcnt(12) lgkmcnt(1)
	v_mfma_f32_32x32x16_bf16 v[0:15], v[36:39], v[32:35], v[0:15]
	v_lshlrev_b32_e32 v32, 3, v73
	v_and_or_b32 v32, v32, s2, v77
	v_lshlrev_b32_e32 v104, 4, v32
	ds_read_b32 v32, v76 offset:16384
	ds_read2_b64 v[34:37], v82 offset1:1
	ds_read2_b64 v[38:41], v82 offset0:4 offset1:5
	ds_read2_b32 v[90:91], v78 offset1:1
	ds_read2_b32 v[94:95], v82 offset0:11 offset1:16
	ds_read2_b64 v[78:81], v82 offset0:8 offset1:9
	s_waitcnt lgkmcnt(4)
	v_sub_f32_e32 v32, v74, v32
	v_sub_f32_e32 v33, v74, v35
	v_min_f32_e32 v32, 0, v32
	v_min_f32_e32 v33, 0, v33
	v_mul_f32_e32 v32, 0x3fb8aa3b, v32
	v_mul_f32_e32 v33, 0x3fb8aa3b, v33
	v_exp_f32_e32 v32, v32
	v_exp_f32_e32 v33, v33
	ds_read2_b32 v[98:99], v82 offset0:19 offset1:24
	ds_read2_b64 v[82:85], v82 offset0:12 offset1:13
	s_movk_i32 s2, 0xff04
	v_pk_mul_f32 v[0:1], v[0:1], v[32:33]
	s_waitcnt lgkmcnt(4)
	v_sub_f32_e32 v32, v74, v91
	v_sub_f32_e32 v33, v74, v37
	v_min_f32_e32 v32, 0, v32
	v_min_f32_e32 v33, 0, v33
	v_mul_f32_e32 v32, 0x3fb8aa3b, v32
	v_mul_f32_e32 v33, 0x3fb8aa3b, v33
	v_exp_f32_e32 v32, v32
	v_exp_f32_e32 v33, v33
	v_cvt_pk_bf16_f32 v0, v0, v1
	v_cndmask_b32_e32 v1, 0, v0, vcc
	v_lshrrev_b32_e32 v0, 16, v0
	v_cmp_lt_i32_e32 vcc, 0, v86
	v_pk_mul_f32 v[2:3], v[2:3], v[32:33]
	v_add_u32_e32 v32, 0x4024, v76
	v_cndmask_b32_e32 v0, 0, v0, vcc
	v_perm_b32 v0, v0, v1, s12
	v_cvt_pk_bf16_f32 v1, v2, v3
	v_cmp_lt_i32_e32 vcc, 1, v86
	v_sub_f32_e32 v3, v74, v39
	v_min_f32_e32 v3, 0, v3
	v_cndmask_b32_e32 v2, 0, v1, vcc
	v_lshrrev_b32_e32 v1, 16, v1
	v_cmp_lt_i32_e32 vcc, 2, v86
	v_mul_f32_e32 v3, 0x3fb8aa3b, v3
	ds_read2_b32 v[92:93], v32 offset1:1
	v_cndmask_b32_e32 v1, 0, v1, vcc
	v_perm_b32 v1, v1, v2, s12
	v_sub_f32_e32 v2, v74, v43
	v_min_f32_e32 v2, 0, v2
	v_mul_f32_e32 v2, 0x3fb8aa3b, v2
	v_exp_f32_e32 v2, v2
	v_exp_f32_e32 v3, v3
	v_cmp_lt_i32_e32 vcc, 7, v86
	v_mad_i32_i24 v39, v73, s2, v102
	v_lshlrev_b32_e32 v32, 3, v71
	v_pk_mul_f32 v[2:3], v[4:5], v[2:3]
	s_waitcnt lgkmcnt(0)
	v_sub_f32_e32 v4, v74, v93
	v_sub_f32_e32 v5, v74, v41
	v_min_f32_e32 v4, 0, v4
	v_min_f32_e32 v5, 0, v5
	v_mul_f32_e32 v4, 0x3fb8aa3b, v4
	v_mul_f32_e32 v5, 0x3fb8aa3b, v5
	v_exp_f32_e32 v4, v4
	v_exp_f32_e32 v5, v5
	v_cvt_pk_bf16_f32 v2, v2, v3
	v_cndmask_b32_e32 v3, 0, v2, vcc
	v_lshrrev_b32_e32 v2, 16, v2
	v_cmp_lt_i32_e32 vcc, 8, v86
	v_pk_mul_f32 v[6:7], v[6:7], v[4:5]
	s_movk_i32 s2, 0x180
	v_cndmask_b32_e32 v2, 0, v2, vcc
	v_perm_b32 v4, v2, v3, s12
	v_cvt_pk_bf16_f32 v2, v6, v7
	v_cmp_lt_i32_e32 vcc, 9, v86
	v_add_u32_e32 v6, 0x4044, v76
	ds_read2_b32 v[96:97], v6 offset1:1
	v_cndmask_b32_e32 v3, 0, v2, vcc
	v_lshrrev_b32_e32 v2, 16, v2
	v_cmp_lt_i32_e32 vcc, 10, v86
	v_sub_f32_e32 v7, v74, v81
	s_waitcnt lgkmcnt(0)
	v_sub_f32_e32 v6, v74, v97
	v_cndmask_b32_e32 v2, 0, v2, vcc
	v_perm_b32 v5, v2, v3, s12
	v_sub_f32_e32 v2, v74, v95
	v_sub_f32_e32 v3, v74, v79
	v_min_f32_e32 v2, 0, v2
	v_min_f32_e32 v3, 0, v3
	v_mul_f32_e32 v2, 0x3fb8aa3b, v2
	v_mul_f32_e32 v3, 0x3fb8aa3b, v3
	v_exp_f32_e32 v2, v2
	v_exp_f32_e32 v3, v3
	v_min_f32_e32 v6, 0, v6
	v_min_f32_e32 v7, 0, v7
	v_mul_f32_e32 v6, 0x3fb8aa3b, v6
	v_mul_f32_e32 v7, 0x3fb8aa3b, v7
	v_exp_f32_e32 v6, v6
	v_exp_f32_e32 v7, v7
	v_pk_mul_f32 v[2:3], v[8:9], v[2:3]
	v_cmp_lt_i32_e32 vcc, 15, v86
	v_cvt_pk_bf16_f32 v2, v2, v3
	v_pk_mul_f32 v[6:7], v[10:11], v[6:7]
	v_cndmask_b32_e32 v3, 0, v2, vcc
	v_lshrrev_b32_e32 v2, 16, v2
	v_cmp_lt_i32_e32 vcc, 16, v86
	v_and_or_b32 v32, v32, s2, v77
	v_lshlrev_b32_e32 v32, 4, v32
	v_cndmask_b32_e32 v2, 0, v2, vcc
	v_perm_b32 v2, v2, v3, s12
	v_cvt_pk_bf16_f32 v3, v6, v7
	v_cmp_lt_i32_e32 vcc, 17, v86
	v_sub_u32_e32 v33, v71, v47
	s_nop 0
	v_cndmask_b32_e32 v6, 0, v3, vcc
	v_lshrrev_b32_e32 v3, 16, v3
	v_cmp_lt_i32_e32 vcc, 18, v86
	s_nop 1
	v_cndmask_b32_e32 v3, 0, v3, vcc
	v_perm_b32 v3, v3, v6, s12
	global_store_dwordx4 v104, v[0:3], s[64:65]
	v_cmp_lt_i32_e32 vcc, 23, v86
	s_nop 0
	v_add_u32_e32 v2, 0x4064, v76
	ds_read2_b32 v[100:101], v2 offset1:1
	v_sub_f32_e32 v0, v74, v99
	v_sub_f32_e32 v1, v74, v83
	v_min_f32_e32 v0, 0, v0
	v_min_f32_e32 v1, 0, v1
	v_mul_f32_e32 v0, 0x3fb8aa3b, v0
	v_mul_f32_e32 v1, 0x3fb8aa3b, v1
	v_exp_f32_e32 v0, v0
	v_exp_f32_e32 v1, v1
	s_waitcnt lgkmcnt(0)
	v_sub_f32_e32 v2, v74, v101
	v_sub_f32_e32 v3, v74, v85
	v_min_f32_e32 v2, 0, v2
	v_min_f32_e32 v3, 0, v3
	v_mul_f32_e32 v2, 0x3fb8aa3b, v2
	v_mul_f32_e32 v3, 0x3fb8aa3b, v3
	v_exp_f32_e32 v2, v2
	v_exp_f32_e32 v3, v3
	v_pk_mul_f32 v[0:1], v[12:13], v[0:1]
	v_pk_mul_f32 v[2:3], v[14:15], v[2:3]
	v_cvt_pk_bf16_f32 v0, v0, v1
	v_cndmask_b32_e32 v1, 0, v0, vcc
	v_lshrrev_b32_e32 v0, 16, v0
	v_cmp_lt_i32_e32 vcc, 24, v86
	s_nop 1
	v_cndmask_b32_e32 v0, 0, v0, vcc
	v_perm_b32 v6, v0, v1, s12
	v_cvt_pk_bf16_f32 v0, v2, v3
	v_cmp_lt_i32_e32 vcc, 25, v86
	s_nop 1
	v_cndmask_b32_e32 v1, 0, v0, vcc
	v_lshrrev_b32_e32 v0, 16, v0
	v_cmp_lt_i32_e32 vcc, 26, v86
	s_nop 1
	v_cndmask_b32_e32 v0, 0, v0, vcc
	v_perm_b32 v7, v0, v1, s12
	global_store_dwordx4 v104, v[4:7], s[64:65] offset:512
	ds_read_b128 v[0:3], v103 offset:17408
	ds_read_b128 v[86:89], v103 offset:17440
	s_waitcnt vmcnt(13) lgkmcnt(1)
	v_mfma_f32_32x32x16_bf16 v[0:15], v[0:3], v[24:27], 0
	ds_read_b32 v37, v39 offset:16512
	v_cmp_lt_u32_e32 vcc, 31, v33
	s_waitcnt lgkmcnt(0)
	v_sub_f32_e32 v34, v37, v34
	v_sub_f32_e32 v35, v37, v90
	s_waitcnt vmcnt(12)
	v_mfma_f32_32x32x16_bf16 v[0:15], v[86:89], v[28:31], v[0:15]
	ds_read_b128 v[86:89], v103 offset:17472
	v_min_f32_e32 v34, 0, v34
	v_min_f32_e32 v35, 0, v35
	v_mul_f32_e32 v34, 0x3fb8aa3b, v34
	v_mul_f32_e32 v35, 0x3fb8aa3b, v35
	v_exp_f32_e32 v34, v34
	v_exp_f32_e32 v35, v35
	s_waitcnt vmcnt(11) lgkmcnt(0)
	v_mfma_f32_32x32x16_bf16 v[0:15], v[86:89], v[20:23], v[0:15]
	ds_read_b128 v[86:89], v103 offset:17504
	s_waitcnt vmcnt(10) lgkmcnt(0)
	v_mfma_f32_32x32x16_bf16 v[0:15], v[86:89], v[16:19], v[0:15]
	s_nop 11
	v_pk_mul_f32 v[0:1], v[0:1], v[34:35]
	v_sub_f32_e32 v34, v37, v36
	v_sub_f32_e32 v35, v37, v42
	v_min_f32_e32 v34, 0, v34
	v_min_f32_e32 v35, 0, v35
	v_mul_f32_e32 v34, 0x3fb8aa3b, v34
	v_mul_f32_e32 v35, 0x3fb8aa3b, v35
	v_exp_f32_e32 v34, v34
	v_exp_f32_e32 v35, v35
	v_cvt_pk_bf16_f32 v0, v0, v1
	v_pk_mul_f32 v[2:3], v[2:3], v[34:35]
	s_nop 0
	v_cvt_pk_bf16_f32 v1, v2, v3
	v_sub_f32_e32 v2, v37, v38
	v_sub_f32_e32 v3, v37, v92
	v_min_f32_e32 v2, 0, v2
	v_min_f32_e32 v3, 0, v3
	v_mul_f32_e32 v2, 0x3fb8aa3b, v2
	v_mul_f32_e32 v3, 0x3fb8aa3b, v3
	v_exp_f32_e32 v2, v2
	v_exp_f32_e32 v3, v3
	s_nop 0
	v_pk_mul_f32 v[2:3], v[4:5], v[2:3]
	v_sub_f32_e32 v4, v37, v40
	v_sub_f32_e32 v5, v37, v94
	v_min_f32_e32 v4, 0, v4
	v_min_f32_e32 v5, 0, v5
	v_mul_f32_e32 v4, 0x3fb8aa3b, v4
	v_mul_f32_e32 v5, 0x3fb8aa3b, v5
	v_exp_f32_e32 v4, v4
	v_exp_f32_e32 v5, v5
	s_nop 0
	v_pk_mul_f32 v[6:7], v[6:7], v[4:5]
	v_cvt_pk_bf16_f32 v4, v2, v3
	v_cvt_pk_bf16_f32 v5, v6, v7
	v_sub_f32_e32 v2, v37, v78
	v_sub_f32_e32 v3, v37, v96
	v_sub_f32_e32 v6, v37, v80
	v_sub_f32_e32 v7, v37, v98
	v_min_f32_e32 v2, 0, v2
	v_min_f32_e32 v3, 0, v3
	v_min_f32_e32 v6, 0, v6
	v_min_f32_e32 v7, 0, v7
	v_mul_f32_e32 v2, 0x3fb8aa3b, v2
	v_mul_f32_e32 v3, 0x3fb8aa3b, v3
	v_mul_f32_e32 v6, 0x3fb8aa3b, v6
	v_mul_f32_e32 v7, 0x3fb8aa3b, v7
	v_exp_f32_e32 v2, v2
	v_exp_f32_e32 v3, v3
	v_exp_f32_e32 v6, v6
	v_exp_f32_e32 v7, v7
	v_pk_mul_f32 v[2:3], v[8:9], v[2:3]
	s_nop 0
	v_cvt_pk_bf16_f32 v2, v2, v3
	v_pk_mul_f32 v[6:7], v[10:11], v[6:7]
	s_nop 0
	v_cvt_pk_bf16_f32 v3, v6, v7
	global_store_dwordx4 v32, v[0:3], s[64:65]
	ds_read_b32 v3, v76 offset:16492
	s_nop 0
	v_sub_f32_e32 v0, v37, v82
	v_sub_f32_e32 v1, v37, v100
	v_sub_f32_e32 v2, v37, v84
	s_waitcnt lgkmcnt(0)
	v_sub_f32_e32 v3, v37, v3
	v_min_f32_e32 v0, 0, v0
	v_min_f32_e32 v1, 0, v1
	v_min_f32_e32 v2, 0, v2
	v_min_f32_e32 v3, 0, v3
	v_mul_f32_e32 v0, 0x3fb8aa3b, v0
	v_mul_f32_e32 v1, 0x3fb8aa3b, v1
	v_mul_f32_e32 v2, 0x3fb8aa3b, v2
	v_mul_f32_e32 v3, 0x3fb8aa3b, v3
	v_exp_f32_e32 v0, v0
	v_exp_f32_e32 v1, v1
	v_exp_f32_e32 v2, v2
	v_exp_f32_e32 v3, v3
	v_pk_mul_f32 v[0:1], v[12:13], v[0:1]
	s_nop 0
	v_cvt_pk_bf16_f32 v6, v0, v1
	v_pk_mul_f32 v[2:3], v[14:15], v[2:3]
	s_nop 0
	v_cvt_pk_bf16_f32 v7, v2, v3
	v_mov_b64_e32 v[0:1], s[4:5]
	v_mov_b64_e32 v[2:3], s[6:7]
	global_store_dwordx4 v32, v[4:7], s[64:65] offset:512
	global_store_dwordx4 v104, v[0:3], s[64:65] offset:1024
	global_store_dwordx4 v104, v[0:3], s[64:65] offset:1536
	ds_read_b128 v[0:3], v103 offset:25600
	ds_read_b128 v[34:37], v103 offset:25632
	s_waitcnt lgkmcnt(1)
	v_mfma_f32_32x32x16_bf16 v[0:15], v[0:3], v[24:27], 0
	ds_read_b128 v[24:27], v103 offset:25664
	s_mov_b64 s[6:7], 0
	s_waitcnt lgkmcnt(0)
	v_mfma_f32_32x32x16_bf16 v[0:15], v[34:37], v[28:31], v[0:15]
	v_mfma_f32_32x32x16_bf16 v[0:15], v[24:27], v[20:23], v[0:15]
	ds_read_b128 v[20:23], v103 offset:25696
	s_waitcnt lgkmcnt(0)
	v_mfma_f32_32x32x16_bf16 v[0:15], v[20:23], v[16:19], v[0:15]
	ds_read_b32 v16, v39 offset:16512
	ds_read_b128 v[18:21], v76 offset:16512
	ds_read_b128 v[22:25], v76 offset:16544
	s_waitcnt lgkmcnt(0)
	v_sub_f32_e32 v17, v16, v18
	v_min_f32_e32 v17, 0, v17
	v_mul_f32_e32 v17, 0x3fb8aa3b, v17
	v_exp_f32_e32 v18, v17
	v_sub_f32_e32 v17, v16, v19
	v_min_f32_e32 v17, 0, v17
	v_mul_f32_e32 v17, 0x3fb8aa3b, v17
	v_exp_f32_e32 v19, v17
	v_sub_f32_e32 v17, v16, v20
	v_min_f32_e32 v17, 0, v17
	v_mul_f32_e32 v17, 0x3fb8aa3b, v17
	v_pk_mul_f32 v[0:1], v[0:1], v[18:19]
	v_exp_f32_e32 v18, v17
	v_sub_f32_e32 v17, v16, v21
	v_min_f32_e32 v17, 0, v17
	v_mul_f32_e32 v17, 0x3fb8aa3b, v17
	v_exp_f32_e32 v19, v17
	v_cvt_pk_bf16_f32 v0, v0, v1
	v_cndmask_b32_e32 v1, 0, v0, vcc
	v_lshrrev_b32_e32 v0, 16, v0
	v_cmp_lt_u32_e32 vcc, 32, v33
	v_pk_mul_f32 v[18:19], v[2:3], v[18:19]
	s_nop 0
	v_cndmask_b32_e32 v0, 0, v0, vcc
	v_perm_b32 v2, v0, v1, s12
	v_cvt_pk_bf16_f32 v0, v18, v19
	v_cmp_lt_u32_e32 vcc, 33, v33
	s_nop 1
	v_cndmask_b32_e32 v1, 0, v0, vcc
	v_lshrrev_b32_e32 v0, 16, v0
	v_cmp_lt_u32_e32 vcc, 34, v33
	s_nop 1
	v_cndmask_b32_e32 v0, 0, v0, vcc
	v_perm_b32 v3, v0, v1, s12
	v_sub_f32_e32 v0, v16, v22
	v_sub_f32_e32 v1, v16, v23
	v_min_f32_e32 v0, 0, v0
	v_min_f32_e32 v1, 0, v1
	v_mul_f32_e32 v0, 0x3fb8aa3b, v0
	v_mul_f32_e32 v1, 0x3fb8aa3b, v1
	v_exp_f32_e32 v0, v0
	v_exp_f32_e32 v1, v1
	v_cmp_lt_u32_e32 vcc, 39, v33
	v_pk_mul_f32 v[0:1], v[4:5], v[0:1]
	v_sub_f32_e32 v4, v16, v24
	v_sub_f32_e32 v5, v16, v25
	v_min_f32_e32 v4, 0, v4
	v_min_f32_e32 v5, 0, v5
	v_mul_f32_e32 v4, 0x3fb8aa3b, v4
	v_mul_f32_e32 v5, 0x3fb8aa3b, v5
	v_exp_f32_e32 v4, v4
	v_exp_f32_e32 v5, v5
	v_cvt_pk_bf16_f32 v0, v0, v1
	v_cndmask_b32_e32 v1, 0, v0, vcc
	v_lshrrev_b32_e32 v0, 16, v0
	v_cmp_lt_u32_e32 vcc, 40, v33
	v_pk_mul_f32 v[4:5], v[6:7], v[4:5]
	s_nop 0
	v_cndmask_b32_e32 v0, 0, v0, vcc
	v_perm_b32 v0, v0, v1, s12
	v_cvt_pk_bf16_f32 v1, v4, v5
	v_cmp_lt_u32_e32 vcc, 41, v33
	s_nop 1
	v_cndmask_b32_e32 v4, 0, v1, vcc
	v_lshrrev_b32_e32 v1, 16, v1
	v_cmp_lt_u32_e32 vcc, 42, v33
	s_nop 1
	v_cndmask_b32_e32 v1, 0, v1, vcc
	v_perm_b32 v1, v1, v4, s12
	ds_read_b128 v[4:7], v76 offset:16576
	v_cmp_lt_u32_e32 vcc, 47, v33
	s_waitcnt lgkmcnt(0)
	v_sub_f32_e32 v4, v16, v4
	v_sub_f32_e32 v5, v16, v5
	v_min_f32_e32 v4, 0, v4
	v_min_f32_e32 v5, 0, v5
	v_mul_f32_e32 v4, 0x3fb8aa3b, v4
	v_mul_f32_e32 v5, 0x3fb8aa3b, v5
	v_exp_f32_e32 v4, v4
	v_exp_f32_e32 v5, v5
	v_sub_f32_e32 v6, v16, v6
	v_sub_f32_e32 v7, v16, v7
	v_min_f32_e32 v6, 0, v6
	v_min_f32_e32 v7, 0, v7
	v_mul_f32_e32 v6, 0x3fb8aa3b, v6
	v_mul_f32_e32 v7, 0x3fb8aa3b, v7
	v_exp_f32_e32 v6, v6
	v_exp_f32_e32 v7, v7
	v_pk_mul_f32 v[4:5], v[8:9], v[4:5]
	v_pk_mul_f32 v[6:7], v[10:11], v[6:7]
	v_cvt_pk_bf16_f32 v4, v4, v5
	v_cndmask_b32_e32 v5, 0, v4, vcc
	v_lshrrev_b32_e32 v4, 16, v4
	v_cmp_lt_u32_e32 vcc, 48, v33
	s_nop 1
	v_cndmask_b32_e32 v4, 0, v4, vcc
	v_perm_b32 v4, v4, v5, s12
	v_cvt_pk_bf16_f32 v5, v6, v7
	v_cmp_lt_u32_e32 vcc, 49, v33
	s_nop 1
	v_cndmask_b32_e32 v6, 0, v5, vcc
	v_lshrrev_b32_e32 v5, 16, v5
	v_cmp_lt_u32_e32 vcc, 50, v33
	s_nop 1
	v_cndmask_b32_e32 v5, 0, v5, vcc
	v_perm_b32 v5, v5, v6, s12
	global_store_dwordx4 v32, v[2:5], s[64:65] offset:1024
	ds_read_b128 v[2:5], v76 offset:16608
	v_cmp_lt_u32_e32 vcc, 55, v33
	s_waitcnt lgkmcnt(0)
	v_sub_f32_e32 v2, v16, v2
	v_sub_f32_e32 v3, v16, v3
	v_min_f32_e32 v2, 0, v2
	v_min_f32_e32 v3, 0, v3
	v_mul_f32_e32 v2, 0x3fb8aa3b, v2
	v_mul_f32_e32 v3, 0x3fb8aa3b, v3
	v_exp_f32_e32 v2, v2
	v_exp_f32_e32 v3, v3
	v_sub_f32_e32 v4, v16, v4
	v_sub_f32_e32 v5, v16, v5
	v_min_f32_e32 v4, 0, v4
	v_min_f32_e32 v5, 0, v5
	v_mul_f32_e32 v4, 0x3fb8aa3b, v4
	v_mul_f32_e32 v5, 0x3fb8aa3b, v5
	v_exp_f32_e32 v4, v4
	v_exp_f32_e32 v5, v5
	v_pk_mul_f32 v[2:3], v[12:13], v[2:3]
	v_pk_mul_f32 v[4:5], v[14:15], v[4:5]
	v_cvt_pk_bf16_f32 v2, v2, v3
	v_cndmask_b32_e32 v3, 0, v2, vcc
	v_cmp_lt_u32_e32 vcc, 56, v33
	s_nop 1
	v_cndmask_b32_sdwa v2, v113, v2, vcc dst_sel:DWORD dst_unused:UNUSED_PAD src0_sel:DWORD src1_sel:WORD_1
	v_perm_b32 v2, v2, v3, s12
	v_cvt_pk_bf16_f32 v3, v4, v5
	v_cmp_lt_u32_e32 vcc, 57, v33
	s_nop 1
	v_cndmask_b32_e32 v4, 0, v3, vcc
	v_cmp_lt_u32_e32 vcc, 58, v33
	s_nop 1
	v_cndmask_b32_sdwa v3, v113, v3, vcc dst_sel:DWORD dst_unused:UNUSED_PAD src0_sel:DWORD src1_sel:WORD_1
	v_perm_b32 v3, v3, v4, s12
	global_store_dwordx4 v32, v[0:3], s[64:65] offset:1536
.LBB0_417:
	s_andn2_b64 vcc, exec, s[6:7]
	s_cbranch_vccnz .LBB0_419
	s_waitcnt vmcnt(15)
	v_lshlrev_b32_e32 v0, 3, v75
	v_lshlrev_b32_e32 v1, 8, v73
	v_lshlrev_b32_e32 v0, 1, v0
	s_waitcnt vmcnt(11)
	v_add3_u32 v25, s27, v1, v0
	s_waitcnt vmcnt(10)
	ds_read_b128 v[26:29], v25 offset:17408
	ds_read_b128 v[30:33], v25 offset:17440
	ds_read_b128 v[34:37], v25 offset:17472
	ds_read_b128 v[38:41], v25 offset:17504
	s_waitcnt lgkmcnt(3)
	v_mfma_f32_32x32x16_bf16 v[0:15], v[26:29], v[26:29], 0
	s_waitcnt vmcnt(8)
	v_lshl_add_u32 v16, v75, 10, s27
	s_movk_i32 s2, 0xfc10
	v_mad_i32_i24 v96, v75, s2, v16
	ds_read_b32 v17, v96 offset:16640
	v_lshl_add_u32 v24, v73, 2, v16
	v_sub_u32_e32 v16, v47, v73
	v_cmp_lt_i32_e32 vcc, 0, v16
	s_waitcnt lgkmcnt(0)
	v_mfma_f32_32x32x16_bf16 v[0:15], v[30:33], v[30:33], v[0:15]
	s_movk_i32 s2, 0xffe1
	v_sub_u32_e32 v47, v47, v71
	v_mfma_f32_32x32x16_bf16 v[0:15], v[34:37], v[34:37], v[0:15]
	v_mfma_f32_32x32x16_bf16 v[0:15], v[38:41], v[38:41], v[0:15]
	s_nop 10
	v_mul_f32_e32 v0, v0, v17
	ds_read_b32 v17, v96 offset:16384
	s_waitcnt lgkmcnt(0)
	v_sub_f32_e32 v17, v17, v74
	v_min_f32_e32 v17, 0, v17
	v_mul_f32_e32 v17, 0x3fb8aa3b, v17
	v_exp_f32_e32 v17, v17
	s_nop 0
	v_mul_f32_e32 v0, v0, v17
	v_cndmask_b32_e32 v0, 0, v0, vcc
	ds_write_b32 v24, v0
	ds_read_b32 v0, v96 offset:16644
	v_cmp_gt_u32_e32 vcc, s2, v16
	s_movk_i32 s2, 0xffef
	s_waitcnt lgkmcnt(0)
	v_mul_f32_e32 v0, v1, v0
	ds_read_b32 v1, v96 offset:16388
	s_waitcnt lgkmcnt(0)
	v_sub_f32_e32 v1, v1, v74
	v_min_f32_e32 v1, 0, v1
	v_mul_f32_e32 v1, 0x3fb8aa3b, v1
	v_exp_f32_e32 v1, v1
	s_nop 0
	v_mul_f32_e32 v0, v0, v1
	v_cndmask_b32_e32 v0, 0, v0, vcc
	ds_write_b32 v24, v0 offset:256
	ds_read_b32 v0, v96 offset:16648
	ds_read_b32 v1, v96 offset:16392
	v_cmp_lt_i32_e32 vcc, -2, v16
	s_waitcnt lgkmcnt(0)
	v_mul_f32_e32 v0, v2, v0
	v_sub_f32_e32 v1, v1, v74
	v_min_f32_e32 v1, 0, v1
	v_mul_f32_e32 v1, 0x3fb8aa3b, v1
	v_exp_f32_e32 v1, v1
	s_nop 0
	v_mul_f32_e32 v0, v0, v1
	v_cndmask_b32_e32 v0, 0, v0, vcc
	ds_write_b32 v24, v0 offset:512
	ds_read_b32 v0, v96 offset:16652
	ds_read_b32 v1, v96 offset:16396
	v_cmp_lt_i32_e32 vcc, -3, v16
	s_waitcnt lgkmcnt(0)
	v_mul_f32_e32 v0, v3, v0
	v_sub_f32_e32 v1, v1, v74
	v_min_f32_e32 v1, 0, v1
	v_mul_f32_e32 v1, 0x3fb8aa3b, v1
	v_exp_f32_e32 v1, v1
	s_nop 0
	v_mul_f32_e32 v0, v0, v1
	v_cndmask_b32_e32 v0, 0, v0, vcc
	ds_write_b32 v24, v0 offset:768
	ds_read_b32 v0, v96 offset:16672
	ds_read_b32 v1, v96 offset:16416
	v_cmp_lt_i32_e32 vcc, -8, v16
	s_waitcnt lgkmcnt(0)
	v_mul_f32_e32 v0, v4, v0
	v_sub_f32_e32 v1, v1, v74
	v_min_f32_e32 v1, 0, v1
	v_mul_f32_e32 v1, 0x3fb8aa3b, v1
	v_exp_f32_e32 v1, v1
	s_nop 0
	v_mul_f32_e32 v0, v0, v1
	v_cndmask_b32_e32 v0, 0, v0, vcc
	ds_write_b32 v24, v0 offset:2048
	ds_read_b32 v0, v96 offset:16676
	ds_read_b32 v1, v96 offset:16420
	v_cmp_lt_i32_e32 vcc, -9, v16
	s_waitcnt lgkmcnt(0)
	v_mul_f32_e32 v0, v5, v0
	v_sub_f32_e32 v1, v1, v74
	v_min_f32_e32 v1, 0, v1
	v_mul_f32_e32 v1, 0x3fb8aa3b, v1
	v_exp_f32_e32 v1, v1
	s_nop 0
	v_mul_f32_e32 v0, v0, v1
	v_cndmask_b32_e32 v0, 0, v0, vcc
	ds_write_b32 v24, v0 offset:2304
	ds_read_b32 v0, v96 offset:16680
	ds_read_b32 v1, v96 offset:16424
	v_cmp_lt_i32_e32 vcc, -10, v16
	s_waitcnt lgkmcnt(0)
	v_mul_f32_e32 v0, v6, v0
	v_sub_f32_e32 v1, v1, v74
	v_min_f32_e32 v1, 0, v1
	v_mul_f32_e32 v1, 0x3fb8aa3b, v1
	v_exp_f32_e32 v1, v1
	s_nop 0
	v_mul_f32_e32 v0, v0, v1
	v_cndmask_b32_e32 v0, 0, v0, vcc
	ds_write_b32 v24, v0 offset:2560
	ds_read_b32 v0, v96 offset:16684
	ds_read_b32 v1, v96 offset:16428
	v_cmp_lt_i32_e32 vcc, -11, v16
	s_waitcnt lgkmcnt(0)
	v_mul_f32_e32 v0, v7, v0
	v_sub_f32_e32 v1, v1, v74
	v_min_f32_e32 v1, 0, v1
	v_mul_f32_e32 v1, 0x3fb8aa3b, v1
	v_exp_f32_e32 v1, v1
	s_nop 0
	v_mul_f32_e32 v0, v0, v1
	v_cndmask_b32_e32 v0, 0, v0, vcc
	ds_write_b32 v24, v0 offset:2816
	ds_read_b32 v0, v96 offset:16704
	ds_read_b32 v1, v96 offset:16448
	v_cmp_lt_i32_e32 vcc, -16, v16
	s_waitcnt lgkmcnt(0)
	v_mul_f32_e32 v0, v8, v0
	v_sub_f32_e32 v1, v1, v74
	v_min_f32_e32 v1, 0, v1
	v_mul_f32_e32 v1, 0x3fb8aa3b, v1
	v_exp_f32_e32 v1, v1
	s_nop 0
	v_mul_f32_e32 v0, v0, v1
	v_cndmask_b32_e32 v0, 0, v0, vcc
	ds_write_b32 v24, v0 offset:4096
	ds_read_b32 v0, v96 offset:16708
	ds_read_b32 v1, v96 offset:16452
	v_cmp_lt_i32_e32 vcc, s2, v16
	s_movk_i32 s2, 0xffee
	s_waitcnt lgkmcnt(0)
	v_mul_f32_e32 v0, v9, v0
	v_sub_f32_e32 v1, v1, v74
	v_min_f32_e32 v1, 0, v1
	v_mul_f32_e32 v1, 0x3fb8aa3b, v1
	v_exp_f32_e32 v1, v1
	s_nop 0
	v_mul_f32_e32 v0, v0, v1
	v_cndmask_b32_e32 v0, 0, v0, vcc
	ds_write_b32 v24, v0 offset:4352
	ds_read_b32 v0, v96 offset:16712
	ds_read_b32 v1, v96 offset:16456
	v_cmp_lt_i32_e32 vcc, s2, v16
	s_movk_i32 s2, 0xffed
	s_waitcnt lgkmcnt(0)
	v_mul_f32_e32 v0, v10, v0
	v_sub_f32_e32 v1, v1, v74
	v_min_f32_e32 v1, 0, v1
	v_mul_f32_e32 v1, 0x3fb8aa3b, v1
	v_exp_f32_e32 v1, v1
	s_nop 0
	v_mul_f32_e32 v0, v0, v1
	v_cndmask_b32_e32 v0, 0, v0, vcc
	ds_write_b32 v24, v0 offset:4608
	ds_read_b32 v0, v96 offset:16716
	ds_read_b32 v1, v96 offset:16460
	v_cmp_lt_i32_e32 vcc, s2, v16
	s_movk_i32 s2, 0xffe8
	s_waitcnt lgkmcnt(0)
	v_mul_f32_e32 v0, v11, v0
	v_sub_f32_e32 v1, v1, v74
	v_min_f32_e32 v1, 0, v1
	v_mul_f32_e32 v1, 0x3fb8aa3b, v1
	v_exp_f32_e32 v1, v1
	s_nop 0
	v_mul_f32_e32 v0, v0, v1
	v_cndmask_b32_e32 v0, 0, v0, vcc
	ds_write_b32 v24, v0 offset:4864
	ds_read_b32 v0, v96 offset:16736
	ds_read_b32 v1, v96 offset:16480
	v_cmp_lt_i32_e32 vcc, s2, v16
	s_movk_i32 s2, 0xffe7
	s_waitcnt lgkmcnt(0)
	v_mul_f32_e32 v0, v12, v0
	v_sub_f32_e32 v1, v1, v74
	v_min_f32_e32 v1, 0, v1
	v_mul_f32_e32 v1, 0x3fb8aa3b, v1
	v_exp_f32_e32 v1, v1
	s_nop 0
	v_mul_f32_e32 v0, v0, v1
	v_cndmask_b32_e32 v0, 0, v0, vcc
	ds_write_b32 v24, v0 offset:6144
	ds_read_b32 v0, v96 offset:16740
	ds_read_b32 v1, v96 offset:16484
	v_cmp_lt_i32_e32 vcc, s2, v16
	s_movk_i32 s2, 0xffe6
	s_waitcnt lgkmcnt(0)
	v_mul_f32_e32 v0, v13, v0
	v_sub_f32_e32 v1, v1, v74
	v_min_f32_e32 v1, 0, v1
	v_mul_f32_e32 v1, 0x3fb8aa3b, v1
	v_exp_f32_e32 v1, v1
	s_nop 0
	v_mul_f32_e32 v0, v0, v1
	v_cndmask_b32_e32 v0, 0, v0, vcc
	ds_write_b32 v24, v0 offset:6400
	ds_read_b32 v0, v96 offset:16744
	ds_read_b32 v1, v96 offset:16488
	v_cmp_lt_i32_e32 vcc, s2, v16
	s_movk_i32 s2, 0xffe5
	s_waitcnt lgkmcnt(0)
	v_mul_f32_e32 v0, v14, v0
	v_sub_f32_e32 v1, v1, v74
	v_min_f32_e32 v1, 0, v1
	v_mul_f32_e32 v1, 0x3fb8aa3b, v1
	v_exp_f32_e32 v1, v1
	s_nop 0
	v_mul_f32_e32 v0, v0, v1
	v_cndmask_b32_e32 v0, 0, v0, vcc
	ds_write_b32 v24, v0 offset:6656
	ds_read_b32 v0, v96 offset:16748
	ds_read_b32 v1, v96 offset:16492
	v_cmp_lt_i32_e32 vcc, s2, v16
	s_movk_i32 s2, 0xffe0
	s_waitcnt lgkmcnt(0)
	v_mul_f32_e32 v0, v15, v0
	v_sub_f32_e32 v1, v1, v74
	v_min_f32_e32 v1, 0, v1
	v_mul_f32_e32 v1, 0x3fb8aa3b, v1
	v_exp_f32_e32 v1, v1
	s_nop 0
	v_mul_f32_e32 v0, v0, v1
	v_cndmask_b32_e32 v0, 0, v0, vcc
	ds_write_b32 v24, v0 offset:6912
	ds_read_b32 v78, v96 offset:16800
	ds_read_b128 v[16:19], v96 offset:16512
	ds_read_b128 v[20:23], v96 offset:16768
	ds_read_b128 v[80:83], v25 offset:25696
	ds_read_b128 v[84:87], v25 offset:25664
	ds_read_b128 v[88:91], v25 offset:25600
	ds_read_b128 v[92:95], v25 offset:25632
	s_waitcnt lgkmcnt(1)
	v_mfma_f32_32x32x16_bf16 v[0:15], v[88:91], v[26:29], 0
	v_sub_f32_e32 v25, v16, v74
	v_min_f32_e32 v25, 0, v25
	v_mul_f32_e32 v25, 0x3fb8aa3b, v25
	v_exp_f32_e32 v25, v25
	v_cmp_lt_u32_e32 vcc, s2, v47
	s_movk_i32 s2, 0xffdf
	ds_read_b32 v72, v72 offset:16512
	s_waitcnt lgkmcnt(0)
	v_mfma_f32_32x32x16_bf16 v[0:15], v[92:95], v[30:33], v[0:15]
	v_sub_f32_e32 v16, v16, v72
	v_min_f32_e32 v16, 0, v16
	v_mul_f32_e32 v16, 0x3fb8aa3b, v16
	v_exp_f32_e32 v16, v16
	v_mfma_f32_32x32x16_bf16 v[0:15], v[84:87], v[34:37], v[0:15]
	v_mfma_f32_32x32x16_bf16 v[0:15], v[80:83], v[38:41], v[0:15]
	s_nop 11
	v_mul_f32_e32 v0, v20, v0
	v_mul_f32_e32 v0, v25, v0
	ds_write_b32 v24, v0 offset:8192
	v_mul_f32_e32 v0, v21, v1
	v_sub_f32_e32 v1, v17, v74
	v_min_f32_e32 v1, 0, v1
	v_mul_f32_e32 v1, 0x3fb8aa3b, v1
	v_exp_f32_e32 v1, v1
	s_nop 0
	v_mul_f32_e32 v0, v1, v0
	v_sub_f32_e32 v1, v18, v74
	v_min_f32_e32 v1, 0, v1
	v_mul_f32_e32 v1, 0x3fb8aa3b, v1
	v_exp_f32_e32 v1, v1
	ds_write_b32 v24, v0 offset:8448
	v_mul_f32_e32 v0, v22, v2
	v_mul_f32_e32 v0, v1, v0
	v_sub_f32_e32 v1, v19, v74
	v_min_f32_e32 v1, 0, v1
	v_mul_f32_e32 v1, 0x3fb8aa3b, v1
	v_exp_f32_e32 v1, v1
	ds_write_b32 v24, v0 offset:8704
	v_mul_f32_e32 v0, v23, v3
	v_mul_f32_e32 v0, v1, v0
	ds_write_b32 v24, v0 offset:8960
	ds_read_b32 v79, v96 offset:16544
	v_mul_f32_e32 v0, v78, v4
	s_waitcnt lgkmcnt(0)
	v_sub_f32_e32 v1, v79, v74
	v_min_f32_e32 v1, 0, v1
	v_mul_f32_e32 v1, 0x3fb8aa3b, v1
	v_exp_f32_e32 v1, v1
	s_nop 0
	v_mul_f32_e32 v0, v0, v1
	ds_write_b32 v24, v0 offset:10240
	ds_read_b32 v76, v96 offset:16804
	ds_read_b32 v77, v96 offset:16548
	s_waitcnt lgkmcnt(0)
	v_mul_f32_e32 v0, v5, v76
	v_sub_f32_e32 v1, v77, v74
	v_min_f32_e32 v1, 0, v1
	v_mul_f32_e32 v1, 0x3fb8aa3b, v1
	v_exp_f32_e32 v1, v1
	s_nop 0
	v_mul_f32_e32 v0, v0, v1
	ds_write_b32 v24, v0 offset:10496
	ds_read_b32 v73, v96 offset:16808
	ds_read_b32 v75, v96 offset:16552
	s_waitcnt lgkmcnt(0)
	v_mul_f32_e32 v0, v6, v73
	v_sub_f32_e32 v1, v75, v74
	v_min_f32_e32 v1, 0, v1
	v_mul_f32_e32 v1, 0x3fb8aa3b, v1
	v_exp_f32_e32 v1, v1
	s_nop 0
	v_mul_f32_e32 v0, v0, v1
	ds_write_b32 v24, v0 offset:10752
	ds_read_b32 v42, v96 offset:16812
	ds_read_b32 v43, v96 offset:16556
	s_waitcnt lgkmcnt(0)
	v_mul_f32_e32 v0, v7, v42
	v_sub_f32_e32 v1, v43, v74
	v_min_f32_e32 v1, 0, v1
	v_mul_f32_e32 v1, 0x3fb8aa3b, v1
	v_exp_f32_e32 v1, v1
	s_nop 0
	v_mul_f32_e32 v0, v0, v1
	ds_write_b32 v24, v0 offset:11008
	ds_read_b32 v40, v96 offset:16832
	ds_read_b32 v41, v96 offset:16576
	s_waitcnt lgkmcnt(0)
	v_mul_f32_e32 v0, v8, v40
	v_sub_f32_e32 v1, v41, v74
	v_min_f32_e32 v1, 0, v1
	v_mul_f32_e32 v1, 0x3fb8aa3b, v1
	v_exp_f32_e32 v1, v1
	s_nop 0
	v_mul_f32_e32 v0, v0, v1
	ds_write_b32 v24, v0 offset:12288
	ds_read_b32 v38, v96 offset:16836
	ds_read_b32 v39, v96 offset:16580
	s_waitcnt lgkmcnt(0)
	v_mul_f32_e32 v0, v9, v38
	v_sub_f32_e32 v1, v39, v74
	v_min_f32_e32 v1, 0, v1
	v_mul_f32_e32 v1, 0x3fb8aa3b, v1
	v_exp_f32_e32 v1, v1
	s_nop 0
	v_mul_f32_e32 v0, v0, v1
	ds_write_b32 v24, v0 offset:12544
	ds_read_b32 v37, v96 offset:16840
	ds_read_b32 v36, v96 offset:16584
	s_waitcnt lgkmcnt(0)
	v_mul_f32_e32 v0, v10, v37
	v_sub_f32_e32 v1, v36, v74
	v_min_f32_e32 v1, 0, v1
	v_mul_f32_e32 v1, 0x3fb8aa3b, v1
	v_exp_f32_e32 v1, v1
	s_nop 0
	v_mul_f32_e32 v0, v0, v1
	ds_write_b32 v24, v0 offset:12800
	ds_read_b32 v35, v96 offset:16844
	ds_read_b32 v34, v96 offset:16588
	s_waitcnt lgkmcnt(0)
	v_mul_f32_e32 v0, v11, v35
	v_sub_f32_e32 v1, v34, v74
	v_min_f32_e32 v1, 0, v1
	v_mul_f32_e32 v1, 0x3fb8aa3b, v1
	v_exp_f32_e32 v1, v1
	s_nop 0
	v_mul_f32_e32 v0, v0, v1
	ds_write_b32 v24, v0 offset:13056
	ds_read_b32 v33, v96 offset:16864
	ds_read_b32 v32, v96 offset:16608
	s_waitcnt lgkmcnt(0)
	v_mul_f32_e32 v0, v12, v33
	v_sub_f32_e32 v1, v32, v74
	v_min_f32_e32 v1, 0, v1
	v_mul_f32_e32 v1, 0x3fb8aa3b, v1
	v_exp_f32_e32 v1, v1
	s_nop 0
	v_mul_f32_e32 v0, v0, v1
	ds_write_b32 v24, v0 offset:14336
	ds_read_b32 v31, v96 offset:16868
	ds_read_b32 v30, v96 offset:16612
	s_waitcnt lgkmcnt(0)
	v_mul_f32_e32 v0, v13, v31
	v_sub_f32_e32 v1, v30, v74
	v_min_f32_e32 v1, 0, v1
	v_mul_f32_e32 v1, 0x3fb8aa3b, v1
	v_exp_f32_e32 v1, v1
	s_nop 0
	v_mul_f32_e32 v0, v0, v1
	ds_write_b32 v24, v0 offset:14592
	ds_read_b32 v29, v96 offset:16872
	ds_read_b32 v28, v96 offset:16616
	s_waitcnt lgkmcnt(0)
	v_mul_f32_e32 v0, v14, v29
	v_sub_f32_e32 v1, v28, v74
	v_min_f32_e32 v1, 0, v1
	v_mul_f32_e32 v1, 0x3fb8aa3b, v1
	v_exp_f32_e32 v1, v1
	s_nop 0
	v_mul_f32_e32 v0, v0, v1
	ds_write_b32 v24, v0 offset:14848
	ds_read_b32 v26, v96 offset:16876
	ds_read_b32 v25, v96 offset:16620
	s_waitcnt lgkmcnt(0)
	v_mul_f32_e32 v0, v15, v26
	v_sub_f32_e32 v1, v25, v74
	v_min_f32_e32 v1, 0, v1
	v_mul_f32_e32 v1, 0x3fb8aa3b, v1
	v_exp_f32_e32 v1, v1
	s_nop 0
	v_mul_f32_e32 v27, v0, v1
	v_mfma_f32_32x32x16_bf16 v[0:15], v[88:91], v[88:91], 0
	v_mfma_f32_32x32x16_bf16 v[0:15], v[92:95], v[92:95], v[0:15]
	v_mfma_f32_32x32x16_bf16 v[0:15], v[84:87], v[84:87], v[0:15]
	v_mfma_f32_32x32x16_bf16 v[0:15], v[80:83], v[80:83], v[0:15]
	s_nop 11
	v_mul_f32_e32 v0, v20, v0
	v_mul_f32_e32 v0, v0, v16
	v_cndmask_b32_e32 v0, 0, v0, vcc
	ds_write_b32 v24, v0 offset:8320
	v_mul_f32_e32 v0, v21, v1
	v_sub_f32_e32 v1, v17, v72
	v_min_f32_e32 v1, 0, v1
	v_mul_f32_e32 v1, 0x3fb8aa3b, v1
	v_exp_f32_e32 v1, v1
	v_cmp_lt_u32_e32 vcc, s2, v47
	s_movk_i32 s2, 0xffde
	v_mul_f32_e32 v0, v0, v1
	v_sub_f32_e32 v1, v18, v72
	v_min_f32_e32 v1, 0, v1
	v_mul_f32_e32 v1, 0x3fb8aa3b, v1
	v_exp_f32_e32 v1, v1
	v_cndmask_b32_e32 v0, 0, v0, vcc
	ds_write_b32 v24, v0 offset:8576
	v_mul_f32_e32 v0, v22, v2
	v_mul_f32_e32 v0, v0, v1
	v_sub_f32_e32 v1, v19, v72
	v_min_f32_e32 v1, 0, v1
	v_mul_f32_e32 v1, 0x3fb8aa3b, v1
	v_exp_f32_e32 v1, v1
	v_cmp_lt_u32_e32 vcc, s2, v47
	s_movk_i32 s2, 0xffdd
	s_nop 0
	v_cndmask_b32_e32 v0, 0, v0, vcc
	ds_write_b32 v24, v0 offset:8832
	v_mul_f32_e32 v0, v23, v3
	v_mul_f32_e32 v0, v0, v1
	v_sub_f32_e32 v1, v79, v72
	v_min_f32_e32 v1, 0, v1
	v_mul_f32_e32 v1, 0x3fb8aa3b, v1
	v_exp_f32_e32 v1, v1
	v_cmp_lt_u32_e32 vcc, s2, v47
	s_movk_i32 s2, 0xffd8
	s_nop 0
	v_cndmask_b32_e32 v0, 0, v0, vcc
	ds_write_b32 v24, v0 offset:9088
	v_mul_f32_e32 v0, v78, v4
	v_mul_f32_e32 v0, v0, v1
	v_sub_f32_e32 v1, v77, v72
	v_min_f32_e32 v1, 0, v1
	v_mul_f32_e32 v1, 0x3fb8aa3b, v1
	v_exp_f32_e32 v1, v1
	v_cmp_lt_u32_e32 vcc, s2, v47
	s_movk_i32 s2, 0xffd7
	s_nop 0
	v_cndmask_b32_e32 v0, 0, v0, vcc
	ds_write_b32 v24, v0 offset:10368
	v_mul_f32_e32 v0, v76, v5
	v_mul_f32_e32 v0, v0, v1
	v_sub_f32_e32 v1, v75, v72
	v_min_f32_e32 v1, 0, v1
	v_mul_f32_e32 v1, 0x3fb8aa3b, v1
	v_exp_f32_e32 v1, v1
	v_cmp_lt_u32_e32 vcc, s2, v47
	s_movk_i32 s2, 0xffd6
	s_nop 0
	v_cndmask_b32_e32 v0, 0, v0, vcc
	ds_write_b32 v24, v0 offset:10624
	v_mul_f32_e32 v0, v73, v6
	v_mul_f32_e32 v0, v0, v1
	v_sub_f32_e32 v1, v43, v72
	v_min_f32_e32 v1, 0, v1
	v_mul_f32_e32 v1, 0x3fb8aa3b, v1
	v_exp_f32_e32 v1, v1
	v_cmp_lt_u32_e32 vcc, s2, v47
	s_movk_i32 s2, 0xffd5
	s_nop 0
	v_cndmask_b32_e32 v0, 0, v0, vcc
	ds_write_b32 v24, v0 offset:10880
	v_mul_f32_e32 v0, v42, v7
	v_mul_f32_e32 v0, v0, v1
	v_sub_f32_e32 v1, v41, v72
	v_min_f32_e32 v1, 0, v1
	v_mul_f32_e32 v1, 0x3fb8aa3b, v1
	v_exp_f32_e32 v1, v1
	v_cmp_lt_u32_e32 vcc, s2, v47
	s_movk_i32 s2, 0xffd0
	s_nop 0
	v_cndmask_b32_e32 v0, 0, v0, vcc
	ds_write_b32 v24, v0 offset:11136
	v_mul_f32_e32 v0, v40, v8
	v_mul_f32_e32 v0, v0, v1
	v_sub_f32_e32 v1, v39, v72
	v_min_f32_e32 v1, 0, v1
	v_mul_f32_e32 v1, 0x3fb8aa3b, v1
	v_exp_f32_e32 v1, v1
	v_cmp_lt_u32_e32 vcc, s2, v47
	s_movk_i32 s2, 0xffcf
	s_nop 0
	v_cndmask_b32_e32 v0, 0, v0, vcc
	ds_write_b32 v24, v0 offset:12416
	v_mul_f32_e32 v0, v38, v9
	v_mul_f32_e32 v0, v0, v1
	v_sub_f32_e32 v1, v36, v72
	v_min_f32_e32 v1, 0, v1
	v_mul_f32_e32 v1, 0x3fb8aa3b, v1
	v_exp_f32_e32 v1, v1
	v_cmp_lt_u32_e32 vcc, s2, v47
	s_movk_i32 s2, 0xffce
	s_nop 0
	v_cndmask_b32_e32 v0, 0, v0, vcc
	ds_write_b32 v24, v0 offset:12672
	v_mul_f32_e32 v0, v37, v10
	v_mul_f32_e32 v0, v0, v1
	v_sub_f32_e32 v1, v34, v72
	v_min_f32_e32 v1, 0, v1
	v_mul_f32_e32 v1, 0x3fb8aa3b, v1
	v_exp_f32_e32 v1, v1
	v_cmp_lt_u32_e32 vcc, s2, v47
	s_movk_i32 s2, 0xffcd
	s_nop 0
	v_cndmask_b32_e32 v0, 0, v0, vcc
	ds_write_b32 v24, v0 offset:12928
	v_mul_f32_e32 v0, v35, v11
	v_mul_f32_e32 v0, v0, v1
	v_sub_f32_e32 v1, v32, v72
	v_min_f32_e32 v1, 0, v1
	v_mul_f32_e32 v1, 0x3fb8aa3b, v1
	v_exp_f32_e32 v1, v1
	v_cmp_lt_u32_e32 vcc, s2, v47
	s_movk_i32 s2, 0xffc8
	s_nop 0
	v_cndmask_b32_e32 v0, 0, v0, vcc
	ds_write_b32 v24, v0 offset:13184
	v_mul_f32_e32 v0, v33, v12
	v_mul_f32_e32 v0, v0, v1
	v_sub_f32_e32 v1, v30, v72
	v_min_f32_e32 v1, 0, v1
	v_mul_f32_e32 v1, 0x3fb8aa3b, v1
	v_exp_f32_e32 v1, v1
	v_cmp_lt_u32_e32 vcc, s2, v47
	s_movk_i32 s2, 0xffc7
	s_nop 0
	v_cndmask_b32_e32 v0, 0, v0, vcc
	ds_write_b32 v24, v0 offset:14464
	v_mul_f32_e32 v0, v31, v13
	v_mul_f32_e32 v0, v0, v1
	v_sub_f32_e32 v1, v28, v72
	v_min_f32_e32 v1, 0, v1
	v_mul_f32_e32 v1, 0x3fb8aa3b, v1
	v_exp_f32_e32 v1, v1
	v_cmp_lt_u32_e32 vcc, s2, v47
	s_movk_i32 s2, 0xffc6
	s_nop 0
	v_cndmask_b32_e32 v0, 0, v0, vcc
	ds_write_b32 v24, v0 offset:14720
	v_mul_f32_e32 v0, v29, v14
	v_mul_f32_e32 v0, v0, v1
	v_cmp_lt_u32_e32 vcc, s2, v47
	v_add_u32_e32 v1, 0x3800, v24
	s_movk_i32 s2, 0xffc5
	v_cndmask_b32_e32 v0, 0, v0, vcc
	ds_write2_b32 v1, v0, v27 offset0:160 offset1:192
	v_sub_f32_e32 v1, v25, v72
	v_min_f32_e32 v1, 0, v1
	v_mul_f32_e32 v1, 0x3fb8aa3b, v1
	v_exp_f32_e32 v1, v1
	v_mul_f32_e32 v0, v26, v15
	v_cmp_lt_u32_e32 vcc, s2, v47
	v_mul_f32_e32 v0, v0, v1
	s_nop 0
	v_cndmask_b32_e32 v0, 0, v0, vcc
	ds_write_b32 v24, v0 offset:15232
.LBB0_419:
	v_lshl_add_u32 v7, v69, 2, s27
	s_waitcnt vmcnt(10)
	v_add_u32_e32 v30, 0x4000, v7
	s_waitcnt lgkmcnt(0)
	s_barrier
	ds_read2_b32 v[12:13], v30 offset0:128 offset1:144
	s_waitcnt vmcnt(7)
	v_lshlrev_b32_e32 v0, 16, v62
	v_and_b32_e32 v1, 0xffff0000, v62
	v_lshlrev_b32_e32 v2, 16, v63
	v_and_b32_e32 v3, 0xffff0000, v63
	s_waitcnt lgkmcnt(0)
	v_pk_mul_f32 v[0:1], v[12:13], v[0:1] op_sel_hi:[0,1]
	v_pk_mul_f32 v[2:3], v[12:13], v[2:3] op_sel_hi:[0,1]
	v_cvt_pk_bf16_f32 v0, v0, v1
	v_cvt_pk_bf16_f32 v1, v2, v3
	s_waitcnt vmcnt(6)
	v_lshlrev_b32_e32 v2, 16, v60
	v_and_b32_e32 v3, 0xffff0000, v60
	v_lshlrev_b32_e32 v4, 16, v61
	v_and_b32_e32 v5, 0xffff0000, v61
	s_add_u32 s64, s40, 0x2000
	v_pk_mul_f32 v[2:3], v[12:13], v[2:3] op_sel_hi:[0,1]
	v_pk_mul_f32 v[4:5], v[12:13], v[4:5] op_sel_hi:[0,1]
	s_addc_u32 s65, s41, 0
	v_lshlrev_b32_e32 v112, 4, v65
	v_cvt_pk_bf16_f32 v2, v2, v3
	v_cvt_pk_bf16_f32 v3, v4, v5
	global_store_dwordx4 v112, v[0:3], s[64:65]
	v_or_b32_e32 v6, v70, v68
	v_lshl_add_u32 v11, v6, 2, s27
	v_lshlrev_b32_e32 v0, 1, v69
	v_sub_u32_e32 v10, v7, v0
	v_lshl_add_u32 v12, v6, 8, v10
	ds_read_u16 v0, v12 offset:17408
	ds_read_u16 v1, v12 offset:17664
	ds_read_b64 v[2:3], v11 offset:17152
	v_add_u32_e32 v26, 0x4000, v11
	s_add_u32 s6, s40, 0x6000
	s_waitcnt lgkmcnt(0)
	v_lshlrev_b32_e32 v0, 16, v0
	v_lshlrev_b32_e32 v1, 16, v1
	v_pk_mul_f32 v[14:15], v[2:3], v[0:1]
	ds_read_u16 v0, v12 offset:17920
	ds_read_u16 v1, v12 offset:18176
	v_mov_b32_e32 v9, s27
	v_cvt_pk_bf16_f32 v14, v14, v15
	v_mov_b32_e32 v8, v13
	s_waitcnt lgkmcnt(0)
	v_lshlrev_b32_e32 v4, 16, v0
	v_lshlrev_b32_e32 v5, 16, v1
	ds_read_b128 v[0:3], v11 offset:17152
	s_addc_u32 s7, s41, 0
	v_cmp_gt_u32_e32 vcc, 64, v65
	s_waitcnt lgkmcnt(0)
	v_pk_mul_f32 v[16:17], v[2:3], v[4:5]
	ds_read_u16 v2, v12 offset:21504
	ds_read_u16 v3, v12 offset:21760
	v_cvt_pk_bf16_f32 v15, v16, v17
	s_waitcnt lgkmcnt(0)
	v_lshlrev_b32_e32 v6, 16, v2
	v_lshlrev_b32_e32 v7, 16, v3
	ds_read2_b64 v[2:5], v26 offset0:97 offset1:104
	s_waitcnt lgkmcnt(0)
	v_pk_mul_f32 v[18:19], v[4:5], v[6:7]
	ds_read_u16 v4, v12 offset:22016
	ds_read_u16 v5, v12 offset:22272
	v_cvt_pk_bf16_f32 v16, v18, v19
	s_waitcnt lgkmcnt(0)
	v_lshlrev_b32_e32 v20, 16, v4
	v_lshlrev_b32_e32 v21, 16, v5
	ds_read_b128 v[4:7], v11 offset:17216
	s_waitcnt lgkmcnt(0)
	v_pk_mul_f32 v[6:7], v[6:7], v[20:21]
	s_nop 0
	v_cvt_pk_bf16_f32 v17, v6, v7
	s_waitcnt vmcnt(6)
	v_lshlrev_b32_e32 v6, 16, v58
	v_and_b32_e32 v7, 0xffff0000, v58
	v_pk_mul_f32 v[6:7], v[8:9], v[6:7] op_sel_hi:[0,1]
	global_store_dwordx4 v112, v[14:17], s[6:7]
	s_nop 1
	v_cvt_pk_bf16_f32 v14, v6, v7
	v_lshlrev_b32_e32 v6, 16, v59
	v_and_b32_e32 v7, 0xffff0000, v59
	v_pk_mul_f32 v[6:7], v[8:9], v[6:7] op_sel_hi:[0,1]
	v_cvt_pk_bf16_f32 v15, v6, v7
	s_waitcnt vmcnt(6)
	v_lshlrev_b32_e32 v6, 16, v56
	v_and_b32_e32 v7, 0xffff0000, v56
	v_pk_mul_f32 v[6:7], v[8:9], v[6:7] op_sel_hi:[0,1]
	v_cvt_pk_bf16_f32 v16, v6, v7
	v_lshlrev_b32_e32 v6, 16, v57
	v_and_b32_e32 v7, 0xffff0000, v57
	v_pk_mul_f32 v[6:7], v[8:9], v[6:7] op_sel_hi:[0,1]
	v_cvt_pk_bf16_f32 v17, v6, v7
	ds_read_u16 v6, v12 offset:17696
	v_or_b32_e32 v8, 0x800, v112
	global_store_dwordx4 v8, v[14:17], s[64:65]
	s_waitcnt lgkmcnt(0)
	v_lshlrev_b32_e32 v7, 16, v6
	ds_read_u16 v6, v12 offset:17440
	ds_read_u16 v13, v12 offset:17472
	ds_read2_b64 v[14:17], v26 offset0:96 offset1:97
	ds_read_u16 v18, v12 offset:17952
	ds_read_u16 v19, v12 offset:18208
	s_waitcnt lgkmcnt(0)
	v_lshlrev_b32_e32 v6, 16, v6
	v_lshlrev_b32_e32 v18, 16, v18
	v_lshlrev_b32_e32 v19, 16, v19
	v_pk_mul_f32 v[24:25], v[16:17], v[18:19]
	ds_read_u16 v18, v12 offset:21536
	ds_read_u16 v19, v12 offset:21792
	v_pk_mul_f32 v[6:7], v[14:15], v[6:7]
	s_waitcnt lgkmcnt(0)
	v_lshlrev_b32_e32 v22, 16, v18
	v_lshlrev_b32_e32 v23, 16, v19
	ds_read2_b64 v[18:21], v26 offset0:104 offset1:105
	s_waitcnt lgkmcnt(0)
	v_pk_mul_f32 v[26:27], v[18:19], v[22:23]
	ds_read_u16 v22, v12 offset:22048
	ds_read_u16 v23, v12 offset:22304
	s_waitcnt lgkmcnt(0)
	v_lshlrev_b32_e32 v22, 16, v22
	v_lshlrev_b32_e32 v23, 16, v23
	v_pk_mul_f32 v[28:29], v[20:21], v[22:23]
	v_cvt_pk_bf16_f32 v22, v6, v7
	ds_read2_b32 v[6:7], v30 offset0:160 offset1:176
	v_cvt_pk_bf16_f32 v23, v24, v25
	v_cvt_pk_bf16_f32 v24, v26, v27
	v_cvt_pk_bf16_f32 v25, v28, v29
	global_store_dwordx4 v8, v[22:25], s[6:7]
	ds_read_u16 v8, v12 offset:17728
	s_waitcnt vmcnt(6)
	v_lshlrev_b32_e32 v26, 16, v53
	v_lshlrev_b32_e32 v22, 16, v54
	v_and_b32_e32 v23, 0xffff0000, v54
	v_lshlrev_b32_e32 v24, 16, v55
	v_and_b32_e32 v25, 0xffff0000, v55
	s_waitcnt lgkmcnt(0)
	v_pk_mul_f32 v[22:23], v[6:7], v[22:23] op_sel_hi:[0,1]
	v_pk_mul_f32 v[24:25], v[6:7], v[24:25] op_sel_hi:[0,1]
	v_cvt_pk_bf16_f32 v22, v22, v23
	v_cvt_pk_bf16_f32 v23, v24, v25
	v_lshlrev_b32_e32 v24, 16, v52
	v_and_b32_e32 v25, 0xffff0000, v52
	v_and_b32_e32 v27, 0xffff0000, v53
	v_pk_mul_f32 v[24:25], v[6:7], v[24:25] op_sel_hi:[0,1]
	v_pk_mul_f32 v[26:27], v[6:7], v[26:27] op_sel_hi:[0,1]
	v_cvt_pk_bf16_f32 v24, v24, v25
	v_cvt_pk_bf16_f32 v25, v26, v27
	v_or_b32_e32 v6, 0x1000, v112
	global_store_dwordx4 v6, v[22:25], s[64:65]
	s_nop 0
	v_lshlrev_b32_e32 v23, 16, v8
	v_lshlrev_b32_e32 v22, 16, v13
	ds_read_u16 v8, v12 offset:17984
	ds_read_u16 v13, v12 offset:18240
	v_pk_mul_f32 v[14:15], v[14:15], v[22:23]
	s_waitcnt lgkmcnt(0)
	v_lshlrev_b32_e32 v22, 16, v8
	v_lshlrev_b32_e32 v23, 16, v13
	ds_read_u16 v8, v12 offset:21568
	ds_read_u16 v13, v12 offset:21824
	v_pk_mul_f32 v[16:17], v[16:17], v[22:23]
	v_cvt_pk_bf16_f32 v14, v14, v15
	v_cvt_pk_bf16_f32 v15, v16, v17
	s_waitcnt lgkmcnt(0)
	v_lshlrev_b32_e32 v22, 16, v8
	v_lshlrev_b32_e32 v23, 16, v13
	ds_read_u16 v8, v12 offset:22080
	ds_read_u16 v13, v12 offset:22336
	v_pk_mul_f32 v[18:19], v[18:19], v[22:23]
	s_waitcnt lgkmcnt(0)
	v_lshlrev_b32_e32 v22, 16, v8
	v_lshlrev_b32_e32 v23, 16, v13
	v_pk_mul_f32 v[20:21], v[20:21], v[22:23]
	v_cvt_pk_bf16_f32 v16, v18, v19
	v_cvt_pk_bf16_f32 v17, v20, v21
	global_store_dwordx4 v6, v[14:17], s[6:7]
	v_mov_b32_e32 v8, v7
	s_waitcnt vmcnt(6)
	v_lshlrev_b32_e32 v18, 16, v49
	v_lshlrev_b32_e32 v14, 16, v50
	v_and_b32_e32 v15, 0xffff0000, v50
	v_lshlrev_b32_e32 v16, 16, v51
	v_and_b32_e32 v17, 0xffff0000, v51
	v_pk_mul_f32 v[14:15], v[8:9], v[14:15] op_sel_hi:[0,1]
	v_pk_mul_f32 v[16:17], v[8:9], v[16:17] op_sel_hi:[0,1]
	v_cvt_pk_bf16_f32 v14, v14, v15
	v_cvt_pk_bf16_f32 v15, v16, v17
	v_lshlrev_b32_e32 v16, 16, v48
	v_and_b32_e32 v17, 0xffff0000, v48
	v_and_b32_e32 v19, 0xffff0000, v49
	v_pk_mul_f32 v[16:17], v[8:9], v[16:17] op_sel_hi:[0,1]
	v_pk_mul_f32 v[18:19], v[8:9], v[18:19] op_sel_hi:[0,1]
	v_cvt_pk_bf16_f32 v16, v16, v17
	v_cvt_pk_bf16_f32 v17, v18, v19
	v_or_b32_e32 v8, 0x1800, v112
	global_store_dwordx4 v8, v[14:17], s[64:65]
	ds_read_u16 v7, v12 offset:17504
	ds_read_u16 v13, v12 offset:17760
	s_waitcnt lgkmcnt(0)
	v_lshlrev_b32_e32 v14, 16, v7
	v_lshlrev_b32_e32 v15, 16, v13
	ds_read_u16 v7, v12 offset:18016
	ds_read_u16 v13, v12 offset:18272
	v_pk_mul_f32 v[0:1], v[0:1], v[14:15]
	s_waitcnt lgkmcnt(0)
	v_lshlrev_b32_e32 v14, 16, v7
	v_lshlrev_b32_e32 v15, 16, v13
	ds_read_u16 v7, v12 offset:21600
	ds_read_u16 v13, v12 offset:21856
	v_pk_mul_f32 v[2:3], v[2:3], v[14:15]
	v_cvt_pk_bf16_f32 v0, v0, v1
	v_cvt_pk_bf16_f32 v1, v2, v3
	s_waitcnt lgkmcnt(0)
	v_lshlrev_b32_e32 v14, 16, v7
	v_lshlrev_b32_e32 v15, 16, v13
	ds_read_u16 v7, v12 offset:22112
	ds_read_u16 v12, v12 offset:22368
	v_pk_mul_f32 v[4:5], v[4:5], v[14:15]
	ds_read_b64 v[14:15], v11 offset:17224
	v_cvt_pk_bf16_f32 v2, v4, v5
	s_waitcnt lgkmcnt(0)
	v_lshlrev_b32_e32 v13, 16, v12
	v_lshlrev_b32_e32 v12, 16, v7
	v_pk_mul_f32 v[12:13], v[14:15], v[12:13]
	v_mov_b32_e32 v7, 1.0
	v_cvt_pk_bf16_f32 v3, v12, v13
	global_store_dwordx4 v8, v[0:3], s[6:7]
	s_nop 1
	v_lshl_add_u32 v0, v65, 1, s27
	ds_read_u16 v4, v0 offset:17408
	ds_read_b32 v5, v9 offset:16640
	v_mov_b32_e32 v9, 1.0
	s_and_saveexec_b64 s[6:7], vcc
	v_mov_b32_e32 v1, s27
	ds_read_b32 v9, v1 offset:16896
	s_or_b64 exec, exec, s[6:7]
	v_mov_b32_e32 v1, s27
	ds_read_u16 v14, v0 offset:17664
	ds_read_b32 v15, v1 offset:16644
	s_and_saveexec_b64 s[6:7], vcc
	v_mov_b32_e32 v1, s27
	ds_read_b32 v7, v1 offset:16900
	s_or_b64 exec, exec, s[6:7]
	v_mov_b32_e32 v1, s27
	ds_read_u16 v25, v0 offset:17920
	ds_read_b32 v106, v1 offset:16648
	v_mov_b32_e32 v11, 1.0
	v_mov_b32_e32 v13, 1.0
	s_and_saveexec_b64 s[6:7], vcc
	v_mov_b32_e32 v1, s27
	ds_read_b32 v13, v1 offset:16904
	s_or_b64 exec, exec, s[6:7]
	v_mov_b32_e32 v1, s27
	ds_read_u16 v114, v0 offset:18176
	ds_read_b32 v115, v1 offset:16652
	s_and_saveexec_b64 s[6:7], vcc
	v_mov_b32_e32 v1, s27
	ds_read_b32 v11, v1 offset:16908
	s_or_b64 exec, exec, s[6:7]
	v_mov_b32_e32 v1, s27
	ds_read_u16 v116, v0 offset:18432
	ds_read_b32 v117, v1 offset:16656
	v_mov_b32_e32 v17, 1.0
	v_mov_b32_e32 v22, 1.0
	s_and_saveexec_b64 s[6:7], vcc
	v_mov_b32_e32 v1, s27
	ds_read_b32 v22, v1 offset:16912
	s_or_b64 exec, exec, s[6:7]
	v_mov_b32_e32 v1, s27
	ds_read_u16 v118, v0 offset:18688
	ds_read_b32 v119, v1 offset:16660
	s_and_saveexec_b64 s[6:7], vcc
	v_mov_b32_e32 v1, s27
	ds_read_b32 v17, v1 offset:16916
	s_or_b64 exec, exec, s[6:7]
	v_mov_b32_e32 v1, s27
	ds_read_u16 v121, v0 offset:18944
	ds_read_b32 v122, v1 offset:16664
	v_mov_b32_e32 v18, 1.0
	v_mov_b32_e32 v108, 1.0
	s_and_saveexec_b64 s[6:7], vcc
	v_mov_b32_e32 v1, s27
	ds_read_b32 v108, v1 offset:16920
	s_or_b64 exec, exec, s[6:7]
	v_mov_b32_e32 v1, s27
	ds_read_u16 v123, v0 offset:19200
	ds_read_b32 v124, v1 offset:16668
	s_and_saveexec_b64 s[6:7], vcc
	v_mov_b32_e32 v1, s27
	ds_read_b32 v18, v1 offset:16924
	s_or_b64 exec, exec, s[6:7]
	v_mov_b32_e32 v1, s27
	ds_read_u16 v125, v0 offset:19456
	ds_read_b32 v126, v1 offset:16672
	v_mov_b32_e32 v19, 1.0
	v_mov_b32_e32 v111, 1.0
	s_and_saveexec_b64 s[6:7], vcc
	v_mov_b32_e32 v1, s27
	ds_read_b32 v111, v1 offset:16928
	s_or_b64 exec, exec, s[6:7]
	v_mov_b32_e32 v1, s27
	ds_read_u16 v127, v0 offset:19712
	ds_read_b32 v128, v1 offset:16676
	s_and_saveexec_b64 s[6:7], vcc
	v_mov_b32_e32 v1, s27
	ds_read_b32 v19, v1 offset:16932
	s_or_b64 exec, exec, s[6:7]
	v_mov_b32_e32 v1, s27
	ds_read_u16 v130, v0 offset:19968
	ds_read_b32 v131, v1 offset:16680
	v_mov_b32_e32 v20, 1.0
	v_mov_b32_e32 v109, 1.0
	s_and_saveexec_b64 s[6:7], vcc
	v_mov_b32_e32 v1, s27
	ds_read_b32 v109, v1 offset:16936
	s_or_b64 exec, exec, s[6:7]
	v_mov_b32_e32 v1, s27
	ds_read_u16 v132, v0 offset:20224
	ds_read_b32 v133, v1 offset:16684
	s_and_saveexec_b64 s[6:7], vcc
	v_mov_b32_e32 v1, s27
	ds_read_b32 v20, v1 offset:16940
	s_or_b64 exec, exec, s[6:7]
	v_mov_b32_e32 v1, s27
	ds_read_u16 v134, v0 offset:20480
	ds_read_b32 v135, v1 offset:16688
	v_mov_b32_e32 v24, 1.0
	v_mov_b32_e32 v107, 1.0
	s_and_saveexec_b64 s[6:7], vcc
	v_mov_b32_e32 v1, s27
	ds_read_b32 v107, v1 offset:16944
	s_or_b64 exec, exec, s[6:7]
	v_mov_b32_e32 v1, s27
	ds_read_u16 v137, v0 offset:20736
	ds_read_b32 v138, v1 offset:16692
	s_and_saveexec_b64 s[6:7], vcc
	v_mov_b32_e32 v1, s27
	ds_read_b32 v24, v1 offset:16948
	s_or_b64 exec, exec, s[6:7]
	v_mov_b32_e32 v1, s27
	ds_read_u16 v139, v0 offset:20992
	ds_read_b32 v140, v1 offset:16696
	v_mov_b32_e32 v27, 1.0
	v_mov_b32_e32 v26, 1.0
	s_and_saveexec_b64 s[6:7], vcc
	v_mov_b32_e32 v1, s27
	ds_read_b32 v26, v1 offset:16952
	s_or_b64 exec, exec, s[6:7]
	v_mov_b32_e32 v1, s27
	ds_read_u16 v141, v0 offset:21248
	ds_read_b32 v142, v1 offset:16700
	s_and_saveexec_b64 s[6:7], vcc
	v_mov_b32_e32 v1, s27
	ds_read_b32 v27, v1 offset:16956
	s_or_b64 exec, exec, s[6:7]
	v_mov_b32_e32 v1, s27
	ds_read_u16 v144, v0 offset:21504
	ds_read_b32 v145, v1 offset:16704
	v_mov_b32_e32 v31, 1.0
	v_mov_b32_e32 v30, 1.0
	s_and_saveexec_b64 s[6:7], vcc
	v_mov_b32_e32 v1, s27
	ds_read_b32 v30, v1 offset:16960
	s_or_b64 exec, exec, s[6:7]
	v_mov_b32_e32 v1, s27
	ds_read_u16 v146, v0 offset:21760
	ds_read_b32 v147, v1 offset:16708
	s_and_saveexec_b64 s[6:7], vcc
	v_mov_b32_e32 v1, s27
	ds_read_b32 v31, v1 offset:16964
	s_or_b64 exec, exec, s[6:7]
	v_mov_b32_e32 v1, s27
	ds_read_u16 v148, v0 offset:22016
	ds_read_b32 v149, v1 offset:16712
	v_mov_b32_e32 v34, 1.0
	v_mov_b32_e32 v32, 1.0
	s_and_saveexec_b64 s[6:7], vcc
	v_mov_b32_e32 v1, s27
	ds_read_b32 v32, v1 offset:16968
	s_or_b64 exec, exec, s[6:7]
	v_mov_b32_e32 v1, s27
	ds_read_u16 v151, v0 offset:22272
	ds_read_b32 v152, v1 offset:16716
	s_and_saveexec_b64 s[6:7], vcc
	v_mov_b32_e32 v1, s27
	ds_read_b32 v34, v1 offset:16972
	s_or_b64 exec, exec, s[6:7]
	v_mov_b32_e32 v1, s27
	ds_read_u16 v153, v0 offset:22528
	ds_read_b32 v154, v1 offset:16720
	v_mov_b32_e32 v38, 1.0
	v_mov_b32_e32 v36, 1.0
	s_and_saveexec_b64 s[6:7], vcc
	v_mov_b32_e32 v1, s27
	ds_read_b32 v36, v1 offset:16976
	s_or_b64 exec, exec, s[6:7]
	v_mov_b32_e32 v1, s27
	ds_read_u16 v156, v0 offset:22784
	ds_read_b32 v157, v1 offset:16724
	s_and_saveexec_b64 s[6:7], vcc
	v_mov_b32_e32 v1, s27
	ds_read_b32 v38, v1 offset:16980
	s_or_b64 exec, exec, s[6:7]
	v_mov_b32_e32 v1, s27
	ds_read_u16 v158, v0 offset:23040
	ds_read_b32 v159, v1 offset:16728
	v_mov_b32_e32 v41, 1.0
	v_mov_b32_e32 v40, 1.0
	s_and_saveexec_b64 s[6:7], vcc
	v_mov_b32_e32 v1, s27
	ds_read_b32 v40, v1 offset:16984
	s_or_b64 exec, exec, s[6:7]
	v_mov_b32_e32 v1, s27
	ds_read_u16 v160, v0 offset:23296
	ds_read_b32 v161, v1 offset:16732
	s_and_saveexec_b64 s[6:7], vcc
	v_mov_b32_e32 v1, s27
	ds_read_b32 v41, v1 offset:16988
	s_or_b64 exec, exec, s[6:7]
	v_mov_b32_e32 v1, s27
	ds_read_u16 v163, v0 offset:23552
	ds_read_b32 v164, v1 offset:16736
	v_mov_b32_e32 v49, 1.0
	v_mov_b32_e32 v43, 1.0
	s_and_saveexec_b64 s[6:7], vcc
	v_mov_b32_e32 v1, s27
	ds_read_b32 v43, v1 offset:16992
	s_or_b64 exec, exec, s[6:7]
	v_mov_b32_e32 v1, s27
	ds_read_u16 v165, v0 offset:23808
	ds_read_b32 v166, v1 offset:16740
	s_and_saveexec_b64 s[6:7], vcc
	v_mov_b32_e32 v1, s27
	ds_read_b32 v49, v1 offset:16996
	s_or_b64 exec, exec, s[6:7]
	v_mov_b32_e32 v1, s27
	ds_read_u16 v167, v0 offset:24064
	ds_read_b32 v168, v1 offset:16744
	v_mov_b32_e32 v53, 1.0
	v_mov_b32_e32 v50, 1.0
	s_and_saveexec_b64 s[6:7], vcc
	v_mov_b32_e32 v1, s27
	ds_read_b32 v50, v1 offset:17000
	s_or_b64 exec, exec, s[6:7]
	v_mov_b32_e32 v1, s27
	ds_read_u16 v162, v0 offset:24320
	ds_read_b32 v169, v1 offset:16748
	s_and_saveexec_b64 s[6:7], vcc
	v_mov_b32_e32 v1, s27
	ds_read_b32 v53, v1 offset:17004
	s_or_b64 exec, exec, s[6:7]
	v_mov_b32_e32 v1, s27
	ds_read_u16 v155, v0 offset:24576
	ds_read_b32 v170, v1 offset:16752
	v_mov_b32_e32 v57, 1.0
	v_mov_b32_e32 v54, 1.0
	s_and_saveexec_b64 s[6:7], vcc
	v_mov_b32_e32 v1, s27
	ds_read_b32 v54, v1 offset:17008
	s_or_b64 exec, exec, s[6:7]
	v_mov_b32_e32 v1, s27
	ds_read_u16 v150, v0 offset:24832
	ds_read_b32 v171, v1 offset:16756
	s_and_saveexec_b64 s[6:7], vcc
	v_mov_b32_e32 v1, s27
	ds_read_b32 v57, v1 offset:17012
	s_or_b64 exec, exec, s[6:7]
	v_mov_b32_e32 v1, s27
	ds_read_u16 v143, v0 offset:25088
	ds_read_b32 v172, v1 offset:16760
	v_mov_b32_e32 v62, 1.0
	v_mov_b32_e32 v59, 1.0
	s_and_saveexec_b64 s[6:7], vcc
	v_mov_b32_e32 v1, s27
	ds_read_b32 v59, v1 offset:17016
	s_or_b64 exec, exec, s[6:7]
	v_mov_b32_e32 v1, s27
	ds_read_u16 v136, v0 offset:25344
	ds_read_b32 v173, v1 offset:16764
	s_and_saveexec_b64 s[6:7], vcc
	v_mov_b32_e32 v1, s27
	ds_read_b32 v62, v1 offset:17020
	s_or_b64 exec, exec, s[6:7]
	v_mov_b32_e32 v1, s27
	ds_read_u16 v129, v0 offset:25600
	ds_read_b32 v174, v1 offset:16768
	v_mov_b32_e32 v71, 1.0
	v_mov_b32_e32 v63, 1.0
	s_and_saveexec_b64 s[6:7], vcc
	v_mov_b32_e32 v1, s27
	ds_read_b32 v63, v1 offset:17024
	s_or_b64 exec, exec, s[6:7]
	v_mov_b32_e32 v1, s27
	ds_read_u16 v120, v0 offset:25856
	ds_read_b32 v175, v1 offset:16772
	s_and_saveexec_b64 s[6:7], vcc
	v_mov_b32_e32 v1, s27
	ds_read_b32 v71, v1 offset:17028
	s_or_b64 exec, exec, s[6:7]
	v_mov_b32_e32 v1, s27
	ds_read_u16 v110, v0 offset:26112
	ds_read_b32 v176, v1 offset:16776
	v_mov_b32_e32 v76, 1.0
	v_mov_b32_e32 v74, 1.0
	s_and_saveexec_b64 s[6:7], vcc
	v_mov_b32_e32 v1, s27
	ds_read_b32 v74, v1 offset:17032
	s_or_b64 exec, exec, s[6:7]
	v_mov_b32_e32 v1, s27
	ds_read_u16 v105, v0 offset:26368
	ds_read_b32 v177, v1 offset:16780
	s_and_saveexec_b64 s[6:7], vcc
	v_mov_b32_e32 v1, s27
	ds_read_b32 v76, v1 offset:17036
	s_or_b64 exec, exec, s[6:7]
	v_mov_b32_e32 v1, s27
	ds_read_u16 v104, v0 offset:26624
	ds_read_b32 v178, v1 offset:16784
	v_mov_b32_e32 v82, 1.0
	v_mov_b32_e32 v79, 1.0
	s_and_saveexec_b64 s[6:7], vcc
	v_mov_b32_e32 v1, s27
	ds_read_b32 v79, v1 offset:17040
	s_or_b64 exec, exec, s[6:7]
	v_mov_b32_e32 v1, s27
	ds_read_u16 v103, v0 offset:26880
	ds_read_b32 v179, v1 offset:16788
	s_and_saveexec_b64 s[6:7], vcc
	v_mov_b32_e32 v1, s27
	ds_read_b32 v82, v1 offset:17044
	s_or_b64 exec, exec, s[6:7]
	v_mov_b32_e32 v1, s27
	ds_read_u16 v102, v0 offset:27136
	ds_read_b32 v180, v1 offset:16792
	v_mov_b32_e32 v87, 1.0
	v_mov_b32_e32 v84, 1.0
	s_and_saveexec_b64 s[6:7], vcc
	v_mov_b32_e32 v1, s27
	ds_read_b32 v84, v1 offset:17048
	s_or_b64 exec, exec, s[6:7]
	v_mov_b32_e32 v1, s27
	ds_read_u16 v101, v0 offset:27392
	ds_read_b32 v181, v1 offset:16796
	s_and_saveexec_b64 s[6:7], vcc
	v_mov_b32_e32 v1, s27
	ds_read_b32 v87, v1 offset:17052
	s_or_b64 exec, exec, s[6:7]
	v_mov_b32_e32 v1, s27
	ds_read_u16 v100, v0 offset:27648
	ds_read_b32 v182, v1 offset:16800
	v_mov_b32_e32 v93, 1.0
	v_mov_b32_e32 v90, 1.0
	s_and_saveexec_b64 s[6:7], vcc
	v_mov_b32_e32 v1, s27
	ds_read_b32 v90, v1 offset:17056
	s_or_b64 exec, exec, s[6:7]
	v_mov_b32_e32 v1, s27
	ds_read_u16 v99, v0 offset:27904
	ds_read_b32 v183, v1 offset:16804
	s_and_saveexec_b64 s[6:7], vcc
	v_mov_b32_e32 v1, s27
	ds_read_b32 v93, v1 offset:17060
	s_or_b64 exec, exec, s[6:7]
	v_mov_b32_e32 v1, s27
	ds_read_u16 v98, v0 offset:28160
	ds_read_b32 v184, v1 offset:16808
	v_mov_b32_e32 v88, 1.0
	v_mov_b32_e32 v91, 1.0
	s_and_saveexec_b64 s[6:7], vcc
	v_mov_b32_e32 v1, s27
	ds_read_b32 v91, v1 offset:17064
	s_or_b64 exec, exec, s[6:7]
	v_mov_b32_e32 v1, s27
	ds_read_u16 v97, v0 offset:28416
	ds_read_b32 v185, v1 offset:16812
	s_and_saveexec_b64 s[6:7], vcc
	v_mov_b32_e32 v1, s27
	ds_read_b32 v88, v1 offset:17068
	s_or_b64 exec, exec, s[6:7]
	v_mov_b32_e32 v1, s27
	ds_read_u16 v96, v0 offset:28672
	ds_read_b32 v186, v1 offset:16816
	v_mov_b32_e32 v83, 1.0
	v_mov_b32_e32 v86, 1.0
	s_and_saveexec_b64 s[6:7], vcc
	v_mov_b32_e32 v1, s27
	ds_read_b32 v86, v1 offset:17072
	s_or_b64 exec, exec, s[6:7]
	v_mov_b32_e32 v1, s27
	ds_read_u16 v95, v0 offset:28928
	ds_read_b32 v187, v1 offset:16820
	s_and_saveexec_b64 s[6:7], vcc
	v_mov_b32_e32 v1, s27
	ds_read_b32 v83, v1 offset:17076
	s_or_b64 exec, exec, s[6:7]
	v_mov_b32_e32 v1, s27
	ds_read_u16 v94, v0 offset:29184
	ds_read_b32 v188, v1 offset:16824
	v_mov_b32_e32 v78, 1.0
	v_mov_b32_e32 v81, 1.0
	s_and_saveexec_b64 s[6:7], vcc
	v_mov_b32_e32 v1, s27
	ds_read_b32 v81, v1 offset:17080
	s_or_b64 exec, exec, s[6:7]
	v_mov_b32_e32 v1, s27
	ds_read_u16 v92, v0 offset:29440
	ds_read_b32 v189, v1 offset:16828
	s_and_saveexec_b64 s[6:7], vcc
	v_mov_b32_e32 v1, s27
	ds_read_b32 v78, v1 offset:17084
	s_or_b64 exec, exec, s[6:7]
	v_mov_b32_e32 v1, s27
	ds_read_u16 v89, v0 offset:29696
	ds_read_b32 v190, v1 offset:16832
	v_mov_b32_e32 v72, 1.0
	v_mov_b32_e32 v75, 1.0
	s_and_saveexec_b64 s[6:7], vcc
	v_mov_b32_e32 v1, s27
	ds_read_b32 v75, v1 offset:17088
	s_or_b64 exec, exec, s[6:7]
	v_mov_b32_e32 v1, s27
	ds_read_u16 v85, v0 offset:29952
	ds_read_b32 v191, v1 offset:16836
	s_and_saveexec_b64 s[6:7], vcc
	v_mov_b32_e32 v1, s27
	ds_read_b32 v72, v1 offset:17092
	s_or_b64 exec, exec, s[6:7]
	v_mov_b32_e32 v1, s27
	ds_read_u16 v80, v0 offset:30208
	ds_read_b32 v192, v1 offset:16840
	v_mov_b32_e32 v61, 1.0
	v_mov_b32_e32 v70, 1.0
	s_and_saveexec_b64 s[6:7], vcc
	v_mov_b32_e32 v1, s27
	ds_read_b32 v70, v1 offset:17096
	s_or_b64 exec, exec, s[6:7]
	v_mov_b32_e32 v1, s27
	ds_read_u16 v77, v0 offset:30464
	ds_read_b32 v193, v1 offset:16844
	s_and_saveexec_b64 s[6:7], vcc
	v_mov_b32_e32 v1, s27
	ds_read_b32 v61, v1 offset:17100
	s_or_b64 exec, exec, s[6:7]
	v_mov_b32_e32 v1, s27
	ds_read_u16 v73, v0 offset:30720
	ds_read_b32 v194, v1 offset:16848
	v_mov_b32_e32 v55, 1.0
	v_mov_b32_e32 v58, 1.0
	s_and_saveexec_b64 s[6:7], vcc
	v_mov_b32_e32 v1, s27
	ds_read_b32 v58, v1 offset:17104
	s_or_b64 exec, exec, s[6:7]
	v_mov_b32_e32 v1, s27
	ds_read_u16 v69, v0 offset:30976
	ds_read_b32 v195, v1 offset:16852
	s_and_saveexec_b64 s[6:7], vcc
	v_mov_b32_e32 v1, s27
	ds_read_b32 v55, v1 offset:17108
	s_or_b64 exec, exec, s[6:7]
	v_mov_b32_e32 v1, s27
	ds_read_u16 v60, v0 offset:31232
	ds_read_b32 v215, v1 offset:16856
	v_mov_b32_e32 v48, 1.0
	v_mov_b32_e32 v52, 1.0
	s_and_saveexec_b64 s[6:7], vcc
	v_mov_b32_e32 v1, s27
	ds_read_b32 v52, v1 offset:17112
	s_or_b64 exec, exec, s[6:7]
	v_mov_b32_e32 v1, s27
	ds_read_u16 v56, v0 offset:31488
	ds_read_b32 v216, v1 offset:16860
	s_and_saveexec_b64 s[6:7], vcc
	v_mov_b32_e32 v1, s27
	ds_read_b32 v48, v1 offset:17116
	s_or_b64 exec, exec, s[6:7]
	v_mov_b32_e32 v1, s27
	ds_read_u16 v51, v0 offset:31744
	ds_read_b32 v217, v1 offset:16864
	v_mov_b32_e32 v37, 1.0
	v_mov_b32_e32 v42, 1.0
	s_and_saveexec_b64 s[6:7], vcc
	v_mov_b32_e32 v1, s27
	ds_read_b32 v42, v1 offset:17120
	s_or_b64 exec, exec, s[6:7]
	v_mov_b32_e32 v1, s27
	ds_read_u16 v47, v0 offset:32000
	ds_read_b32 v218, v1 offset:16868
	s_and_saveexec_b64 s[6:7], vcc
	v_mov_b32_e32 v1, s27
	ds_read_b32 v37, v1 offset:17124
	s_or_b64 exec, exec, s[6:7]
	v_mov_b32_e32 v1, s27
	ds_read_u16 v39, v0 offset:32256
	ds_read_b32 v219, v1 offset:16872
	v_mov_b32_e32 v28, 1.0
	v_mov_b32_e32 v33, 1.0
	s_and_saveexec_b64 s[6:7], vcc
	v_mov_b32_e32 v1, s27
	ds_read_b32 v33, v1 offset:17128
	s_or_b64 exec, exec, s[6:7]
	v_mov_b32_e32 v1, s27
	ds_read_u16 v35, v0 offset:32512
	ds_read_b32 v220, v1 offset:16876
	s_and_saveexec_b64 s[6:7], vcc
	v_mov_b32_e32 v1, s27
	ds_read_b32 v28, v1 offset:17132
	s_or_b64 exec, exec, s[6:7]
	v_mov_b32_e32 v1, s27
	ds_read_u16 v29, v0 offset:32768
	ds_read_b32 v221, v1 offset:16880
	v_mov_b32_e32 v16, 1.0
	v_mov_b32_e32 v23, 1.0
	s_and_saveexec_b64 s[6:7], vcc
	v_mov_b32_e32 v1, s27
	ds_read_b32 v23, v1 offset:17136
	s_or_b64 exec, exec, s[6:7]
	v_mov_b32_e32 v1, s27
	ds_read_u16 v21, v0 offset:33024
	ds_read_b32 v222, v1 offset:16884
	s_and_saveexec_b64 s[6:7], vcc
	v_mov_b32_e32 v1, s27
	ds_read_b32 v16, v1 offset:17140
	s_or_b64 exec, exec, s[6:7]
	v_mov_b32_e32 v1, s27
	ds_read_u16 v2, v0 offset:33280
	ds_read_b32 v12, v1 offset:16888
	v_mov_b32_e32 v1, 1.0
	v_mov_b32_e32 v3, 1.0
	s_and_saveexec_b64 s[6:7], vcc
	v_mov_b32_e32 v3, s27
	ds_read_b32 v3, v3 offset:17144
	s_or_b64 exec, exec, s[6:7]
	v_mov_b32_e32 v206, s27
	ds_read_u16 v223, v0 offset:33536
	ds_read_b32 v224, v206 offset:16892
	s_and_saveexec_b64 s[6:7], vcc
	s_cbranch_execz .LBB0_410
	v_mov_b32_e32 v1, s27
	ds_read_b32 v1, v1 offset:17148
	s_branch .LBB0_410

.LBB0_548:
	v_readlane_b32 s6, v255, 20
	v_readlane_b32 s7, v255, 21
	s_mul_i32 s2, s6, 11
	v_readlane_b32 s6, v252, 2
	s_add_i32 s2, s2, 5
	v_readlane_b32 s7, v252, 3
	s_cmp_ge_i32 s2, s7
	s_mov_b32 s30, s1
	s_cbranch_scc1 .LBB0_598
	s_waitcnt vmcnt(0)
	s_barrier
	s_mov_b64 s[6:7], exec
	v_readlane_b32 s12, v252, 22
	v_readlane_b32 s13, v252, 23
	s_and_b64 s[12:13], s[6:7], s[12:13]
	s_mov_b64 exec, s[12:13]
	s_cbranch_execz .LBB0_597
	v_readlane_b32 s4, v254, 44
	s_waitcnt vmcnt(0) expcnt(0) lgkmcnt(0)
	s_nop 0
	v_mov_b32_e32 v0, s4
	ds_read_b32 v2, v0
	v_readlane_b32 s4, v254, 45
	s_waitcnt lgkmcnt(0)
	v_cmp_ne_u32_e32 vcc, 0, v2
	v_mov_b32_e32 v0, s4
	ds_read_b32 v0, v0
	s_cbranch_vccnz .LBB0_565
	v_readlane_b32 s14, v252, 24
	v_readlane_b32 s15, v252, 25
	s_load_dwordx2 s[12:13], s[14:15], 0x0
	s_load_dword s4, s[14:15], 0x8
	s_waitcnt lgkmcnt(0)
	s_mul_i32 s12, s13, s12
	s_mul_i32 s4, s12, s4
	s_mov_b32 s12, 1
	s_branch .LBB0_553

.LBB0_608:
	s_add_i32 s42, s36, s49
	s_ashr_i32 s43, s42, 31
	s_mul_i32 s30, s42, 0xa000
	s_mul_hi_i32 s29, s42, 0xa000
	s_add_u32 s46, s18, s30
	s_addc_u32 s47, s19, s29
	v_lshl_add_u64 v[16:17], s[46:47], 0, v[46:47]
	s_mov_b64 s[46:47], 0x44008000
	v_lshl_add_u64 v[18:19], v[16:17], 0, s[46:47]
	s_mov_b32 s29, 0x44008000
	s_lshl_b64 s[46:47], s[42:43], 2
	v_add_co_u32_e32 v16, vcc, s29, v16
	s_add_u32 s46, s67, s46
	s_nop 0
	v_addc_co_u32_e32 v17, vcc, 0, v17, vcc
	s_addc_u32 s47, s0, s47
	global_load_dwordx4 v[28:31], v[16:17], off
	global_load_dwordx4 v[24:27], v[18:19], off offset:16
	global_load_dword v58, v113, s[46:47]
	s_waitcnt vmcnt(0)
	s_cmpk_lg_i32 s48, 0x10c0
	s_mov_b64 s[46:47], -1
	s_waitcnt lgkmcnt(0)
	s_barrier
	s_cbranch_scc0 .LBB0_610
	s_add_i32 s43, s28, 0x10000
	s_add_i32 s30, s42, 1
	s_and_b32 s29, s43, 0x10000
	s_mul_hi_i32 s31, s30, 0xa000
	s_mul_i32 s30, s30, 0xa000
	s_add_u32 s30, s10, s30
	s_addc_u32 s31, s11, s31
	s_add_u32 s46, s30, s12
	s_addc_u32 s47, s31, 0
	s_add_i32 s29, s13, s29
	v_lshl_add_u64 v[16:17], s[46:47], 0, v[44:45]
	s_mov_b32 m0, s29
	v_lshl_add_u64 v[18:19], v[16:17], 0, s[72:73]
	global_load_lds_dwordx4 v[16:17], off
	s_add_i32 m0, s29, 0x400
	s_nop 0
	global_load_lds_dwordx4 v[18:19], off
	v_lshl_add_u64 v[18:19], v[16:17], 0, s[80:81]
	s_add_i32 m0, s29, 0x800
	v_lshl_add_u64 v[16:17], v[16:17], 0, s[64:65]
	global_load_lds_dwordx4 v[18:19], off
	s_add_i32 m0, s29, 0xc00
	s_add_u32 s46, s30, s14
	global_load_lds_dwordx4 v[16:17], off
	s_addc_u32 s47, s31, 0
	s_add_i32 m0, s29, 0x1000
	v_lshl_add_u64 v[16:17], s[46:47], 0, v[44:45]
	s_add_u32 s46, s30, s25
	global_load_lds_dwordx4 v[16:17], off
	s_addc_u32 s47, s31, 0
	s_add_i32 m0, s29, 0x1400
	v_lshl_add_u64 v[16:17], s[46:47], 0, v[44:45]
	s_add_u32 s46, s30, s27
	global_load_lds_dwordx4 v[16:17], off
	s_addc_u32 s47, s31, 0
	s_add_i32 m0, s29, 0x1800
	v_lshl_add_u64 v[16:17], s[46:47], 0, v[44:45]
	s_add_u32 s46, s30, s33
	s_addc_u32 s47, s31, 0
	global_load_lds_dwordx4 v[16:17], off
	v_lshl_add_u64 v[16:17], s[46:47], 0, v[44:45]
	s_add_i32 m0, s29, 0x1c00
	s_mov_b64 s[46:47], 0
	global_load_lds_dwordx4 v[16:17], off

.LBB0_612:
	s_waitcnt vmcnt(0)
	s_barrier
	s_and_saveexec_b64 s[6:7], s[40:41]
	s_mov_b32 s30, 0x358637bd
	s_mov_b32 s36, 0x3c800000
	s_cbranch_execz .LBB0_605
	global_load_dwordx4 v[0:3], v[50:51], off
	v_mad_i64_i32 v[8:9], s[28:29], s37, v250, v[56:57]
	v_mad_i64_i32 v[4:5], s[28:29], s37, v249, v[54:55]
	v_mad_i64_i32 v[6:7], s[28:29], s37, v249, v[52:53]
	v_lshlrev_b64 v[8:9], 1, v[8:9]
	s_mov_b64 s[46:47], 0
	v_mov_b32_e32 v42, v63

.LBB0_632:
	s_bitcmp1_b32 s12, 0
	s_cselect_b32 s14, 0, 0x5400
	s_cselect_b32 s13, 0x5400, 0
	s_add_i32 s14, s14, 0
	v_add3_u32 v234, s14, v220, v223
	global_load_dwordx4 v[158:161], v[194:195], off offset:-256
	global_load_dwordx4 v[162:165], v[194:195], off
	ds_read_b128 v[206:209], v234
	ds_read_b128 v[210:213], v234 offset:32
	ds_read_b128 v[226:229], v234 offset:64
	ds_read_b128 v[230:233], v234 offset:96
	s_waitcnt lgkmcnt(0)
	v_add_u32_e32 v225, s14, v221
	v_mfma_f32_32x32x16_bf16 v[96:111], v[206:209], v[134:137], 0.5
	v_add3_u32 v225, v225, v222, v224
	s_add_i32 s12, s12, 1
	s_add_i32 s13, s13, 0
	s_add_i32 s14, s4, s12
	v_lshl_add_u64 v[194:195], v[194:195], 0, s[84:85]
	s_cmp_eq_u32 s14, 2
	v_mfma_f32_32x32x16_bf16 v[80:95], v[206:209], v[118:121], 0.5
	v_mfma_f32_32x32x16_bf16 v[96:111], v[210:213], v[138:141], v[96:111]
	v_mfma_f32_32x32x16_bf16 v[80:95], v[210:213], v[122:125], v[80:95]
	v_mfma_f32_32x32x16_bf16 v[96:111], v[226:229], v[142:145], v[96:111]
	v_mfma_f32_32x32x16_bf16 v[80:95], v[226:229], v[126:129], v[80:95]
	v_mfma_f32_32x32x16_bf16 v[96:111], v[230:233], v[146:149], v[96:111]
	v_mfma_f32_32x32x16_bf16 v[80:95], v[230:233], v[130:133], v[80:95]
	ds_read_b64_tr_b16 v[206:207], v225 offset:9216
	ds_read_b64_tr_b16 v[208:209], v225 offset:10752
	ds_read_b64_tr_b16 v[210:211], v225 offset:12288
	ds_read_b64_tr_b16 v[212:213], v225 offset:13824
	ds_read_b64_tr_b16 v[226:227], v225 offset:9280
	ds_read_b64_tr_b16 v[228:229], v225 offset:10816
	ds_read_b64_tr_b16 v[230:231], v225 offset:12352
	ds_read_b64_tr_b16 v[232:233], v225 offset:13888
	s_nop 2
	v_cvt_pknorm_i16_f32 v96, v96, v97
	v_cvt_pknorm_i16_f32 v97, v98, v99
	v_cvt_pknorm_i16_f32 v98, v100, v101
	v_cvt_pknorm_i16_f32 v99, v102, v103
	v_cvt_pknorm_i16_f32 v104, v104, v105
	v_cvt_pknorm_i16_f32 v105, v106, v107
	v_cvt_pknorm_i16_f32 v80, v80, v81
	v_cvt_pknorm_i16_f32 v81, v82, v83
	v_cvt_pknorm_i16_f32 v82, v84, v85
	v_cvt_pknorm_i16_f32 v83, v86, v87
	s_waitcnt lgkmcnt(6)
	v_mfma_f32_32x32x16_bf16 v[48:63], v[206:209], v[96:99], v[48:63]
	v_cvt_pknorm_i16_f32 v106, v108, v109
	v_cvt_pknorm_i16_f32 v107, v110, v111
	v_cvt_pknorm_i16_f32 v88, v88, v89
	v_cvt_pknorm_i16_f32 v89, v90, v91
	v_cvt_pknorm_i16_f32 v90, v92, v93
	v_cvt_pknorm_i16_f32 v91, v94, v95
	s_waitcnt lgkmcnt(2)
	v_mfma_f32_32x32x16_bf16 v[32:47], v[226:229], v[96:99], v[32:47]
	v_mfma_f32_32x32x16_bf16 v[16:31], v[206:209], v[80:83], v[16:31]
	v_mfma_f32_32x32x16_bf16 v[0:15], v[226:229], v[80:83], v[0:15]
	v_mfma_f32_16x16x32_bf16 v[100:103], v[114:117], v[96:99], v[150:153]
	v_mfma_f32_16x16x32_bf16 v[84:87], v[114:117], v[80:83], v[154:157]
	v_mfma_f32_32x32x16_bf16 v[48:63], v[210:213], v[104:107], v[48:63]
	s_waitcnt lgkmcnt(0)
	v_mfma_f32_32x32x16_bf16 v[32:47], v[230:233], v[104:107], v[32:47]
	v_mfma_f32_32x32x16_bf16 v[16:31], v[210:213], v[88:91], v[16:31]
	v_mfma_f32_32x32x16_bf16 v[0:15], v[230:233], v[88:91], v[0:15]
	ds_read_b128 v[206:209], v234 offset:4608
	ds_read_b128 v[210:213], v234 offset:4640
	ds_read_b128 v[226:229], v234 offset:4672
	ds_read_b128 v[230:233], v234 offset:4704
	s_waitcnt lgkmcnt(0)
	v_mfma_f32_16x16x32_bf16 v[150:153], v[114:117], v[104:107], v[100:103]
	v_mfma_f32_16x16x32_bf16 v[154:157], v[114:117], v[88:91], v[84:87]
	v_mfma_f32_32x32x16_bf16 v[96:111], v[206:209], v[134:137], 0.5
	v_mfma_f32_32x32x16_bf16 v[80:95], v[206:209], v[118:121], 0.5
	ds_read_b64_tr_b16 v[64:65], v225 offset:15360
	ds_read_b64_tr_b16 v[66:67], v225 offset:16896
	ds_read_b64_tr_b16 v[68:69], v225 offset:18432
	ds_read_b64_tr_b16 v[70:71], v225 offset:19968
	ds_read_b64_tr_b16 v[72:73], v225 offset:15424
	ds_read_b64_tr_b16 v[74:75], v225 offset:16960
	ds_read_b64_tr_b16 v[76:77], v225 offset:18496
	ds_read_b64_tr_b16 v[78:79], v225 offset:20032
	v_mfma_f32_32x32x16_bf16 v[96:111], v[210:213], v[138:141], v[96:111]
	v_mfma_f32_32x32x16_bf16 v[80:95], v[210:213], v[122:125], v[80:95]
	v_mfma_f32_32x32x16_bf16 v[96:111], v[226:229], v[142:145], v[96:111]
	v_mfma_f32_32x32x16_bf16 v[80:95], v[226:229], v[126:129], v[80:95]
	v_mfma_f32_32x32x16_bf16 v[96:111], v[230:233], v[146:149], v[96:111]
	v_mfma_f32_32x32x16_bf16 v[80:95], v[230:233], v[130:133], v[80:95]
	s_nop 10
	v_cvt_pknorm_i16_f32 v96, v96, v97
	v_cvt_pknorm_i16_f32 v97, v98, v99
	v_cvt_pknorm_i16_f32 v98, v100, v101
	v_cvt_pknorm_i16_f32 v99, v102, v103
	v_cvt_pknorm_i16_f32 v104, v104, v105
	v_cvt_pknorm_i16_f32 v105, v106, v107
	v_cvt_pknorm_i16_f32 v106, v108, v109
	v_cvt_pknorm_i16_f32 v80, v80, v81
	v_cvt_pknorm_i16_f32 v81, v82, v83
	v_cvt_pknorm_i16_f32 v82, v84, v85
	v_cvt_pknorm_i16_f32 v83, v86, v87
	s_waitcnt lgkmcnt(6)
	v_mfma_f32_32x32x16_bf16 v[48:63], v[64:67], v[96:99], v[48:63]
	v_cvt_pknorm_i16_f32 v107, v110, v111
	v_cvt_pknorm_i16_f32 v88, v88, v89
	v_cvt_pknorm_i16_f32 v89, v90, v91
	v_cvt_pknorm_i16_f32 v90, v92, v93
	v_cvt_pknorm_i16_f32 v91, v94, v95
	s_waitcnt lgkmcnt(2)
	v_mfma_f32_32x32x16_bf16 v[32:47], v[72:75], v[96:99], v[32:47]
	v_mfma_f32_32x32x16_bf16 v[16:31], v[64:67], v[80:83], v[16:31]
	v_add3_u32 v64, s13, v217, v218
	v_add3_u32 v65, s13, v219, v218
	s_waitcnt vmcnt(1)
	ds_write_b128 v64, v[158:161]
	s_waitcnt vmcnt(0)
	ds_write_b128 v65, v[162:165] offset:9216
	s_waitcnt lgkmcnt(0)
	s_barrier
	v_mfma_f32_32x32x16_bf16 v[0:15], v[72:75], v[80:83], v[0:15]
	v_mfma_f32_16x16x32_bf16 v[100:103], v[114:117], v[96:99], v[150:153]
	v_mfma_f32_32x32x16_bf16 v[48:63], v[68:71], v[104:107], v[48:63]
	v_mfma_f32_32x32x16_bf16 v[32:47], v[76:79], v[104:107], v[32:47]
	v_mfma_f32_16x16x32_bf16 v[84:87], v[114:117], v[80:83], v[154:157]
	v_mfma_f32_32x32x16_bf16 v[16:31], v[68:71], v[88:91], v[16:31]
	v_mfma_f32_32x32x16_bf16 v[0:15], v[76:79], v[88:91], v[0:15]
	v_mfma_f32_16x16x32_bf16 v[150:153], v[114:117], v[104:107], v[100:103]
	v_mfma_f32_16x16x32_bf16 v[154:157], v[114:117], v[88:91], v[84:87]
	s_cbranch_scc0 .LBB0_632
	v_add3_u32 v194, s13, v220, v223
	v_mov_b64_e32 v[64:65], s[68:69]
	ds_read_b128 v[158:161], v194
	v_mov_b64_e32 v[66:67], s[70:71]
	v_mov_b64_e32 v[68:69], s[72:73]
	v_mov_b64_e32 v[70:71], s[74:75]
	v_mov_b64_e32 v[72:73], s[76:77]
	v_mov_b64_e32 v[74:75], s[78:79]
	v_mov_b64_e32 v[76:77], s[80:81]
	v_mov_b64_e32 v[78:79], s[82:83]
	ds_read_b128 v[162:165], v194 offset:32
	ds_read_b128 v[206:209], v194 offset:64
	ds_read_b128 v[210:213], v194 offset:96
	s_waitcnt lgkmcnt(2)
	v_mfma_f32_32x32x16_bf16 v[96:111], v[158:161], v[134:137], v[64:79]
	s_waitcnt lgkmcnt(0)
	v_mfma_f32_32x32x16_bf16 v[80:95], v[158:161], v[118:121], v[64:79]
	v_add_u32_e32 v158, s13, v221
	v_add3_u32 v195, v158, v222, v224
	ds_read_b64_tr_b16 v[158:159], v195 offset:9216
	ds_read_b64_tr_b16 v[160:161], v195 offset:10752
	v_mfma_f32_32x32x16_bf16 v[96:111], v[162:165], v[138:141], v[96:111]
	v_mfma_f32_32x32x16_bf16 v[80:95], v[162:165], v[122:125], v[80:95]
	v_mfma_f32_32x32x16_bf16 v[96:111], v[206:209], v[142:145], v[96:111]
	v_mfma_f32_32x32x16_bf16 v[80:95], v[206:209], v[126:129], v[80:95]
	v_mfma_f32_32x32x16_bf16 v[96:111], v[210:213], v[146:149], v[96:111]
	v_mfma_f32_32x32x16_bf16 v[80:95], v[210:213], v[130:133], v[80:95]
	s_nop 10
	v_cvt_pknorm_i16_f32 v96, v96, v97
	v_cvt_pknorm_i16_f32 v97, v98, v99
	v_cvt_pknorm_i16_f32 v98, v100, v101
	v_cvt_pknorm_i16_f32 v99, v102, v103
	ds_read_b64_tr_b16 v[102:103], v195 offset:10816
	ds_read_b64_tr_b16 v[100:101], v195 offset:9280
	ds_read_b64_tr_b16 v[162:163], v195 offset:12288
	ds_read_b64_tr_b16 v[164:165], v195 offset:13824
	v_cvt_pknorm_i16_f32 v104, v104, v105
	v_cvt_pknorm_i16_f32 v206, v80, v81
	v_cvt_pknorm_i16_f32 v207, v82, v83
	v_cvt_pknorm_i16_f32 v208, v84, v85
	v_cvt_pknorm_i16_f32 v209, v86, v87
	s_waitcnt lgkmcnt(4)
	v_mfma_f32_32x32x16_bf16 v[48:63], v[158:161], v[96:99], v[48:63]
	v_cvt_pknorm_i16_f32 v105, v106, v107
	v_cvt_pknorm_i16_f32 v106, v108, v109
	v_cvt_pknorm_i16_f32 v107, v110, v111
	ds_read_b64_tr_b16 v[110:111], v195 offset:13888
	ds_read_b64_tr_b16 v[108:109], v195 offset:12352
	s_waitcnt lgkmcnt(4)
	v_mfma_f32_32x32x16_bf16 v[32:47], v[100:103], v[96:99], v[32:47]
	v_mfma_f32_32x32x16_bf16 v[16:31], v[158:161], v[206:209], v[16:31]
	v_cvt_pknorm_i16_f32 v158, v88, v89
	v_cvt_pknorm_i16_f32 v159, v90, v91
	v_cvt_pknorm_i16_f32 v160, v92, v93
	v_cvt_pknorm_i16_f32 v161, v94, v95
	v_mfma_f32_32x32x16_bf16 v[0:15], v[100:103], v[206:209], v[0:15]
	s_waitcnt lgkmcnt(2)
	v_mfma_f32_32x32x16_bf16 v[48:63], v[162:165], v[104:107], v[48:63]
	s_waitcnt lgkmcnt(0)
	v_mfma_f32_32x32x16_bf16 v[32:47], v[108:111], v[104:107], v[32:47]
	v_mfma_f32_32x32x16_bf16 v[16:31], v[162:165], v[158:161], v[16:31]
	v_mfma_f32_32x32x16_bf16 v[0:15], v[108:111], v[158:161], v[0:15]
	ds_read_b128 v[100:103], v194 offset:4608
	ds_read_b128 v[108:111], v194 offset:4640
	ds_read_b128 v[162:165], v194 offset:4672
	ds_read_b128 v[210:213], v194 offset:4704
	s_waitcnt lgkmcnt(0)
	v_mfma_f32_32x32x16_bf16 v[80:95], v[100:103], v[134:137], v[64:79]
	v_mfma_f32_32x32x16_bf16 v[64:79], v[100:103], v[118:121], v[64:79]
	ds_read_b64_tr_b16 v[100:101], v195 offset:15360
	ds_read_b64_tr_b16 v[102:103], v195 offset:16896
	v_mfma_f32_32x32x16_bf16 v[80:95], v[108:111], v[138:141], v[80:95]
	v_mfma_f32_32x32x16_bf16 v[64:79], v[108:111], v[122:125], v[64:79]
	v_mfma_f32_32x32x16_bf16 v[80:95], v[162:165], v[142:145], v[80:95]
	v_mfma_f32_32x32x16_bf16 v[64:79], v[162:165], v[126:129], v[64:79]
	v_mfma_f32_32x32x16_bf16 v[80:95], v[210:213], v[146:149], v[80:95]
	v_mfma_f32_32x32x16_bf16 v[64:79], v[210:213], v[130:133], v[64:79]
	s_nop 10
	v_cvt_pknorm_i16_f32 v80, v80, v81
	v_cvt_pknorm_i16_f32 v81, v82, v83
	v_cvt_pknorm_i16_f32 v82, v84, v85
	v_cvt_pknorm_i16_f32 v83, v86, v87
	ds_read_b64_tr_b16 v[86:87], v195 offset:16960
	ds_read_b64_tr_b16 v[84:85], v195 offset:15424
	ds_read_b64_tr_b16 v[108:109], v195 offset:18432
	ds_read_b64_tr_b16 v[110:111], v195 offset:19968
	v_cvt_pknorm_i16_f32 v88, v88, v89
	v_cvt_pknorm_i16_f32 v64, v64, v65
	v_cvt_pknorm_i16_f32 v65, v66, v67
	v_cvt_pknorm_i16_f32 v66, v68, v69
	v_cvt_pknorm_i16_f32 v67, v70, v71
	v_cvt_pknorm_i16_f32 v89, v90, v91
	v_cvt_pknorm_i16_f32 v90, v92, v93
	s_waitcnt lgkmcnt(2)
	v_mfma_f32_32x32x16_bf16 v[0:15], v[84:87], v[64:67], v[0:15]
	v_cvt_pknorm_i16_f32 v91, v94, v95
	ds_read_b64_tr_b16 v[94:95], v195 offset:20032
	ds_read_b64_tr_b16 v[92:93], v195 offset:18496
	v_cvt_pknorm_i16_f32 v68, v72, v73
	v_cvt_pknorm_i16_f32 v69, v74, v75
	v_cvt_pknorm_i16_f32 v70, v76, v77
	v_cvt_pknorm_i16_f32 v71, v78, v79
	s_waitcnt lgkmcnt(0)
	v_mfma_f32_16x16x32_bf16 v[72:75], v[114:117], v[96:99], v[150:153]
	s_barrier
	v_mfma_f32_16x16x32_bf16 v[76:79], v[114:117], v[206:209], v[154:157]
	v_mfma_f32_32x32x16_bf16 v[48:63], v[100:103], v[80:83], v[48:63]
	v_mfma_f32_32x32x16_bf16 v[32:47], v[84:87], v[80:83], v[32:47]
	v_mfma_f32_32x32x16_bf16 v[16:31], v[100:103], v[64:67], v[16:31]
	v_mfma_f32_16x16x32_bf16 v[72:75], v[114:117], v[104:107], v[72:75]
	v_mfma_f32_16x16x32_bf16 v[76:79], v[114:117], v[158:161], v[76:79]
	v_mfma_f32_32x32x16_bf16 v[0:15], v[92:95], v[68:71], v[0:15]
	v_mfma_f32_16x16x32_bf16 v[72:75], v[114:117], v[80:83], v[72:75]
	v_mfma_f32_16x16x32_bf16 v[64:67], v[114:117], v[64:67], v[76:79]
	v_mfma_f32_32x32x16_bf16 v[48:63], v[108:111], v[88:91], v[48:63]
	v_mfma_f32_32x32x16_bf16 v[32:47], v[92:95], v[88:91], v[32:47]
	v_mfma_f32_32x32x16_bf16 v[16:31], v[108:111], v[68:71], v[16:31]
	v_mfma_f32_16x16x32_bf16 v[72:75], v[114:117], v[88:91], v[72:75]
	v_mfma_f32_16x16x32_bf16 v[64:67], v[114:117], v[68:71], v[64:67]
	s_setprio 0
	s_nop 6
	ds_bpermute_b32 v66, v181, v72
	ds_bpermute_b32 v67, v181, v73
	ds_bpermute_b32 v64, v181, v64
	ds_bpermute_b32 v65, v181, v65
	v_lshl_add_u64 v[150:151], v[192:193], 0, s[56:57]
	s_mov_b64 s[46:47], 0
	s_waitcnt lgkmcnt(2)
	v_cndmask_b32_e64 v66, v67, v66, s[40:41]
	v_div_scale_f32 v67, s[12:13], v66, v66, 1.0
	v_rcp_f32_e32 v68, v67
	s_waitcnt lgkmcnt(0)
	v_cndmask_b32_e64 v64, v65, v64, s[40:41]
	v_div_scale_f32 v65, s[12:13], v64, v64, 1.0
	v_fma_f32 v69, -v67, v68, 1.0
	v_fmac_f32_e32 v68, v69, v68
	v_div_scale_f32 v69, vcc, 1.0, v66, 1.0
	v_mul_f32_e32 v70, v69, v68
	v_fma_f32 v71, -v67, v70, v69
	v_fmac_f32_e32 v70, v71, v68
	v_fma_f32 v67, -v67, v70, v69
	v_div_fmas_f32 v67, v67, v68, v70
	v_div_fixup_f32 v66, v67, v66, 1.0
	v_rcp_f32_e32 v67, v65
	v_readlane_b32 s70, v255, 14
	s_mov_b32 s21, s20
	s_mov_b32 s71, s66
	v_fma_f32 v68, -v65, v67, 1.0
	v_fmac_f32_e32 v67, v68, v67
	v_div_scale_f32 v68, vcc, 1.0, v64, 1.0
	v_mul_f32_e32 v69, v68, v67
	v_fma_f32 v70, -v65, v69, v68
	v_fmac_f32_e32 v69, v70, v67
	v_fma_f32 v65, -v65, v69, v68
	v_div_fmas_f32 v65, v65, v67, v69
	v_div_fixup_f32 v64, v65, v64, 1.0
	v_pk_mul_f32 v[48:49], v[48:49], v[66:67] op_sel_hi:[1,0]
	v_pk_mul_f32 v[50:51], v[50:51], v[66:67] op_sel_hi:[1,0]
	v_pk_mul_f32 v[32:33], v[32:33], v[66:67] op_sel_hi:[1,0]
	v_pk_mul_f32 v[34:35], v[34:35], v[66:67] op_sel_hi:[1,0]
	v_pk_mul_f32 v[16:17], v[16:17], v[64:65] op_sel_hi:[1,0]
	v_pk_mul_f32 v[18:19], v[18:19], v[64:65] op_sel_hi:[1,0]
	v_pk_mul_f32 v[0:1], v[0:1], v[64:65] op_sel_hi:[1,0]
	v_pk_mul_f32 v[2:3], v[2:3], v[64:65] op_sel_hi:[1,0]
	v_cvt_pk_bf16_f32 v48, v48, v49
	v_cvt_pk_bf16_f32 v49, v50, v51
	v_lshl_add_u64 v[50:51], v[182:183], 1, v[192:193]
	v_cvt_pk_bf16_f32 v32, v32, v33
	v_cvt_pk_bf16_f32 v33, v34, v35
	v_cvt_pk_bf16_f32 v16, v16, v17
	v_cvt_pk_bf16_f32 v17, v18, v19
	v_cvt_pk_bf16_f32 v0, v0, v1
	v_cvt_pk_bf16_f32 v1, v2, v3
	global_store_dwordx2 v[50:51], v[48:49], off
	v_pk_mul_f32 v[48:49], v[52:53], v[66:67] op_sel_hi:[1,0]
	v_pk_mul_f32 v[52:53], v[54:55], v[66:67] op_sel_hi:[1,0]
	global_store_dwordx2 v[50:51], v[32:33], off offset:64
	v_pk_mul_f32 v[32:33], v[36:37], v[66:67] op_sel_hi:[1,0]
	v_pk_mul_f32 v[34:35], v[38:39], v[66:67] op_sel_hi:[1,0]
	global_store_dwordx2 v[50:51], v[16:17], off offset:128
	v_pk_mul_f32 v[16:17], v[20:21], v[64:65] op_sel_hi:[1,0]
	v_pk_mul_f32 v[18:19], v[22:23], v[64:65] op_sel_hi:[1,0]
	global_store_dwordx2 v[50:51], v[0:1], off offset:192
	v_pk_mul_f32 v[0:1], v[4:5], v[64:65] op_sel_hi:[1,0]
	v_pk_mul_f32 v[2:3], v[6:7], v[64:65] op_sel_hi:[1,0]
	v_cvt_pk_bf16_f32 v48, v48, v49
	v_cvt_pk_bf16_f32 v49, v52, v53
	v_cvt_pk_bf16_f32 v32, v32, v33
	v_cvt_pk_bf16_f32 v33, v34, v35
	v_cvt_pk_bf16_f32 v16, v16, v17
	v_cvt_pk_bf16_f32 v17, v18, v19
	v_cvt_pk_bf16_f32 v0, v0, v1
	v_cvt_pk_bf16_f32 v1, v2, v3
	global_store_dwordx2 v[50:51], v[48:49], off offset:16
	v_pk_mul_f32 v[48:49], v[56:57], v[66:67] op_sel_hi:[1,0]
	v_pk_mul_f32 v[52:53], v[58:59], v[66:67] op_sel_hi:[1,0]
	global_store_dwordx2 v[50:51], v[32:33], off offset:80
	v_pk_mul_f32 v[32:33], v[40:41], v[66:67] op_sel_hi:[1,0]
	v_pk_mul_f32 v[34:35], v[42:43], v[66:67] op_sel_hi:[1,0]
	global_store_dwordx2 v[50:51], v[16:17], off offset:144
	v_pk_mul_f32 v[16:17], v[24:25], v[64:65] op_sel_hi:[1,0]
	v_pk_mul_f32 v[18:19], v[26:27], v[64:65] op_sel_hi:[1,0]
	global_store_dwordx2 v[50:51], v[0:1], off offset:208
	v_pk_mul_f32 v[0:1], v[8:9], v[64:65] op_sel_hi:[1,0]
	v_pk_mul_f32 v[2:3], v[10:11], v[64:65] op_sel_hi:[1,0]
	v_cvt_pk_bf16_f32 v48, v48, v49
	v_cvt_pk_bf16_f32 v49, v52, v53
	v_cvt_pk_bf16_f32 v32, v32, v33
	v_cvt_pk_bf16_f32 v33, v34, v35
	v_cvt_pk_bf16_f32 v16, v16, v17
	v_cvt_pk_bf16_f32 v17, v18, v19
	v_cvt_pk_bf16_f32 v0, v0, v1
	v_cvt_pk_bf16_f32 v1, v2, v3
	global_store_dwordx2 v[50:51], v[48:49], off offset:32
	v_pk_mul_f32 v[48:49], v[60:61], v[66:67] op_sel_hi:[1,0]
	v_pk_mul_f32 v[52:53], v[62:63], v[66:67] op_sel_hi:[1,0]
	global_store_dwordx2 v[50:51], v[32:33], off offset:96
	v_pk_mul_f32 v[32:33], v[44:45], v[66:67] op_sel_hi:[1,0]
	v_pk_mul_f32 v[34:35], v[46:47], v[66:67] op_sel_hi:[1,0]
	global_store_dwordx2 v[50:51], v[16:17], off offset:160
	v_pk_mul_f32 v[16:17], v[28:29], v[64:65] op_sel_hi:[1,0]
	v_pk_mul_f32 v[18:19], v[30:31], v[64:65] op_sel_hi:[1,0]
	global_store_dwordx2 v[50:51], v[0:1], off offset:224
	v_pk_mul_f32 v[0:1], v[12:13], v[64:65] op_sel_hi:[1,0]
	v_cvt_pk_bf16_f32 v48, v48, v49
	v_cvt_pk_bf16_f32 v49, v52, v53
	v_cvt_pk_bf16_f32 v32, v32, v33
	v_cvt_pk_bf16_f32 v33, v34, v35
	v_cvt_pk_bf16_f32 v16, v16, v17
	v_cvt_pk_bf16_f32 v17, v18, v19
	v_cvt_pk_bf16_f32 v0, v0, v1
	v_pk_mul_f32 v[2:3], v[14:15], v[64:65] op_sel_hi:[1,0]
	global_store_dwordx2 v[50:51], v[48:49], off offset:48
	global_store_dwordx2 v[50:51], v[32:33], off offset:112
	global_store_dwordx2 v[50:51], v[16:17], off offset:176

.LBB0_642:
	s_bitcmp1_b32 s2, 0
	s_mov_b32 s14, 0x2200000
	s_cselect_b32 s13, 0, 0x5400
	v_add_co_u32_e32 v64, vcc, s14, v152
	s_cselect_b32 s12, 0x5400, 0
	s_add_i32 s13, s13, 0
	global_load_dwordx4 v[142:145], v[152:153], off
	v_addc_co_u32_e32 v65, vcc, 0, v153, vcc
	global_load_dwordx4 v[146:149], v[64:65], off
	v_add3_u32 v206, s13, v220, v223
	ds_read_b128 v[80:83], v206
	ds_read_b128 v[84:87], v206 offset:32
	ds_read_b128 v[154:157], v206 offset:64
	ds_read_b128 v[158:161], v206 offset:96
	s_waitcnt lgkmcnt(0)
	v_add_u32_e32 v112, s13, v221
	v_mfma_f32_32x32x16_bf16 v[96:111], v[80:83], v[126:129], 0.5
	v_add3_u32 v112, v112, v222, v224
	s_add_i32 s2, s2, 1
	s_add_i32 s12, s12, 0
	s_add_i32 s13, s4, s2
	v_lshl_add_u64 v[152:153], v[152:153], 0, s[84:85]
	s_cmp_eq_u32 s13, 2
	v_mfma_f32_32x32x16_bf16 v[96:111], v[84:87], v[130:133], v[96:111]
	v_mfma_f32_32x32x16_bf16 v[80:95], v[154:157], v[118:121], 0.5
	s_nop 10
	v_cvt_pknorm_i16_f32 v96, v96, v97
	v_cvt_pknorm_i16_f32 v97, v98, v99
	v_cvt_pknorm_i16_f32 v98, v100, v101
	v_cvt_pknorm_i16_f32 v99, v102, v103
	v_cvt_pknorm_i16_f32 v104, v104, v105
	v_cvt_pknorm_i16_f32 v105, v106, v107
	v_cvt_pknorm_i16_f32 v106, v108, v109
	v_mfma_f32_32x32x16_bf16 v[80:95], v[158:161], v[122:125], v[80:95]
	ds_read_b64_tr_b16 v[154:155], v112 offset:9216
	ds_read_b64_tr_b16 v[156:157], v112 offset:10752
	ds_read_b64_tr_b16 v[158:159], v112 offset:12288
	ds_read_b64_tr_b16 v[160:161], v112 offset:13824
	ds_read_b64_tr_b16 v[162:163], v112 offset:9280
	ds_read_b64_tr_b16 v[164:165], v112 offset:10816
	ds_read_b64_tr_b16 v[192:193], v112 offset:12352
	ds_read_b64_tr_b16 v[194:195], v112 offset:13888
	v_cvt_pknorm_i16_f32 v107, v110, v111
	s_nop 2
	v_cvt_pknorm_i16_f32 v80, v80, v81
	v_cvt_pknorm_i16_f32 v81, v82, v83
	v_cvt_pknorm_i16_f32 v82, v84, v85
	v_cvt_pknorm_i16_f32 v83, v86, v87
	s_waitcnt lgkmcnt(6)
	v_mfma_f32_32x32x16_bf16 v[32:47], v[154:157], v[96:99], v[32:47]
	v_cvt_pknorm_i16_f32 v88, v88, v89
	v_cvt_pknorm_i16_f32 v89, v90, v91
	v_cvt_pknorm_i16_f32 v90, v92, v93
	v_cvt_pknorm_i16_f32 v91, v94, v95
	v_mfma_f32_32x32x16_bf16 v[48:63], v[154:157], v[80:83], v[48:63]
	s_waitcnt lgkmcnt(2)
	v_mfma_f32_32x32x16_bf16 v[0:15], v[162:165], v[96:99], v[0:15]
	v_mfma_f32_16x16x32_bf16 v[84:87], v[114:117], v[80:83], v[138:141]
	v_mfma_f32_16x16x32_bf16 v[100:103], v[114:117], v[96:99], v[134:137]
	v_mfma_f32_32x32x16_bf16 v[32:47], v[158:161], v[104:107], v[32:47]
	v_mfma_f32_16x16x32_bf16 v[138:141], v[114:117], v[88:91], v[84:87]
	v_mfma_f32_32x32x16_bf16 v[48:63], v[158:161], v[88:91], v[48:63]
	v_mfma_f32_32x32x16_bf16 v[16:31], v[162:165], v[80:83], v[16:31]
	ds_read_b128 v[80:83], v206 offset:4608
	s_nop 1
	ds_read_b128 v[84:87], v206 offset:4640
	ds_read_b128 v[154:157], v206 offset:4672
	ds_read_b128 v[158:161], v206 offset:4704
	s_waitcnt lgkmcnt(0)
	v_mfma_f32_16x16x32_bf16 v[134:137], v[114:117], v[104:107], v[100:103]
	v_mfma_f32_32x32x16_bf16 v[0:15], v[192:195], v[104:107], v[0:15]
	v_mfma_f32_32x32x16_bf16 v[96:111], v[80:83], v[126:129], 0.5
	v_mfma_f32_32x32x16_bf16 v[16:31], v[192:195], v[88:91], v[16:31]
	v_mfma_f32_32x32x16_bf16 v[96:111], v[84:87], v[130:133], v[96:111]
	v_mfma_f32_32x32x16_bf16 v[80:95], v[154:157], v[118:121], 0.5
	ds_read_b64_tr_b16 v[64:65], v112 offset:15360
	ds_read_b64_tr_b16 v[66:67], v112 offset:16896
	ds_read_b64_tr_b16 v[68:69], v112 offset:18432
	ds_read_b64_tr_b16 v[70:71], v112 offset:19968
	ds_read_b64_tr_b16 v[72:73], v112 offset:15424
	ds_read_b64_tr_b16 v[74:75], v112 offset:16960
	ds_read_b64_tr_b16 v[76:77], v112 offset:18496
	ds_read_b64_tr_b16 v[78:79], v112 offset:20032
	v_cvt_pknorm_i16_f32 v96, v96, v97
	v_cvt_pknorm_i16_f32 v97, v98, v99
	v_cvt_pknorm_i16_f32 v98, v100, v101
	v_cvt_pknorm_i16_f32 v99, v102, v103
	v_cvt_pknorm_i16_f32 v104, v104, v105
	v_cvt_pknorm_i16_f32 v105, v106, v107
	v_mfma_f32_32x32x16_bf16 v[80:95], v[158:161], v[122:125], v[80:95]
	v_cvt_pknorm_i16_f32 v106, v108, v109
	v_cvt_pknorm_i16_f32 v107, v110, v111
	s_waitcnt lgkmcnt(6)
	v_mfma_f32_32x32x16_bf16 v[32:47], v[64:67], v[96:99], v[32:47]
	s_nop 7
	v_cvt_pknorm_i16_f32 v80, v80, v81
	v_cvt_pknorm_i16_f32 v81, v82, v83
	v_cvt_pknorm_i16_f32 v82, v84, v85
	v_cvt_pknorm_i16_f32 v83, v86, v87
	v_cvt_pknorm_i16_f32 v88, v88, v89
	v_cvt_pknorm_i16_f32 v89, v90, v91
	v_cvt_pknorm_i16_f32 v90, v92, v93
	s_waitcnt lgkmcnt(2)
	v_mfma_f32_32x32x16_bf16 v[0:15], v[72:75], v[96:99], v[0:15]
	v_cvt_pknorm_i16_f32 v91, v94, v95
	v_mfma_f32_32x32x16_bf16 v[48:63], v[64:67], v[80:83], v[48:63]
	v_add3_u32 v64, s12, v217, v218
	v_add3_u32 v65, s12, v219, v218
	s_waitcnt vmcnt(1)
	ds_write_b128 v64, v[142:145]
	s_waitcnt vmcnt(0)
	ds_write_b128 v65, v[146:149] offset:9216
	s_waitcnt lgkmcnt(0)
	s_barrier
	v_mfma_f32_32x32x16_bf16 v[16:31], v[72:75], v[80:83], v[16:31]
	v_mfma_f32_16x16x32_bf16 v[100:103], v[114:117], v[96:99], v[134:137]
	v_mfma_f32_32x32x16_bf16 v[32:47], v[68:71], v[104:107], v[32:47]
	v_mfma_f32_32x32x16_bf16 v[0:15], v[76:79], v[104:107], v[0:15]
	v_mfma_f32_16x16x32_bf16 v[84:87], v[114:117], v[80:83], v[138:141]
	v_mfma_f32_32x32x16_bf16 v[48:63], v[68:71], v[88:91], v[48:63]
	v_mfma_f32_32x32x16_bf16 v[16:31], v[76:79], v[88:91], v[16:31]
	v_mfma_f32_16x16x32_bf16 v[134:137], v[114:117], v[104:107], v[100:103]
	v_mfma_f32_16x16x32_bf16 v[138:141], v[114:117], v[88:91], v[84:87]
	s_cbranch_scc0 .LBB0_642
	v_add3_u32 v112, s12, v220, v223
	v_mov_b64_e32 v[64:65], s[68:69]
	ds_read_b128 v[80:83], v112
	v_mov_b64_e32 v[66:67], s[70:71]
	v_mov_b64_e32 v[68:69], s[72:73]
	v_mov_b64_e32 v[70:71], s[74:75]
	v_mov_b64_e32 v[72:73], s[76:77]
	v_mov_b64_e32 v[74:75], s[78:79]
	v_mov_b64_e32 v[76:77], s[80:81]
	v_mov_b64_e32 v[78:79], s[82:83]
	ds_read_b128 v[84:87], v112 offset:32
	ds_read_b128 v[142:145], v112 offset:64
	ds_read_b128 v[146:149], v112 offset:96
	s_waitcnt lgkmcnt(2)
	v_mfma_f32_32x32x16_bf16 v[96:111], v[80:83], v[126:129], v[64:79]
	s_waitcnt lgkmcnt(0)
	v_mfma_f32_32x32x16_bf16 v[96:111], v[84:87], v[130:133], v[96:111]
	v_mfma_f32_32x32x16_bf16 v[80:95], v[142:145], v[118:121], v[64:79]
	v_add_u32_e32 v142, s12, v221
	v_add3_u32 v160, v142, v222, v224
	ds_read_b64_tr_b16 v[142:143], v160 offset:9216
	ds_read_b64_tr_b16 v[144:145], v160 offset:10752
	s_nop 6
	v_cvt_pknorm_i16_f32 v96, v96, v97
	v_cvt_pknorm_i16_f32 v97, v98, v99
	v_cvt_pknorm_i16_f32 v98, v100, v101
	v_cvt_pknorm_i16_f32 v99, v102, v103
	v_mfma_f32_32x32x16_bf16 v[80:95], v[146:149], v[122:125], v[80:95]
	ds_read_b64_tr_b16 v[102:103], v160 offset:10816
	ds_read_b64_tr_b16 v[100:101], v160 offset:9280
	ds_read_b64_tr_b16 v[146:147], v160 offset:12288
	ds_read_b64_tr_b16 v[148:149], v160 offset:13824
	v_cvt_pknorm_i16_f32 v104, v104, v105
	v_cvt_pknorm_i16_f32 v105, v106, v107
	v_cvt_pknorm_i16_f32 v106, v108, v109
	v_cvt_pknorm_i16_f32 v107, v110, v111
	ds_read_b64_tr_b16 v[110:111], v160 offset:13888
	ds_read_b64_tr_b16 v[108:109], v160 offset:12352
	s_nop 1
	v_cvt_pknorm_i16_f32 v152, v80, v81
	v_cvt_pknorm_i16_f32 v153, v82, v83
	v_cvt_pknorm_i16_f32 v154, v84, v85
	v_cvt_pknorm_i16_f32 v155, v86, v87
	s_waitcnt lgkmcnt(6)
	v_mfma_f32_32x32x16_bf16 v[32:47], v[142:145], v[96:99], v[32:47]
	s_waitcnt lgkmcnt(4)
	v_mfma_f32_32x32x16_bf16 v[0:15], v[100:103], v[96:99], v[0:15]
	v_mfma_f32_32x32x16_bf16 v[48:63], v[142:145], v[152:155], v[48:63]
	v_cvt_pknorm_i16_f32 v142, v88, v89
	v_cvt_pknorm_i16_f32 v143, v90, v91
	v_cvt_pknorm_i16_f32 v144, v92, v93
	v_cvt_pknorm_i16_f32 v145, v94, v95
	v_mfma_f32_32x32x16_bf16 v[16:31], v[100:103], v[152:155], v[16:31]
	s_waitcnt lgkmcnt(2)
	v_mfma_f32_32x32x16_bf16 v[32:47], v[146:149], v[104:107], v[32:47]
	s_waitcnt lgkmcnt(0)
	v_mfma_f32_32x32x16_bf16 v[0:15], v[108:111], v[104:107], v[0:15]
	v_mfma_f32_32x32x16_bf16 v[48:63], v[146:149], v[142:145], v[48:63]
	v_mfma_f32_32x32x16_bf16 v[16:31], v[108:111], v[142:145], v[16:31]
	ds_read_b128 v[100:103], v112 offset:4608
	ds_read_b128 v[108:111], v112 offset:4640
	ds_read_b128 v[146:149], v112 offset:4672
	ds_read_b128 v[156:159], v112 offset:4704
	s_waitcnt lgkmcnt(0)
	v_mfma_f32_32x32x16_bf16 v[80:95], v[100:103], v[126:129], v[64:79]
	ds_read_b64_tr_b16 v[100:101], v160 offset:15360
	ds_read_b64_tr_b16 v[102:103], v160 offset:16896
	v_mfma_f32_32x32x16_bf16 v[80:95], v[108:111], v[130:133], v[80:95]
	v_mfma_f32_32x32x16_bf16 v[64:79], v[146:149], v[118:121], v[64:79]
	s_nop 10
	v_cvt_pknorm_i16_f32 v80, v80, v81
	v_cvt_pknorm_i16_f32 v81, v82, v83
	v_cvt_pknorm_i16_f32 v82, v84, v85
	v_cvt_pknorm_i16_f32 v83, v86, v87
	ds_read_b64_tr_b16 v[86:87], v160 offset:16960
	ds_read_b64_tr_b16 v[84:85], v160 offset:15424
	ds_read_b64_tr_b16 v[108:109], v160 offset:18432
	ds_read_b64_tr_b16 v[110:111], v160 offset:19968
	v_cvt_pknorm_i16_f32 v88, v88, v89
	v_mfma_f32_32x32x16_bf16 v[64:79], v[156:159], v[122:125], v[64:79]
	v_cvt_pknorm_i16_f32 v89, v90, v91
	v_cvt_pknorm_i16_f32 v90, v92, v93
	v_cvt_pknorm_i16_f32 v91, v94, v95
	ds_read_b64_tr_b16 v[94:95], v160 offset:20032
	ds_read_b64_tr_b16 v[92:93], v160 offset:18496
	s_load_dword s2, s[6:7], 0x180
	s_waitcnt lgkmcnt(0)
	s_barrier
	v_mfma_f32_32x32x16_bf16 v[0:15], v[84:87], v[80:83], v[0:15]
	s_nop 2
	v_cvt_pknorm_i16_f32 v64, v64, v65
	v_cvt_pknorm_i16_f32 v65, v66, v67
	v_cvt_pknorm_i16_f32 v66, v68, v69
	v_cvt_pknorm_i16_f32 v68, v72, v73
	v_cvt_pknorm_i16_f32 v69, v74, v75
	v_cvt_pknorm_i16_f32 v67, v70, v71
	v_cvt_pknorm_i16_f32 v70, v76, v77
	v_mfma_f32_16x16x32_bf16 v[72:75], v[114:117], v[96:99], v[134:137]
	v_cvt_pknorm_i16_f32 v71, v78, v79
	v_mfma_f32_16x16x32_bf16 v[76:79], v[114:117], v[152:155], v[138:141]
	v_mfma_f32_16x16x32_bf16 v[72:75], v[114:117], v[104:107], v[72:75]
	v_mfma_f32_32x32x16_bf16 v[32:47], v[100:103], v[80:83], v[32:47]
	v_mfma_f32_32x32x16_bf16 v[0:15], v[92:95], v[88:91], v[0:15]
	v_mfma_f32_32x32x16_bf16 v[48:63], v[100:103], v[64:67], v[48:63]
	v_mfma_f32_32x32x16_bf16 v[16:31], v[84:87], v[64:67], v[16:31]
	v_mfma_f32_16x16x32_bf16 v[76:79], v[114:117], v[142:145], v[76:79]
	v_mfma_f32_16x16x32_bf16 v[72:75], v[114:117], v[80:83], v[72:75]
	v_mfma_f32_16x16x32_bf16 v[64:67], v[114:117], v[64:67], v[76:79]
	v_mfma_f32_16x16x32_bf16 v[72:75], v[114:117], v[88:91], v[72:75]
	v_mfma_f32_32x32x16_bf16 v[32:47], v[108:111], v[88:91], v[32:47]
	s_nop 6
	v_sub_f32_e64 v74, 1.0, s2
	v_mfma_f32_32x32x16_bf16 v[48:63], v[108:111], v[68:71], v[48:63]
	v_mfma_f32_16x16x32_bf16 v[64:67], v[114:117], v[68:71], v[64:67]
	v_mfma_f32_32x32x16_bf16 v[16:31], v[92:95], v[68:71], v[16:31]
	s_setprio 0
	s_nop 5
	ds_bpermute_b32 v66, v181, v72
	ds_bpermute_b32 v67, v181, v73
	ds_bpermute_b32 v64, v181, v64
	ds_bpermute_b32 v65, v181, v65
	v_readlane_b32 s70, v255, 14
	s_mov_b32 s21, s20
	s_waitcnt lgkmcnt(2)
	v_cndmask_b32_e64 v66, v67, v66, s[40:41]
	v_div_scale_f32 v67, s[12:13], v66, v66, 1.0
	v_rcp_f32_e32 v68, v67
	s_waitcnt lgkmcnt(0)
	v_cndmask_b32_e64 v64, v65, v64, s[40:41]
	v_div_scale_f32 v65, s[12:13], v64, v64, 1.0
	v_fma_f32 v69, -v67, v68, 1.0
	v_fmac_f32_e32 v68, v69, v68
	v_div_scale_f32 v69, vcc, 1.0, v66, 1.0
	v_mul_f32_e32 v70, v69, v68
	v_fma_f32 v71, -v67, v70, v69
	v_fmac_f32_e32 v70, v71, v68
	v_fma_f32 v67, -v67, v70, v69
	v_div_fmas_f32 v67, v67, v68, v70
	v_div_fixup_f32 v66, v67, v66, 1.0
	v_rcp_f32_e32 v67, v65
	s_mov_b32 s71, s66
	v_fma_f32 v68, -v65, v67, 1.0
	v_fmac_f32_e32 v67, v68, v67
	v_div_scale_f32 v68, vcc, 1.0, v64, 1.0
	v_mul_f32_e32 v69, v68, v67
	v_fma_f32 v70, -v65, v69, v68
	v_fmac_f32_e32 v69, v70, v67
	v_fma_f32 v65, -v65, v69, v68
	v_div_fmas_f32 v65, v65, v67, v69
	global_load_dwordx4 v[68:71], v[186:187], off
	v_div_fixup_f32 v72, v65, v64, 1.0
	v_pk_mul_f32 v[30:31], v[30:31], v[72:73] op_sel_hi:[1,0]
	v_pk_mul_f32 v[18:19], v[18:19], v[72:73] op_sel_hi:[1,0]
	v_pk_mul_f32 v[30:31], v[166:167], v[30:31]
	v_pk_mul_f32 v[18:19], v[166:167], v[18:19]
	v_pk_fma_f32 v[14:15], v[14:15], v[66:67], v[30:31] op_sel_hi:[1,0,1] neg_lo:[0,0,1] neg_hi:[0,0,1]
	v_pk_mul_f32 v[30:31], v[50:51], v[72:73] op_sel_hi:[1,0]
	v_pk_fma_f32 v[18:19], v[2:3], v[66:67], v[18:19] op_sel_hi:[1,0,1] neg_lo:[0,0,1] neg_hi:[0,0,1]
	v_pk_mul_f32 v[30:31], v[166:167], v[30:31]
	v_pk_mul_f32 v[2:3], v[16:17], v[72:73] op_sel_hi:[1,0]
	v_pk_fma_f32 v[30:31], v[34:35], v[66:67], v[30:31] op_sel_hi:[1,0,1] neg_lo:[0,0,1] neg_hi:[0,0,1]
	v_pk_mul_f32 v[34:35], v[48:49], v[72:73] op_sel_hi:[1,0]
	v_mul_f32_e32 v48, v31, v31
	v_pk_mul_f32 v[34:35], v[166:167], v[34:35]
	v_pk_mul_f32 v[2:3], v[166:167], v[2:3]
	v_pk_fma_f32 v[32:33], v[32:33], v[66:67], v[34:35] op_sel_hi:[1,0,1] neg_lo:[0,0,1] neg_hi:[0,0,1]
	v_pk_fma_f32 v[16:17], v[0:1], v[66:67], v[2:3] op_sel_hi:[1,0,1] neg_lo:[0,0,1] neg_hi:[0,0,1]
	v_mul_f32_e32 v34, v33, v33
	v_pk_fma_f32 v[34:35], v[32:33], v[32:33], v[34:35] op_sel_hi:[1,1,0]
	v_mul_f32_e32 v2, v17, v17
	v_pk_fma_f32 v[34:35], v[30:31], v[30:31], v[34:35]
	v_lshl_add_u64 v[64:65], v[182:183], 1, v[150:151]
	v_pk_add_f32 v[34:35], v[48:49], v[34:35] op_sel_hi:[0,1]
	v_pk_mul_f32 v[48:49], v[54:55], v[72:73] op_sel_hi:[1,0]
	s_nop 0
	v_pk_mul_f32 v[48:49], v[166:167], v[48:49]
	s_nop 0
	v_pk_fma_f32 v[38:39], v[38:39], v[66:67], v[48:49] op_sel_hi:[1,0,1] neg_lo:[0,0,1] neg_hi:[0,0,1]
	v_pk_mul_f32 v[48:49], v[52:53], v[72:73] op_sel_hi:[1,0]
	s_nop 0
	v_pk_mul_f32 v[48:49], v[166:167], v[48:49]
	s_nop 0
	v_pk_fma_f32 v[36:37], v[36:37], v[66:67], v[48:49] op_sel_hi:[1,0,1] neg_lo:[0,0,1] neg_hi:[0,0,1]
	s_nop 0
	v_pk_fma_f32 v[34:35], v[36:37], v[36:37], v[34:35]
	v_mul_f32_e32 v48, v37, v37
	v_pk_add_f32 v[34:35], v[48:49], v[34:35] op_sel_hi:[0,1]
	v_pk_fma_f32 v[34:35], v[38:39], v[38:39], v[34:35]
	v_mul_f32_e32 v48, v39, v39
	v_pk_add_f32 v[34:35], v[48:49], v[34:35] op_sel_hi:[0,1]
	v_pk_mul_f32 v[48:49], v[58:59], v[72:73] op_sel_hi:[1,0]
	s_nop 0
	v_pk_mul_f32 v[48:49], v[166:167], v[48:49]
	s_nop 0
	v_pk_fma_f32 v[42:43], v[42:43], v[66:67], v[48:49] op_sel_hi:[1,0,1] neg_lo:[0,0,1] neg_hi:[0,0,1]
	v_pk_mul_f32 v[48:49], v[56:57], v[72:73] op_sel_hi:[1,0]
	s_nop 0
	v_pk_mul_f32 v[48:49], v[166:167], v[48:49]
	s_nop 0
	v_pk_fma_f32 v[40:41], v[40:41], v[66:67], v[48:49] op_sel_hi:[1,0,1] neg_lo:[0,0,1] neg_hi:[0,0,1]
	s_nop 0
	v_pk_fma_f32 v[34:35], v[40:41], v[40:41], v[34:35]
	v_mul_f32_e32 v48, v41, v41
	v_pk_add_f32 v[34:35], v[48:49], v[34:35] op_sel_hi:[0,1]
	v_pk_fma_f32 v[34:35], v[42:43], v[42:43], v[34:35]
	v_mul_f32_e32 v48, v43, v43
	v_pk_add_f32 v[34:35], v[48:49], v[34:35] op_sel_hi:[0,1]
	v_pk_mul_f32 v[48:49], v[62:63], v[72:73] op_sel_hi:[1,0]
	s_nop 0
	v_pk_mul_f32 v[48:49], v[166:167], v[48:49]
	s_nop 0
	v_pk_fma_f32 v[46:47], v[46:47], v[66:67], v[48:49] op_sel_hi:[1,0,1] neg_lo:[0,0,1] neg_hi:[0,0,1]
	v_pk_mul_f32 v[48:49], v[60:61], v[72:73] op_sel_hi:[1,0]
	s_nop 0
	v_pk_mul_f32 v[48:49], v[166:167], v[48:49]
	s_nop 0
	v_pk_fma_f32 v[44:45], v[44:45], v[66:67], v[48:49] op_sel_hi:[1,0,1] neg_lo:[0,0,1] neg_hi:[0,0,1]
	s_nop 0
	v_pk_fma_f32 v[34:35], v[44:45], v[44:45], v[34:35]
	v_mul_f32_e32 v48, v45, v45
	v_pk_add_f32 v[34:35], v[48:49], v[34:35] op_sel_hi:[0,1]
	v_pk_fma_f32 v[34:35], v[46:47], v[46:47], v[34:35]
	v_mul_f32_e32 v48, v47, v47
	v_pk_add_f32 v[34:35], v[48:49], v[34:35] op_sel_hi:[0,1]
	v_pk_fma_f32 v[0:1], v[16:17], v[16:17], v[34:35]
	s_nop 0
	v_pk_add_f32 v[0:1], v[2:3], v[0:1] op_sel_hi:[0,1]
	v_pk_fma_f32 v[0:1], v[18:19], v[18:19], v[0:1]
	v_mul_f32_e32 v2, v19, v19
	v_pk_add_f32 v[0:1], v[2:3], v[0:1] op_sel_hi:[0,1]
	v_pk_mul_f32 v[2:3], v[22:23], v[72:73] op_sel_hi:[1,0]
	s_nop 0
	v_pk_mul_f32 v[2:3], v[166:167], v[2:3]
	s_nop 0
	v_pk_fma_f32 v[6:7], v[6:7], v[66:67], v[2:3] op_sel_hi:[1,0,1] neg_lo:[0,0,1] neg_hi:[0,0,1]
	v_pk_mul_f32 v[2:3], v[20:21], v[72:73] op_sel_hi:[1,0]
	s_nop 0
	v_pk_mul_f32 v[2:3], v[166:167], v[2:3]
	s_nop 0
	v_pk_fma_f32 v[4:5], v[4:5], v[66:67], v[2:3] op_sel_hi:[1,0,1] neg_lo:[0,0,1] neg_hi:[0,0,1]
	s_nop 0
	v_pk_fma_f32 v[0:1], v[4:5], v[4:5], v[0:1]
	v_mul_f32_e32 v2, v5, v5
	v_pk_add_f32 v[0:1], v[2:3], v[0:1] op_sel_hi:[0,1]
	v_pk_fma_f32 v[0:1], v[6:7], v[6:7], v[0:1]
	v_mul_f32_e32 v2, v7, v7
	v_pk_add_f32 v[0:1], v[2:3], v[0:1] op_sel_hi:[0,1]
	v_pk_mul_f32 v[2:3], v[26:27], v[72:73] op_sel_hi:[1,0]
	s_nop 0
	v_pk_mul_f32 v[2:3], v[166:167], v[2:3]
	s_nop 0
	v_pk_fma_f32 v[10:11], v[10:11], v[66:67], v[2:3] op_sel_hi:[1,0,1] neg_lo:[0,0,1] neg_hi:[0,0,1]
	v_pk_mul_f32 v[2:3], v[24:25], v[72:73] op_sel_hi:[1,0]
	s_nop 0
	v_pk_mul_f32 v[2:3], v[166:167], v[2:3]
	s_nop 0
	v_pk_fma_f32 v[8:9], v[8:9], v[66:67], v[2:3] op_sel_hi:[1,0,1] neg_lo:[0,0,1] neg_hi:[0,0,1]
	s_nop 0
	v_pk_fma_f32 v[0:1], v[8:9], v[8:9], v[0:1]
	v_mul_f32_e32 v2, v9, v9
	v_pk_add_f32 v[0:1], v[2:3], v[0:1] op_sel_hi:[0,1]
	v_pk_fma_f32 v[0:1], v[10:11], v[10:11], v[0:1]
	v_mul_f32_e32 v2, v11, v11
	v_pk_add_f32 v[0:1], v[2:3], v[0:1] op_sel_hi:[0,1]
	v_pk_mul_f32 v[2:3], v[28:29], v[72:73] op_sel_hi:[1,0]
	s_nop 0
	v_pk_mul_f32 v[2:3], v[166:167], v[2:3]
	s_nop 0
	v_pk_fma_f32 v[12:13], v[12:13], v[66:67], v[2:3] op_sel_hi:[1,0,1] neg_lo:[0,0,1] neg_hi:[0,0,1]
	s_nop 0
	v_pk_fma_f32 v[0:1], v[12:13], v[12:13], v[0:1]
	v_mul_f32_e32 v2, v13, v13
	v_pk_add_f32 v[0:1], v[2:3], v[0:1] op_sel_hi:[0,1]
	v_pk_fma_f32 v[0:1], v[14:15], v[14:15], v[0:1]
	v_mul_f32_e32 v2, v15, v15
	v_pk_add_f32 v[0:1], v[2:3], v[0:1] op_sel_hi:[0,1]
	v_mov_b32_e32 v1, v0
	s_nop 1
	v_permlane32_swap_b32_e32 v0, v1
	v_add_f32_e32 v0, v0, v1
	v_fmamk_f32 v0, v0, 0x3c800000, v196
	v_cmp_gt_f32_e32 vcc, s35, v0
	v_mul_f32_e32 v1, 0x4b800000, v0
	s_nop 0
	v_cndmask_b32_e32 v0, v0, v1, vcc
	v_rsq_f32_e32 v0, v0
	s_nop 0
	v_mul_f32_e32 v1, 0x45800000, v0
	v_cndmask_b32_e32 v0, v0, v1, vcc
	v_mul_f32_e32 v20, v74, v0
	v_pk_mul_f32 v[0:1], v[32:33], v[20:21] op_sel_hi:[1,0]
	v_pk_mul_f32 v[2:3], v[30:31], v[20:21] op_sel_hi:[1,0]
	s_waitcnt vmcnt(0)
	v_pk_mul_f32 v[0:1], v[68:69], v[0:1]
	v_pk_mul_f32 v[2:3], v[70:71], v[2:3]
	v_cvt_pk_bf16_f32 v0, v0, v1
	v_cvt_pk_bf16_f32 v1, v2, v3
	global_store_dwordx2 v[64:65], v[0:1], off
	global_load_dwordx4 v[0:3], v[186:187], off offset:32
	v_pk_mul_f32 v[22:23], v[36:37], v[20:21] op_sel_hi:[1,0]
	v_pk_mul_f32 v[16:17], v[16:17], v[20:21] op_sel_hi:[1,0]
	v_pk_mul_f32 v[4:5], v[4:5], v[20:21] op_sel_hi:[1,0]
	s_waitcnt vmcnt(0)
	v_pk_mul_f32 v[0:1], v[0:1], v[22:23]
	v_pk_mul_f32 v[22:23], v[38:39], v[20:21] op_sel_hi:[1,0]
	v_cvt_pk_bf16_f32 v0, v0, v1
	v_pk_mul_f32 v[2:3], v[2:3], v[22:23]
	v_pk_mul_f32 v[22:23], v[40:41], v[20:21] op_sel_hi:[1,0]
	v_cvt_pk_bf16_f32 v1, v2, v3
	global_store_dwordx2 v[64:65], v[0:1], off offset:16
	global_load_dwordx4 v[0:3], v[186:187], off offset:64
	s_waitcnt vmcnt(0)
	v_pk_mul_f32 v[0:1], v[0:1], v[22:23]
	v_pk_mul_f32 v[22:23], v[42:43], v[20:21] op_sel_hi:[1,0]
	v_cvt_pk_bf16_f32 v0, v0, v1
	v_pk_mul_f32 v[2:3], v[2:3], v[22:23]
	v_pk_mul_f32 v[22:23], v[44:45], v[20:21] op_sel_hi:[1,0]
	v_cvt_pk_bf16_f32 v1, v2, v3
	global_store_dwordx2 v[64:65], v[0:1], off offset:32
	global_load_dwordx4 v[0:3], v[186:187], off offset:96
	s_waitcnt vmcnt(0)
	v_pk_mul_f32 v[0:1], v[0:1], v[22:23]
	v_pk_mul_f32 v[22:23], v[46:47], v[20:21] op_sel_hi:[1,0]
	v_cvt_pk_bf16_f32 v0, v0, v1
	v_pk_mul_f32 v[2:3], v[2:3], v[22:23]
	s_nop 0
	v_cvt_pk_bf16_f32 v1, v2, v3
	global_store_dwordx2 v[64:65], v[0:1], off offset:48
	global_load_dwordx4 v[0:3], v[186:187], off offset:128
	s_waitcnt vmcnt(0)
	v_pk_mul_f32 v[0:1], v[0:1], v[16:17]
	v_pk_mul_f32 v[16:17], v[18:19], v[20:21] op_sel_hi:[1,0]
	v_cvt_pk_bf16_f32 v0, v0, v1
	v_pk_mul_f32 v[2:3], v[2:3], v[16:17]
	s_nop 0
	v_cvt_pk_bf16_f32 v1, v2, v3
	global_store_dwordx2 v[64:65], v[0:1], off offset:64
	global_load_dwordx4 v[0:3], v[186:187], off offset:160
	s_waitcnt vmcnt(0)
	v_pk_mul_f32 v[0:1], v[0:1], v[4:5]
	v_pk_mul_f32 v[4:5], v[6:7], v[20:21] op_sel_hi:[1,0]
	v_cvt_pk_bf16_f32 v0, v0, v1
	v_pk_mul_f32 v[2:3], v[2:3], v[4:5]
	v_pk_mul_f32 v[4:5], v[8:9], v[20:21] op_sel_hi:[1,0]
	v_cvt_pk_bf16_f32 v1, v2, v3
	global_store_dwordx2 v[64:65], v[0:1], off offset:80
	global_load_dwordx4 v[0:3], v[186:187], off offset:192
	s_waitcnt vmcnt(0)
	v_pk_mul_f32 v[0:1], v[4:5], v[0:1]
	v_pk_mul_f32 v[4:5], v[10:11], v[20:21] op_sel_hi:[1,0]
	v_cvt_pk_bf16_f32 v0, v0, v1
	v_pk_mul_f32 v[2:3], v[4:5], v[2:3]
	v_pk_mul_f32 v[4:5], v[12:13], v[20:21] op_sel_hi:[1,0]
	v_cvt_pk_bf16_f32 v1, v2, v3
	global_store_dwordx2 v[64:65], v[0:1], off offset:96
	global_load_dwordx4 v[0:3], v[186:187], off offset:224
	s_waitcnt vmcnt(0)
	v_pk_mul_f32 v[0:1], v[4:5], v[0:1]
	v_pk_mul_f32 v[4:5], v[14:15], v[20:21] op_sel_hi:[1,0]
	v_cvt_pk_bf16_f32 v0, v0, v1
	v_pk_mul_f32 v[2:3], v[4:5], v[2:3]
	s_branch .LBB0_617

.Lpeel_gate:
	s_add_u32 s28, s82, 0xfffe0080
	s_addc_u32 s29, s83, -1
	s_add_i32 s85, 0, 0x10000
	s_cmp_eq_u32 s84, 4
	s_cselect_b32 vcc_hi, s37, s29
	s_cselect_b32 vcc_lo, s50, s28
	s_cselect_b32 s97, s51, s75
	s_cselect_b32 s96, s71, s73
	s_add_i32 s28, 0, 0x14000
	v_add_u32_e32 v0, s85, v183
	v_add_u32_e32 v12, s28, v183
	ds_read_b128 v[16:19], v0
	ds_read_b128 v[20:23], v0 offset:1024
	ds_read_b128 v[24:27], v0 offset:2048
	ds_read_b128 v[28:31], v0 offset:3072
	ds_read_b128 v[0:3], v12
	ds_read_b128 v[4:7], v12 offset:1024
	ds_read_b128 v[8:11], v12 offset:2048
	ds_read_b128 v[12:15], v12 offset:3072
	v_lshl_add_u64 v[194:195], s[82:83], 0, v[170:171]
	s_add_i32 m0, s6, 0xc000
	ds_read_b128 v[174:177], v184
	ds_read_b128 v[178:181], v184 offset:1024
	ds_read_b128 v[186:189], v184 offset:2048
	ds_read_b128 v[190:193], v184 offset:3072
	ds_read_b128 v[216:219], v184 offset:4096
	ds_read_b128 v[220:223], v184 offset:5120
	ds_read_b128 v[224:227], v184 offset:6144
	ds_read_b128 v[228:231], v184 offset:7168
	global_load_lds_dwordx4 v[194:195], off
	v_lshl_add_u64 v[194:195], s[82:83], 0, v[172:173]
	s_add_i32 m0, s6, 0xe000
	s_nop 0
	global_load_lds_dwordx4 v[194:195], off
	s_waitcnt vmcnt(8)
	s_waitcnt lgkmcnt(0)
	s_barrier
	s_setprio 1
	v_mfma_scale_f32_16x16x128_f8f6f4 v[158:161], v[16:23], v[174:181], 0, v200, v201 op_sel_hi:[0,0,0]
	v_mfma_scale_f32_16x16x128_f8f6f4 v[154:157], v[24:31], v[174:181], 0, v200, v201 op_sel_hi:[0,0,0]
	v_mfma_scale_f32_16x16x128_f8f6f4 v[150:153], v[16:23], v[186:193], 0, v200, v201 op_sel_hi:[0,0,0]
	v_mfma_scale_f32_16x16x128_f8f6f4 v[146:149], v[24:31], v[186:193], 0, v200, v201 op_sel_hi:[0,0,0]
	v_mfma_scale_f32_16x16x128_f8f6f4 v[134:137], v[16:23], v[216:223], 0, v200, v201 op_sel_hi:[0,0,0]
	v_mfma_scale_f32_16x16x128_f8f6f4 v[130:133], v[24:31], v[216:223], 0, v200, v201 op_sel_hi:[0,0,0]
	v_mfma_scale_f32_16x16x128_f8f6f4 v[118:121], v[16:23], v[224:231], 0, v200, v201 op_sel_hi:[0,0,0]
	v_mfma_scale_f32_16x16x128_f8f6f4 v[114:117], v[24:31], v[224:231], 0, v200, v201 op_sel_hi:[0,0,0]
	s_setprio 0
	s_setprio 1
	v_mfma_scale_f32_16x16x128_f8f6f4 v[142:145], v[0:7], v[174:181], 0, v200, v201 op_sel_hi:[0,0,0]
	v_mfma_scale_f32_16x16x128_f8f6f4 v[138:141], v[8:15], v[174:181], 0, v200, v201 op_sel_hi:[0,0,0]
	v_mfma_scale_f32_16x16x128_f8f6f4 v[126:129], v[0:7], v[186:193], 0, v200, v201 op_sel_hi:[0,0,0]
	v_mfma_scale_f32_16x16x128_f8f6f4 v[122:125], v[8:15], v[186:193], 0, v200, v201 op_sel_hi:[0,0,0]
	v_mfma_scale_f32_16x16x128_f8f6f4 v[108:111], v[0:7], v[216:223], 0, v200, v201 op_sel_hi:[0,0,0]
	v_mfma_scale_f32_16x16x128_f8f6f4 v[104:107], v[8:15], v[216:223], 0, v200, v201 op_sel_hi:[0,0,0]
	v_mfma_scale_f32_16x16x128_f8f6f4 v[100:103], v[0:7], v[224:231], 0, v200, v201 op_sel_hi:[0,0,0]
	v_mfma_scale_f32_16x16x128_f8f6f4 v[96:99], v[8:15], v[224:231], 0, v200, v201 op_sel_hi:[0,0,0]
	s_setprio 0
	s_barrier
	s_add_i32 s29, s85, s14
	v_lshl_add_u64 v[174:175], s[96:97], 0, v[164:165]
	s_mov_b32 m0, s29
	ds_read_b128 v[186:189], v184 offset:16384
	ds_read_b128 v[190:193], v184 offset:17408
	ds_read_b128 v[216:219], v184 offset:18432
	ds_read_b128 v[220:223], v184 offset:19456
	ds_read_b128 v[224:227], v184 offset:20480
	ds_read_b128 v[228:231], v184 offset:21504
	ds_read_b128 v[232:235], v184 offset:22528
	ds_read_b128 v[236:239], v184 offset:23552
	global_load_lds_dwordx4 v[174:175], off
	s_add_i32 m0, s29, 0x2000
	s_add_u32 s30, s96, 0x20000
	v_lshl_add_u64 v[176:177], s[96:97], 0, v[168:169]
	s_addc_u32 s31, s97, 0
	s_add_i32 s28, s28, s14
	global_load_lds_dwordx4 v[176:177], off
	v_lshl_add_u64 v[178:179], s[30:31], 0, v[164:165]
	s_mov_b32 m0, s28
	v_lshl_add_u64 v[180:181], vcc, 0, v[166:167]
	global_load_lds_dwordx4 v[178:179], off
	v_lshl_add_u64 v[178:179], s[30:31], 0, v[168:169]
	s_add_i32 m0, s28, 0x2000
	s_nop 0
	global_load_lds_dwordx4 v[178:179], off
	v_lshl_add_u64 v[178:179], vcc, 0, v[162:163]
	s_mov_b32 m0, s6
	s_nop 0
	global_load_lds_dwordx4 v[178:179], off
	s_mov_b32 m0, s7
	s_nop 0
	global_load_lds_dwordx4 v[180:181], off
	s_waitcnt vmcnt(8)
	s_waitcnt lgkmcnt(0)
	s_barrier
	s_setprio 1
	v_mfma_scale_f32_16x16x128_f8f6f4 v[92:95], v[16:23], v[186:193], 0, v200, v201 op_sel_hi:[0,0,0]
	v_mfma_scale_f32_16x16x128_f8f6f4 v[88:91], v[24:31], v[186:193], 0, v200, v201 op_sel_hi:[0,0,0]
	v_mfma_scale_f32_16x16x128_f8f6f4 v[84:87], v[16:23], v[216:223], 0, v200, v201 op_sel_hi:[0,0,0]
	v_mfma_scale_f32_16x16x128_f8f6f4 v[80:83], v[24:31], v[216:223], 0, v200, v201 op_sel_hi:[0,0,0]
	v_mfma_scale_f32_16x16x128_f8f6f4 v[68:71], v[16:23], v[224:231], 0, v200, v201 op_sel_hi:[0,0,0]
	v_mfma_scale_f32_16x16x128_f8f6f4 v[64:67], v[24:31], v[224:231], 0, v200, v201 op_sel_hi:[0,0,0]
	v_mfma_scale_f32_16x16x128_f8f6f4 v[52:55], v[16:23], v[232:239], 0, v200, v201 op_sel_hi:[0,0,0]
	v_mfma_scale_f32_16x16x128_f8f6f4 v[48:51], v[24:31], v[232:239], 0, v200, v201 op_sel_hi:[0,0,0]
	s_setprio 0
	s_setprio 1
	v_mfma_scale_f32_16x16x128_f8f6f4 v[76:79], v[0:7], v[186:193], 0, v200, v201 op_sel_hi:[0,0,0]
	v_mfma_scale_f32_16x16x128_f8f6f4 v[72:75], v[8:15], v[186:193], 0, v200, v201 op_sel_hi:[0,0,0]
	v_mfma_scale_f32_16x16x128_f8f6f4 v[60:63], v[0:7], v[216:223], 0, v200, v201 op_sel_hi:[0,0,0]
	v_mfma_scale_f32_16x16x128_f8f6f4 v[56:59], v[8:15], v[216:223], 0, v200, v201 op_sel_hi:[0,0,0]
	v_mfma_scale_f32_16x16x128_f8f6f4 v[44:47], v[0:7], v[224:231], 0, v200, v201 op_sel_hi:[0,0,0]
	v_mfma_scale_f32_16x16x128_f8f6f4 v[40:43], v[8:15], v[224:231], 0, v200, v201 op_sel_hi:[0,0,0]
	v_mfma_scale_f32_16x16x128_f8f6f4 v[36:39], v[0:7], v[232:239], 0, v200, v201 op_sel_hi:[0,0,0]
	v_mfma_scale_f32_16x16x128_f8f6f4 v[32:35], v[8:15], v[232:239], 0, v200, v201 op_sel_hi:[0,0,0]
	s_setprio 0
	s_barrier
	s_add_i32 s30, 0, 0x18000
	s_add_i32 s31, 0, 0x1c000
	v_add_u32_e32 v12, s30, v183
	v_add_u32_e32 v28, s31, v183
	ds_read_b128 v[0:3], v12
	ds_read_b128 v[4:7], v12 offset:1024
	ds_read_b128 v[8:11], v12 offset:2048
	ds_read_b128 v[12:15], v12 offset:3072
	ds_read_b128 v[16:19], v28
	ds_read_b128 v[20:23], v28 offset:1024
	ds_read_b128 v[24:27], v28 offset:2048
	ds_read_b128 v[28:31], v28 offset:3072
	s_add_u32 s28, vcc_lo, 0x20000
	s_addc_u32 s29, vcc_hi, 0
	s_mov_b32 m0, s86
	v_lshl_add_u64 v[194:195], s[28:29], 0, v[162:163]
	ds_read_b128 v[186:189], v184 offset:32768
	ds_read_b128 v[190:193], v184 offset:33792
	ds_read_b128 v[216:219], v184 offset:34816
	ds_read_b128 v[220:223], v184 offset:35840
	ds_read_b128 v[224:227], v184 offset:36864
	ds_read_b128 v[228:231], v184 offset:37888
	ds_read_b128 v[232:235], v184 offset:38912
	ds_read_b128 v[236:239], v184 offset:39936
	global_load_lds_dwordx4 v[194:195], off
	v_lshl_add_u64 v[194:195], s[28:29], 0, v[166:167]
	s_mov_b32 m0, s33
	s_nop 0
	global_load_lds_dwordx4 v[194:195], off
	s_waitcnt vmcnt(8)
	s_waitcnt lgkmcnt(0)
	s_barrier
	s_setprio 1
	v_mfma_scale_f32_16x16x128_f8f6f4 v[158:161], v[0:7], v[186:193], v[158:161], v200, v201 op_sel_hi:[0,0,0]
	v_mfma_scale_f32_16x16x128_f8f6f4 v[154:157], v[8:15], v[186:193], v[154:157], v200, v201 op_sel_hi:[0,0,0]
	v_mfma_scale_f32_16x16x128_f8f6f4 v[150:153], v[0:7], v[216:223], v[150:153], v200, v201 op_sel_hi:[0,0,0]
	v_mfma_scale_f32_16x16x128_f8f6f4 v[146:149], v[8:15], v[216:223], v[146:149], v200, v201 op_sel_hi:[0,0,0]
	v_mfma_scale_f32_16x16x128_f8f6f4 v[134:137], v[0:7], v[224:231], v[134:137], v200, v201 op_sel_hi:[0,0,0]
	v_mfma_scale_f32_16x16x128_f8f6f4 v[130:133], v[8:15], v[224:231], v[130:133], v200, v201 op_sel_hi:[0,0,0]
	v_mfma_scale_f32_16x16x128_f8f6f4 v[118:121], v[0:7], v[232:239], v[118:121], v200, v201 op_sel_hi:[0,0,0]
	v_mfma_scale_f32_16x16x128_f8f6f4 v[114:117], v[8:15], v[232:239], v[114:117], v200, v201 op_sel_hi:[0,0,0]
	s_setprio 0
	s_setprio 1
	v_mfma_scale_f32_16x16x128_f8f6f4 v[142:145], v[16:23], v[186:193], v[142:145], v200, v201 op_sel_hi:[0,0,0]
	v_mfma_scale_f32_16x16x128_f8f6f4 v[138:141], v[24:31], v[186:193], v[138:141], v200, v201 op_sel_hi:[0,0,0]
	v_mfma_scale_f32_16x16x128_f8f6f4 v[126:129], v[16:23], v[216:223], v[126:129], v200, v201 op_sel_hi:[0,0,0]
	v_mfma_scale_f32_16x16x128_f8f6f4 v[122:125], v[24:31], v[216:223], v[122:125], v200, v201 op_sel_hi:[0,0,0]
	v_mfma_scale_f32_16x16x128_f8f6f4 v[108:111], v[16:23], v[224:231], v[108:111], v200, v201 op_sel_hi:[0,0,0]
	v_mfma_scale_f32_16x16x128_f8f6f4 v[104:107], v[24:31], v[224:231], v[104:107], v200, v201 op_sel_hi:[0,0,0]
	v_mfma_scale_f32_16x16x128_f8f6f4 v[100:103], v[16:23], v[232:239], v[100:103], v200, v201 op_sel_hi:[0,0,0]
	v_mfma_scale_f32_16x16x128_f8f6f4 v[96:99], v[24:31], v[232:239], v[96:99], v200, v201 op_sel_hi:[0,0,0]
	s_setprio 0
	s_barrier
	s_add_i32 s28, s30, s14
	v_lshl_add_u64 v[174:175], v[174:175], 0, s[56:57]
	s_mov_b32 m0, s28
	ds_read_b128 v[186:189], v184 offset:49152
	ds_read_b128 v[190:193], v184 offset:50176
	ds_read_b128 v[216:219], v184 offset:51200
	ds_read_b128 v[220:223], v184 offset:52224
	ds_read_b128 v[224:227], v184 offset:53248
	ds_read_b128 v[228:231], v184 offset:54272
	ds_read_b128 v[232:235], v184 offset:55296
	ds_read_b128 v[236:239], v184 offset:56320
	global_load_lds_dwordx4 v[174:175], off
	s_add_i32 m0, s28, 0x2000
	s_add_u32 s28, s96, 0x20080
	v_lshl_add_u64 v[174:175], v[176:177], 0, s[56:57]
	s_addc_u32 s29, s97, 0
	s_add_i32 s30, s31, s14
	global_load_lds_dwordx4 v[174:175], off
	v_lshl_add_u64 v[174:175], s[28:29], 0, v[164:165]
	s_mov_b32 m0, s30
	s_nop 0
	global_load_lds_dwordx4 v[174:175], off
	v_lshl_add_u64 v[174:175], s[28:29], 0, v[168:169]
	s_add_i32 m0, s30, 0x2000
	s_nop 0
	global_load_lds_dwordx4 v[174:175], off
	v_lshl_add_u64 v[174:175], v[178:179], 0, s[56:57]
	s_mov_b32 m0, s54
	s_nop 0
	global_load_lds_dwordx4 v[174:175], off
	v_lshl_add_u64 v[174:175], v[180:181], 0, s[56:57]
	s_mov_b32 m0, s55
	s_nop 0
	global_load_lds_dwordx4 v[174:175], off
	s_waitcnt vmcnt(8)
	s_waitcnt lgkmcnt(0)
	s_barrier
	s_setprio 1
	v_mfma_scale_f32_16x16x128_f8f6f4 v[92:95], v[0:7], v[186:193], v[92:95], v200, v201 op_sel_hi:[0,0,0]
	v_mfma_scale_f32_16x16x128_f8f6f4 v[88:91], v[8:15], v[186:193], v[88:91], v200, v201 op_sel_hi:[0,0,0]
	v_mfma_scale_f32_16x16x128_f8f6f4 v[84:87], v[0:7], v[216:223], v[84:87], v200, v201 op_sel_hi:[0,0,0]
	v_mfma_scale_f32_16x16x128_f8f6f4 v[80:83], v[8:15], v[216:223], v[80:83], v200, v201 op_sel_hi:[0,0,0]
	v_mfma_scale_f32_16x16x128_f8f6f4 v[68:71], v[0:7], v[224:231], v[68:71], v200, v201 op_sel_hi:[0,0,0]
	v_mfma_scale_f32_16x16x128_f8f6f4 v[64:67], v[8:15], v[224:231], v[64:67], v200, v201 op_sel_hi:[0,0,0]
	v_mfma_scale_f32_16x16x128_f8f6f4 v[52:55], v[0:7], v[232:239], v[52:55], v200, v201 op_sel_hi:[0,0,0]
	v_mfma_scale_f32_16x16x128_f8f6f4 v[48:51], v[8:15], v[232:239], v[48:51], v200, v201 op_sel_hi:[0,0,0]
	s_setprio 0
	s_setprio 1
	v_mfma_scale_f32_16x16x128_f8f6f4 v[76:79], v[16:23], v[186:193], v[76:79], v200, v201 op_sel_hi:[0,0,0]
	v_mfma_scale_f32_16x16x128_f8f6f4 v[72:75], v[24:31], v[186:193], v[72:75], v200, v201 op_sel_hi:[0,0,0]
	v_mfma_scale_f32_16x16x128_f8f6f4 v[60:63], v[16:23], v[216:223], v[60:63], v200, v201 op_sel_hi:[0,0,0]
	v_mfma_scale_f32_16x16x128_f8f6f4 v[56:59], v[24:31], v[216:223], v[56:59], v200, v201 op_sel_hi:[0,0,0]
	v_mfma_scale_f32_16x16x128_f8f6f4 v[44:47], v[16:23], v[224:231], v[44:47], v200, v201 op_sel_hi:[0,0,0]
	v_mfma_scale_f32_16x16x128_f8f6f4 v[40:43], v[24:31], v[224:231], v[40:43], v200, v201 op_sel_hi:[0,0,0]
	v_mfma_scale_f32_16x16x128_f8f6f4 v[36:39], v[16:23], v[232:239], v[36:39], v200, v201 op_sel_hi:[0,0,0]
	v_mfma_scale_f32_16x16x128_f8f6f4 v[32:35], v[24:31], v[232:239], v[32:35], v200, v201 op_sel_hi:[0,0,0]
	s_setprio 0
	s_barrier
	s_add_i32 s84, s84, 2
	s_add_u32 s82, s82, 0x100
	s_addc_u32 s83, s83, 0
	s_add_u32 s73, s73, 0x100
	s_addc_u32 s75, s75, 0
	s_cmp_gt_u32 s84, 5
.LBB0_666:
	s_add_u32 s28, s82, 0xfffe0080
	s_addc_u32 s29, s83, -1
	s_add_i32 s85, 0, 0x10000
	s_cmp_eq_u32 s84, 4
	s_cselect_b32 vcc_hi, s37, s29
	s_cselect_b32 vcc_lo, s50, s28
	s_cselect_b32 s97, s51, s75
	s_cselect_b32 s96, s71, s73
	s_add_i32 s28, 0, 0x14000
	v_add_u32_e32 v0, s85, v183
	v_add_u32_e32 v12, s28, v183
	ds_read_b128 v[16:19], v0
	ds_read_b128 v[20:23], v0 offset:1024
	ds_read_b128 v[24:27], v0 offset:2048
	ds_read_b128 v[28:31], v0 offset:3072
	ds_read_b128 v[0:3], v12
	ds_read_b128 v[4:7], v12 offset:1024
	ds_read_b128 v[8:11], v12 offset:2048
	ds_read_b128 v[12:15], v12 offset:3072
	v_lshl_add_u64 v[194:195], s[82:83], 0, v[170:171]
	s_add_i32 m0, s6, 0xc000
	ds_read_b128 v[174:177], v184
	ds_read_b128 v[178:181], v184 offset:1024
	ds_read_b128 v[186:189], v184 offset:2048
	ds_read_b128 v[190:193], v184 offset:3072
	ds_read_b128 v[216:219], v184 offset:4096
	ds_read_b128 v[220:223], v184 offset:5120
	ds_read_b128 v[224:227], v184 offset:6144
	ds_read_b128 v[228:231], v184 offset:7168
	global_load_lds_dwordx4 v[194:195], off
	v_lshl_add_u64 v[194:195], s[82:83], 0, v[172:173]
	s_add_i32 m0, s6, 0xe000
	s_nop 0
	global_load_lds_dwordx4 v[194:195], off
	s_waitcnt vmcnt(8)
	s_waitcnt lgkmcnt(0)
	s_barrier
	s_setprio 1
	v_mfma_scale_f32_16x16x128_f8f6f4 v[158:161], v[16:23], v[174:181], v[158:161], v200, v201 op_sel_hi:[0,0,0]
	v_mfma_scale_f32_16x16x128_f8f6f4 v[154:157], v[24:31], v[174:181], v[154:157], v200, v201 op_sel_hi:[0,0,0]
	v_mfma_scale_f32_16x16x128_f8f6f4 v[150:153], v[16:23], v[186:193], v[150:153], v200, v201 op_sel_hi:[0,0,0]
	v_mfma_scale_f32_16x16x128_f8f6f4 v[146:149], v[24:31], v[186:193], v[146:149], v200, v201 op_sel_hi:[0,0,0]
	v_mfma_scale_f32_16x16x128_f8f6f4 v[134:137], v[16:23], v[216:223], v[134:137], v200, v201 op_sel_hi:[0,0,0]
	v_mfma_scale_f32_16x16x128_f8f6f4 v[130:133], v[24:31], v[216:223], v[130:133], v200, v201 op_sel_hi:[0,0,0]
	v_mfma_scale_f32_16x16x128_f8f6f4 v[118:121], v[16:23], v[224:231], v[118:121], v200, v201 op_sel_hi:[0,0,0]
	v_mfma_scale_f32_16x16x128_f8f6f4 v[114:117], v[24:31], v[224:231], v[114:117], v200, v201 op_sel_hi:[0,0,0]
	s_setprio 0
	s_setprio 1
	v_mfma_scale_f32_16x16x128_f8f6f4 v[142:145], v[0:7], v[174:181], v[142:145], v200, v201 op_sel_hi:[0,0,0]
	v_mfma_scale_f32_16x16x128_f8f6f4 v[138:141], v[8:15], v[174:181], v[138:141], v200, v201 op_sel_hi:[0,0,0]
	v_mfma_scale_f32_16x16x128_f8f6f4 v[126:129], v[0:7], v[186:193], v[126:129], v200, v201 op_sel_hi:[0,0,0]
	v_mfma_scale_f32_16x16x128_f8f6f4 v[122:125], v[8:15], v[186:193], v[122:125], v200, v201 op_sel_hi:[0,0,0]
	v_mfma_scale_f32_16x16x128_f8f6f4 v[108:111], v[0:7], v[216:223], v[108:111], v200, v201 op_sel_hi:[0,0,0]
	v_mfma_scale_f32_16x16x128_f8f6f4 v[104:107], v[8:15], v[216:223], v[104:107], v200, v201 op_sel_hi:[0,0,0]
	v_mfma_scale_f32_16x16x128_f8f6f4 v[100:103], v[0:7], v[224:231], v[100:103], v200, v201 op_sel_hi:[0,0,0]
	v_mfma_scale_f32_16x16x128_f8f6f4 v[96:99], v[8:15], v[224:231], v[96:99], v200, v201 op_sel_hi:[0,0,0]
	s_setprio 0
	s_barrier
	s_add_i32 s29, s85, s14
	v_lshl_add_u64 v[174:175], s[96:97], 0, v[164:165]
	s_mov_b32 m0, s29
	ds_read_b128 v[186:189], v184 offset:16384
	ds_read_b128 v[190:193], v184 offset:17408
	ds_read_b128 v[216:219], v184 offset:18432
	ds_read_b128 v[220:223], v184 offset:19456
	ds_read_b128 v[224:227], v184 offset:20480
	ds_read_b128 v[228:231], v184 offset:21504
	ds_read_b128 v[232:235], v184 offset:22528
	ds_read_b128 v[236:239], v184 offset:23552
	global_load_lds_dwordx4 v[174:175], off
	s_add_i32 m0, s29, 0x2000
	s_add_u32 s30, s96, 0x20000
	v_lshl_add_u64 v[176:177], s[96:97], 0, v[168:169]
	s_addc_u32 s31, s97, 0
	s_add_i32 s28, s28, s14
	global_load_lds_dwordx4 v[176:177], off
	v_lshl_add_u64 v[178:179], s[30:31], 0, v[164:165]
	s_mov_b32 m0, s28
	v_lshl_add_u64 v[180:181], vcc, 0, v[166:167]
	global_load_lds_dwordx4 v[178:179], off
	v_lshl_add_u64 v[178:179], s[30:31], 0, v[168:169]
	s_add_i32 m0, s28, 0x2000
	s_nop 0
	global_load_lds_dwordx4 v[178:179], off
	v_lshl_add_u64 v[178:179], vcc, 0, v[162:163]
	s_mov_b32 m0, s6
	s_nop 0
	global_load_lds_dwordx4 v[178:179], off
	s_mov_b32 m0, s7
	s_nop 0
	global_load_lds_dwordx4 v[180:181], off
	s_waitcnt vmcnt(8)
	s_waitcnt lgkmcnt(0)
	s_barrier
	s_setprio 1
	v_mfma_scale_f32_16x16x128_f8f6f4 v[92:95], v[16:23], v[186:193], v[92:95], v200, v201 op_sel_hi:[0,0,0]
	v_mfma_scale_f32_16x16x128_f8f6f4 v[88:91], v[24:31], v[186:193], v[88:91], v200, v201 op_sel_hi:[0,0,0]
	v_mfma_scale_f32_16x16x128_f8f6f4 v[84:87], v[16:23], v[216:223], v[84:87], v200, v201 op_sel_hi:[0,0,0]
	v_mfma_scale_f32_16x16x128_f8f6f4 v[80:83], v[24:31], v[216:223], v[80:83], v200, v201 op_sel_hi:[0,0,0]
	v_mfma_scale_f32_16x16x128_f8f6f4 v[68:71], v[16:23], v[224:231], v[68:71], v200, v201 op_sel_hi:[0,0,0]
	v_mfma_scale_f32_16x16x128_f8f6f4 v[64:67], v[24:31], v[224:231], v[64:67], v200, v201 op_sel_hi:[0,0,0]
	v_mfma_scale_f32_16x16x128_f8f6f4 v[52:55], v[16:23], v[232:239], v[52:55], v200, v201 op_sel_hi:[0,0,0]
	v_mfma_scale_f32_16x16x128_f8f6f4 v[48:51], v[24:31], v[232:239], v[48:51], v200, v201 op_sel_hi:[0,0,0]
	s_setprio 0
	s_setprio 1
	v_mfma_scale_f32_16x16x128_f8f6f4 v[76:79], v[0:7], v[186:193], v[76:79], v200, v201 op_sel_hi:[0,0,0]
	v_mfma_scale_f32_16x16x128_f8f6f4 v[72:75], v[8:15], v[186:193], v[72:75], v200, v201 op_sel_hi:[0,0,0]
	v_mfma_scale_f32_16x16x128_f8f6f4 v[60:63], v[0:7], v[216:223], v[60:63], v200, v201 op_sel_hi:[0,0,0]
	v_mfma_scale_f32_16x16x128_f8f6f4 v[56:59], v[8:15], v[216:223], v[56:59], v200, v201 op_sel_hi:[0,0,0]
	v_mfma_scale_f32_16x16x128_f8f6f4 v[44:47], v[0:7], v[224:231], v[44:47], v200, v201 op_sel_hi:[0,0,0]
	v_mfma_scale_f32_16x16x128_f8f6f4 v[40:43], v[8:15], v[224:231], v[40:43], v200, v201 op_sel_hi:[0,0,0]
	v_mfma_scale_f32_16x16x128_f8f6f4 v[36:39], v[0:7], v[232:239], v[36:39], v200, v201 op_sel_hi:[0,0,0]
	v_mfma_scale_f32_16x16x128_f8f6f4 v[32:35], v[8:15], v[232:239], v[32:35], v200, v201 op_sel_hi:[0,0,0]
	s_setprio 0
	s_barrier
	s_add_i32 s30, 0, 0x18000
	s_add_i32 s31, 0, 0x1c000
	v_add_u32_e32 v12, s30, v183
	v_add_u32_e32 v28, s31, v183
	ds_read_b128 v[0:3], v12
	ds_read_b128 v[4:7], v12 offset:1024
	ds_read_b128 v[8:11], v12 offset:2048
	ds_read_b128 v[12:15], v12 offset:3072
	ds_read_b128 v[16:19], v28
	ds_read_b128 v[20:23], v28 offset:1024
	ds_read_b128 v[24:27], v28 offset:2048
	ds_read_b128 v[28:31], v28 offset:3072
	s_add_u32 s28, vcc_lo, 0x20000
	s_addc_u32 s29, vcc_hi, 0
	s_mov_b32 m0, s86
	v_lshl_add_u64 v[194:195], s[28:29], 0, v[162:163]
	ds_read_b128 v[186:189], v184 offset:32768
	ds_read_b128 v[190:193], v184 offset:33792
	ds_read_b128 v[216:219], v184 offset:34816
	ds_read_b128 v[220:223], v184 offset:35840
	ds_read_b128 v[224:227], v184 offset:36864
	ds_read_b128 v[228:231], v184 offset:37888
	ds_read_b128 v[232:235], v184 offset:38912
	ds_read_b128 v[236:239], v184 offset:39936
	global_load_lds_dwordx4 v[194:195], off
	v_lshl_add_u64 v[194:195], s[28:29], 0, v[166:167]
	s_mov_b32 m0, s33
	s_nop 0
	global_load_lds_dwordx4 v[194:195], off
	s_waitcnt vmcnt(8)
	s_waitcnt lgkmcnt(0)
	s_barrier
	s_setprio 1
	v_mfma_scale_f32_16x16x128_f8f6f4 v[158:161], v[0:7], v[186:193], v[158:161], v200, v201 op_sel_hi:[0,0,0]
	v_mfma_scale_f32_16x16x128_f8f6f4 v[154:157], v[8:15], v[186:193], v[154:157], v200, v201 op_sel_hi:[0,0,0]
	v_mfma_scale_f32_16x16x128_f8f6f4 v[150:153], v[0:7], v[216:223], v[150:153], v200, v201 op_sel_hi:[0,0,0]
	v_mfma_scale_f32_16x16x128_f8f6f4 v[146:149], v[8:15], v[216:223], v[146:149], v200, v201 op_sel_hi:[0,0,0]
	v_mfma_scale_f32_16x16x128_f8f6f4 v[134:137], v[0:7], v[224:231], v[134:137], v200, v201 op_sel_hi:[0,0,0]
	v_mfma_scale_f32_16x16x128_f8f6f4 v[130:133], v[8:15], v[224:231], v[130:133], v200, v201 op_sel_hi:[0,0,0]
	v_mfma_scale_f32_16x16x128_f8f6f4 v[118:121], v[0:7], v[232:239], v[118:121], v200, v201 op_sel_hi:[0,0,0]
	v_mfma_scale_f32_16x16x128_f8f6f4 v[114:117], v[8:15], v[232:239], v[114:117], v200, v201 op_sel_hi:[0,0,0]
	s_setprio 0
	s_setprio 1
	v_mfma_scale_f32_16x16x128_f8f6f4 v[142:145], v[16:23], v[186:193], v[142:145], v200, v201 op_sel_hi:[0,0,0]
	v_mfma_scale_f32_16x16x128_f8f6f4 v[138:141], v[24:31], v[186:193], v[138:141], v200, v201 op_sel_hi:[0,0,0]
	v_mfma_scale_f32_16x16x128_f8f6f4 v[126:129], v[16:23], v[216:223], v[126:129], v200, v201 op_sel_hi:[0,0,0]
	v_mfma_scale_f32_16x16x128_f8f6f4 v[122:125], v[24:31], v[216:223], v[122:125], v200, v201 op_sel_hi:[0,0,0]
	v_mfma_scale_f32_16x16x128_f8f6f4 v[108:111], v[16:23], v[224:231], v[108:111], v200, v201 op_sel_hi:[0,0,0]
	v_mfma_scale_f32_16x16x128_f8f6f4 v[104:107], v[24:31], v[224:231], v[104:107], v200, v201 op_sel_hi:[0,0,0]
	v_mfma_scale_f32_16x16x128_f8f6f4 v[100:103], v[16:23], v[232:239], v[100:103], v200, v201 op_sel_hi:[0,0,0]
	v_mfma_scale_f32_16x16x128_f8f6f4 v[96:99], v[24:31], v[232:239], v[96:99], v200, v201 op_sel_hi:[0,0,0]
	s_setprio 0
	s_barrier
	s_add_i32 s28, s30, s14
	v_lshl_add_u64 v[174:175], v[174:175], 0, s[56:57]
	s_mov_b32 m0, s28
	ds_read_b128 v[186:189], v184 offset:49152
	ds_read_b128 v[190:193], v184 offset:50176
	ds_read_b128 v[216:219], v184 offset:51200
	ds_read_b128 v[220:223], v184 offset:52224
	ds_read_b128 v[224:227], v184 offset:53248
	ds_read_b128 v[228:231], v184 offset:54272
	ds_read_b128 v[232:235], v184 offset:55296
	ds_read_b128 v[236:239], v184 offset:56320
	global_load_lds_dwordx4 v[174:175], off
	s_add_i32 m0, s28, 0x2000
	s_add_u32 s28, s96, 0x20080
	v_lshl_add_u64 v[174:175], v[176:177], 0, s[56:57]
	s_addc_u32 s29, s97, 0
	s_add_i32 s30, s31, s14
	global_load_lds_dwordx4 v[174:175], off
	v_lshl_add_u64 v[174:175], s[28:29], 0, v[164:165]
	s_mov_b32 m0, s30
	s_nop 0
	global_load_lds_dwordx4 v[174:175], off
	v_lshl_add_u64 v[174:175], s[28:29], 0, v[168:169]
	s_add_i32 m0, s30, 0x2000
	s_nop 0
	global_load_lds_dwordx4 v[174:175], off
	v_lshl_add_u64 v[174:175], v[178:179], 0, s[56:57]
	s_mov_b32 m0, s54
	s_nop 0
	global_load_lds_dwordx4 v[174:175], off
	v_lshl_add_u64 v[174:175], v[180:181], 0, s[56:57]
	s_mov_b32 m0, s55
	s_nop 0
	global_load_lds_dwordx4 v[174:175], off
	s_waitcnt vmcnt(8)
	s_waitcnt lgkmcnt(0)
	s_barrier
	s_setprio 1
	v_mfma_scale_f32_16x16x128_f8f6f4 v[92:95], v[0:7], v[186:193], v[92:95], v200, v201 op_sel_hi:[0,0,0]
	v_mfma_scale_f32_16x16x128_f8f6f4 v[88:91], v[8:15], v[186:193], v[88:91], v200, v201 op_sel_hi:[0,0,0]
	v_mfma_scale_f32_16x16x128_f8f6f4 v[84:87], v[0:7], v[216:223], v[84:87], v200, v201 op_sel_hi:[0,0,0]
	v_mfma_scale_f32_16x16x128_f8f6f4 v[80:83], v[8:15], v[216:223], v[80:83], v200, v201 op_sel_hi:[0,0,0]
	v_mfma_scale_f32_16x16x128_f8f6f4 v[68:71], v[0:7], v[224:231], v[68:71], v200, v201 op_sel_hi:[0,0,0]
	v_mfma_scale_f32_16x16x128_f8f6f4 v[64:67], v[8:15], v[224:231], v[64:67], v200, v201 op_sel_hi:[0,0,0]
	v_mfma_scale_f32_16x16x128_f8f6f4 v[52:55], v[0:7], v[232:239], v[52:55], v200, v201 op_sel_hi:[0,0,0]
	v_mfma_scale_f32_16x16x128_f8f6f4 v[48:51], v[8:15], v[232:239], v[48:51], v200, v201 op_sel_hi:[0,0,0]
	s_setprio 0
	s_setprio 1
	v_mfma_scale_f32_16x16x128_f8f6f4 v[76:79], v[16:23], v[186:193], v[76:79], v200, v201 op_sel_hi:[0,0,0]
	v_mfma_scale_f32_16x16x128_f8f6f4 v[72:75], v[24:31], v[186:193], v[72:75], v200, v201 op_sel_hi:[0,0,0]
	v_mfma_scale_f32_16x16x128_f8f6f4 v[60:63], v[16:23], v[216:223], v[60:63], v200, v201 op_sel_hi:[0,0,0]
	v_mfma_scale_f32_16x16x128_f8f6f4 v[56:59], v[24:31], v[216:223], v[56:59], v200, v201 op_sel_hi:[0,0,0]
	v_mfma_scale_f32_16x16x128_f8f6f4 v[44:47], v[16:23], v[224:231], v[44:47], v200, v201 op_sel_hi:[0,0,0]
	v_mfma_scale_f32_16x16x128_f8f6f4 v[40:43], v[24:31], v[224:231], v[40:43], v200, v201 op_sel_hi:[0,0,0]
	v_mfma_scale_f32_16x16x128_f8f6f4 v[36:39], v[16:23], v[232:239], v[36:39], v200, v201 op_sel_hi:[0,0,0]
	v_mfma_scale_f32_16x16x128_f8f6f4 v[32:35], v[24:31], v[232:239], v[32:35], v200, v201 op_sel_hi:[0,0,0]
	s_setprio 0
	s_barrier
	s_add_i32 s84, s84, 2
	s_add_u32 s82, s82, 0x100
	s_addc_u32 s83, s83, 0
	s_add_u32 s73, s73, 0x100
	s_addc_u32 s75, s75, 0
	s_cmp_gt_u32 s84, 5
	s_cbranch_scc0 .LBB0_666
	s_and_b64 vcc, exec, s[64:65]
	s_cbranch_vccz .LBB0_669
	s_barrier

.LBB0_758:
	s_add_u32 s30, s76, s80
	s_addc_u32 s31, s77, s81
	s_add_u32 s49, s30, 0x100
	s_addc_u32 s60, s31, 0
	s_and_b64 s[28:29], s[50:51], exec
	s_cselect_b32 s97, s65, s60
	s_cselect_b32 s96, s64, s49
	s_add_u32 s28, s72, s80
	s_addc_u32 s29, s73, s81
	s_add_u32 s49, s28, 0x100
	s_addc_u32 s60, s29, 0
	s_add_i32 s69, 0, 0x10000
	s_and_b64 s[28:29], s[50:51], exec
	s_cselect_b32 vcc_hi, s7, s60
	s_cselect_b32 vcc_lo, s37, s49
	s_add_i32 s49, 0, 0x14000
	s_add_u32 s30, s30, 0x10080
	s_addc_u32 s31, s31, 0
	s_add_i32 s84, s69, s25
	s_add_i32 m0, s26, 0xc000
	s_add_i32 s75, s26, 0xe000
	s_add_i32 s85, s84, 0x2000
	v_add_u32_e32 v112, s69, v175
	s_add_u32 s50, vcc_lo, 0x10000
	ds_read_b128 v[132:135], v112
	ds_read_b128 v[136:139], v112 offset:1024
	ds_read_b128 v[140:143], v112 offset:2048
	ds_read_b128 v[144:147], v112 offset:3072
	v_add_u32_e32 v112, s49, v175
	s_addc_u32 s51, vcc_hi, 0
	s_add_i32 s86, s49, s25
	ds_read_b128 v[148:151], v112
	ds_read_b128 v[152:155], v112 offset:1024
	ds_read_b128 v[156:159], v112 offset:2048
	ds_read_b128 v[160:163], v112 offset:3072
	s_add_i32 s63, s86, 0x2000
	s_add_i32 s29, 0, 0x18000
	s_add_i32 s60, 0, 0x1c000
	s_add_u32 s82, s96, 0x10000
	s_addc_u32 s83, s97, 0
	s_add_i32 s28, s29, s25
	s_add_i32 s45, s28, 0x2000
	s_add_u32 s80, vcc_lo, 0x10080
	s_addc_u32 s81, vcc_hi, 0
	s_add_i32 s69, s60, s25
	s_add_i32 s49, s69, 0x2000
	v_lshl_add_u64 v[114:115], s[30:31], 0, v[164:165]
	ds_read_b128 v[178:181], v176
	ds_read_b128 v[182:185], v176 offset:1024
	ds_read_b128 v[186:189], v176 offset:2048
	ds_read_b128 v[190:193], v176 offset:3072
	ds_read_b128 v[206:209], v176 offset:4096
	ds_read_b128 v[210:213], v176 offset:5120
	ds_read_b128 v[216:219], v176 offset:6144
	ds_read_b128 v[220:223], v176 offset:7168
	global_load_lds_dwordx4 v[114:115], off
	v_lshl_add_u64 v[114:115], s[30:31], 0, v[168:169]
	s_mov_b32 m0, s75
	s_nop 0
	global_load_lds_dwordx4 v[114:115], off
	s_waitcnt vmcnt(8)
	s_waitcnt lgkmcnt(0)
	s_barrier
	s_setprio 1
	v_mfma_f32_16x16x32_bf16 v[128:131], v[132:135], v[178:181], v[128:131]
	v_mfma_f32_16x16x32_bf16 v[124:127], v[140:143], v[178:181], v[124:127]
	v_mfma_f32_16x16x32_bf16 v[120:123], v[132:135], v[186:189], v[120:123]
	v_mfma_f32_16x16x32_bf16 v[114:117], v[140:143], v[186:189], v[116:119]
	v_mfma_f32_16x16x32_bf16 v[108:111], v[132:135], v[206:209], v[108:111]
	v_mfma_f32_16x16x32_bf16 v[104:107], v[140:143], v[206:209], v[104:107]
	v_mfma_f32_16x16x32_bf16 v[100:103], v[132:135], v[216:219], v[100:103]
	v_mfma_f32_16x16x32_bf16 v[96:99], v[140:143], v[216:219], v[96:99]
	v_mfma_f32_16x16x32_bf16 v[128:131], v[136:139], v[182:185], v[128:131]
	v_mfma_f32_16x16x32_bf16 v[124:127], v[144:147], v[182:185], v[124:127]
	v_mfma_f32_16x16x32_bf16 v[120:123], v[136:139], v[190:193], v[120:123]
	v_mfma_f32_16x16x32_bf16 v[114:117], v[144:147], v[190:193], v[114:117]
	v_mfma_f32_16x16x32_bf16 v[108:111], v[136:139], v[210:213], v[108:111]
	v_mfma_f32_16x16x32_bf16 v[104:107], v[144:147], v[210:213], v[104:107]
	v_mfma_f32_16x16x32_bf16 v[100:103], v[136:139], v[220:223], v[100:103]
	v_mfma_f32_16x16x32_bf16 v[96:99], v[144:147], v[220:223], v[96:99]
	s_setprio 0
	s_setprio 1
	v_mfma_f32_16x16x32_bf16 v[92:95], v[148:151], v[178:181], v[92:95]
	v_mfma_f32_16x16x32_bf16 v[88:91], v[156:159], v[178:181], v[88:91]
	v_mfma_f32_16x16x32_bf16 v[84:87], v[148:151], v[186:189], v[84:87]
	v_mfma_f32_16x16x32_bf16 v[80:83], v[156:159], v[186:189], v[80:83]
	v_mfma_f32_16x16x32_bf16 v[76:79], v[148:151], v[206:209], v[76:79]
	v_mfma_f32_16x16x32_bf16 v[72:75], v[156:159], v[206:209], v[72:75]
	v_mfma_f32_16x16x32_bf16 v[68:71], v[148:151], v[216:219], v[68:71]
	v_mfma_f32_16x16x32_bf16 v[64:67], v[156:159], v[216:219], v[64:67]
	v_mfma_f32_16x16x32_bf16 v[92:95], v[152:155], v[182:185], v[92:95]
	v_mfma_f32_16x16x32_bf16 v[88:91], v[160:163], v[182:185], v[88:91]
	v_mfma_f32_16x16x32_bf16 v[84:87], v[152:155], v[190:193], v[84:87]
	v_mfma_f32_16x16x32_bf16 v[80:83], v[160:163], v[190:193], v[80:83]
	v_mfma_f32_16x16x32_bf16 v[76:79], v[152:155], v[210:213], v[76:79]
	v_mfma_f32_16x16x32_bf16 v[72:75], v[160:163], v[210:213], v[72:75]
	v_mfma_f32_16x16x32_bf16 v[68:71], v[152:155], v[220:223], v[68:71]
	v_mfma_f32_16x16x32_bf16 v[64:67], v[160:163], v[220:223], v[64:67]
	s_setprio 0
	s_barrier
	s_mov_b32 m0, s84
	v_lshl_add_u64 v[172:173], vcc, 0, v[166:167]
	ds_read_b128 v[178:181], v176 offset:16384
	ds_read_b128 v[182:185], v176 offset:17408
	ds_read_b128 v[186:189], v176 offset:18432
	ds_read_b128 v[190:193], v176 offset:19456
	ds_read_b128 v[206:209], v176 offset:20480
	ds_read_b128 v[210:213], v176 offset:21504
	ds_read_b128 v[216:219], v176 offset:22528
	ds_read_b128 v[220:223], v176 offset:23552
	global_load_lds_dwordx4 v[172:173], off
	v_lshl_add_u64 v[194:195], vcc, 0, v[170:171]
	s_mov_b32 m0, s85
	v_lshl_add_u64 v[118:119], s[50:51], 0, v[166:167]
	global_load_lds_dwordx4 v[194:195], off
	s_mov_b32 m0, s86
	v_lshl_add_u64 v[224:225], s[96:97], 0, v[164:165]
	global_load_lds_dwordx4 v[118:119], off
	v_lshl_add_u64 v[118:119], s[50:51], 0, v[170:171]
	s_mov_b32 m0, s63
	v_lshl_add_u64 v[226:227], s[96:97], 0, v[168:169]
	global_load_lds_dwordx4 v[118:119], off
	s_mov_b32 m0, s26
	s_nop 0
	global_load_lds_dwordx4 v[224:225], off
	s_mov_b32 m0, s27
	s_nop 0
	global_load_lds_dwordx4 v[226:227], off
	s_waitcnt vmcnt(8)
	s_waitcnt lgkmcnt(0)
	s_barrier
	s_setprio 1
	v_mfma_f32_16x16x32_bf16 v[60:63], v[132:135], v[178:181], v[60:63]
	v_mfma_f32_16x16x32_bf16 v[56:59], v[140:143], v[178:181], v[56:59]
	v_mfma_f32_16x16x32_bf16 v[52:55], v[132:135], v[186:189], v[52:55]
	v_mfma_f32_16x16x32_bf16 v[48:51], v[140:143], v[186:189], v[48:51]
	v_mfma_f32_16x16x32_bf16 v[44:47], v[132:135], v[206:209], v[44:47]
	v_mfma_f32_16x16x32_bf16 v[40:43], v[140:143], v[206:209], v[40:43]
	v_mfma_f32_16x16x32_bf16 v[36:39], v[132:135], v[216:219], v[36:39]
	v_mfma_f32_16x16x32_bf16 v[32:35], v[140:143], v[216:219], v[32:35]
	v_mfma_f32_16x16x32_bf16 v[60:63], v[136:139], v[182:185], v[60:63]
	v_mfma_f32_16x16x32_bf16 v[56:59], v[144:147], v[182:185], v[56:59]
	v_mfma_f32_16x16x32_bf16 v[52:55], v[136:139], v[190:193], v[52:55]
	v_mfma_f32_16x16x32_bf16 v[48:51], v[144:147], v[190:193], v[48:51]
	v_mfma_f32_16x16x32_bf16 v[44:47], v[136:139], v[210:213], v[44:47]
	v_mfma_f32_16x16x32_bf16 v[40:43], v[144:147], v[210:213], v[40:43]
	v_mfma_f32_16x16x32_bf16 v[36:39], v[136:139], v[220:223], v[36:39]
	v_mfma_f32_16x16x32_bf16 v[32:35], v[144:147], v[220:223], v[32:35]
	s_setprio 0
	s_setprio 1
	v_mfma_f32_16x16x32_bf16 v[28:31], v[148:151], v[178:181], v[28:31]
	v_mfma_f32_16x16x32_bf16 v[24:27], v[156:159], v[178:181], v[24:27]
	v_mfma_f32_16x16x32_bf16 v[20:23], v[148:151], v[186:189], v[20:23]
	v_mfma_f32_16x16x32_bf16 v[16:19], v[156:159], v[186:189], v[16:19]
	v_mfma_f32_16x16x32_bf16 v[12:15], v[148:151], v[206:209], v[12:15]
	v_mfma_f32_16x16x32_bf16 v[8:11], v[156:159], v[206:209], v[8:11]
	v_mfma_f32_16x16x32_bf16 v[4:7], v[148:151], v[216:219], v[4:7]
	v_mfma_f32_16x16x32_bf16 v[0:3], v[156:159], v[216:219], v[0:3]
	v_mfma_f32_16x16x32_bf16 v[28:31], v[152:155], v[182:185], v[28:31]
	v_mfma_f32_16x16x32_bf16 v[24:27], v[160:163], v[182:185], v[24:27]
	v_mfma_f32_16x16x32_bf16 v[20:23], v[152:155], v[190:193], v[20:23]
	v_mfma_f32_16x16x32_bf16 v[16:19], v[160:163], v[190:193], v[16:19]
	v_mfma_f32_16x16x32_bf16 v[12:15], v[152:155], v[210:213], v[12:15]
	v_mfma_f32_16x16x32_bf16 v[8:11], v[160:163], v[210:213], v[8:11]
	v_mfma_f32_16x16x32_bf16 v[4:7], v[152:155], v[220:223], v[4:7]
	v_mfma_f32_16x16x32_bf16 v[0:3], v[160:163], v[220:223], v[0:3]
	s_setprio 0
	s_barrier
	v_add_u32_e32 v112, s29, v175
	ds_read_b128 v[132:135], v112
	ds_read_b128 v[136:139], v112 offset:1024
	ds_read_b128 v[140:143], v112 offset:2048
	ds_read_b128 v[144:147], v112 offset:3072
	v_add_u32_e32 v112, s60, v175
	ds_read_b128 v[148:151], v112
	ds_read_b128 v[152:155], v112 offset:1024
	ds_read_b128 v[156:159], v112 offset:2048
	ds_read_b128 v[160:163], v112 offset:3072
	s_mov_b32 m0, s33
	v_lshl_add_u64 v[118:119], s[82:83], 0, v[164:165]
	ds_read_b128 v[178:181], v176 offset:32768
	ds_read_b128 v[182:185], v176 offset:33792
	ds_read_b128 v[186:189], v176 offset:34816
	ds_read_b128 v[190:193], v176 offset:35840
	ds_read_b128 v[206:209], v176 offset:36864
	ds_read_b128 v[210:213], v176 offset:37888
	ds_read_b128 v[216:219], v176 offset:38912
	ds_read_b128 v[220:223], v176 offset:39936
	global_load_lds_dwordx4 v[118:119], off
	v_lshl_add_u64 v[118:119], s[82:83], 0, v[168:169]
	s_mov_b32 m0, s34
	s_nop 0
	global_load_lds_dwordx4 v[118:119], off
	s_waitcnt vmcnt(8)
	s_waitcnt lgkmcnt(0)
	s_barrier
	s_setprio 1
	v_mfma_f32_16x16x32_bf16 v[128:131], v[132:135], v[178:181], v[128:131]
	v_mfma_f32_16x16x32_bf16 v[124:127], v[140:143], v[178:181], v[124:127]
	v_mfma_f32_16x16x32_bf16 v[118:121], v[132:135], v[186:189], v[120:123]
	v_mfma_f32_16x16x32_bf16 v[114:117], v[140:143], v[186:189], v[114:117]
	v_mfma_f32_16x16x32_bf16 v[108:111], v[132:135], v[206:209], v[108:111]
	v_mfma_f32_16x16x32_bf16 v[104:107], v[140:143], v[206:209], v[104:107]
	v_mfma_f32_16x16x32_bf16 v[100:103], v[132:135], v[216:219], v[100:103]
	v_mfma_f32_16x16x32_bf16 v[96:99], v[140:143], v[216:219], v[96:99]
	v_mfma_f32_16x16x32_bf16 v[128:131], v[136:139], v[182:185], v[128:131]
	v_mfma_f32_16x16x32_bf16 v[124:127], v[144:147], v[182:185], v[124:127]
	v_mfma_f32_16x16x32_bf16 v[120:123], v[136:139], v[190:193], v[118:121]
	v_mfma_f32_16x16x32_bf16 v[116:119], v[144:147], v[190:193], v[114:117]
	v_mfma_f32_16x16x32_bf16 v[108:111], v[136:139], v[210:213], v[108:111]
	v_mfma_f32_16x16x32_bf16 v[104:107], v[144:147], v[210:213], v[104:107]
	v_mfma_f32_16x16x32_bf16 v[100:103], v[136:139], v[220:223], v[100:103]
	v_mfma_f32_16x16x32_bf16 v[96:99], v[144:147], v[220:223], v[96:99]
	s_setprio 0
	s_setprio 1
	v_mfma_f32_16x16x32_bf16 v[92:95], v[148:151], v[178:181], v[92:95]
	v_mfma_f32_16x16x32_bf16 v[88:91], v[156:159], v[178:181], v[88:91]
	v_mfma_f32_16x16x32_bf16 v[84:87], v[148:151], v[186:189], v[84:87]
	v_mfma_f32_16x16x32_bf16 v[80:83], v[156:159], v[186:189], v[80:83]
	v_mfma_f32_16x16x32_bf16 v[76:79], v[148:151], v[206:209], v[76:79]
	v_mfma_f32_16x16x32_bf16 v[72:75], v[156:159], v[206:209], v[72:75]
	v_mfma_f32_16x16x32_bf16 v[68:71], v[148:151], v[216:219], v[68:71]
	v_mfma_f32_16x16x32_bf16 v[64:67], v[156:159], v[216:219], v[64:67]
	v_mfma_f32_16x16x32_bf16 v[92:95], v[152:155], v[182:185], v[92:95]
	v_mfma_f32_16x16x32_bf16 v[88:91], v[160:163], v[182:185], v[88:91]
	v_mfma_f32_16x16x32_bf16 v[84:87], v[152:155], v[190:193], v[84:87]
	v_mfma_f32_16x16x32_bf16 v[80:83], v[160:163], v[190:193], v[80:83]
	v_mfma_f32_16x16x32_bf16 v[76:79], v[152:155], v[210:213], v[76:79]
	v_mfma_f32_16x16x32_bf16 v[72:75], v[160:163], v[210:213], v[72:75]
	v_mfma_f32_16x16x32_bf16 v[68:71], v[152:155], v[220:223], v[68:71]
	v_mfma_f32_16x16x32_bf16 v[64:67], v[160:163], v[220:223], v[64:67]
	s_setprio 0
	s_barrier
	s_mov_b32 m0, s28
	v_lshl_add_u64 v[114:115], v[172:173], 0, s[56:57]
	ds_read_b128 v[178:181], v176 offset:49152
	ds_read_b128 v[182:185], v176 offset:50176
	ds_read_b128 v[186:189], v176 offset:51200
	ds_read_b128 v[190:193], v176 offset:52224
	ds_read_b128 v[206:209], v176 offset:53248
	ds_read_b128 v[210:213], v176 offset:54272
	ds_read_b128 v[216:219], v176 offset:55296
	ds_read_b128 v[220:223], v176 offset:56320
	global_load_lds_dwordx4 v[114:115], off
	v_lshl_add_u64 v[114:115], v[194:195], 0, s[56:57]
	s_mov_b32 m0, s45
	s_nop 0
	global_load_lds_dwordx4 v[114:115], off
	v_lshl_add_u64 v[114:115], s[80:81], 0, v[166:167]
	s_mov_b32 m0, s69
	s_nop 0
	global_load_lds_dwordx4 v[114:115], off
	v_lshl_add_u64 v[114:115], s[80:81], 0, v[170:171]
	s_mov_b32 m0, s49
	s_nop 0
	global_load_lds_dwordx4 v[114:115], off
	v_lshl_add_u64 v[114:115], v[224:225], 0, s[56:57]
	s_mov_b32 m0, s54
	s_nop 0
	global_load_lds_dwordx4 v[114:115], off
	v_lshl_add_u64 v[114:115], v[226:227], 0, s[56:57]
	s_mov_b32 m0, s55
	s_nop 0
	global_load_lds_dwordx4 v[114:115], off
	s_waitcnt vmcnt(8)
	s_waitcnt lgkmcnt(0)
	s_barrier
	s_setprio 1
	v_mfma_f32_16x16x32_bf16 v[60:63], v[132:135], v[178:181], v[60:63]
	v_mfma_f32_16x16x32_bf16 v[56:59], v[140:143], v[178:181], v[56:59]
	v_mfma_f32_16x16x32_bf16 v[52:55], v[132:135], v[186:189], v[52:55]
	v_mfma_f32_16x16x32_bf16 v[48:51], v[140:143], v[186:189], v[48:51]
	v_mfma_f32_16x16x32_bf16 v[44:47], v[132:135], v[206:209], v[44:47]
	v_mfma_f32_16x16x32_bf16 v[40:43], v[140:143], v[206:209], v[40:43]
	v_mfma_f32_16x16x32_bf16 v[36:39], v[132:135], v[216:219], v[36:39]
	v_mfma_f32_16x16x32_bf16 v[32:35], v[140:143], v[216:219], v[32:35]
	v_mfma_f32_16x16x32_bf16 v[60:63], v[136:139], v[182:185], v[60:63]
	v_mfma_f32_16x16x32_bf16 v[56:59], v[144:147], v[182:185], v[56:59]
	v_mfma_f32_16x16x32_bf16 v[52:55], v[136:139], v[190:193], v[52:55]
	v_mfma_f32_16x16x32_bf16 v[48:51], v[144:147], v[190:193], v[48:51]
	v_mfma_f32_16x16x32_bf16 v[44:47], v[136:139], v[210:213], v[44:47]
	v_mfma_f32_16x16x32_bf16 v[40:43], v[144:147], v[210:213], v[40:43]
	v_mfma_f32_16x16x32_bf16 v[36:39], v[136:139], v[220:223], v[36:39]
	v_mfma_f32_16x16x32_bf16 v[32:35], v[144:147], v[220:223], v[32:35]
	s_setprio 0
	s_setprio 1
	v_mfma_f32_16x16x32_bf16 v[28:31], v[148:151], v[178:181], v[28:31]
	v_mfma_f32_16x16x32_bf16 v[24:27], v[156:159], v[178:181], v[24:27]
	v_mfma_f32_16x16x32_bf16 v[20:23], v[148:151], v[186:189], v[20:23]
	v_mfma_f32_16x16x32_bf16 v[16:19], v[156:159], v[186:189], v[16:19]
	v_mfma_f32_16x16x32_bf16 v[12:15], v[148:151], v[206:209], v[12:15]
	v_mfma_f32_16x16x32_bf16 v[8:11], v[156:159], v[206:209], v[8:11]
	v_mfma_f32_16x16x32_bf16 v[4:7], v[148:151], v[216:219], v[4:7]
	v_mfma_f32_16x16x32_bf16 v[0:3], v[156:159], v[216:219], v[0:3]
	v_mfma_f32_16x16x32_bf16 v[28:31], v[152:155], v[182:185], v[28:31]
	v_mfma_f32_16x16x32_bf16 v[24:27], v[160:163], v[182:185], v[24:27]
	v_mfma_f32_16x16x32_bf16 v[20:23], v[152:155], v[190:193], v[20:23]
	v_mfma_f32_16x16x32_bf16 v[16:19], v[160:163], v[190:193], v[16:19]
	v_mfma_f32_16x16x32_bf16 v[12:15], v[152:155], v[210:213], v[12:15]
	v_mfma_f32_16x16x32_bf16 v[8:11], v[160:163], v[210:213], v[8:11]
	v_mfma_f32_16x16x32_bf16 v[4:7], v[152:155], v[220:223], v[4:7]
	v_mfma_f32_16x16x32_bf16 v[0:3], v[160:163], v[220:223], v[0:3]
	s_setprio 0
	s_barrier
	s_andn2_b64 vcc, exec, s[78:79]
	s_mov_b64 s[50:51], -1
	s_mov_b64 s[78:79], 0
	s_mov_b64 s[80:81], 0x100
	s_cbranch_vccz .LBB0_758
	s_and_b64 vcc, exec, s[46:47]
	s_cbranch_vccz .LBB0_761
	s_barrier

.LBB0_771:
	v_readlane_b32 s2, v255, 22
	v_readlane_b32 s6, v252, 2
	s_add_i32 s2, s2, 7
	v_readlane_b32 s7, v252, 3
	s_cmp_ge_i32 s2, s7
	s_cbranch_scc1 .LBB0_821
	s_waitcnt vmcnt(0)
	s_waitcnt lgkmcnt(0)
	s_barrier
	s_mov_b64 s[6:7], exec
	v_readlane_b32 s12, v252, 22
	v_readlane_b32 s13, v252, 23
	s_and_b64 s[12:13], s[6:7], s[12:13]
	s_mov_b64 exec, s[12:13]
	s_cbranch_execz .LBB0_820
	v_readlane_b32 s4, v254, 44
	s_waitcnt vmcnt(0) expcnt(0) lgkmcnt(0)
	s_nop 0
	v_mov_b32_e32 v0, s4
	ds_read_b32 v2, v0
	v_readlane_b32 s4, v254, 45
	s_waitcnt lgkmcnt(0)
	v_cmp_ne_u32_e32 vcc, 0, v2
	v_mov_b32_e32 v0, s4
	ds_read_b32 v0, v0
	s_cbranch_vccnz .LBB0_788
	v_readlane_b32 s14, v252, 24
	v_readlane_b32 s15, v252, 25
	s_load_dwordx2 s[12:13], s[14:15], 0x0
	s_load_dword s4, s[14:15], 0x8
	s_waitcnt lgkmcnt(0)
	s_mul_i32 s12, s13, s12
	s_mul_i32 s4, s12, s4
	s_mov_b32 s12, 1
	s_branch .LBB0_776

.Lpeel_wo:
	s_add_u32 s28, s78, 0xfffc0080
	s_addc_u32 s29, s79, -1
	s_add_i32 s30, 0, 0x10000
	s_cmp_eq_u32 s84, 12
	s_cselect_b32 s83, s37, s29
	s_cselect_b32 s82, s50, s28
	v_add_u32_e32 v112, s30, v183
	s_cselect_b32 s81, s51, s77
	s_cselect_b32 s80, s65, s71
	s_add_i32 s31, 0, 0x14000
	ds_read_b128 v[130:133], v112
	ds_read_b128 v[134:137], v112 offset:1024
	ds_read_b128 v[150:153], v112 offset:2048
	ds_read_b128 v[154:157], v112 offset:3072
	v_add_u32_e32 v112, s31, v183
	ds_read_b128 v[158:161], v112
	ds_read_b128 v[162:165], v112 offset:1024
	ds_read_b128 v[166:169], v112 offset:2048
	ds_read_b128 v[170:173], v112 offset:3072
	v_lshl_add_u64 v[194:195], s[78:79], 0, v[146:147]
	s_add_i32 m0, s34, 0xc000
	ds_read_b128 v[174:177], v184
	ds_read_b128 v[178:181], v184 offset:1024
	ds_read_b128 v[186:189], v184 offset:2048
	ds_read_b128 v[190:193], v184 offset:3072
	ds_read_b128 v[206:209], v184 offset:4096
	ds_read_b128 v[210:213], v184 offset:5120
	ds_read_b128 v[216:219], v184 offset:6144
	ds_read_b128 v[220:223], v184 offset:7168
	global_load_lds_dwordx4 v[194:195], off
	v_lshl_add_u64 v[194:195], s[78:79], 0, v[148:149]
	s_add_i32 m0, s34, 0xe000
	s_nop 0
	global_load_lds_dwordx4 v[194:195], off
	s_waitcnt vmcnt(8)
	s_waitcnt lgkmcnt(0)
	s_barrier
	s_setprio 1
	v_mfma_f32_16x16x32_bf16 v[126:129], v[130:133], v[174:177], 0
	v_mfma_f32_16x16x32_bf16 v[122:125], v[150:153], v[174:177], 0
	v_mfma_f32_16x16x32_bf16 v[118:121], v[130:133], v[186:189], 0
	v_mfma_f32_16x16x32_bf16 v[114:117], v[150:153], v[186:189], 0
	v_mfma_f32_16x16x32_bf16 v[108:111], v[130:133], v[206:209], 0
	v_mfma_f32_16x16x32_bf16 v[104:107], v[150:153], v[206:209], 0
	v_mfma_f32_16x16x32_bf16 v[100:103], v[130:133], v[216:219], 0
	v_mfma_f32_16x16x32_bf16 v[96:99], v[150:153], v[216:219], 0
	v_mfma_f32_16x16x32_bf16 v[126:129], v[134:137], v[178:181], v[126:129]
	v_mfma_f32_16x16x32_bf16 v[122:125], v[154:157], v[178:181], v[122:125]
	v_mfma_f32_16x16x32_bf16 v[118:121], v[134:137], v[190:193], v[118:121]
	v_mfma_f32_16x16x32_bf16 v[114:117], v[154:157], v[190:193], v[114:117]
	v_mfma_f32_16x16x32_bf16 v[108:111], v[134:137], v[210:213], v[108:111]
	v_mfma_f32_16x16x32_bf16 v[104:107], v[154:157], v[210:213], v[104:107]
	v_mfma_f32_16x16x32_bf16 v[100:103], v[134:137], v[220:223], v[100:103]
	v_mfma_f32_16x16x32_bf16 v[96:99], v[154:157], v[220:223], v[96:99]
	s_setprio 0
	s_setprio 1
	v_mfma_f32_16x16x32_bf16 v[60:63], v[158:161], v[174:177], 0
	v_mfma_f32_16x16x32_bf16 v[56:59], v[166:169], v[174:177], 0
	v_mfma_f32_16x16x32_bf16 v[52:55], v[158:161], v[186:189], 0
	v_mfma_f32_16x16x32_bf16 v[48:51], v[166:169], v[186:189], 0
	v_mfma_f32_16x16x32_bf16 v[44:47], v[158:161], v[206:209], 0
	v_mfma_f32_16x16x32_bf16 v[40:43], v[166:169], v[206:209], 0
	v_mfma_f32_16x16x32_bf16 v[36:39], v[158:161], v[216:219], 0
	v_mfma_f32_16x16x32_bf16 v[32:35], v[166:169], v[216:219], 0
	v_mfma_f32_16x16x32_bf16 v[60:63], v[162:165], v[178:181], v[60:63]
	v_mfma_f32_16x16x32_bf16 v[56:59], v[170:173], v[178:181], v[56:59]
	v_mfma_f32_16x16x32_bf16 v[52:55], v[162:165], v[190:193], v[52:55]
	v_mfma_f32_16x16x32_bf16 v[48:51], v[170:173], v[190:193], v[48:51]
	v_mfma_f32_16x16x32_bf16 v[44:47], v[162:165], v[210:213], v[44:47]
	v_mfma_f32_16x16x32_bf16 v[40:43], v[170:173], v[210:213], v[40:43]
	v_mfma_f32_16x16x32_bf16 v[36:39], v[162:165], v[220:223], v[36:39]
	v_mfma_f32_16x16x32_bf16 v[32:35], v[170:173], v[220:223], v[32:35]
	s_setprio 0
	s_barrier
	s_add_i32 s28, s30, s33
	v_lshl_add_u64 v[194:195], s[80:81], 0, v[140:141]
	s_mov_b32 m0, s28
	ds_read_b128 v[174:177], v184 offset:16384
	ds_read_b128 v[178:181], v184 offset:17408
	ds_read_b128 v[186:189], v184 offset:18432
	ds_read_b128 v[190:193], v184 offset:19456
	ds_read_b128 v[206:209], v184 offset:20480
	ds_read_b128 v[210:213], v184 offset:21504
	ds_read_b128 v[216:219], v184 offset:22528
	ds_read_b128 v[220:223], v184 offset:23552
	global_load_lds_dwordx4 v[194:195], off
	s_add_i32 m0, s28, 0x2000
	s_add_u32 s28, s80, 0x40000
	v_lshl_add_u64 v[224:225], s[80:81], 0, v[144:145]
	s_addc_u32 s29, s81, 0
	s_add_i32 s30, s31, s33
	global_load_lds_dwordx4 v[224:225], off
	v_lshl_add_u64 v[226:227], s[28:29], 0, v[140:141]
	s_mov_b32 m0, s30
	v_lshl_add_u64 v[228:229], s[82:83], 0, v[142:143]
	global_load_lds_dwordx4 v[226:227], off
	v_lshl_add_u64 v[226:227], s[28:29], 0, v[144:145]
	s_add_i32 m0, s30, 0x2000
	s_nop 0
	global_load_lds_dwordx4 v[226:227], off
	v_lshl_add_u64 v[226:227], s[82:83], 0, v[138:139]
	s_mov_b32 m0, s34
	s_nop 0
	global_load_lds_dwordx4 v[226:227], off
	s_mov_b32 m0, s54
	s_nop 0
	global_load_lds_dwordx4 v[228:229], off
	s_waitcnt vmcnt(8)
	s_waitcnt lgkmcnt(0)
	s_barrier
	s_setprio 1
	v_mfma_f32_16x16x32_bf16 v[92:95], v[130:133], v[174:177], 0
	v_mfma_f32_16x16x32_bf16 v[88:91], v[150:153], v[174:177], 0
	v_mfma_f32_16x16x32_bf16 v[84:87], v[130:133], v[186:189], 0
	v_mfma_f32_16x16x32_bf16 v[80:83], v[150:153], v[186:189], 0
	v_mfma_f32_16x16x32_bf16 v[76:79], v[130:133], v[206:209], 0
	v_mfma_f32_16x16x32_bf16 v[72:75], v[150:153], v[206:209], 0
	v_mfma_f32_16x16x32_bf16 v[68:71], v[130:133], v[216:219], 0
	v_mfma_f32_16x16x32_bf16 v[64:67], v[150:153], v[216:219], 0
	v_mfma_f32_16x16x32_bf16 v[92:95], v[134:137], v[178:181], v[92:95]
	v_mfma_f32_16x16x32_bf16 v[88:91], v[154:157], v[178:181], v[88:91]
	v_mfma_f32_16x16x32_bf16 v[84:87], v[134:137], v[190:193], v[84:87]
	v_mfma_f32_16x16x32_bf16 v[80:83], v[154:157], v[190:193], v[80:83]
	v_mfma_f32_16x16x32_bf16 v[76:79], v[134:137], v[210:213], v[76:79]
	v_mfma_f32_16x16x32_bf16 v[72:75], v[154:157], v[210:213], v[72:75]
	v_mfma_f32_16x16x32_bf16 v[68:71], v[134:137], v[220:223], v[68:71]
	v_mfma_f32_16x16x32_bf16 v[64:67], v[154:157], v[220:223], v[64:67]
	s_setprio 0
	s_setprio 1
	v_mfma_f32_16x16x32_bf16 v[28:31], v[158:161], v[174:177], 0
	v_mfma_f32_16x16x32_bf16 v[24:27], v[166:169], v[174:177], 0
	v_mfma_f32_16x16x32_bf16 v[20:23], v[158:161], v[186:189], 0
	v_mfma_f32_16x16x32_bf16 v[16:19], v[166:169], v[186:189], 0
	v_mfma_f32_16x16x32_bf16 v[12:15], v[158:161], v[206:209], 0
	v_mfma_f32_16x16x32_bf16 v[8:11], v[166:169], v[206:209], 0
	v_mfma_f32_16x16x32_bf16 v[4:7], v[158:161], v[216:219], 0
	v_mfma_f32_16x16x32_bf16 v[0:3], v[166:169], v[216:219], 0
	v_mfma_f32_16x16x32_bf16 v[28:31], v[162:165], v[178:181], v[28:31]
	v_mfma_f32_16x16x32_bf16 v[24:27], v[170:173], v[178:181], v[24:27]
	v_mfma_f32_16x16x32_bf16 v[20:23], v[162:165], v[190:193], v[20:23]
	v_mfma_f32_16x16x32_bf16 v[16:19], v[170:173], v[190:193], v[16:19]
	v_mfma_f32_16x16x32_bf16 v[12:15], v[162:165], v[210:213], v[12:15]
	v_mfma_f32_16x16x32_bf16 v[8:11], v[170:173], v[210:213], v[8:11]
	v_mfma_f32_16x16x32_bf16 v[4:7], v[162:165], v[220:223], v[4:7]
	v_mfma_f32_16x16x32_bf16 v[0:3], v[170:173], v[220:223], v[0:3]
	s_setprio 0
	s_barrier
	s_add_i32 s30, 0, 0x18000
	v_add_u32_e32 v112, s30, v183
	s_add_i32 s31, 0, 0x1c000
	ds_read_b128 v[130:133], v112
	ds_read_b128 v[134:137], v112 offset:1024
	ds_read_b128 v[150:153], v112 offset:2048
	ds_read_b128 v[154:157], v112 offset:3072
	v_add_u32_e32 v112, s31, v183
	ds_read_b128 v[158:161], v112
	ds_read_b128 v[162:165], v112 offset:1024
	ds_read_b128 v[166:169], v112 offset:2048
	ds_read_b128 v[170:173], v112 offset:3072
	s_add_u32 s28, s82, 0x40000
	s_addc_u32 s29, s83, 0
	s_mov_b32 m0, s55
	v_lshl_add_u64 v[230:231], s[28:29], 0, v[138:139]
	ds_read_b128 v[174:177], v184 offset:32768
	ds_read_b128 v[178:181], v184 offset:33792
	ds_read_b128 v[186:189], v184 offset:34816
	ds_read_b128 v[190:193], v184 offset:35840
	ds_read_b128 v[206:209], v184 offset:36864
	ds_read_b128 v[210:213], v184 offset:37888
	ds_read_b128 v[216:219], v184 offset:38912
	ds_read_b128 v[220:223], v184 offset:39936
	global_load_lds_dwordx4 v[230:231], off
	v_lshl_add_u64 v[230:231], s[28:29], 0, v[142:143]
	s_mov_b32 m0, s58
	s_nop 0
	global_load_lds_dwordx4 v[230:231], off
	s_waitcnt vmcnt(8)
	s_waitcnt lgkmcnt(0)
	s_barrier
	s_setprio 1
	v_mfma_f32_16x16x32_bf16 v[126:129], v[130:133], v[174:177], v[126:129]
	v_mfma_f32_16x16x32_bf16 v[122:125], v[150:153], v[174:177], v[122:125]
	v_mfma_f32_16x16x32_bf16 v[118:121], v[130:133], v[186:189], v[118:121]
	v_mfma_f32_16x16x32_bf16 v[114:117], v[150:153], v[186:189], v[114:117]
	v_mfma_f32_16x16x32_bf16 v[108:111], v[130:133], v[206:209], v[108:111]
	v_mfma_f32_16x16x32_bf16 v[104:107], v[150:153], v[206:209], v[104:107]
	v_mfma_f32_16x16x32_bf16 v[100:103], v[130:133], v[216:219], v[100:103]
	v_mfma_f32_16x16x32_bf16 v[96:99], v[150:153], v[216:219], v[96:99]
	v_mfma_f32_16x16x32_bf16 v[126:129], v[134:137], v[178:181], v[126:129]
	v_mfma_f32_16x16x32_bf16 v[122:125], v[154:157], v[178:181], v[122:125]
	v_mfma_f32_16x16x32_bf16 v[118:121], v[134:137], v[190:193], v[118:121]
	v_mfma_f32_16x16x32_bf16 v[114:117], v[154:157], v[190:193], v[114:117]
	v_mfma_f32_16x16x32_bf16 v[108:111], v[134:137], v[210:213], v[108:111]
	v_mfma_f32_16x16x32_bf16 v[104:107], v[154:157], v[210:213], v[104:107]
	v_mfma_f32_16x16x32_bf16 v[100:103], v[134:137], v[220:223], v[100:103]
	v_mfma_f32_16x16x32_bf16 v[96:99], v[154:157], v[220:223], v[96:99]
	s_setprio 0
	s_setprio 1
	v_mfma_f32_16x16x32_bf16 v[60:63], v[158:161], v[174:177], v[60:63]
	v_mfma_f32_16x16x32_bf16 v[56:59], v[166:169], v[174:177], v[56:59]
	v_mfma_f32_16x16x32_bf16 v[52:55], v[158:161], v[186:189], v[52:55]
	v_mfma_f32_16x16x32_bf16 v[48:51], v[166:169], v[186:189], v[48:51]
	v_mfma_f32_16x16x32_bf16 v[44:47], v[158:161], v[206:209], v[44:47]
	v_mfma_f32_16x16x32_bf16 v[40:43], v[166:169], v[206:209], v[40:43]
	v_mfma_f32_16x16x32_bf16 v[36:39], v[158:161], v[216:219], v[36:39]
	v_mfma_f32_16x16x32_bf16 v[32:35], v[166:169], v[216:219], v[32:35]
	v_mfma_f32_16x16x32_bf16 v[60:63], v[162:165], v[178:181], v[60:63]
	v_mfma_f32_16x16x32_bf16 v[56:59], v[170:173], v[178:181], v[56:59]
	v_mfma_f32_16x16x32_bf16 v[52:55], v[162:165], v[190:193], v[52:55]
	v_mfma_f32_16x16x32_bf16 v[48:51], v[170:173], v[190:193], v[48:51]
	v_mfma_f32_16x16x32_bf16 v[44:47], v[162:165], v[210:213], v[44:47]
	v_mfma_f32_16x16x32_bf16 v[40:43], v[170:173], v[210:213], v[40:43]
	v_mfma_f32_16x16x32_bf16 v[36:39], v[162:165], v[220:223], v[36:39]
	v_mfma_f32_16x16x32_bf16 v[32:35], v[170:173], v[220:223], v[32:35]
	s_setprio 0
	s_barrier
	s_add_i32 s28, s30, s33
	v_lshl_add_u64 v[194:195], v[194:195], 0, s[56:57]
	s_mov_b32 m0, s28
	ds_read_b128 v[174:177], v184 offset:49152
	ds_read_b128 v[178:181], v184 offset:50176
	ds_read_b128 v[186:189], v184 offset:51200
	ds_read_b128 v[190:193], v184 offset:52224
	ds_read_b128 v[206:209], v184 offset:53248
	ds_read_b128 v[210:213], v184 offset:54272
	ds_read_b128 v[216:219], v184 offset:55296
	ds_read_b128 v[220:223], v184 offset:56320
	global_load_lds_dwordx4 v[194:195], off
	s_add_i32 m0, s28, 0x2000
	s_add_u32 s28, s80, 0x40080
	v_lshl_add_u64 v[194:195], v[224:225], 0, s[56:57]
	s_addc_u32 s29, s81, 0
	s_add_i32 s30, s31, s33
	global_load_lds_dwordx4 v[194:195], off
	v_lshl_add_u64 v[194:195], s[28:29], 0, v[140:141]
	s_mov_b32 m0, s30
	s_nop 0
	global_load_lds_dwordx4 v[194:195], off
	v_lshl_add_u64 v[194:195], s[28:29], 0, v[144:145]
	s_add_i32 m0, s30, 0x2000
	s_nop 0
	global_load_lds_dwordx4 v[194:195], off
	v_lshl_add_u64 v[194:195], v[226:227], 0, s[56:57]
	s_mov_b32 m0, s86
	s_nop 0
	global_load_lds_dwordx4 v[194:195], off
	v_lshl_add_u64 v[194:195], v[228:229], 0, s[56:57]
	s_mov_b32 m0, s96
	s_nop 0
	global_load_lds_dwordx4 v[194:195], off
	s_waitcnt vmcnt(8)
	s_waitcnt lgkmcnt(0)
	s_barrier
	s_setprio 1
	v_mfma_f32_16x16x32_bf16 v[92:95], v[130:133], v[174:177], v[92:95]
	v_mfma_f32_16x16x32_bf16 v[88:91], v[150:153], v[174:177], v[88:91]
	v_mfma_f32_16x16x32_bf16 v[84:87], v[130:133], v[186:189], v[84:87]
	v_mfma_f32_16x16x32_bf16 v[80:83], v[150:153], v[186:189], v[80:83]
	v_mfma_f32_16x16x32_bf16 v[76:79], v[130:133], v[206:209], v[76:79]
	v_mfma_f32_16x16x32_bf16 v[72:75], v[150:153], v[206:209], v[72:75]
	v_mfma_f32_16x16x32_bf16 v[68:71], v[130:133], v[216:219], v[68:71]
	v_mfma_f32_16x16x32_bf16 v[64:67], v[150:153], v[216:219], v[64:67]
	v_mfma_f32_16x16x32_bf16 v[92:95], v[134:137], v[178:181], v[92:95]
	v_mfma_f32_16x16x32_bf16 v[88:91], v[154:157], v[178:181], v[88:91]
	v_mfma_f32_16x16x32_bf16 v[84:87], v[134:137], v[190:193], v[84:87]
	v_mfma_f32_16x16x32_bf16 v[80:83], v[154:157], v[190:193], v[80:83]
	v_mfma_f32_16x16x32_bf16 v[76:79], v[134:137], v[210:213], v[76:79]
	v_mfma_f32_16x16x32_bf16 v[72:75], v[154:157], v[210:213], v[72:75]
	v_mfma_f32_16x16x32_bf16 v[68:71], v[134:137], v[220:223], v[68:71]
	v_mfma_f32_16x16x32_bf16 v[64:67], v[154:157], v[220:223], v[64:67]
	s_setprio 0
	s_setprio 1
	v_mfma_f32_16x16x32_bf16 v[28:31], v[158:161], v[174:177], v[28:31]
	v_mfma_f32_16x16x32_bf16 v[24:27], v[166:169], v[174:177], v[24:27]
	v_mfma_f32_16x16x32_bf16 v[20:23], v[158:161], v[186:189], v[20:23]
	v_mfma_f32_16x16x32_bf16 v[16:19], v[166:169], v[186:189], v[16:19]
	v_mfma_f32_16x16x32_bf16 v[12:15], v[158:161], v[206:209], v[12:15]
	v_mfma_f32_16x16x32_bf16 v[8:11], v[166:169], v[206:209], v[8:11]
	v_mfma_f32_16x16x32_bf16 v[4:7], v[158:161], v[216:219], v[4:7]
	v_mfma_f32_16x16x32_bf16 v[0:3], v[166:169], v[216:219], v[0:3]
	v_mfma_f32_16x16x32_bf16 v[28:31], v[162:165], v[178:181], v[28:31]
	v_mfma_f32_16x16x32_bf16 v[24:27], v[170:173], v[178:181], v[24:27]
	v_mfma_f32_16x16x32_bf16 v[20:23], v[162:165], v[190:193], v[20:23]
	v_mfma_f32_16x16x32_bf16 v[16:19], v[170:173], v[190:193], v[16:19]
	v_mfma_f32_16x16x32_bf16 v[12:15], v[162:165], v[210:213], v[12:15]
	v_mfma_f32_16x16x32_bf16 v[8:11], v[170:173], v[210:213], v[8:11]
	v_mfma_f32_16x16x32_bf16 v[4:7], v[162:165], v[220:223], v[4:7]
	v_mfma_f32_16x16x32_bf16 v[0:3], v[170:173], v[220:223], v[0:3]
	s_setprio 0
	s_barrier
	s_add_i32 s84, s84, 2
	s_add_u32 s78, s78, 0x100
	s_addc_u32 s79, s79, 0
	s_add_u32 s71, s71, 0x100
	s_addc_u32 s77, s77, 0
	s_cmp_gt_u32 s84, 13
.LBB0_836:
	s_add_u32 s28, s78, 0xfffc0080
	s_addc_u32 s29, s79, -1
	s_add_i32 s30, 0, 0x10000
	s_cmp_eq_u32 s84, 12
	s_cselect_b32 s83, s37, s29
	s_cselect_b32 s82, s50, s28
	v_add_u32_e32 v112, s30, v183
	s_cselect_b32 s81, s51, s77
	s_cselect_b32 s80, s65, s71
	s_add_i32 s31, 0, 0x14000
	ds_read_b128 v[130:133], v112
	ds_read_b128 v[134:137], v112 offset:1024
	ds_read_b128 v[150:153], v112 offset:2048
	ds_read_b128 v[154:157], v112 offset:3072
	v_add_u32_e32 v112, s31, v183
	ds_read_b128 v[158:161], v112
	ds_read_b128 v[162:165], v112 offset:1024
	ds_read_b128 v[166:169], v112 offset:2048
	ds_read_b128 v[170:173], v112 offset:3072
	v_lshl_add_u64 v[194:195], s[78:79], 0, v[146:147]
	s_add_i32 m0, s34, 0xc000
	ds_read_b128 v[174:177], v184
	ds_read_b128 v[178:181], v184 offset:1024
	ds_read_b128 v[186:189], v184 offset:2048
	ds_read_b128 v[190:193], v184 offset:3072
	ds_read_b128 v[206:209], v184 offset:4096
	ds_read_b128 v[210:213], v184 offset:5120
	ds_read_b128 v[216:219], v184 offset:6144
	ds_read_b128 v[220:223], v184 offset:7168
	global_load_lds_dwordx4 v[194:195], off
	v_lshl_add_u64 v[194:195], s[78:79], 0, v[148:149]
	s_add_i32 m0, s34, 0xe000
	s_nop 0
	global_load_lds_dwordx4 v[194:195], off
	s_waitcnt vmcnt(8)
	s_waitcnt lgkmcnt(0)
	s_barrier
	s_setprio 1
	v_mfma_f32_16x16x32_bf16 v[126:129], v[130:133], v[174:177], v[126:129]
	v_mfma_f32_16x16x32_bf16 v[122:125], v[150:153], v[174:177], v[122:125]
	v_mfma_f32_16x16x32_bf16 v[118:121], v[130:133], v[186:189], v[118:121]
	v_mfma_f32_16x16x32_bf16 v[114:117], v[150:153], v[186:189], v[114:117]
	v_mfma_f32_16x16x32_bf16 v[108:111], v[130:133], v[206:209], v[108:111]
	v_mfma_f32_16x16x32_bf16 v[104:107], v[150:153], v[206:209], v[104:107]
	v_mfma_f32_16x16x32_bf16 v[100:103], v[130:133], v[216:219], v[100:103]
	v_mfma_f32_16x16x32_bf16 v[96:99], v[150:153], v[216:219], v[96:99]
	v_mfma_f32_16x16x32_bf16 v[126:129], v[134:137], v[178:181], v[126:129]
	v_mfma_f32_16x16x32_bf16 v[122:125], v[154:157], v[178:181], v[122:125]
	v_mfma_f32_16x16x32_bf16 v[118:121], v[134:137], v[190:193], v[118:121]
	v_mfma_f32_16x16x32_bf16 v[114:117], v[154:157], v[190:193], v[114:117]
	v_mfma_f32_16x16x32_bf16 v[108:111], v[134:137], v[210:213], v[108:111]
	v_mfma_f32_16x16x32_bf16 v[104:107], v[154:157], v[210:213], v[104:107]
	v_mfma_f32_16x16x32_bf16 v[100:103], v[134:137], v[220:223], v[100:103]
	v_mfma_f32_16x16x32_bf16 v[96:99], v[154:157], v[220:223], v[96:99]
	s_setprio 0
	s_setprio 1
	v_mfma_f32_16x16x32_bf16 v[60:63], v[158:161], v[174:177], v[60:63]
	v_mfma_f32_16x16x32_bf16 v[56:59], v[166:169], v[174:177], v[56:59]
	v_mfma_f32_16x16x32_bf16 v[52:55], v[158:161], v[186:189], v[52:55]
	v_mfma_f32_16x16x32_bf16 v[48:51], v[166:169], v[186:189], v[48:51]
	v_mfma_f32_16x16x32_bf16 v[44:47], v[158:161], v[206:209], v[44:47]
	v_mfma_f32_16x16x32_bf16 v[40:43], v[166:169], v[206:209], v[40:43]
	v_mfma_f32_16x16x32_bf16 v[36:39], v[158:161], v[216:219], v[36:39]
	v_mfma_f32_16x16x32_bf16 v[32:35], v[166:169], v[216:219], v[32:35]
	v_mfma_f32_16x16x32_bf16 v[60:63], v[162:165], v[178:181], v[60:63]
	v_mfma_f32_16x16x32_bf16 v[56:59], v[170:173], v[178:181], v[56:59]
	v_mfma_f32_16x16x32_bf16 v[52:55], v[162:165], v[190:193], v[52:55]
	v_mfma_f32_16x16x32_bf16 v[48:51], v[170:173], v[190:193], v[48:51]
	v_mfma_f32_16x16x32_bf16 v[44:47], v[162:165], v[210:213], v[44:47]
	v_mfma_f32_16x16x32_bf16 v[40:43], v[170:173], v[210:213], v[40:43]
	v_mfma_f32_16x16x32_bf16 v[36:39], v[162:165], v[220:223], v[36:39]
	v_mfma_f32_16x16x32_bf16 v[32:35], v[170:173], v[220:223], v[32:35]
	s_setprio 0
	s_barrier
	s_add_i32 s28, s30, s33
	v_lshl_add_u64 v[194:195], s[80:81], 0, v[140:141]
	s_mov_b32 m0, s28
	ds_read_b128 v[174:177], v184 offset:16384
	ds_read_b128 v[178:181], v184 offset:17408
	ds_read_b128 v[186:189], v184 offset:18432
	ds_read_b128 v[190:193], v184 offset:19456
	ds_read_b128 v[206:209], v184 offset:20480
	ds_read_b128 v[210:213], v184 offset:21504
	ds_read_b128 v[216:219], v184 offset:22528
	ds_read_b128 v[220:223], v184 offset:23552
	global_load_lds_dwordx4 v[194:195], off
	s_add_i32 m0, s28, 0x2000
	s_add_u32 s28, s80, 0x40000
	v_lshl_add_u64 v[224:225], s[80:81], 0, v[144:145]
	s_addc_u32 s29, s81, 0
	s_add_i32 s30, s31, s33
	global_load_lds_dwordx4 v[224:225], off
	v_lshl_add_u64 v[226:227], s[28:29], 0, v[140:141]
	s_mov_b32 m0, s30
	v_lshl_add_u64 v[228:229], s[82:83], 0, v[142:143]
	global_load_lds_dwordx4 v[226:227], off
	v_lshl_add_u64 v[226:227], s[28:29], 0, v[144:145]
	s_add_i32 m0, s30, 0x2000
	s_nop 0
	global_load_lds_dwordx4 v[226:227], off
	v_lshl_add_u64 v[226:227], s[82:83], 0, v[138:139]
	s_mov_b32 m0, s34
	s_nop 0
	global_load_lds_dwordx4 v[226:227], off
	s_mov_b32 m0, s54
	s_nop 0
	global_load_lds_dwordx4 v[228:229], off
	s_waitcnt vmcnt(8)
	s_waitcnt lgkmcnt(0)
	s_barrier
	s_setprio 1
	v_mfma_f32_16x16x32_bf16 v[92:95], v[130:133], v[174:177], v[92:95]
	v_mfma_f32_16x16x32_bf16 v[88:91], v[150:153], v[174:177], v[88:91]
	v_mfma_f32_16x16x32_bf16 v[84:87], v[130:133], v[186:189], v[84:87]
	v_mfma_f32_16x16x32_bf16 v[80:83], v[150:153], v[186:189], v[80:83]
	v_mfma_f32_16x16x32_bf16 v[76:79], v[130:133], v[206:209], v[76:79]
	v_mfma_f32_16x16x32_bf16 v[72:75], v[150:153], v[206:209], v[72:75]
	v_mfma_f32_16x16x32_bf16 v[68:71], v[130:133], v[216:219], v[68:71]
	v_mfma_f32_16x16x32_bf16 v[64:67], v[150:153], v[216:219], v[64:67]
	v_mfma_f32_16x16x32_bf16 v[92:95], v[134:137], v[178:181], v[92:95]
	v_mfma_f32_16x16x32_bf16 v[88:91], v[154:157], v[178:181], v[88:91]
	v_mfma_f32_16x16x32_bf16 v[84:87], v[134:137], v[190:193], v[84:87]
	v_mfma_f32_16x16x32_bf16 v[80:83], v[154:157], v[190:193], v[80:83]
	v_mfma_f32_16x16x32_bf16 v[76:79], v[134:137], v[210:213], v[76:79]
	v_mfma_f32_16x16x32_bf16 v[72:75], v[154:157], v[210:213], v[72:75]
	v_mfma_f32_16x16x32_bf16 v[68:71], v[134:137], v[220:223], v[68:71]
	v_mfma_f32_16x16x32_bf16 v[64:67], v[154:157], v[220:223], v[64:67]
	s_setprio 0
	s_setprio 1
	v_mfma_f32_16x16x32_bf16 v[28:31], v[158:161], v[174:177], v[28:31]
	v_mfma_f32_16x16x32_bf16 v[24:27], v[166:169], v[174:177], v[24:27]
	v_mfma_f32_16x16x32_bf16 v[20:23], v[158:161], v[186:189], v[20:23]
	v_mfma_f32_16x16x32_bf16 v[16:19], v[166:169], v[186:189], v[16:19]
	v_mfma_f32_16x16x32_bf16 v[12:15], v[158:161], v[206:209], v[12:15]
	v_mfma_f32_16x16x32_bf16 v[8:11], v[166:169], v[206:209], v[8:11]
	v_mfma_f32_16x16x32_bf16 v[4:7], v[158:161], v[216:219], v[4:7]
	v_mfma_f32_16x16x32_bf16 v[0:3], v[166:169], v[216:219], v[0:3]
	v_mfma_f32_16x16x32_bf16 v[28:31], v[162:165], v[178:181], v[28:31]
	v_mfma_f32_16x16x32_bf16 v[24:27], v[170:173], v[178:181], v[24:27]
	v_mfma_f32_16x16x32_bf16 v[20:23], v[162:165], v[190:193], v[20:23]
	v_mfma_f32_16x16x32_bf16 v[16:19], v[170:173], v[190:193], v[16:19]
	v_mfma_f32_16x16x32_bf16 v[12:15], v[162:165], v[210:213], v[12:15]
	v_mfma_f32_16x16x32_bf16 v[8:11], v[170:173], v[210:213], v[8:11]
	v_mfma_f32_16x16x32_bf16 v[4:7], v[162:165], v[220:223], v[4:7]
	v_mfma_f32_16x16x32_bf16 v[0:3], v[170:173], v[220:223], v[0:3]
	s_setprio 0
	s_barrier
	s_add_i32 s30, 0, 0x18000
	v_add_u32_e32 v112, s30, v183
	s_add_i32 s31, 0, 0x1c000
	ds_read_b128 v[130:133], v112
	ds_read_b128 v[134:137], v112 offset:1024
	ds_read_b128 v[150:153], v112 offset:2048
	ds_read_b128 v[154:157], v112 offset:3072
	v_add_u32_e32 v112, s31, v183
	ds_read_b128 v[158:161], v112
	ds_read_b128 v[162:165], v112 offset:1024
	ds_read_b128 v[166:169], v112 offset:2048
	ds_read_b128 v[170:173], v112 offset:3072
	s_add_u32 s28, s82, 0x40000
	s_addc_u32 s29, s83, 0
	s_mov_b32 m0, s55
	v_lshl_add_u64 v[230:231], s[28:29], 0, v[138:139]
	ds_read_b128 v[174:177], v184 offset:32768
	ds_read_b128 v[178:181], v184 offset:33792
	ds_read_b128 v[186:189], v184 offset:34816
	ds_read_b128 v[190:193], v184 offset:35840
	ds_read_b128 v[206:209], v184 offset:36864
	ds_read_b128 v[210:213], v184 offset:37888
	ds_read_b128 v[216:219], v184 offset:38912
	ds_read_b128 v[220:223], v184 offset:39936
	global_load_lds_dwordx4 v[230:231], off
	v_lshl_add_u64 v[230:231], s[28:29], 0, v[142:143]
	s_mov_b32 m0, s58
	s_nop 0
	global_load_lds_dwordx4 v[230:231], off
	s_waitcnt vmcnt(8)
	s_waitcnt lgkmcnt(0)
	s_barrier
	s_setprio 1
	v_mfma_f32_16x16x32_bf16 v[126:129], v[130:133], v[174:177], v[126:129]
	v_mfma_f32_16x16x32_bf16 v[122:125], v[150:153], v[174:177], v[122:125]
	v_mfma_f32_16x16x32_bf16 v[118:121], v[130:133], v[186:189], v[118:121]
	v_mfma_f32_16x16x32_bf16 v[114:117], v[150:153], v[186:189], v[114:117]
	v_mfma_f32_16x16x32_bf16 v[108:111], v[130:133], v[206:209], v[108:111]
	v_mfma_f32_16x16x32_bf16 v[104:107], v[150:153], v[206:209], v[104:107]
	v_mfma_f32_16x16x32_bf16 v[100:103], v[130:133], v[216:219], v[100:103]
	v_mfma_f32_16x16x32_bf16 v[96:99], v[150:153], v[216:219], v[96:99]
	v_mfma_f32_16x16x32_bf16 v[126:129], v[134:137], v[178:181], v[126:129]
	v_mfma_f32_16x16x32_bf16 v[122:125], v[154:157], v[178:181], v[122:125]
	v_mfma_f32_16x16x32_bf16 v[118:121], v[134:137], v[190:193], v[118:121]
	v_mfma_f32_16x16x32_bf16 v[114:117], v[154:157], v[190:193], v[114:117]
	v_mfma_f32_16x16x32_bf16 v[108:111], v[134:137], v[210:213], v[108:111]
	v_mfma_f32_16x16x32_bf16 v[104:107], v[154:157], v[210:213], v[104:107]
	v_mfma_f32_16x16x32_bf16 v[100:103], v[134:137], v[220:223], v[100:103]
	v_mfma_f32_16x16x32_bf16 v[96:99], v[154:157], v[220:223], v[96:99]
	s_setprio 0
	s_setprio 1
	v_mfma_f32_16x16x32_bf16 v[60:63], v[158:161], v[174:177], v[60:63]
	v_mfma_f32_16x16x32_bf16 v[56:59], v[166:169], v[174:177], v[56:59]
	v_mfma_f32_16x16x32_bf16 v[52:55], v[158:161], v[186:189], v[52:55]
	v_mfma_f32_16x16x32_bf16 v[48:51], v[166:169], v[186:189], v[48:51]
	v_mfma_f32_16x16x32_bf16 v[44:47], v[158:161], v[206:209], v[44:47]
	v_mfma_f32_16x16x32_bf16 v[40:43], v[166:169], v[206:209], v[40:43]
	v_mfma_f32_16x16x32_bf16 v[36:39], v[158:161], v[216:219], v[36:39]
	v_mfma_f32_16x16x32_bf16 v[32:35], v[166:169], v[216:219], v[32:35]
	v_mfma_f32_16x16x32_bf16 v[60:63], v[162:165], v[178:181], v[60:63]
	v_mfma_f32_16x16x32_bf16 v[56:59], v[170:173], v[178:181], v[56:59]
	v_mfma_f32_16x16x32_bf16 v[52:55], v[162:165], v[190:193], v[52:55]
	v_mfma_f32_16x16x32_bf16 v[48:51], v[170:173], v[190:193], v[48:51]
	v_mfma_f32_16x16x32_bf16 v[44:47], v[162:165], v[210:213], v[44:47]
	v_mfma_f32_16x16x32_bf16 v[40:43], v[170:173], v[210:213], v[40:43]
	v_mfma_f32_16x16x32_bf16 v[36:39], v[162:165], v[220:223], v[36:39]
	v_mfma_f32_16x16x32_bf16 v[32:35], v[170:173], v[220:223], v[32:35]
	s_setprio 0
	s_barrier
	s_add_i32 s28, s30, s33
	v_lshl_add_u64 v[194:195], v[194:195], 0, s[56:57]
	s_mov_b32 m0, s28
	ds_read_b128 v[174:177], v184 offset:49152
	ds_read_b128 v[178:181], v184 offset:50176
	ds_read_b128 v[186:189], v184 offset:51200
	ds_read_b128 v[190:193], v184 offset:52224
	ds_read_b128 v[206:209], v184 offset:53248
	ds_read_b128 v[210:213], v184 offset:54272
	ds_read_b128 v[216:219], v184 offset:55296
	ds_read_b128 v[220:223], v184 offset:56320
	global_load_lds_dwordx4 v[194:195], off
	s_add_i32 m0, s28, 0x2000
	s_add_u32 s28, s80, 0x40080
	v_lshl_add_u64 v[194:195], v[224:225], 0, s[56:57]
	s_addc_u32 s29, s81, 0
	s_add_i32 s30, s31, s33
	global_load_lds_dwordx4 v[194:195], off
	v_lshl_add_u64 v[194:195], s[28:29], 0, v[140:141]
	s_mov_b32 m0, s30
	s_nop 0
	global_load_lds_dwordx4 v[194:195], off
	v_lshl_add_u64 v[194:195], s[28:29], 0, v[144:145]
	s_add_i32 m0, s30, 0x2000
	s_nop 0
	global_load_lds_dwordx4 v[194:195], off
	v_lshl_add_u64 v[194:195], v[226:227], 0, s[56:57]
	s_mov_b32 m0, s86
	s_nop 0
	global_load_lds_dwordx4 v[194:195], off
	v_lshl_add_u64 v[194:195], v[228:229], 0, s[56:57]
	s_mov_b32 m0, s96
	s_nop 0
	global_load_lds_dwordx4 v[194:195], off
	s_waitcnt vmcnt(8)
	s_waitcnt lgkmcnt(0)
	s_barrier
	s_setprio 1
	v_mfma_f32_16x16x32_bf16 v[92:95], v[130:133], v[174:177], v[92:95]
	v_mfma_f32_16x16x32_bf16 v[88:91], v[150:153], v[174:177], v[88:91]
	v_mfma_f32_16x16x32_bf16 v[84:87], v[130:133], v[186:189], v[84:87]
	v_mfma_f32_16x16x32_bf16 v[80:83], v[150:153], v[186:189], v[80:83]
	v_mfma_f32_16x16x32_bf16 v[76:79], v[130:133], v[206:209], v[76:79]
	v_mfma_f32_16x16x32_bf16 v[72:75], v[150:153], v[206:209], v[72:75]
	v_mfma_f32_16x16x32_bf16 v[68:71], v[130:133], v[216:219], v[68:71]
	v_mfma_f32_16x16x32_bf16 v[64:67], v[150:153], v[216:219], v[64:67]
	v_mfma_f32_16x16x32_bf16 v[92:95], v[134:137], v[178:181], v[92:95]
	v_mfma_f32_16x16x32_bf16 v[88:91], v[154:157], v[178:181], v[88:91]
	v_mfma_f32_16x16x32_bf16 v[84:87], v[134:137], v[190:193], v[84:87]
	v_mfma_f32_16x16x32_bf16 v[80:83], v[154:157], v[190:193], v[80:83]
	v_mfma_f32_16x16x32_bf16 v[76:79], v[134:137], v[210:213], v[76:79]
	v_mfma_f32_16x16x32_bf16 v[72:75], v[154:157], v[210:213], v[72:75]
	v_mfma_f32_16x16x32_bf16 v[68:71], v[134:137], v[220:223], v[68:71]
	v_mfma_f32_16x16x32_bf16 v[64:67], v[154:157], v[220:223], v[64:67]
	s_setprio 0
	s_setprio 1
	v_mfma_f32_16x16x32_bf16 v[28:31], v[158:161], v[174:177], v[28:31]
	v_mfma_f32_16x16x32_bf16 v[24:27], v[166:169], v[174:177], v[24:27]
	v_mfma_f32_16x16x32_bf16 v[20:23], v[158:161], v[186:189], v[20:23]
	v_mfma_f32_16x16x32_bf16 v[16:19], v[166:169], v[186:189], v[16:19]
	v_mfma_f32_16x16x32_bf16 v[12:15], v[158:161], v[206:209], v[12:15]
	v_mfma_f32_16x16x32_bf16 v[8:11], v[166:169], v[206:209], v[8:11]
	v_mfma_f32_16x16x32_bf16 v[4:7], v[158:161], v[216:219], v[4:7]
	v_mfma_f32_16x16x32_bf16 v[0:3], v[166:169], v[216:219], v[0:3]
	v_mfma_f32_16x16x32_bf16 v[28:31], v[162:165], v[178:181], v[28:31]
	v_mfma_f32_16x16x32_bf16 v[24:27], v[170:173], v[178:181], v[24:27]
	v_mfma_f32_16x16x32_bf16 v[20:23], v[162:165], v[190:193], v[20:23]
	v_mfma_f32_16x16x32_bf16 v[16:19], v[170:173], v[190:193], v[16:19]
	v_mfma_f32_16x16x32_bf16 v[12:15], v[162:165], v[210:213], v[12:15]
	v_mfma_f32_16x16x32_bf16 v[8:11], v[170:173], v[210:213], v[8:11]
	v_mfma_f32_16x16x32_bf16 v[4:7], v[162:165], v[220:223], v[4:7]
	v_mfma_f32_16x16x32_bf16 v[0:3], v[170:173], v[220:223], v[0:3]
	s_setprio 0
	s_barrier
	s_add_i32 s84, s84, 2
	s_add_u32 s78, s78, 0x100
	s_addc_u32 s79, s79, 0
	s_add_u32 s71, s71, 0x100
	s_addc_u32 s77, s77, 0
	s_cmp_gt_u32 s84, 13
	s_cbranch_scc0 .LBB0_836
	s_and_b64 vcc, exec, s[46:47]
	s_cbranch_vccz .LBB0_839
	s_barrier

.LBB0_848:
	v_readlane_b32 s2, v255, 22
	v_readlane_b32 s6, v252, 2
	s_add_i32 s2, s2, 8
	v_readlane_b32 s7, v252, 3
	s_cmp_ge_i32 s2, s7
	s_cbranch_scc1 .LBB0_898
	s_waitcnt vmcnt(0)
	s_waitcnt lgkmcnt(0)
	s_barrier
	s_mov_b64 s[6:7], exec
	v_readlane_b32 s12, v252, 22
	v_readlane_b32 s13, v252, 23
	s_and_b64 s[12:13], s[6:7], s[12:13]
	s_mov_b64 exec, s[12:13]
	s_cbranch_execz .LBB0_897
	v_readlane_b32 s4, v254, 44
	s_waitcnt vmcnt(0) expcnt(0) lgkmcnt(0)
	s_nop 0
	v_mov_b32_e32 v0, s4
	ds_read_b32 v2, v0
	v_readlane_b32 s4, v254, 45
	s_waitcnt lgkmcnt(0)
	v_cmp_ne_u32_e32 vcc, 0, v2
	v_mov_b32_e32 v0, s4
	ds_read_b32 v0, v0
	s_cbranch_vccnz .LBB0_865
	v_readlane_b32 s14, v252, 24
	v_readlane_b32 s15, v252, 25
	s_load_dwordx2 s[12:13], s[14:15], 0x0
	s_load_dword s4, s[14:15], 0x8
	s_waitcnt lgkmcnt(0)
	s_mul_i32 s12, s13, s12
	s_mul_i32 s4, s12, s4
	s_mov_b32 s12, 1
	s_branch .LBB0_853

.LBB0_935:
	v_ashrrev_i32_e32 v19, 31, v18
	v_lshlrev_b64 v[0:1], 11, v[18:19]
	v_lshl_add_u64 v[20:21], v[16:17], 0, v[0:1]
	global_load_dwordx4 v[26:29], v[20:21], off
	global_load_dwordx4 v[30:33], v[20:21], off offset:32
	global_load_dwordx4 v[34:37], v[20:21], off offset:64
	global_load_dwordx4 v[38:41], v[20:21], off offset:96
	global_load_dwordx4 v[42:45], v[20:21], off offset:128
	global_load_dwordx4 v[46:49], v[20:21], off offset:160
	global_load_dwordx4 v[50:53], v[20:21], off offset:192
	global_load_dwordx4 v[54:57], v[20:21], off offset:224
	global_load_dwordx4 v[58:61], v[20:21], off offset:256
	global_load_dwordx4 v[68:71], v[20:21], off offset:288
	global_load_dwordx4 v[72:75], v[20:21], off offset:320
	global_load_dwordx4 v[76:79], v[20:21], off offset:352
	global_load_dwordx4 v[80:83], v[20:21], off offset:384
	global_load_dwordx4 v[84:87], v[20:21], off offset:416
	global_load_dwordx4 v[88:91], v[20:21], off offset:448
	global_load_dwordx4 v[92:95], v[20:21], off offset:480
	s_waitcnt vmcnt(8)
	ds_read_b128 v[0:3], v22
	ds_read_b128 v[96:99], v22 offset:32
	ds_read_b128 v[104:107], v23
	ds_read_b128 v[108:111], v23 offset:32
	s_waitcnt lgkmcnt(3)
	v_mfma_f32_32x32x16_bf16 v[0:15], v[0:3], v[26:29], 0
	s_waitcnt lgkmcnt(1)
	v_mfma_f32_32x32x16_bf16 v[0:15], v[104:107], v[26:29], v[0:15]
	v_mfma_f32_32x32x16_bf16 v[0:15], v[96:99], v[30:33], v[0:15]
	s_waitcnt lgkmcnt(0)
	v_mfma_f32_32x32x16_bf16 v[0:15], v[108:111], v[30:33], v[0:15]
	ds_read_b128 v[26:29], v22 offset:64
	ds_read_b128 v[30:33], v22 offset:96
	s_waitcnt lgkmcnt(1)
	v_mfma_f32_32x32x16_bf16 v[0:15], v[26:29], v[34:37], v[0:15]
	ds_read_b128 v[26:29], v23 offset:64
	ds_read_b128 v[96:99], v23 offset:96
	s_waitcnt lgkmcnt(1)
	v_mfma_f32_32x32x16_bf16 v[0:15], v[26:29], v[34:37], v[0:15]
	v_mfma_f32_32x32x16_bf16 v[0:15], v[30:33], v[38:41], v[0:15]
	ds_read_b128 v[26:29], v22 offset:128
	ds_read_b128 v[30:33], v22 offset:160
	s_waitcnt lgkmcnt(2)
	v_mfma_f32_32x32x16_bf16 v[0:15], v[96:99], v[38:41], v[0:15]
	s_waitcnt lgkmcnt(1)
	v_mfma_f32_32x32x16_bf16 v[0:15], v[26:29], v[42:45], v[0:15]
	ds_read_b128 v[26:29], v23 offset:128
	ds_read_b128 v[34:37], v23 offset:160
	s_waitcnt lgkmcnt(1)
	v_mfma_f32_32x32x16_bf16 v[0:15], v[26:29], v[42:45], v[0:15]
	v_mfma_f32_32x32x16_bf16 v[0:15], v[30:33], v[46:49], v[0:15]
	ds_read_b128 v[26:29], v22 offset:192
	ds_read_b128 v[30:33], v22 offset:224
	s_waitcnt lgkmcnt(2)
	v_mfma_f32_32x32x16_bf16 v[0:15], v[34:37], v[46:49], v[0:15]
	s_waitcnt lgkmcnt(1)
	v_mfma_f32_32x32x16_bf16 v[0:15], v[26:29], v[50:53], v[0:15]
	ds_read_b128 v[26:29], v23 offset:192
	ds_read_b128 v[34:37], v23 offset:224
	global_load_dwordx4 v[38:41], v[20:21], off offset:512
	global_load_dwordx4 v[42:45], v[20:21], off offset:544
	s_waitcnt lgkmcnt(1)
	v_mfma_f32_32x32x16_bf16 v[0:15], v[26:29], v[50:53], v[0:15]
	global_load_dwordx4 v[26:29], v[20:21], off offset:576
	global_load_dwordx4 v[46:49], v[20:21], off offset:608
	global_load_dwordx4 v[50:53], v[20:21], off offset:640
	global_load_dwordx4 v[96:99], v[20:21], off offset:672
	global_load_dwordx4 v[104:107], v[20:21], off offset:704
	global_load_dwordx4 v[108:111], v[20:21], off offset:736
	s_waitcnt vmcnt(10)
	v_mfma_f32_32x32x16_bf16 v[0:15], v[30:33], v[54:57], v[0:15]
	s_waitcnt vmcnt(8)
	s_waitcnt lgkmcnt(0)
	v_mfma_f32_32x32x16_bf16 v[0:15], v[34:37], v[54:57], v[0:15]
	ds_read_b128 v[30:33], v22 offset:256
	ds_read_b128 v[34:37], v22 offset:288
	s_waitcnt lgkmcnt(1)
	v_mfma_f32_32x32x16_bf16 v[0:15], v[30:33], v[58:61], v[0:15]
	ds_read_b128 v[30:33], v23 offset:256
	ds_read_b128 v[54:57], v23 offset:288
	s_waitcnt lgkmcnt(1)
	v_mfma_f32_32x32x16_bf16 v[0:15], v[30:33], v[58:61], v[0:15]
	v_mfma_f32_32x32x16_bf16 v[0:15], v[34:37], v[68:71], v[0:15]
	ds_read_b128 v[30:33], v22 offset:320
	ds_read_b128 v[34:37], v22 offset:352
	s_waitcnt lgkmcnt(2)
	v_mfma_f32_32x32x16_bf16 v[0:15], v[54:57], v[68:71], v[0:15]
	s_waitcnt lgkmcnt(1)
	v_mfma_f32_32x32x16_bf16 v[0:15], v[30:33], v[72:75], v[0:15]
	ds_read_b128 v[30:33], v23 offset:320
	ds_read_b128 v[54:57], v23 offset:352
	s_waitcnt lgkmcnt(1)
	v_mfma_f32_32x32x16_bf16 v[0:15], v[30:33], v[72:75], v[0:15]
	v_mfma_f32_32x32x16_bf16 v[0:15], v[34:37], v[76:79], v[0:15]
	ds_read_b128 v[30:33], v22 offset:384
	ds_read_b128 v[34:37], v22 offset:416
	s_waitcnt lgkmcnt(2)
	v_mfma_f32_32x32x16_bf16 v[0:15], v[54:57], v[76:79], v[0:15]
	s_waitcnt lgkmcnt(1)
	v_mfma_f32_32x32x16_bf16 v[0:15], v[30:33], v[80:83], v[0:15]
	ds_read_b128 v[30:33], v23 offset:384
	ds_read_b128 v[54:57], v23 offset:416
	s_waitcnt lgkmcnt(1)
	v_mfma_f32_32x32x16_bf16 v[0:15], v[30:33], v[80:83], v[0:15]
	v_mfma_f32_32x32x16_bf16 v[0:15], v[34:37], v[84:87], v[0:15]
	ds_read_b128 v[30:33], v22 offset:448
	ds_read_b128 v[34:37], v22 offset:480
	s_waitcnt lgkmcnt(2)
	v_mfma_f32_32x32x16_bf16 v[0:15], v[54:57], v[84:87], v[0:15]
	s_waitcnt lgkmcnt(1)
	v_mfma_f32_32x32x16_bf16 v[0:15], v[30:33], v[88:91], v[0:15]
	ds_read_b128 v[30:33], v23 offset:448
	ds_read_b128 v[54:57], v23 offset:480
	global_load_dwordx4 v[58:61], v[20:21], off offset:768
	global_load_dwordx4 v[68:71], v[20:21], off offset:800
	s_waitcnt lgkmcnt(1)
	v_mfma_f32_32x32x16_bf16 v[0:15], v[30:33], v[88:91], v[0:15]
	global_load_dwordx4 v[30:33], v[20:21], off offset:832
	global_load_dwordx4 v[72:75], v[20:21], off offset:864
	global_load_dwordx4 v[76:79], v[20:21], off offset:896
	global_load_dwordx4 v[80:83], v[20:21], off offset:928
	global_load_dwordx4 v[84:87], v[20:21], off offset:960
	global_load_dwordx4 v[88:91], v[20:21], off offset:992
	s_waitcnt vmcnt(10)
	v_mfma_f32_32x32x16_bf16 v[0:15], v[34:37], v[92:95], v[0:15]
	s_waitcnt vmcnt(8)
	s_waitcnt lgkmcnt(0)
	v_mfma_f32_32x32x16_bf16 v[0:15], v[54:57], v[92:95], v[0:15]
	ds_read_b128 v[34:37], v22 offset:512
	ds_read_b128 v[54:57], v22 offset:544
	s_waitcnt lgkmcnt(1)
	v_mfma_f32_32x32x16_bf16 v[0:15], v[34:37], v[38:41], v[0:15]
	ds_read_b128 v[34:37], v23 offset:512
	ds_read_b128 v[92:95], v23 offset:544
	s_waitcnt lgkmcnt(1)
	v_mfma_f32_32x32x16_bf16 v[0:15], v[34:37], v[38:41], v[0:15]
	ds_read_b128 v[34:37], v22 offset:576
	ds_read_b128 v[38:41], v22 offset:608
	v_mfma_f32_32x32x16_bf16 v[0:15], v[54:57], v[42:45], v[0:15]
	s_waitcnt lgkmcnt(2)
	v_mfma_f32_32x32x16_bf16 v[0:15], v[92:95], v[42:45], v[0:15]
	s_waitcnt lgkmcnt(1)
	v_mfma_f32_32x32x16_bf16 v[0:15], v[34:37], v[26:29], v[0:15]
	ds_read_b128 v[34:37], v23 offset:576
	ds_read_b128 v[42:45], v23 offset:608
	s_waitcnt lgkmcnt(1)
	v_mfma_f32_32x32x16_bf16 v[0:15], v[34:37], v[26:29], v[0:15]
	ds_read_b128 v[26:29], v22 offset:640
	ds_read_b128 v[34:37], v22 offset:672
	v_mfma_f32_32x32x16_bf16 v[0:15], v[38:41], v[46:49], v[0:15]
	s_waitcnt lgkmcnt(2)
	v_mfma_f32_32x32x16_bf16 v[0:15], v[42:45], v[46:49], v[0:15]
	s_waitcnt lgkmcnt(1)
	v_mfma_f32_32x32x16_bf16 v[0:15], v[26:29], v[50:53], v[0:15]
	ds_read_b128 v[26:29], v23 offset:640
	ds_read_b128 v[38:41], v23 offset:672
	s_waitcnt lgkmcnt(1)
	v_mfma_f32_32x32x16_bf16 v[0:15], v[26:29], v[50:53], v[0:15]
	v_mfma_f32_32x32x16_bf16 v[0:15], v[34:37], v[96:99], v[0:15]
	ds_read_b128 v[26:29], v22 offset:704
	ds_read_b128 v[34:37], v22 offset:736
	s_waitcnt lgkmcnt(2)
	v_mfma_f32_32x32x16_bf16 v[0:15], v[38:41], v[96:99], v[0:15]
	s_waitcnt lgkmcnt(1)
	v_mfma_f32_32x32x16_bf16 v[0:15], v[26:29], v[104:107], v[0:15]
	ds_read_b128 v[26:29], v23 offset:704
	ds_read_b128 v[38:41], v23 offset:736
	global_load_dwordx4 v[42:45], v[20:21], off offset:1024
	global_load_dwordx4 v[46:49], v[20:21], off offset:1056
	s_waitcnt lgkmcnt(1)
	v_mfma_f32_32x32x16_bf16 v[0:15], v[26:29], v[104:107], v[0:15]
	global_load_dwordx4 v[26:29], v[20:21], off offset:1088
	global_load_dwordx4 v[50:53], v[20:21], off offset:1120
	global_load_dwordx4 v[54:57], v[20:21], off offset:1152
	global_load_dwordx4 v[92:95], v[20:21], off offset:1184
	global_load_dwordx4 v[96:99], v[20:21], off offset:1216
	global_load_dwordx4 v[104:107], v[20:21], off offset:1248
	s_waitcnt vmcnt(10)
	v_mfma_f32_32x32x16_bf16 v[0:15], v[34:37], v[108:111], v[0:15]
	s_waitcnt vmcnt(8)
	s_waitcnt lgkmcnt(0)
	v_mfma_f32_32x32x16_bf16 v[0:15], v[38:41], v[108:111], v[0:15]
	ds_read_b128 v[34:37], v22 offset:768
	ds_read_b128 v[38:41], v22 offset:800
	s_waitcnt lgkmcnt(1)
	v_mfma_f32_32x32x16_bf16 v[0:15], v[34:37], v[58:61], v[0:15]
	ds_read_b128 v[34:37], v23 offset:768
	ds_read_b128 v[108:111], v23 offset:800
	s_waitcnt lgkmcnt(1)
	v_mfma_f32_32x32x16_bf16 v[0:15], v[34:37], v[58:61], v[0:15]
	v_mfma_f32_32x32x16_bf16 v[0:15], v[38:41], v[68:71], v[0:15]
	ds_read_b128 v[34:37], v22 offset:832
	ds_read_b128 v[38:41], v22 offset:864
	s_waitcnt lgkmcnt(2)
	v_mfma_f32_32x32x16_bf16 v[0:15], v[108:111], v[68:71], v[0:15]
	s_waitcnt lgkmcnt(1)
	v_mfma_f32_32x32x16_bf16 v[0:15], v[34:37], v[30:33], v[0:15]
	ds_read_b128 v[34:37], v23 offset:832
	ds_read_b128 v[58:61], v23 offset:864
	s_waitcnt lgkmcnt(1)
	v_mfma_f32_32x32x16_bf16 v[0:15], v[34:37], v[30:33], v[0:15]
	ds_read_b128 v[30:33], v22 offset:896
	ds_read_b128 v[34:37], v22 offset:928
	v_mfma_f32_32x32x16_bf16 v[0:15], v[38:41], v[72:75], v[0:15]
	s_waitcnt lgkmcnt(2)
	v_mfma_f32_32x32x16_bf16 v[0:15], v[58:61], v[72:75], v[0:15]
	s_waitcnt lgkmcnt(1)
	v_mfma_f32_32x32x16_bf16 v[0:15], v[30:33], v[76:79], v[0:15]
	ds_read_b128 v[30:33], v23 offset:896
	ds_read_b128 v[38:41], v23 offset:928
	s_waitcnt lgkmcnt(1)
	v_mfma_f32_32x32x16_bf16 v[0:15], v[30:33], v[76:79], v[0:15]
	v_mfma_f32_32x32x16_bf16 v[0:15], v[34:37], v[80:83], v[0:15]
	ds_read_b128 v[30:33], v22 offset:960
	ds_read_b128 v[34:37], v22 offset:992
	s_waitcnt lgkmcnt(2)
	v_mfma_f32_32x32x16_bf16 v[0:15], v[38:41], v[80:83], v[0:15]
	s_waitcnt lgkmcnt(1)
	v_mfma_f32_32x32x16_bf16 v[0:15], v[30:33], v[84:87], v[0:15]
	ds_read_b128 v[30:33], v23 offset:960
	ds_read_b128 v[38:41], v23 offset:992
	global_load_dwordx4 v[58:61], v[20:21], off offset:1280
	global_load_dwordx4 v[68:71], v[20:21], off offset:1312
	s_waitcnt lgkmcnt(1)
	v_mfma_f32_32x32x16_bf16 v[0:15], v[30:33], v[84:87], v[0:15]
	global_load_dwordx4 v[30:33], v[20:21], off offset:1344
	global_load_dwordx4 v[72:75], v[20:21], off offset:1376
	global_load_dwordx4 v[76:79], v[20:21], off offset:1408
	global_load_dwordx4 v[80:83], v[20:21], off offset:1440
	global_load_dwordx4 v[84:87], v[20:21], off offset:1472
	global_load_dwordx4 v[108:111], v[20:21], off offset:1504
	s_waitcnt vmcnt(10)
	v_mfma_f32_32x32x16_bf16 v[0:15], v[34:37], v[88:91], v[0:15]
	s_waitcnt vmcnt(8)
	s_waitcnt lgkmcnt(0)
	v_mfma_f32_32x32x16_bf16 v[0:15], v[38:41], v[88:91], v[0:15]
	ds_read_b128 v[34:37], v22 offset:1024
	ds_read_b128 v[38:41], v22 offset:1056
	s_waitcnt lgkmcnt(1)
	v_mfma_f32_32x32x16_bf16 v[0:15], v[34:37], v[42:45], v[0:15]
	ds_read_b128 v[34:37], v23 offset:1024
	ds_read_b128 v[88:91], v23 offset:1056
	s_waitcnt lgkmcnt(1)
	v_mfma_f32_32x32x16_bf16 v[0:15], v[34:37], v[42:45], v[0:15]
	v_mfma_f32_32x32x16_bf16 v[0:15], v[38:41], v[46:49], v[0:15]
	ds_read_b128 v[34:37], v22 offset:1088
	ds_read_b128 v[38:41], v22 offset:1120
	s_waitcnt lgkmcnt(2)
	v_mfma_f32_32x32x16_bf16 v[0:15], v[88:91], v[46:49], v[0:15]
	s_waitcnt lgkmcnt(1)
	v_mfma_f32_32x32x16_bf16 v[0:15], v[34:37], v[26:29], v[0:15]
	ds_read_b128 v[34:37], v23 offset:1088
	ds_read_b128 v[42:45], v23 offset:1120
	s_waitcnt lgkmcnt(1)
	v_mfma_f32_32x32x16_bf16 v[0:15], v[34:37], v[26:29], v[0:15]
	ds_read_b128 v[26:29], v22 offset:1152
	ds_read_b128 v[34:37], v22 offset:1184
	v_mfma_f32_32x32x16_bf16 v[0:15], v[38:41], v[50:53], v[0:15]
	s_waitcnt lgkmcnt(2)
	v_mfma_f32_32x32x16_bf16 v[0:15], v[42:45], v[50:53], v[0:15]
	s_waitcnt lgkmcnt(1)
	v_mfma_f32_32x32x16_bf16 v[0:15], v[26:29], v[54:57], v[0:15]
	ds_read_b128 v[26:29], v23 offset:1152
	ds_read_b128 v[38:41], v23 offset:1184
	s_waitcnt lgkmcnt(1)
	v_mfma_f32_32x32x16_bf16 v[0:15], v[26:29], v[54:57], v[0:15]
	v_mfma_f32_32x32x16_bf16 v[0:15], v[34:37], v[92:95], v[0:15]
	ds_read_b128 v[26:29], v22 offset:1216
	ds_read_b128 v[34:37], v22 offset:1248
	s_waitcnt lgkmcnt(2)
	v_mfma_f32_32x32x16_bf16 v[0:15], v[38:41], v[92:95], v[0:15]
	s_waitcnt lgkmcnt(1)
	v_mfma_f32_32x32x16_bf16 v[0:15], v[26:29], v[96:99], v[0:15]
	ds_read_b128 v[26:29], v23 offset:1216
	ds_read_b128 v[38:41], v23 offset:1248
	global_load_dwordx4 v[42:45], v[20:21], off offset:1536
	global_load_dwordx4 v[46:49], v[20:21], off offset:1568
	s_waitcnt lgkmcnt(1)
	v_mfma_f32_32x32x16_bf16 v[0:15], v[26:29], v[96:99], v[0:15]
	global_load_dwordx4 v[26:29], v[20:21], off offset:1600
	global_load_dwordx4 v[50:53], v[20:21], off offset:1632
	global_load_dwordx4 v[54:57], v[20:21], off offset:1664
	global_load_dwordx4 v[88:91], v[20:21], off offset:1696
	global_load_dwordx4 v[92:95], v[20:21], off offset:1728
	global_load_dwordx4 v[96:99], v[20:21], off offset:1760
	s_waitcnt vmcnt(10)
	v_mfma_f32_32x32x16_bf16 v[0:15], v[34:37], v[104:107], v[0:15]
	s_waitcnt vmcnt(8)
	s_waitcnt lgkmcnt(0)
	v_mfma_f32_32x32x16_bf16 v[0:15], v[38:41], v[104:107], v[0:15]
	ds_read_b128 v[34:37], v22 offset:1280
	ds_read_b128 v[38:41], v22 offset:1312
	s_waitcnt lgkmcnt(1)
	v_mfma_f32_32x32x16_bf16 v[0:15], v[34:37], v[58:61], v[0:15]
	ds_read_b128 v[34:37], v23 offset:1280
	ds_read_b128 v[104:107], v23 offset:1312
	s_waitcnt lgkmcnt(1)
	v_mfma_f32_32x32x16_bf16 v[0:15], v[34:37], v[58:61], v[0:15]
	v_mfma_f32_32x32x16_bf16 v[0:15], v[38:41], v[68:71], v[0:15]
	ds_read_b128 v[34:37], v22 offset:1344
	ds_read_b128 v[38:41], v22 offset:1376
	s_waitcnt lgkmcnt(2)
	v_mfma_f32_32x32x16_bf16 v[0:15], v[104:107], v[68:71], v[0:15]
	s_waitcnt lgkmcnt(1)
	v_mfma_f32_32x32x16_bf16 v[0:15], v[34:37], v[30:33], v[0:15]
	ds_read_b128 v[34:37], v23 offset:1344
	ds_read_b128 v[58:61], v23 offset:1376
	s_waitcnt lgkmcnt(1)
	v_mfma_f32_32x32x16_bf16 v[0:15], v[34:37], v[30:33], v[0:15]
	ds_read_b128 v[30:33], v22 offset:1408
	ds_read_b128 v[34:37], v22 offset:1440
	v_mfma_f32_32x32x16_bf16 v[0:15], v[38:41], v[72:75], v[0:15]
	s_waitcnt lgkmcnt(2)
	v_mfma_f32_32x32x16_bf16 v[0:15], v[58:61], v[72:75], v[0:15]
	s_waitcnt lgkmcnt(1)
	v_mfma_f32_32x32x16_bf16 v[0:15], v[30:33], v[76:79], v[0:15]
	ds_read_b128 v[30:33], v23 offset:1408
	ds_read_b128 v[38:41], v23 offset:1440
	s_waitcnt lgkmcnt(1)
	v_mfma_f32_32x32x16_bf16 v[0:15], v[30:33], v[76:79], v[0:15]
	v_mfma_f32_32x32x16_bf16 v[0:15], v[34:37], v[80:83], v[0:15]
	ds_read_b128 v[30:33], v22 offset:1472
	ds_read_b128 v[34:37], v22 offset:1504
	s_waitcnt lgkmcnt(2)
	v_mfma_f32_32x32x16_bf16 v[0:15], v[38:41], v[80:83], v[0:15]
	s_waitcnt lgkmcnt(1)
	v_mfma_f32_32x32x16_bf16 v[0:15], v[30:33], v[84:87], v[0:15]
	ds_read_b128 v[30:33], v23 offset:1472
	ds_read_b128 v[38:41], v23 offset:1504
	global_load_dwordx4 v[58:61], v[20:21], off offset:1792
	global_load_dwordx4 v[68:71], v[20:21], off offset:1824
	s_waitcnt lgkmcnt(1)
	v_mfma_f32_32x32x16_bf16 v[0:15], v[30:33], v[84:87], v[0:15]
	global_load_dwordx4 v[30:33], v[20:21], off offset:1856
	global_load_dwordx4 v[72:75], v[20:21], off offset:1888
	global_load_dwordx4 v[76:79], v[20:21], off offset:1920
	global_load_dwordx4 v[80:83], v[20:21], off offset:1952
	global_load_dwordx4 v[84:87], v[20:21], off offset:1984
	global_load_dwordx4 v[104:107], v[20:21], off offset:2016
	s_waitcnt vmcnt(10)
	v_mfma_f32_32x32x16_bf16 v[0:15], v[34:37], v[108:111], v[0:15]
	s_waitcnt vmcnt(8)
	s_waitcnt lgkmcnt(0)
	v_mfma_f32_32x32x16_bf16 v[0:15], v[38:41], v[108:111], v[0:15]
	ds_read_b128 v[34:37], v22 offset:1536
	ds_read_b128 v[38:41], v22 offset:1568
	s_waitcnt lgkmcnt(1)
	v_mfma_f32_32x32x16_bf16 v[0:15], v[34:37], v[42:45], v[0:15]
	ds_read_b128 v[34:37], v23 offset:1536
	ds_read_b128 v[108:111], v23 offset:1568
	s_waitcnt lgkmcnt(1)
	v_mfma_f32_32x32x16_bf16 v[0:15], v[34:37], v[42:45], v[0:15]
	v_mfma_f32_32x32x16_bf16 v[0:15], v[38:41], v[46:49], v[0:15]
	ds_read_b128 v[34:37], v22 offset:1600
	ds_read_b128 v[38:41], v22 offset:1632
	s_waitcnt lgkmcnt(2)
	v_mfma_f32_32x32x16_bf16 v[0:15], v[108:111], v[46:49], v[0:15]
	s_waitcnt lgkmcnt(1)
	v_mfma_f32_32x32x16_bf16 v[0:15], v[34:37], v[26:29], v[0:15]
	ds_read_b128 v[34:37], v23 offset:1600
	ds_read_b128 v[42:45], v23 offset:1632
	s_waitcnt lgkmcnt(1)
	v_mfma_f32_32x32x16_bf16 v[0:15], v[34:37], v[26:29], v[0:15]
	ds_read_b128 v[26:29], v22 offset:1664
	ds_read_b128 v[34:37], v22 offset:1696
	v_mfma_f32_32x32x16_bf16 v[0:15], v[38:41], v[50:53], v[0:15]
	s_waitcnt lgkmcnt(2)
	v_mfma_f32_32x32x16_bf16 v[0:15], v[42:45], v[50:53], v[0:15]
	s_waitcnt lgkmcnt(1)
	v_mfma_f32_32x32x16_bf16 v[0:15], v[26:29], v[54:57], v[0:15]
	ds_read_b128 v[26:29], v23 offset:1664
	ds_read_b128 v[38:41], v23 offset:1696
	s_waitcnt lgkmcnt(1)
	v_mfma_f32_32x32x16_bf16 v[0:15], v[26:29], v[54:57], v[0:15]
	v_mfma_f32_32x32x16_bf16 v[0:15], v[34:37], v[88:91], v[0:15]
	ds_read_b128 v[26:29], v22 offset:1728
	ds_read_b128 v[34:37], v22 offset:1760
	s_waitcnt lgkmcnt(2)
	v_mfma_f32_32x32x16_bf16 v[0:15], v[38:41], v[88:91], v[0:15]
	s_waitcnt lgkmcnt(1)
	v_mfma_f32_32x32x16_bf16 v[0:15], v[26:29], v[92:95], v[0:15]
	ds_read_b128 v[26:29], v23 offset:1728
	ds_read_b128 v[38:41], v23 offset:1760
	s_waitcnt vmcnt(2)
	s_waitcnt lgkmcnt(1)
	v_mfma_f32_32x32x16_bf16 v[0:15], v[26:29], v[92:95], v[0:15]
	s_waitcnt vmcnt(0)
	v_mfma_f32_32x32x16_bf16 v[0:15], v[34:37], v[96:99], v[0:15]
	ds_read_b128 v[26:29], v22 offset:1792
	ds_read_b128 v[34:37], v22 offset:1824
	s_waitcnt lgkmcnt(2)
	v_mfma_f32_32x32x16_bf16 v[0:15], v[38:41], v[96:99], v[0:15]
	s_waitcnt lgkmcnt(1)
	v_mfma_f32_32x32x16_bf16 v[0:15], v[26:29], v[58:61], v[0:15]
	ds_read_b128 v[26:29], v23 offset:1792
	ds_read_b128 v[38:41], v23 offset:1824
	s_waitcnt lgkmcnt(1)
	v_mfma_f32_32x32x16_bf16 v[0:15], v[26:29], v[58:61], v[0:15]
	v_mfma_f32_32x32x16_bf16 v[0:15], v[34:37], v[68:71], v[0:15]
	ds_read_b128 v[26:29], v22 offset:1856
	ds_read_b128 v[34:37], v22 offset:1888
	s_waitcnt lgkmcnt(2)
	v_mfma_f32_32x32x16_bf16 v[0:15], v[38:41], v[68:71], v[0:15]
	s_waitcnt lgkmcnt(1)
	v_mfma_f32_32x32x16_bf16 v[0:15], v[26:29], v[30:33], v[0:15]
	ds_read_b128 v[26:29], v23 offset:1856
	ds_read_b128 v[38:41], v23 offset:1888
	s_waitcnt lgkmcnt(1)
	v_mfma_f32_32x32x16_bf16 v[0:15], v[26:29], v[30:33], v[0:15]
	ds_read_b128 v[26:29], v22 offset:1920
	ds_read_b128 v[30:33], v22 offset:1952
	v_mfma_f32_32x32x16_bf16 v[0:15], v[34:37], v[72:75], v[0:15]
	s_waitcnt lgkmcnt(2)
	v_mfma_f32_32x32x16_bf16 v[0:15], v[38:41], v[72:75], v[0:15]
	s_waitcnt lgkmcnt(1)
	v_mfma_f32_32x32x16_bf16 v[0:15], v[26:29], v[76:79], v[0:15]
	ds_read_b128 v[26:29], v23 offset:1920
	ds_read_b128 v[34:37], v23 offset:1952
	s_waitcnt lgkmcnt(1)
	v_mfma_f32_32x32x16_bf16 v[0:15], v[26:29], v[76:79], v[0:15]
	v_mfma_f32_32x32x16_bf16 v[0:15], v[30:33], v[80:83], v[0:15]
	ds_read_b128 v[26:29], v22 offset:1984
	ds_read_b128 v[30:33], v22 offset:2016
	s_waitcnt lgkmcnt(2)
	v_mfma_f32_32x32x16_bf16 v[0:15], v[34:37], v[80:83], v[0:15]
	s_waitcnt lgkmcnt(1)
	v_mfma_f32_32x32x16_bf16 v[0:15], v[26:29], v[84:87], v[0:15]
	ds_read_b128 v[26:29], v23 offset:1984
	ds_read_b128 v[34:37], v23 offset:2016
	s_waitcnt lgkmcnt(1)
	v_mfma_f32_32x32x16_bf16 v[0:15], v[26:29], v[84:87], v[0:15]
	v_mfma_f32_32x32x16_bf16 v[0:15], v[30:33], v[104:107], v[0:15]
	s_waitcnt lgkmcnt(0)
	v_mfma_f32_32x32x16_bf16 v[0:15], v[34:37], v[104:107], v[0:15]
	s_nop 11
	v_mov_b32_e32 v37, v0
	v_mov_b32_e32 v40, v1
	v_mov_b32_e32 v39, v2
	v_mov_b32_e32 v36, v3
	v_mov_b32_e32 v38, v4
	v_mov_b32_e32 v35, v5
	v_mov_b32_e32 v34, v6
	v_mov_b32_e32 v32, v7
	v_mov_b32_e32 v33, v8
	v_mov_b32_e32 v31, v9
	v_mov_b32_e32 v30, v10
	v_mov_b32_e32 v28, v11
	v_mov_b32_e32 v29, v12
	v_mov_b32_e32 v27, v13
	v_mov_b32_e32 v26, v14
	v_mov_b32_e32 v20, v15
	v_permlane32_swap_b32_e32 v0, v37
	v_permlane32_swap_b32_e32 v1, v40
	v_permlane32_swap_b32_e32 v2, v39
	v_permlane32_swap_b32_e32 v3, v36
	v_permlane32_swap_b32_e32 v4, v38
	v_permlane32_swap_b32_e32 v5, v35
	v_permlane32_swap_b32_e32 v6, v34
	v_permlane32_swap_b32_e32 v7, v32
	v_permlane32_swap_b32_e32 v8, v33
	v_permlane32_swap_b32_e32 v9, v31
	v_permlane32_swap_b32_e32 v10, v30
	v_permlane32_swap_b32_e32 v11, v28
	v_permlane32_swap_b32_e32 v12, v29
	v_permlane32_swap_b32_e32 v13, v27
	v_permlane32_swap_b32_e32 v14, v26
	v_permlane32_swap_b32_e32 v15, v20
	s_and_saveexec_b64 s[26:27], s[40:41]
	s_cbranch_execz .LBB0_932
	global_load_dwordx4 v[42:45], v113, s[6:7] offset:64
	global_load_dwordx4 v[46:49], v113, s[6:7] offset:80
	global_load_dwordx4 v[50:53], v113, s[6:7] offset:96
	global_load_dwordx4 v[54:57], v113, s[6:7] offset:112
	s_mov_b32 s4, 0xff800000
	s_waitcnt vmcnt(3)
	v_add_f32_e32 v8, v42, v8
	s_waitcnt vmcnt(2)
	v_add_f32_e32 v28, v49, v28
	s_waitcnt vmcnt(1)
	v_add_f32_e32 v21, v53, v15
	s_waitcnt vmcnt(0)
	v_add_f32_e32 v20, v57, v20
	v_add_f32_e32 v15, v56, v26
	v_add_f32_e32 v26, v52, v14
	v_add_f32_e32 v14, v55, v27
	v_add_f32_e32 v27, v51, v13
	v_add_f32_e32 v13, v54, v29
	v_add_f32_e32 v12, v50, v12
	v_add_f32_e32 v29, v45, v11
	v_add_f32_e32 v11, v48, v30
	v_add_f32_e32 v30, v44, v10
	v_add_f32_e32 v10, v47, v31
	v_add_f32_e32 v31, v43, v9
	v_add_f32_e32 v9, v46, v33
	global_load_dwordx4 v[42:45], v113, s[6:7]
	global_load_dwordx4 v[46:49], v113, s[6:7] offset:16
	global_load_dwordx4 v[50:53], v113, s[6:7] offset:32
	global_load_dwordx4 v[54:57], v113, s[6:7] offset:48
	s_waitcnt vmcnt(3)
	v_add_f32_e32 v41, v42, v0
	v_cmp_lg_f32_e32 vcc, s4, v41
	s_waitcnt vmcnt(1)
	v_add_f32_e32 v33, v53, v7
	s_waitcnt vmcnt(0)
	v_add_f32_e32 v7, v56, v34
	v_add_f32_e32 v34, v52, v6
	v_add_f32_e32 v6, v55, v35
	v_add_f32_e32 v35, v51, v5
	v_add_f32_e32 v5, v54, v38
	v_add_f32_e32 v38, v45, v3
	v_add_f32_e32 v3, v48, v39
	v_add_f32_e32 v39, v44, v2
	v_add_f32_e32 v2, v47, v40
	v_add_f32_e32 v40, v43, v1
	v_cndmask_b32_e32 v0, v205, v41, vcc
	v_cmp_gt_f32_e32 vcc, v40, v0
	v_add_f32_e32 v37, v46, v37
	v_add_f32_e32 v36, v49, v36
	v_cndmask_b32_e32 v0, v0, v40, vcc
	v_cndmask_b32_e64 v1, 0, 1, vcc
	v_cmp_gt_f32_e32 vcc, v39, v0
	v_add_f32_e32 v4, v50, v4
	v_add_f32_e32 v32, v57, v32
	v_cndmask_b32_e32 v0, v0, v39, vcc
	v_cndmask_b32_e64 v1, v1, 2, vcc
	v_cmp_gt_f32_e32 vcc, v38, v0
	s_nop 1
	v_cndmask_b32_e32 v0, v0, v38, vcc
	v_cndmask_b32_e64 v1, v1, 3, vcc
	v_cmp_gt_f32_e32 vcc, v37, v0
	s_nop 1
	v_cndmask_b32_e32 v0, v0, v37, vcc
	v_cndmask_b32_e64 v1, v1, 4, vcc
	v_cmp_gt_f32_e32 vcc, v2, v0
	s_nop 1
	v_cndmask_b32_e32 v0, v0, v2, vcc
	v_cndmask_b32_e64 v1, v1, 5, vcc
	v_cmp_gt_f32_e32 vcc, v3, v0
	s_nop 1
	v_cndmask_b32_e32 v0, v0, v3, vcc
	v_cndmask_b32_e64 v1, v1, 6, vcc
	v_cmp_gt_f32_e32 vcc, v36, v0
	s_nop 1
	v_cndmask_b32_e32 v0, v0, v36, vcc
	v_cndmask_b32_e64 v1, v1, 7, vcc
	v_cmp_gt_f32_e32 vcc, v4, v0
	s_nop 1
	v_cndmask_b32_e32 v0, v0, v4, vcc
	v_cndmask_b32_e64 v1, v1, 8, vcc
	v_cmp_gt_f32_e32 vcc, v35, v0
	s_nop 1
	v_cndmask_b32_e32 v0, v0, v35, vcc
	v_cndmask_b32_e64 v1, v1, 9, vcc
	v_cmp_gt_f32_e32 vcc, v34, v0
	s_nop 1
	v_cndmask_b32_e32 v0, v0, v34, vcc
	v_cndmask_b32_e64 v1, v1, 10, vcc
	v_cmp_gt_f32_e32 vcc, v33, v0
	s_nop 1
	v_cndmask_b32_e32 v0, v0, v33, vcc
	v_cndmask_b32_e64 v1, v1, 11, vcc
	v_cmp_gt_f32_e32 vcc, v5, v0
	s_nop 1
	v_cndmask_b32_e32 v0, v0, v5, vcc
	v_cndmask_b32_e64 v1, v1, 12, vcc
	v_cmp_gt_f32_e32 vcc, v6, v0
	s_nop 1
	v_cndmask_b32_e32 v0, v0, v6, vcc
	v_cndmask_b32_e64 v1, v1, 13, vcc
	v_cmp_gt_f32_e32 vcc, v7, v0
	s_nop 1
	v_cndmask_b32_e32 v0, v0, v7, vcc
	v_cndmask_b32_e64 v1, v1, 14, vcc
	v_cmp_gt_f32_e32 vcc, v32, v0
	s_nop 1
	v_cndmask_b32_e32 v0, v0, v32, vcc
	v_cndmask_b32_e64 v1, v1, 15, vcc
	v_cmp_gt_f32_e32 vcc, v8, v0
	s_nop 1
	v_cndmask_b32_e32 v0, v0, v8, vcc
	v_cndmask_b32_e64 v1, v1, 16, vcc
	v_cmp_gt_f32_e32 vcc, v31, v0
	s_nop 1
	v_cndmask_b32_e32 v0, v0, v31, vcc
	v_cndmask_b32_e64 v1, v1, 17, vcc
	v_cmp_gt_f32_e32 vcc, v30, v0
	s_nop 1
	v_cndmask_b32_e32 v0, v0, v30, vcc
	v_cndmask_b32_e64 v1, v1, 18, vcc
	v_cmp_gt_f32_e32 vcc, v29, v0
	s_nop 1
	v_cndmask_b32_e32 v0, v0, v29, vcc
	v_cndmask_b32_e64 v1, v1, 19, vcc
	v_cmp_gt_f32_e32 vcc, v9, v0
	s_nop 1
	v_cndmask_b32_e32 v0, v0, v9, vcc
	v_cndmask_b32_e64 v1, v1, 20, vcc
	v_cmp_gt_f32_e32 vcc, v10, v0
	s_nop 1
	v_cndmask_b32_e32 v0, v0, v10, vcc
	v_cndmask_b32_e64 v1, v1, 21, vcc
	v_cmp_gt_f32_e32 vcc, v11, v0
	s_nop 1
	v_cndmask_b32_e32 v0, v0, v11, vcc
	v_cndmask_b32_e64 v1, v1, 22, vcc
	v_cmp_gt_f32_e32 vcc, v28, v0
	s_nop 1
	v_cndmask_b32_e32 v0, v0, v28, vcc
	v_cndmask_b32_e64 v1, v1, 23, vcc
	v_cmp_gt_f32_e32 vcc, v12, v0
	s_nop 1
	v_cndmask_b32_e32 v0, v0, v12, vcc
	v_cndmask_b32_e64 v1, v1, 24, vcc
	v_cmp_gt_f32_e32 vcc, v27, v0
	s_nop 1
	v_cndmask_b32_e32 v0, v0, v27, vcc
	v_cndmask_b32_e64 v1, v1, 25, vcc
	v_cmp_gt_f32_e32 vcc, v26, v0
	s_nop 1
	v_cndmask_b32_e32 v0, v0, v26, vcc
	v_cndmask_b32_e64 v1, v1, 26, vcc
	v_cmp_gt_f32_e32 vcc, v21, v0
	s_nop 1
	v_cndmask_b32_e32 v0, v0, v21, vcc
	v_cndmask_b32_e64 v1, v1, 27, vcc
	v_cmp_gt_f32_e32 vcc, v13, v0
	s_nop 1
	v_cndmask_b32_e32 v0, v0, v13, vcc
	v_cndmask_b32_e64 v1, v1, 28, vcc
	v_cmp_gt_f32_e32 vcc, v14, v0
	s_nop 1
	v_cndmask_b32_e32 v0, v0, v14, vcc
	v_cndmask_b32_e64 v1, v1, 29, vcc
	v_cmp_gt_f32_e32 vcc, v15, v0
	s_nop 1
	v_cndmask_b32_e32 v42, v0, v15, vcc
	v_cndmask_b32_e64 v1, v1, 30, vcc
	v_cmp_gt_f32_e32 vcc, v20, v42
	s_nop 1
	v_cndmask_b32_e64 v0, v1, 31, vcc
	v_cndmask_b32_e32 v1, v42, v20, vcc
	v_cmp_eq_u32_e64 s[42:43], 0, v0
	v_cmp_nlg_f32_e32 vcc, s4, v41
	v_lshlrev_b32_e64 v42, v0, 1
	s_or_b64 s[42:43], s[42:43], vcc
	v_cndmask_b32_e64 v43, v41, v205, s[42:43]
	v_and_b32_e32 v44, 2, v42
	v_cmp_eq_u32_e64 s[42:43], 0, v44
	v_cmp_gt_f32_e64 s[46:47], v40, v43
	s_and_b64 s[42:43], s[42:43], s[46:47]
	v_cndmask_b32_e64 v43, v43, v40, s[42:43]
	v_and_b32_e32 v45, 4, v42
	v_cndmask_b32_e64 v44, 0, 1, s[42:43]
	v_cmp_eq_u32_e64 s[42:43], 0, v45
	v_cmp_gt_f32_e64 s[46:47], v39, v43
	s_and_b64 s[42:43], s[42:43], s[46:47]
	v_cndmask_b32_e64 v43, v43, v39, s[42:43]
	v_and_b32_e32 v45, 8, v42
	v_cndmask_b32_e64 v44, v44, 2, s[42:43]
	v_cmp_eq_u32_e64 s[42:43], 0, v45
	v_cmp_gt_f32_e64 s[46:47], v38, v43
	s_and_b64 s[42:43], s[42:43], s[46:47]
	v_cndmask_b32_e64 v43, v43, v38, s[42:43]
	v_and_b32_e32 v45, 16, v42
	v_cndmask_b32_e64 v44, v44, 3, s[42:43]
	v_cmp_eq_u32_e64 s[42:43], 0, v45
	v_cmp_gt_f32_e64 s[46:47], v37, v43
	s_and_b64 s[42:43], s[42:43], s[46:47]
	v_cndmask_b32_e64 v43, v43, v37, s[42:43]
	v_and_b32_e32 v45, 32, v42
	v_cndmask_b32_e64 v44, v44, 4, s[42:43]
	v_cmp_eq_u32_e64 s[42:43], 0, v45
	v_cmp_gt_f32_e64 s[46:47], v2, v43
	s_and_b64 s[42:43], s[42:43], s[46:47]
	v_cndmask_b32_e64 v43, v43, v2, s[42:43]
	v_and_b32_e32 v45, 64, v42
	v_cndmask_b32_e64 v44, v44, 5, s[42:43]
	v_cmp_eq_u32_e64 s[42:43], 0, v45
	v_cmp_gt_f32_e64 s[46:47], v3, v43
	s_and_b64 s[42:43], s[42:43], s[46:47]
	v_cndmask_b32_e64 v43, v43, v3, s[42:43]
	v_and_b32_e32 v45, 0x80, v42
	v_cndmask_b32_e64 v44, v44, 6, s[42:43]
	v_cmp_eq_u32_e64 s[42:43], 0, v45
	v_cmp_gt_f32_e64 s[46:47], v36, v43
	s_and_b64 s[42:43], s[42:43], s[46:47]
	v_cndmask_b32_e64 v43, v43, v36, s[42:43]
	v_and_b32_e32 v45, 0x100, v42
	v_cndmask_b32_e64 v44, v44, 7, s[42:43]
	v_cmp_eq_u32_e64 s[42:43], 0, v45
	v_cmp_gt_f32_e64 s[46:47], v4, v43
	s_and_b64 s[42:43], s[42:43], s[46:47]
	v_cndmask_b32_e64 v43, v43, v4, s[42:43]
	v_and_b32_e32 v45, 0x200, v42
	v_cndmask_b32_e64 v44, v44, 8, s[42:43]
	v_cmp_eq_u32_e64 s[42:43], 0, v45
	v_cmp_gt_f32_e64 s[46:47], v35, v43
	s_and_b64 s[42:43], s[42:43], s[46:47]
	v_cndmask_b32_e64 v43, v43, v35, s[42:43]
	v_and_b32_e32 v45, 0x400, v42
	v_cndmask_b32_e64 v44, v44, 9, s[42:43]
	v_cmp_eq_u32_e64 s[42:43], 0, v45
	v_cmp_gt_f32_e64 s[46:47], v34, v43
	s_and_b64 s[42:43], s[42:43], s[46:47]
	v_cndmask_b32_e64 v43, v43, v34, s[42:43]
	v_and_b32_e32 v45, 0x800, v42
	v_cndmask_b32_e64 v44, v44, 10, s[42:43]
	v_cmp_eq_u32_e64 s[42:43], 0, v45
	v_cmp_gt_f32_e64 s[46:47], v33, v43
	s_and_b64 s[42:43], s[42:43], s[46:47]
	v_cndmask_b32_e64 v43, v43, v33, s[42:43]
	v_and_b32_e32 v45, 0x1000, v42
	v_cndmask_b32_e64 v44, v44, 11, s[42:43]
	v_cmp_eq_u32_e64 s[42:43], 0, v45
	v_cmp_gt_f32_e64 s[46:47], v5, v43
	s_and_b64 s[42:43], s[42:43], s[46:47]
	v_cndmask_b32_e64 v43, v43, v5, s[42:43]
	v_and_b32_e32 v45, 0x2000, v42
	v_cndmask_b32_e64 v44, v44, 12, s[42:43]
	v_cmp_eq_u32_e64 s[42:43], 0, v45
	v_cmp_gt_f32_e64 s[46:47], v6, v43
	s_and_b64 s[42:43], s[42:43], s[46:47]
	v_cndmask_b32_e64 v43, v43, v6, s[42:43]
	v_and_b32_e32 v45, 0x4000, v42
	v_cndmask_b32_e64 v44, v44, 13, s[42:43]
	v_cmp_eq_u32_e64 s[42:43], 0, v45
	v_cmp_gt_f32_e64 s[46:47], v7, v43
	s_and_b64 s[42:43], s[42:43], s[46:47]
	v_cndmask_b32_e64 v43, v43, v7, s[42:43]
	v_and_b32_e32 v45, 0x8000, v42
	v_cndmask_b32_e64 v44, v44, 14, s[42:43]
	v_cmp_eq_u32_e64 s[42:43], 0, v45
	v_cmp_gt_f32_e64 s[46:47], v32, v43
	s_and_b64 s[42:43], s[42:43], s[46:47]
	v_cndmask_b32_e64 v43, v43, v32, s[42:43]
	v_and_b32_e32 v45, 0x10000, v42
	v_cndmask_b32_e64 v44, v44, 15, s[42:43]
	v_cmp_eq_u32_e64 s[42:43], 0, v45
	v_cmp_gt_f32_e64 s[46:47], v8, v43
	s_and_b64 s[42:43], s[42:43], s[46:47]
	v_cndmask_b32_e64 v43, v43, v8, s[42:43]
	v_and_b32_e32 v45, 0x20000, v42
	v_cndmask_b32_e64 v44, v44, 16, s[42:43]
	v_cmp_eq_u32_e64 s[42:43], 0, v45
	v_cmp_gt_f32_e64 s[46:47], v31, v43
	s_and_b64 s[42:43], s[42:43], s[46:47]
	v_cndmask_b32_e64 v43, v43, v31, s[42:43]
	v_and_b32_e32 v45, 0x40000, v42
	v_cndmask_b32_e64 v44, v44, 17, s[42:43]
	v_cmp_eq_u32_e64 s[42:43], 0, v45
	v_cmp_gt_f32_e64 s[46:47], v30, v43
	s_and_b64 s[42:43], s[42:43], s[46:47]
	v_cndmask_b32_e64 v43, v43, v30, s[42:43]
	v_and_b32_e32 v45, 0x80000, v42
	v_cndmask_b32_e64 v44, v44, 18, s[42:43]
	v_cmp_eq_u32_e64 s[42:43], 0, v45
	v_cmp_gt_f32_e64 s[46:47], v29, v43
	s_and_b64 s[42:43], s[42:43], s[46:47]
	v_cndmask_b32_e64 v43, v43, v29, s[42:43]
	v_and_b32_e32 v45, 0x100000, v42
	v_cndmask_b32_e64 v44, v44, 19, s[42:43]
	v_cmp_eq_u32_e64 s[42:43], 0, v45
	v_cmp_gt_f32_e64 s[46:47], v9, v43
	s_and_b64 s[42:43], s[42:43], s[46:47]
	v_cndmask_b32_e64 v43, v43, v9, s[42:43]
	v_and_b32_e32 v45, 0x200000, v42
	v_cndmask_b32_e64 v44, v44, 20, s[42:43]
	v_cmp_eq_u32_e64 s[42:43], 0, v45
	v_cmp_gt_f32_e64 s[46:47], v10, v43
	s_and_b64 s[42:43], s[42:43], s[46:47]
	v_cndmask_b32_e64 v43, v43, v10, s[42:43]
	v_and_b32_e32 v45, 0x400000, v42
	v_cndmask_b32_e64 v44, v44, 21, s[42:43]
	v_cmp_eq_u32_e64 s[42:43], 0, v45
	v_cmp_gt_f32_e64 s[46:47], v11, v43
	s_and_b64 s[42:43], s[42:43], s[46:47]
	v_cndmask_b32_e64 v43, v43, v11, s[42:43]
	v_and_b32_e32 v45, 0x800000, v42
	v_cndmask_b32_e64 v44, v44, 22, s[42:43]
	v_cmp_eq_u32_e64 s[42:43], 0, v45
	v_cmp_gt_f32_e64 s[46:47], v28, v43
	s_and_b64 s[42:43], s[42:43], s[46:47]
	v_cndmask_b32_e64 v43, v43, v28, s[42:43]
	v_and_b32_e32 v45, 0x1000000, v42
	v_cndmask_b32_e64 v44, v44, 23, s[42:43]
	v_cmp_eq_u32_e64 s[42:43], 0, v45
	v_cmp_gt_f32_e64 s[46:47], v12, v43
	s_and_b64 s[42:43], s[42:43], s[46:47]
	v_cndmask_b32_e64 v43, v43, v12, s[42:43]
	v_and_b32_e32 v45, 0x2000000, v42
	v_cndmask_b32_e64 v44, v44, 24, s[42:43]
	v_cmp_eq_u32_e64 s[42:43], 0, v45
	v_cmp_gt_f32_e64 s[46:47], v27, v43
	s_and_b64 s[42:43], s[42:43], s[46:47]
	v_cndmask_b32_e64 v43, v43, v27, s[42:43]
	v_and_b32_e32 v45, 0x4000000, v42
	v_cndmask_b32_e64 v44, v44, 25, s[42:43]
	v_cmp_eq_u32_e64 s[42:43], 0, v45
	v_cmp_gt_f32_e64 s[46:47], v26, v43
	s_and_b64 s[42:43], s[42:43], s[46:47]
	v_cndmask_b32_e64 v43, v43, v26, s[42:43]
	v_and_b32_e32 v45, 0x8000000, v42
	v_cndmask_b32_e64 v44, v44, 26, s[42:43]
	v_cmp_eq_u32_e64 s[42:43], 0, v45
	v_cmp_gt_f32_e64 s[46:47], v21, v43
	s_and_b64 s[42:43], s[42:43], s[46:47]
	v_cndmask_b32_e64 v43, v43, v21, s[42:43]
	v_and_b32_e32 v45, 0x10000000, v42
	v_cndmask_b32_e64 v44, v44, 27, s[42:43]
	v_cmp_eq_u32_e64 s[42:43], 0, v45
	v_cmp_gt_f32_e64 s[46:47], v13, v43
	s_and_b64 s[42:43], s[42:43], s[46:47]
	v_cndmask_b32_e64 v43, v43, v13, s[42:43]
	v_and_b32_e32 v45, 0x20000000, v42
	v_cndmask_b32_e64 v44, v44, 28, s[42:43]
	v_cmp_eq_u32_e64 s[42:43], 0, v45
	v_cmp_gt_f32_e64 s[46:47], v14, v43
	s_and_b64 s[42:43], s[42:43], s[46:47]
	v_cndmask_b32_e64 v43, v43, v14, s[42:43]
	v_and_b32_e32 v45, 2.0, v42
	v_cndmask_b32_e64 v44, v44, 29, s[42:43]
	v_cmp_eq_u32_e64 s[42:43], 0, v45
	v_cmp_gt_f32_e64 s[46:47], v15, v43
	s_and_b64 s[42:43], s[42:43], s[46:47]
	v_cndmask_b32_e64 v43, v43, v15, s[42:43]
	v_cndmask_b32_e64 v44, v44, 30, s[42:43]
	v_cmp_ne_u32_e64 s[42:43], 31, v0
	v_cmp_gt_f32_e64 s[46:47], v20, v43
	s_and_b64 s[42:43], s[42:43], s[46:47]
	v_cndmask_b32_e64 v44, v44, 31, s[42:43]
	v_lshl_or_b32 v42, 1, v44, v42
	v_and_b32_e32 v45, 1, v42
	v_cndmask_b32_e64 v43, v43, v20, s[42:43]
	v_cmp_eq_u32_e64 s[42:43], 1, v45
	s_or_b64 s[42:43], s[42:43], vcc
	v_and_b32_e32 v46, 2, v42
	v_cndmask_b32_e64 v45, v41, v205, s[42:43]
	v_cmp_eq_u32_e64 s[42:43], 0, v46
	v_cmp_gt_f32_e64 s[46:47], v40, v45
	s_and_b64 s[42:43], s[42:43], s[46:47]
	v_cndmask_b32_e64 v45, v45, v40, s[42:43]
	v_and_b32_e32 v47, 4, v42
	v_cndmask_b32_e64 v46, 0, 1, s[42:43]
	v_cmp_eq_u32_e64 s[42:43], 0, v47
	v_cmp_gt_f32_e64 s[46:47], v39, v45
	s_and_b64 s[42:43], s[42:43], s[46:47]
	v_cndmask_b32_e64 v45, v45, v39, s[42:43]
	v_and_b32_e32 v47, 8, v42
	v_cndmask_b32_e64 v46, v46, 2, s[42:43]
	v_cmp_eq_u32_e64 s[42:43], 0, v47
	v_cmp_gt_f32_e64 s[46:47], v38, v45
	s_and_b64 s[42:43], s[42:43], s[46:47]
	v_cndmask_b32_e64 v45, v45, v38, s[42:43]
	v_and_b32_e32 v47, 16, v42
	v_cndmask_b32_e64 v46, v46, 3, s[42:43]
	v_cmp_eq_u32_e64 s[42:43], 0, v47
	v_cmp_gt_f32_e64 s[46:47], v37, v45
	s_and_b64 s[42:43], s[42:43], s[46:47]
	v_cndmask_b32_e64 v45, v45, v37, s[42:43]
	v_and_b32_e32 v47, 32, v42
	v_cndmask_b32_e64 v46, v46, 4, s[42:43]
	v_cmp_eq_u32_e64 s[42:43], 0, v47
	v_cmp_gt_f32_e64 s[46:47], v2, v45
	s_and_b64 s[42:43], s[42:43], s[46:47]
	v_cndmask_b32_e64 v45, v45, v2, s[42:43]
	v_and_b32_e32 v47, 64, v42
	v_cndmask_b32_e64 v46, v46, 5, s[42:43]
	v_cmp_eq_u32_e64 s[42:43], 0, v47
	v_cmp_gt_f32_e64 s[46:47], v3, v45
	s_and_b64 s[42:43], s[42:43], s[46:47]
	v_cndmask_b32_e64 v45, v45, v3, s[42:43]
	v_and_b32_e32 v47, 0x80, v42
	v_cndmask_b32_e64 v46, v46, 6, s[42:43]
	v_cmp_eq_u32_e64 s[42:43], 0, v47
	v_cmp_gt_f32_e64 s[46:47], v36, v45
	s_and_b64 s[42:43], s[42:43], s[46:47]
	v_cndmask_b32_e64 v45, v45, v36, s[42:43]
	v_and_b32_e32 v47, 0x100, v42
	v_cndmask_b32_e64 v46, v46, 7, s[42:43]
	v_cmp_eq_u32_e64 s[42:43], 0, v47
	v_cmp_gt_f32_e64 s[46:47], v4, v45
	s_and_b64 s[42:43], s[42:43], s[46:47]
	v_cndmask_b32_e64 v45, v45, v4, s[42:43]
	v_and_b32_e32 v47, 0x200, v42
	v_cndmask_b32_e64 v46, v46, 8, s[42:43]
	v_cmp_eq_u32_e64 s[42:43], 0, v47
	v_cmp_gt_f32_e64 s[46:47], v35, v45
	s_and_b64 s[42:43], s[42:43], s[46:47]
	v_cndmask_b32_e64 v45, v45, v35, s[42:43]
	v_and_b32_e32 v47, 0x400, v42
	v_cndmask_b32_e64 v46, v46, 9, s[42:43]
	v_cmp_eq_u32_e64 s[42:43], 0, v47
	v_cmp_gt_f32_e64 s[46:47], v34, v45
	s_and_b64 s[42:43], s[42:43], s[46:47]
	v_cndmask_b32_e64 v45, v45, v34, s[42:43]
	v_and_b32_e32 v47, 0x800, v42
	v_cndmask_b32_e64 v46, v46, 10, s[42:43]
	v_cmp_eq_u32_e64 s[42:43], 0, v47
	v_cmp_gt_f32_e64 s[46:47], v33, v45
	s_and_b64 s[42:43], s[42:43], s[46:47]
	v_cndmask_b32_e64 v45, v45, v33, s[42:43]
	v_and_b32_e32 v47, 0x1000, v42
	v_cndmask_b32_e64 v46, v46, 11, s[42:43]
	v_cmp_eq_u32_e64 s[42:43], 0, v47
	v_cmp_gt_f32_e64 s[46:47], v5, v45
	s_and_b64 s[42:43], s[42:43], s[46:47]
	v_cndmask_b32_e64 v45, v45, v5, s[42:43]
	v_and_b32_e32 v47, 0x2000, v42
	v_cndmask_b32_e64 v46, v46, 12, s[42:43]
	v_cmp_eq_u32_e64 s[42:43], 0, v47
	v_cmp_gt_f32_e64 s[46:47], v6, v45
	s_and_b64 s[42:43], s[42:43], s[46:47]
	v_cndmask_b32_e64 v45, v45, v6, s[42:43]
	v_and_b32_e32 v47, 0x4000, v42
	v_cndmask_b32_e64 v46, v46, 13, s[42:43]
	v_cmp_eq_u32_e64 s[42:43], 0, v47
	v_cmp_gt_f32_e64 s[46:47], v7, v45
	s_and_b64 s[42:43], s[42:43], s[46:47]
	v_cndmask_b32_e64 v45, v45, v7, s[42:43]
	v_and_b32_e32 v47, 0x8000, v42
	v_cndmask_b32_e64 v46, v46, 14, s[42:43]
	v_cmp_eq_u32_e64 s[42:43], 0, v47
	v_cmp_gt_f32_e64 s[46:47], v32, v45
	s_and_b64 s[42:43], s[42:43], s[46:47]
	v_cndmask_b32_e64 v45, v45, v32, s[42:43]
	v_and_b32_e32 v47, 0x10000, v42
	v_cndmask_b32_e64 v46, v46, 15, s[42:43]
	v_cmp_eq_u32_e64 s[42:43], 0, v47
	v_cmp_gt_f32_e64 s[46:47], v8, v45
	s_and_b64 s[42:43], s[42:43], s[46:47]
	v_cndmask_b32_e64 v45, v45, v8, s[42:43]
	v_and_b32_e32 v47, 0x20000, v42
	v_cndmask_b32_e64 v46, v46, 16, s[42:43]
	v_cmp_eq_u32_e64 s[42:43], 0, v47
	v_cmp_gt_f32_e64 s[46:47], v31, v45
	s_and_b64 s[42:43], s[42:43], s[46:47]
	v_cndmask_b32_e64 v45, v45, v31, s[42:43]
	v_and_b32_e32 v47, 0x40000, v42
	v_cndmask_b32_e64 v46, v46, 17, s[42:43]
	v_cmp_eq_u32_e64 s[42:43], 0, v47
	v_cmp_gt_f32_e64 s[46:47], v30, v45
	s_and_b64 s[42:43], s[42:43], s[46:47]
	v_cndmask_b32_e64 v45, v45, v30, s[42:43]
	v_and_b32_e32 v47, 0x80000, v42
	v_cndmask_b32_e64 v46, v46, 18, s[42:43]
	v_cmp_eq_u32_e64 s[42:43], 0, v47
	v_cmp_gt_f32_e64 s[46:47], v29, v45
	s_and_b64 s[42:43], s[42:43], s[46:47]
	v_cndmask_b32_e64 v45, v45, v29, s[42:43]
	v_and_b32_e32 v47, 0x100000, v42
	v_cndmask_b32_e64 v46, v46, 19, s[42:43]
	v_cmp_eq_u32_e64 s[42:43], 0, v47
	v_cmp_gt_f32_e64 s[46:47], v9, v45
	s_and_b64 s[42:43], s[42:43], s[46:47]
	v_cndmask_b32_e64 v45, v45, v9, s[42:43]
	v_and_b32_e32 v47, 0x200000, v42
	v_cndmask_b32_e64 v46, v46, 20, s[42:43]
	v_cmp_eq_u32_e64 s[42:43], 0, v47
	v_cmp_gt_f32_e64 s[46:47], v10, v45
	s_and_b64 s[42:43], s[42:43], s[46:47]
	v_cndmask_b32_e64 v45, v45, v10, s[42:43]
	v_and_b32_e32 v47, 0x400000, v42
	v_cndmask_b32_e64 v46, v46, 21, s[42:43]
	v_cmp_eq_u32_e64 s[42:43], 0, v47
	v_cmp_gt_f32_e64 s[46:47], v11, v45
	s_and_b64 s[42:43], s[42:43], s[46:47]
	v_cndmask_b32_e64 v45, v45, v11, s[42:43]
	v_and_b32_e32 v47, 0x800000, v42
	v_cndmask_b32_e64 v46, v46, 22, s[42:43]
	v_cmp_eq_u32_e64 s[42:43], 0, v47
	v_cmp_gt_f32_e64 s[46:47], v28, v45
	s_and_b64 s[42:43], s[42:43], s[46:47]
	v_cndmask_b32_e64 v45, v45, v28, s[42:43]
	v_and_b32_e32 v47, 0x1000000, v42
	v_cndmask_b32_e64 v46, v46, 23, s[42:43]
	v_cmp_eq_u32_e64 s[42:43], 0, v47
	v_cmp_gt_f32_e64 s[46:47], v12, v45
	s_and_b64 s[42:43], s[42:43], s[46:47]
	v_cndmask_b32_e64 v45, v45, v12, s[42:43]
	v_and_b32_e32 v47, 0x2000000, v42
	v_cndmask_b32_e64 v46, v46, 24, s[42:43]
	v_cmp_eq_u32_e64 s[42:43], 0, v47
	v_cmp_gt_f32_e64 s[46:47], v27, v45
	s_and_b64 s[42:43], s[42:43], s[46:47]
	v_cndmask_b32_e64 v45, v45, v27, s[42:43]
	v_and_b32_e32 v47, 0x4000000, v42
	v_cndmask_b32_e64 v46, v46, 25, s[42:43]
	v_cmp_eq_u32_e64 s[42:43], 0, v47
	v_cmp_gt_f32_e64 s[46:47], v26, v45
	s_and_b64 s[42:43], s[42:43], s[46:47]
	v_cndmask_b32_e64 v45, v45, v26, s[42:43]
	v_and_b32_e32 v47, 0x8000000, v42
	v_cndmask_b32_e64 v46, v46, 26, s[42:43]
	v_cmp_eq_u32_e64 s[42:43], 0, v47
	v_cmp_gt_f32_e64 s[46:47], v21, v45
	s_and_b64 s[42:43], s[42:43], s[46:47]
	v_cndmask_b32_e64 v45, v45, v21, s[42:43]
	v_and_b32_e32 v47, 0x10000000, v42
	v_cndmask_b32_e64 v46, v46, 27, s[42:43]
	v_cmp_eq_u32_e64 s[42:43], 0, v47
	v_cmp_gt_f32_e64 s[46:47], v13, v45
	s_and_b64 s[42:43], s[42:43], s[46:47]
	v_cndmask_b32_e64 v45, v45, v13, s[42:43]
	v_and_b32_e32 v47, 0x20000000, v42
	v_cndmask_b32_e64 v46, v46, 28, s[42:43]
	v_cmp_eq_u32_e64 s[42:43], 0, v47
	v_cmp_gt_f32_e64 s[46:47], v14, v45
	s_and_b64 s[42:43], s[42:43], s[46:47]
	v_cndmask_b32_e64 v45, v45, v14, s[42:43]
	v_and_b32_e32 v47, 2.0, v42
	v_cndmask_b32_e64 v46, v46, 29, s[42:43]
	v_cmp_eq_u32_e64 s[42:43], 0, v47
	v_cmp_gt_f32_e64 s[46:47], v15, v45
	s_and_b64 s[42:43], s[42:43], s[46:47]
	v_cndmask_b32_e64 v45, v45, v15, s[42:43]
	v_cndmask_b32_e64 v46, v46, 30, s[42:43]
	v_cmp_lt_i32_e64 s[42:43], -1, v42
	v_cmp_gt_f32_e64 s[46:47], v20, v45
	s_and_b64 s[42:43], s[42:43], s[46:47]
	v_cndmask_b32_e64 v46, v46, 31, s[42:43]
	v_lshlrev_b32_e64 v47, v46, 1
	v_or_b32_e32 v48, v47, v42
	v_and_b32_e32 v49, 1, v48
	v_cndmask_b32_e64 v45, v45, v20, s[42:43]
	v_cmp_eq_u32_e64 s[42:43], 1, v49
	s_or_b64 vcc, s[42:43], vcc
	v_cndmask_b32_e32 v41, v41, v205, vcc
	v_bitop3_b32 v49, v47, 2, v42 bitop3:0xc8
	v_cmp_eq_u32_e32 vcc, 0, v49
	v_cmp_gt_f32_e64 s[42:43], v40, v41
	s_and_b64 vcc, vcc, s[42:43]
	v_cndmask_b32_e32 v40, v41, v40, vcc
	v_bitop3_b32 v41, v47, 4, v42 bitop3:0xc8
	v_cndmask_b32_e64 v49, 0, 1, vcc
	v_cmp_eq_u32_e32 vcc, 0, v41
	v_cmp_gt_f32_e64 s[42:43], v39, v40
	s_and_b64 vcc, vcc, s[42:43]
	v_cndmask_b32_e32 v39, v40, v39, vcc
	v_bitop3_b32 v40, v47, 8, v42 bitop3:0xc8
	v_cndmask_b32_e64 v41, v49, 2, vcc
	v_cmp_eq_u32_e32 vcc, 0, v40
	v_cmp_gt_f32_e64 s[42:43], v38, v39
	s_and_b64 vcc, vcc, s[42:43]
	v_cndmask_b32_e32 v38, v39, v38, vcc
	v_bitop3_b32 v39, v47, 16, v42 bitop3:0xc8
	v_cndmask_b32_e64 v40, v41, 3, vcc
	v_cmp_eq_u32_e32 vcc, 0, v39
	v_cmp_gt_f32_e64 s[42:43], v37, v38
	s_and_b64 vcc, vcc, s[42:43]
	v_cndmask_b32_e32 v37, v38, v37, vcc
	v_bitop3_b32 v38, v47, 32, v42 bitop3:0xc8
	v_cndmask_b32_e64 v39, v40, 4, vcc
	v_cmp_eq_u32_e32 vcc, 0, v38
	v_cmp_gt_f32_e64 s[42:43], v2, v37
	s_and_b64 vcc, vcc, s[42:43]
	v_cndmask_b32_e32 v2, v37, v2, vcc
	v_bitop3_b32 v37, v47, 64, v42 bitop3:0xc8
	v_cndmask_b32_e64 v38, v39, 5, vcc
	v_cmp_eq_u32_e32 vcc, 0, v37
	v_cmp_gt_f32_e64 s[42:43], v3, v2
	s_and_b64 vcc, vcc, s[42:43]
	s_movk_i32 s4, 0x80
	v_cndmask_b32_e32 v2, v2, v3, vcc
	v_bitop3_b32 v3, v47, s4, v42 bitop3:0xc8
	v_cndmask_b32_e64 v37, v38, 6, vcc
	v_cmp_eq_u32_e32 vcc, 0, v3
	v_cmp_gt_f32_e64 s[42:43], v36, v2
	s_and_b64 vcc, vcc, s[42:43]
	s_movk_i32 s4, 0x100
	v_cndmask_b32_e32 v2, v2, v36, vcc
	v_bitop3_b32 v36, v47, s4, v42 bitop3:0xc8
	v_cndmask_b32_e64 v3, v37, 7, vcc
	v_cmp_eq_u32_e32 vcc, 0, v36
	v_cmp_gt_f32_e64 s[42:43], v4, v2
	s_and_b64 vcc, vcc, s[42:43]
	s_movk_i32 s4, 0x200
	v_cndmask_b32_e32 v2, v2, v4, vcc
	v_bitop3_b32 v4, v47, s4, v42 bitop3:0xc8
	v_cndmask_b32_e64 v3, v3, 8, vcc
	v_cmp_eq_u32_e32 vcc, 0, v4
	v_cmp_gt_f32_e64 s[42:43], v35, v2
	s_and_b64 vcc, vcc, s[42:43]
	s_movk_i32 s4, 0x400
	v_cndmask_b32_e32 v2, v2, v35, vcc
	v_bitop3_b32 v4, v47, s4, v42 bitop3:0xc8
	v_cndmask_b32_e64 v3, v3, 9, vcc
	v_cmp_eq_u32_e32 vcc, 0, v4
	v_cmp_gt_f32_e64 s[42:43], v34, v2
	s_and_b64 vcc, vcc, s[42:43]
	s_movk_i32 s4, 0x800
	v_cndmask_b32_e32 v2, v2, v34, vcc
	v_bitop3_b32 v4, v47, s4, v42 bitop3:0xc8
	v_cndmask_b32_e64 v3, v3, 10, vcc
	v_cmp_eq_u32_e32 vcc, 0, v4
	v_cmp_gt_f32_e64 s[42:43], v33, v2
	s_and_b64 vcc, vcc, s[42:43]
	s_movk_i32 s4, 0x1000
	v_cndmask_b32_e32 v2, v2, v33, vcc
	v_bitop3_b32 v4, v47, s4, v42 bitop3:0xc8
	v_cndmask_b32_e64 v3, v3, 11, vcc
	v_cmp_eq_u32_e32 vcc, 0, v4
	v_cmp_gt_f32_e64 s[42:43], v5, v2
	s_and_b64 vcc, vcc, s[42:43]
	v_cndmask_b32_e32 v2, v2, v5, vcc
	v_bitop3_b32 v4, v47, s59, v42 bitop3:0xc8
	v_cndmask_b32_e64 v3, v3, 12, vcc
	v_cmp_eq_u32_e32 vcc, 0, v4
	v_cmp_gt_f32_e64 s[42:43], v6, v2
	s_and_b64 vcc, vcc, s[42:43]
	v_cndmask_b32_e32 v2, v2, v6, vcc
	v_bitop3_b32 v4, v47, s62, v42 bitop3:0xc8
	v_cndmask_b32_e64 v3, v3, 13, vcc
	v_cmp_eq_u32_e32 vcc, 0, v4
	v_cmp_gt_f32_e64 s[42:43], v7, v2
	s_and_b64 vcc, vcc, s[42:43]
	v_cndmask_b32_e32 v2, v2, v7, vcc
	v_bitop3_b32 v4, v47, s24, v42 bitop3:0xc8
	v_cndmask_b32_e64 v3, v3, 14, vcc
	v_cmp_eq_u32_e32 vcc, 0, v4
	v_cmp_gt_f32_e64 s[42:43], v32, v2
	s_and_b64 vcc, vcc, s[42:43]
	s_mov_b32 s4, 0x10000
	v_cndmask_b32_e32 v2, v2, v32, vcc
	v_bitop3_b32 v4, v47, s4, v42 bitop3:0xc8
	v_cndmask_b32_e64 v3, v3, 15, vcc
	v_cmp_eq_u32_e32 vcc, 0, v4
	v_cmp_gt_f32_e64 s[42:43], v8, v2
	s_and_b64 vcc, vcc, s[42:43]
	s_mov_b32 s4, 0x20000
	v_cndmask_b32_e32 v2, v2, v8, vcc
	v_bitop3_b32 v4, v47, s4, v42 bitop3:0xc8
	v_cndmask_b32_e64 v3, v3, 16, vcc
	v_cmp_eq_u32_e32 vcc, 0, v4
	v_cmp_gt_f32_e64 s[42:43], v31, v2
	s_and_b64 vcc, vcc, s[42:43]
	s_mov_b32 s4, 0x40000
	v_cndmask_b32_e32 v2, v2, v31, vcc
	v_bitop3_b32 v4, v47, s4, v42 bitop3:0xc8
	v_cndmask_b32_e64 v3, v3, 17, vcc
	v_cmp_eq_u32_e32 vcc, 0, v4
	v_cmp_gt_f32_e64 s[42:43], v30, v2
	s_and_b64 vcc, vcc, s[42:43]
	s_mov_b32 s4, 0x80000
	v_cndmask_b32_e32 v2, v2, v30, vcc
	v_bitop3_b32 v4, v47, s4, v42 bitop3:0xc8
	v_cndmask_b32_e64 v3, v3, 18, vcc
	v_cmp_eq_u32_e32 vcc, 0, v4
	v_cmp_gt_f32_e64 s[42:43], v29, v2
	s_and_b64 vcc, vcc, s[42:43]
	s_mov_b32 s4, 0x100000
	v_cndmask_b32_e32 v2, v2, v29, vcc
	v_bitop3_b32 v4, v47, s4, v42 bitop3:0xc8
	v_cndmask_b32_e64 v3, v3, 19, vcc
	v_cmp_eq_u32_e32 vcc, 0, v4
	v_cmp_gt_f32_e64 s[42:43], v9, v2
	s_and_b64 vcc, vcc, s[42:43]
	s_mov_b32 s4, 0x200000
	v_cndmask_b32_e32 v2, v2, v9, vcc
	v_bitop3_b32 v4, v47, s4, v42 bitop3:0xc8
	v_cndmask_b32_e64 v3, v3, 20, vcc
	v_cmp_eq_u32_e32 vcc, 0, v4
	v_cmp_gt_f32_e64 s[42:43], v10, v2
	s_and_b64 vcc, vcc, s[42:43]
	s_mov_b32 s4, 0x400000
	v_cndmask_b32_e32 v2, v2, v10, vcc
	v_bitop3_b32 v4, v47, s4, v42 bitop3:0xc8
	v_cndmask_b32_e64 v3, v3, 21, vcc
	v_cmp_eq_u32_e32 vcc, 0, v4
	v_cmp_gt_f32_e64 s[42:43], v11, v2
	s_and_b64 vcc, vcc, s[42:43]
	v_cndmask_b32_e32 v2, v2, v11, vcc
	v_bitop3_b32 v4, v47, s35, v42 bitop3:0xc8
	v_cndmask_b32_e64 v3, v3, 22, vcc
	v_cmp_eq_u32_e32 vcc, 0, v4
	v_cmp_gt_f32_e64 s[42:43], v28, v2
	s_and_b64 vcc, vcc, s[42:43]
	s_mov_b32 s4, 0x1000000
	v_cndmask_b32_e32 v2, v2, v28, vcc
	v_bitop3_b32 v4, v47, s4, v42 bitop3:0xc8
	v_cndmask_b32_e64 v3, v3, 23, vcc
	v_cmp_eq_u32_e32 vcc, 0, v4
	v_cmp_gt_f32_e64 s[42:43], v12, v2
	s_and_b64 vcc, vcc, s[42:43]
	s_brev_b32 s4, 64
	v_cndmask_b32_e32 v2, v2, v12, vcc
	v_bitop3_b32 v4, v47, s4, v42 bitop3:0xc8
	v_cndmask_b32_e64 v3, v3, 24, vcc
	v_cmp_eq_u32_e32 vcc, 0, v4
	v_cmp_gt_f32_e64 s[42:43], v27, v2
	s_and_b64 vcc, vcc, s[42:43]
	s_brev_b32 s4, 32
	v_cndmask_b32_e32 v2, v2, v27, vcc
	v_bitop3_b32 v4, v47, s4, v42 bitop3:0xc8
	v_cndmask_b32_e64 v3, v3, 25, vcc
	v_cmp_eq_u32_e32 vcc, 0, v4
	v_cmp_gt_f32_e64 s[42:43], v26, v2
	s_and_b64 vcc, vcc, s[42:43]
	s_brev_b32 s4, 16
	v_cndmask_b32_e32 v2, v2, v26, vcc
	v_bitop3_b32 v4, v47, s4, v42 bitop3:0xc8
	v_cndmask_b32_e64 v3, v3, 26, vcc
	v_cmp_eq_u32_e32 vcc, 0, v4
	v_cmp_gt_f32_e64 s[42:43], v21, v2
	s_and_b64 vcc, vcc, s[42:43]
	s_brev_b32 s4, 8
	v_cndmask_b32_e32 v2, v2, v21, vcc
	v_bitop3_b32 v4, v47, s4, v42 bitop3:0xc8
	v_cndmask_b32_e64 v3, v3, 27, vcc
	v_cmp_eq_u32_e32 vcc, 0, v4
	v_cmp_gt_f32_e64 s[42:43], v13, v2
	s_and_b64 vcc, vcc, s[42:43]
	s_brev_b32 s4, 4
	v_cndmask_b32_e32 v2, v2, v13, vcc
	v_bitop3_b32 v4, v47, s4, v42 bitop3:0xc8
	v_cndmask_b32_e64 v3, v3, 28, vcc
	v_cmp_eq_u32_e32 vcc, 0, v4
	v_cmp_gt_f32_e64 s[42:43], v14, v2
	s_and_b64 vcc, vcc, s[42:43]
	v_cndmask_b32_e32 v2, v2, v14, vcc
	v_bitop3_b32 v4, v47, 2.0, v42 bitop3:0xc8
	v_cndmask_b32_e64 v3, v3, 29, vcc
	v_cmp_eq_u32_e32 vcc, 0, v4
	v_cmp_gt_f32_e64 s[42:43], v15, v2
	s_and_b64 vcc, vcc, s[42:43]
	v_cndmask_b32_e32 v2, v2, v15, vcc
	v_cndmask_b32_e64 v3, v3, 30, vcc
	v_cmp_lt_i32_e32 vcc, -1, v48
	v_cmp_gt_f32_e64 s[42:43], v20, v2
	s_and_b64 vcc, vcc, s[42:43]
	v_cndmask_b32_e64 v10, v3, 31, vcc
	v_sub_f32_e32 v3, v43, v1
	v_mul_f32_e32 v3, 0x3fb8aa3b, v3
	v_cndmask_b32_e32 v2, v2, v20, vcc
	v_exp_f32_e32 v4, v3
	v_sub_f32_e32 v3, v45, v1
	v_mul_f32_e32 v3, 0x3fb8aa3b, v3
	v_sub_f32_e32 v1, v2, v1
	v_exp_f32_e32 v5, v3
	v_mul_f32_e32 v1, 0x3fb8aa3b, v1
	v_exp_f32_e32 v1, v1
	v_add_f32_e32 v2, 1.0, v4
	v_add_f32_e32 v2, v2, v5
	s_add_i32 s4, 0, 0x21600
	v_add_f32_e32 v2, v2, v1
	v_div_scale_f32 v3, s[12:13], v2, v2, 1.0
	v_rcp_f32_e32 v6, v3
	v_readlane_b32 s12, v254, 20
	v_readlane_b32 s13, v254, 21
	v_fma_f32 v7, -v3, v6, 1.0
	v_fmac_f32_e32 v6, v7, v6
	v_div_scale_f32 v7, vcc, 1.0, v2, 1.0
	v_mul_f32_e32 v8, v7, v6
	v_fma_f32 v9, -v3, v8, v7
	v_fmac_f32_e32 v8, v9, v6
	v_fma_f32 v3, -v3, v8, v7
	v_div_fmas_f32 v3, v3, v6, v8
	v_div_fixup_f32 v2, v3, v2, 1.0
	v_pk_mul_f32 v[6:7], v[4:5], v[2:3] op_sel_hi:[1,0]
	v_mul_f32_e32 v5, v1, v2
	v_lshl_add_u64 v[8:9], v[18:19], 4, s[12:13]
	v_mov_b32_e32 v3, v6
	v_mov_b32_e32 v4, v7
	global_store_dwordx4 v[8:9], v[2:5], off
	v_lshl_add_u32 v1, v0, 2, s4
	ds_add_rtn_u32 v1, v1, v197
	s_waitcnt lgkmcnt(0)
	v_lshl_or_b32 v0, v1, 5, v0
	ds_write_b32 v24, v0
	v_lshl_add_u32 v0, v44, 2, s4
	ds_add_rtn_u32 v0, v0, v197
	s_waitcnt lgkmcnt(0)
	v_lshl_or_b32 v0, v0, 5, v44
	ds_write_b32 v24, v0 offset:4
	v_lshl_add_u32 v0, v46, 2, s4
	ds_add_rtn_u32 v0, v0, v197
	s_waitcnt lgkmcnt(0)
	v_lshl_or_b32 v0, v0, 5, v46
	ds_write_b32 v24, v0 offset:8
	v_lshl_add_u32 v0, v10, 2, s4
	ds_add_rtn_u32 v0, v0, v197
	s_waitcnt lgkmcnt(0)
	v_lshl_or_b32 v0, v0, 5, v10
	ds_write_b32 v24, v0 offset:12
	s_branch .LBB0_932

.Lpeel_up_body:
	s_add_u32 s30, s94, s72
	s_addc_u32 s31, s95, s73
	s_add_u32 s45, s30, 0x28dd9100
	s_addc_u32 s55, s31, 0
	s_and_b64 s[30:31], s[40:41], exec
	s_cselect_b32 s77, s91, s55
	s_cselect_b32 s76, s90, s45
	s_add_u32 s45, s37, s72
	s_addc_u32 s55, s47, s73
	s_and_b64 s[30:31], s[40:41], exec
	s_cselect_b32 s75, s65, s55
	s_cselect_b32 s74, s64, s45
	s_add_i32 s55, 0, 0x10000
	s_add_i32 s58, 0, 0x14000
	v_add_u32_e32 v0, s55, v193
	v_add_u32_e32 v12, s58, v193
	ds_read_b128 v[16:19], v0
	ds_read_b128 v[20:23], v0 offset:1024
	ds_read_b128 v[24:27], v0 offset:2048
	ds_read_b128 v[28:31], v0 offset:3072
	ds_read_b128 v[0:3], v12
	ds_read_b128 v[4:7], v12 offset:1024
	ds_read_b128 v[8:11], v12 offset:2048
	ds_read_b128 v[12:15], v12 offset:3072
	v_lshl_add_u64 v[206:207], v[178:179], 0, s[72:73]
	s_add_i32 m0, s7, 0xc000
	ds_read_b128 v[180:183], v169
	ds_read_b128 v[184:187], v169 offset:1024
	ds_read_b128 v[224:227], v169 offset:2048
	ds_read_b128 v[228:231], v169 offset:3072
	ds_read_b128 v[232:235], v169 offset:4096
	ds_read_b128 v[236:239], v169 offset:5120
	ds_read_b128 v[240:243], v169 offset:6144
	ds_read_b128 v[244:247], v169 offset:7168
	global_load_lds_dwordx4 v[206:207], off
	v_lshl_add_u64 v[206:207], v[176:177], 0, s[72:73]
	s_add_i32 m0, s7, 0xe000
	s_nop 0
	global_load_lds_dwordx4 v[206:207], off
	s_waitcnt vmcnt(8)
	s_waitcnt lgkmcnt(0)
	s_barrier
	s_setprio 1
	v_mfma_scale_f32_16x16x128_f8f6f4 v[158:161], v[16:23], v[180:187], 0, v200, v201 op_sel_hi:[0,0,0]
	v_mfma_scale_f32_16x16x128_f8f6f4 v[150:153], v[24:31], v[180:187], 0, v200, v201 op_sel_hi:[0,0,0]
	v_mfma_scale_f32_16x16x128_f8f6f4 v[142:145], v[16:23], v[224:231], 0, v200, v201 op_sel_hi:[0,0,0]
	v_mfma_scale_f32_16x16x128_f8f6f4 v[134:137], v[24:31], v[224:231], 0, v200, v201 op_sel_hi:[0,0,0]
	v_mfma_scale_f32_16x16x128_f8f6f4 v[126:129], v[16:23], v[232:239], 0, v200, v201 op_sel_hi:[0,0,0]
	v_mfma_scale_f32_16x16x128_f8f6f4 v[118:121], v[24:31], v[232:239], 0, v200, v201 op_sel_hi:[0,0,0]
	v_mfma_scale_f32_16x16x128_f8f6f4 v[108:111], v[16:23], v[240:247], 0, v200, v201 op_sel_hi:[0,0,0]
	v_mfma_scale_f32_16x16x128_f8f6f4 v[100:103], v[24:31], v[240:247], 0, v200, v201 op_sel_hi:[0,0,0]
	s_setprio 0
	s_setprio 1
	v_mfma_scale_f32_16x16x128_f8f6f4 v[154:157], v[0:7], v[180:187], 0, v200, v201 op_sel_hi:[0,0,0]
	v_mfma_scale_f32_16x16x128_f8f6f4 v[146:149], v[8:15], v[180:187], 0, v200, v201 op_sel_hi:[0,0,0]
	v_mfma_scale_f32_16x16x128_f8f6f4 v[138:141], v[0:7], v[224:231], 0, v200, v201 op_sel_hi:[0,0,0]
	v_mfma_scale_f32_16x16x128_f8f6f4 v[130:133], v[8:15], v[224:231], 0, v200, v201 op_sel_hi:[0,0,0]
	v_mfma_scale_f32_16x16x128_f8f6f4 v[122:125], v[0:7], v[232:239], 0, v200, v201 op_sel_hi:[0,0,0]
	v_mfma_scale_f32_16x16x128_f8f6f4 v[114:117], v[8:15], v[232:239], 0, v200, v201 op_sel_hi:[0,0,0]
	v_mfma_scale_f32_16x16x128_f8f6f4 v[104:107], v[0:7], v[240:247], 0, v200, v201 op_sel_hi:[0,0,0]
	v_mfma_scale_f32_16x16x128_f8f6f4 v[96:99], v[8:15], v[240:247], 0, v200, v201 op_sel_hi:[0,0,0]
	s_setprio 0
	s_barrier
	s_add_i32 s30, s55, s14
	v_lshl_add_u64 v[180:181], s[74:75], 0, v[164:165]
	s_mov_b32 m0, s30
	ds_read_b128 v[224:227], v169 offset:16384
	ds_read_b128 v[228:231], v169 offset:17408
	ds_read_b128 v[232:235], v169 offset:18432
	ds_read_b128 v[236:239], v169 offset:19456
	ds_read_b128 v[240:243], v169 offset:20480
	ds_read_b128 v[244:247], v169 offset:21504
	ds_read_b128 v[206:209], v169 offset:22528
	ds_read_b128 v[210:213], v169 offset:23552
	global_load_lds_dwordx4 v[180:181], off
	s_add_i32 m0, s30, 0x2000
	s_add_u32 s30, s74, 0x20000
	v_lshl_add_u64 v[182:183], s[74:75], 0, v[162:163]
	s_addc_u32 s31, s75, 0
	s_add_i32 s45, s58, s14
	global_load_lds_dwordx4 v[182:183], off
	v_lshl_add_u64 v[184:185], s[30:31], 0, v[164:165]
	s_mov_b32 m0, s45
	v_cndmask_b32_e64 v112, v168, v173, s[40:41]
	global_load_lds_dwordx4 v[184:185], off
	v_lshl_add_u64 v[184:185], s[30:31], 0, v[162:163]
	s_add_i32 m0, s45, 0x2000
	s_nop 0
	global_load_lds_dwordx4 v[184:185], off
	s_mov_b32 m0, s7
	v_lshl_add_u64 v[184:185], s[76:77], 0, v[112:113]
	global_load_lds_dwordx4 v112, s[76:77]
	v_cndmask_b32_e64 v112, v170, v175, s[40:41]
	s_mov_b32 m0, s33
	v_lshl_add_u64 v[186:187], s[76:77], 0, v[112:113]
	global_load_lds_dwordx4 v112, s[76:77]
	s_waitcnt vmcnt(8)
	s_waitcnt lgkmcnt(0)
	s_barrier
	s_setprio 1
	v_mfma_scale_f32_16x16x128_f8f6f4 v[92:95], v[16:23], v[224:231], 0, v200, v201 op_sel_hi:[0,0,0]
	v_mfma_scale_f32_16x16x128_f8f6f4 v[84:87], v[24:31], v[224:231], 0, v200, v201 op_sel_hi:[0,0,0]
	v_mfma_scale_f32_16x16x128_f8f6f4 v[76:79], v[16:23], v[232:239], 0, v200, v201 op_sel_hi:[0,0,0]
	v_mfma_scale_f32_16x16x128_f8f6f4 v[68:71], v[24:31], v[232:239], 0, v200, v201 op_sel_hi:[0,0,0]
	v_mfma_scale_f32_16x16x128_f8f6f4 v[60:63], v[16:23], v[240:247], 0, v200, v201 op_sel_hi:[0,0,0]
	v_mfma_scale_f32_16x16x128_f8f6f4 v[52:55], v[24:31], v[240:247], 0, v200, v201 op_sel_hi:[0,0,0]
	v_mfma_scale_f32_16x16x128_f8f6f4 v[44:47], v[16:23], v[206:213], 0, v200, v201 op_sel_hi:[0,0,0]
	v_mfma_scale_f32_16x16x128_f8f6f4 v[36:39], v[24:31], v[206:213], 0, v200, v201 op_sel_hi:[0,0,0]
	s_setprio 0
	s_setprio 1
	v_mfma_scale_f32_16x16x128_f8f6f4 v[88:91], v[0:7], v[224:231], 0, v200, v201 op_sel_hi:[0,0,0]
	v_mfma_scale_f32_16x16x128_f8f6f4 v[80:83], v[8:15], v[224:231], 0, v200, v201 op_sel_hi:[0,0,0]
	v_mfma_scale_f32_16x16x128_f8f6f4 v[72:75], v[0:7], v[232:239], 0, v200, v201 op_sel_hi:[0,0,0]
	v_mfma_scale_f32_16x16x128_f8f6f4 v[64:67], v[8:15], v[232:239], 0, v200, v201 op_sel_hi:[0,0,0]
	v_mfma_scale_f32_16x16x128_f8f6f4 v[56:59], v[0:7], v[240:247], 0, v200, v201 op_sel_hi:[0,0,0]
	v_mfma_scale_f32_16x16x128_f8f6f4 v[48:51], v[8:15], v[240:247], 0, v200, v201 op_sel_hi:[0,0,0]
	v_mfma_scale_f32_16x16x128_f8f6f4 v[40:43], v[0:7], v[206:213], 0, v200, v201 op_sel_hi:[0,0,0]
	v_mfma_scale_f32_16x16x128_f8f6f4 v[32:35], v[8:15], v[206:213], 0, v200, v201 op_sel_hi:[0,0,0]
	s_setprio 0
	s_barrier
	s_add_i32 s30, 0, 0x18000
	s_add_i32 s45, 0, 0x1c000
	v_add_u32_e32 v12, s30, v193
	v_add_u32_e32 v28, s45, v193
	ds_read_b128 v[0:3], v12
	ds_read_b128 v[4:7], v12 offset:1024
	ds_read_b128 v[8:11], v12 offset:2048
	ds_read_b128 v[12:15], v12 offset:3072
	ds_read_b128 v[16:19], v28
	ds_read_b128 v[20:23], v28 offset:1024
	ds_read_b128 v[24:27], v28 offset:2048
	ds_read_b128 v[28:31], v28 offset:3072
	s_mov_b32 m0, s34
	v_cndmask_b32_e64 v112, v172, v217, s[40:41]
	ds_read_b128 v[206:209], v169 offset:32768
	ds_read_b128 v[210:213], v169 offset:33792
	ds_read_b128 v[224:227], v169 offset:34816
	ds_read_b128 v[228:231], v169 offset:35840
	ds_read_b128 v[232:235], v169 offset:36864
	ds_read_b128 v[236:239], v169 offset:37888
	ds_read_b128 v[240:243], v169 offset:38912
	ds_read_b128 v[244:247], v169 offset:39936
	global_load_lds_dwordx4 v112, s[76:77]
	v_cndmask_b32_e64 v112, v174, v218, s[40:41]
	s_mov_b32 m0, s50
	s_nop 0
	global_load_lds_dwordx4 v112, s[76:77]
	s_waitcnt vmcnt(8)
	s_waitcnt lgkmcnt(0)
	s_barrier
	s_setprio 1
	v_mfma_scale_f32_16x16x128_f8f6f4 v[158:161], v[0:7], v[206:213], v[158:161], v200, v201 op_sel_hi:[0,0,0]
	v_mfma_scale_f32_16x16x128_f8f6f4 v[150:153], v[8:15], v[206:213], v[150:153], v200, v201 op_sel_hi:[0,0,0]
	v_mfma_scale_f32_16x16x128_f8f6f4 v[142:145], v[0:7], v[224:231], v[142:145], v200, v201 op_sel_hi:[0,0,0]
	v_mfma_scale_f32_16x16x128_f8f6f4 v[134:137], v[8:15], v[224:231], v[134:137], v200, v201 op_sel_hi:[0,0,0]
	v_mfma_scale_f32_16x16x128_f8f6f4 v[126:129], v[0:7], v[232:239], v[126:129], v200, v201 op_sel_hi:[0,0,0]
	v_mfma_scale_f32_16x16x128_f8f6f4 v[118:121], v[8:15], v[232:239], v[118:121], v200, v201 op_sel_hi:[0,0,0]
	v_mfma_scale_f32_16x16x128_f8f6f4 v[108:111], v[0:7], v[240:247], v[108:111], v200, v201 op_sel_hi:[0,0,0]
	v_mfma_scale_f32_16x16x128_f8f6f4 v[100:103], v[8:15], v[240:247], v[100:103], v200, v201 op_sel_hi:[0,0,0]
	s_setprio 0
	s_setprio 1
	v_mfma_scale_f32_16x16x128_f8f6f4 v[154:157], v[16:23], v[206:213], v[154:157], v200, v201 op_sel_hi:[0,0,0]
	v_mfma_scale_f32_16x16x128_f8f6f4 v[146:149], v[24:31], v[206:213], v[146:149], v200, v201 op_sel_hi:[0,0,0]
	v_mfma_scale_f32_16x16x128_f8f6f4 v[138:141], v[16:23], v[224:231], v[138:141], v200, v201 op_sel_hi:[0,0,0]
	v_mfma_scale_f32_16x16x128_f8f6f4 v[130:133], v[24:31], v[224:231], v[130:133], v200, v201 op_sel_hi:[0,0,0]
	v_mfma_scale_f32_16x16x128_f8f6f4 v[122:125], v[16:23], v[232:239], v[122:125], v200, v201 op_sel_hi:[0,0,0]
	v_mfma_scale_f32_16x16x128_f8f6f4 v[114:117], v[24:31], v[232:239], v[114:117], v200, v201 op_sel_hi:[0,0,0]
	v_mfma_scale_f32_16x16x128_f8f6f4 v[104:107], v[16:23], v[240:247], v[104:107], v200, v201 op_sel_hi:[0,0,0]
	v_mfma_scale_f32_16x16x128_f8f6f4 v[96:99], v[24:31], v[240:247], v[96:99], v200, v201 op_sel_hi:[0,0,0]
	s_setprio 0
	s_barrier
	s_add_i32 s30, s30, s14
	v_lshl_add_u64 v[180:181], v[180:181], 0, s[56:57]
	s_mov_b32 m0, s30
	ds_read_b128 v[206:209], v169 offset:49152
	ds_read_b128 v[210:213], v169 offset:50176
	ds_read_b128 v[224:227], v169 offset:51200
	ds_read_b128 v[228:231], v169 offset:52224
	ds_read_b128 v[232:235], v169 offset:53248
	ds_read_b128 v[236:239], v169 offset:54272
	ds_read_b128 v[240:243], v169 offset:55296
	ds_read_b128 v[244:247], v169 offset:56320
	global_load_lds_dwordx4 v[180:181], off
	s_add_i32 m0, s30, 0x2000
	s_add_u32 s30, s74, 0x20080
	v_lshl_add_u64 v[180:181], v[182:183], 0, s[56:57]
	s_addc_u32 s31, s75, 0
	s_add_i32 s40, s45, s14
	global_load_lds_dwordx4 v[180:181], off
	v_lshl_add_u64 v[180:181], s[30:31], 0, v[164:165]
	s_mov_b32 m0, s40
	s_nop 0
	global_load_lds_dwordx4 v[180:181], off
	v_lshl_add_u64 v[180:181], s[30:31], 0, v[162:163]
	s_add_i32 m0, s40, 0x2000
	s_nop 0
	global_load_lds_dwordx4 v[180:181], off
	v_lshl_add_u64 v[180:181], v[184:185], 0, s[56:57]
	s_mov_b32 m0, s4
	s_nop 0
	global_load_lds_dwordx4 v[180:181], off
	v_lshl_add_u64 v[180:181], v[186:187], 0, s[56:57]
	s_mov_b32 m0, s51
	s_nop 0
	global_load_lds_dwordx4 v[180:181], off
	s_waitcnt vmcnt(8)
	s_waitcnt lgkmcnt(0)
	s_barrier
	s_setprio 1
	v_mfma_scale_f32_16x16x128_f8f6f4 v[92:95], v[0:7], v[206:213], v[92:95], v200, v201 op_sel_hi:[0,0,0]
	v_mfma_scale_f32_16x16x128_f8f6f4 v[84:87], v[8:15], v[206:213], v[84:87], v200, v201 op_sel_hi:[0,0,0]
	v_mfma_scale_f32_16x16x128_f8f6f4 v[76:79], v[0:7], v[224:231], v[76:79], v200, v201 op_sel_hi:[0,0,0]
	v_mfma_scale_f32_16x16x128_f8f6f4 v[68:71], v[8:15], v[224:231], v[68:71], v200, v201 op_sel_hi:[0,0,0]
	v_mfma_scale_f32_16x16x128_f8f6f4 v[60:63], v[0:7], v[232:239], v[60:63], v200, v201 op_sel_hi:[0,0,0]
	v_mfma_scale_f32_16x16x128_f8f6f4 v[52:55], v[8:15], v[232:239], v[52:55], v200, v201 op_sel_hi:[0,0,0]
	v_mfma_scale_f32_16x16x128_f8f6f4 v[44:47], v[0:7], v[240:247], v[44:47], v200, v201 op_sel_hi:[0,0,0]
	v_mfma_scale_f32_16x16x128_f8f6f4 v[36:39], v[8:15], v[240:247], v[36:39], v200, v201 op_sel_hi:[0,0,0]
	s_setprio 0
	s_setprio 1
	v_mfma_scale_f32_16x16x128_f8f6f4 v[88:91], v[16:23], v[206:213], v[88:91], v200, v201 op_sel_hi:[0,0,0]
	v_mfma_scale_f32_16x16x128_f8f6f4 v[80:83], v[24:31], v[206:213], v[80:83], v200, v201 op_sel_hi:[0,0,0]
	v_mfma_scale_f32_16x16x128_f8f6f4 v[72:75], v[16:23], v[224:231], v[72:75], v200, v201 op_sel_hi:[0,0,0]
	v_mfma_scale_f32_16x16x128_f8f6f4 v[64:67], v[24:31], v[224:231], v[64:67], v200, v201 op_sel_hi:[0,0,0]
	v_mfma_scale_f32_16x16x128_f8f6f4 v[56:59], v[16:23], v[232:239], v[56:59], v200, v201 op_sel_hi:[0,0,0]
	v_mfma_scale_f32_16x16x128_f8f6f4 v[48:51], v[24:31], v[232:239], v[48:51], v200, v201 op_sel_hi:[0,0,0]
	v_mfma_scale_f32_16x16x128_f8f6f4 v[40:43], v[16:23], v[240:247], v[40:43], v200, v201 op_sel_hi:[0,0,0]
	v_mfma_scale_f32_16x16x128_f8f6f4 v[32:35], v[24:31], v[240:247], v[32:35], v200, v201 op_sel_hi:[0,0,0]
	s_setprio 0
	s_barrier
	s_add_i32 s49, s49, 2
	s_add_u32 s72, s72, 0x100
	s_addc_u32 s73, s73, 0
	s_cmp_gt_u32 s49, 5
	s_cbranch_scc1 .LBB0_1092
	s_branch .LBB0_1090
.LBB0_1089:
	s_add_u32 s30, s94, s72
	s_addc_u32 s31, s95, s73
	s_add_u32 s45, s30, 0x28dd9100
	s_addc_u32 s55, s31, 0
	s_and_b64 s[30:31], s[40:41], exec
	s_cselect_b32 s77, s91, s55
	s_cselect_b32 s76, s90, s45
	s_add_u32 s45, s37, s72
	s_addc_u32 s55, s47, s73
	s_and_b64 s[30:31], s[40:41], exec
	s_cselect_b32 s75, s65, s55
	s_cselect_b32 s74, s64, s45
	s_add_i32 s55, 0, 0x10000
	s_add_i32 s58, 0, 0x14000
	v_add_u32_e32 v0, s55, v193
	v_add_u32_e32 v12, s58, v193
	ds_read_b128 v[16:19], v0
	ds_read_b128 v[20:23], v0 offset:1024
	ds_read_b128 v[24:27], v0 offset:2048
	ds_read_b128 v[28:31], v0 offset:3072
	ds_read_b128 v[0:3], v12
	ds_read_b128 v[4:7], v12 offset:1024
	ds_read_b128 v[8:11], v12 offset:2048
	ds_read_b128 v[12:15], v12 offset:3072
	v_lshl_add_u64 v[206:207], v[178:179], 0, s[72:73]
	s_add_i32 m0, s7, 0xc000
	ds_read_b128 v[180:183], v169
	ds_read_b128 v[184:187], v169 offset:1024
	ds_read_b128 v[224:227], v169 offset:2048
	ds_read_b128 v[228:231], v169 offset:3072
	ds_read_b128 v[232:235], v169 offset:4096
	ds_read_b128 v[236:239], v169 offset:5120
	ds_read_b128 v[240:243], v169 offset:6144
	ds_read_b128 v[244:247], v169 offset:7168
	global_load_lds_dwordx4 v[206:207], off
	v_lshl_add_u64 v[206:207], v[176:177], 0, s[72:73]
	s_add_i32 m0, s7, 0xe000
	s_nop 0
	global_load_lds_dwordx4 v[206:207], off
	s_waitcnt vmcnt(8)
	s_waitcnt lgkmcnt(0)
	s_barrier
	s_setprio 1
	v_mfma_scale_f32_16x16x128_f8f6f4 v[158:161], v[16:23], v[180:187], v[158:161], v200, v201 op_sel_hi:[0,0,0]
	v_mfma_scale_f32_16x16x128_f8f6f4 v[150:153], v[24:31], v[180:187], v[150:153], v200, v201 op_sel_hi:[0,0,0]
	v_mfma_scale_f32_16x16x128_f8f6f4 v[142:145], v[16:23], v[224:231], v[142:145], v200, v201 op_sel_hi:[0,0,0]
	v_mfma_scale_f32_16x16x128_f8f6f4 v[134:137], v[24:31], v[224:231], v[134:137], v200, v201 op_sel_hi:[0,0,0]
	v_mfma_scale_f32_16x16x128_f8f6f4 v[126:129], v[16:23], v[232:239], v[126:129], v200, v201 op_sel_hi:[0,0,0]
	v_mfma_scale_f32_16x16x128_f8f6f4 v[118:121], v[24:31], v[232:239], v[118:121], v200, v201 op_sel_hi:[0,0,0]
	v_mfma_scale_f32_16x16x128_f8f6f4 v[108:111], v[16:23], v[240:247], v[108:111], v200, v201 op_sel_hi:[0,0,0]
	v_mfma_scale_f32_16x16x128_f8f6f4 v[100:103], v[24:31], v[240:247], v[100:103], v200, v201 op_sel_hi:[0,0,0]
	s_setprio 0
	s_setprio 1
	v_mfma_scale_f32_16x16x128_f8f6f4 v[154:157], v[0:7], v[180:187], v[154:157], v200, v201 op_sel_hi:[0,0,0]
	v_mfma_scale_f32_16x16x128_f8f6f4 v[146:149], v[8:15], v[180:187], v[146:149], v200, v201 op_sel_hi:[0,0,0]
	v_mfma_scale_f32_16x16x128_f8f6f4 v[138:141], v[0:7], v[224:231], v[138:141], v200, v201 op_sel_hi:[0,0,0]
	v_mfma_scale_f32_16x16x128_f8f6f4 v[130:133], v[8:15], v[224:231], v[130:133], v200, v201 op_sel_hi:[0,0,0]
	v_mfma_scale_f32_16x16x128_f8f6f4 v[122:125], v[0:7], v[232:239], v[122:125], v200, v201 op_sel_hi:[0,0,0]
	v_mfma_scale_f32_16x16x128_f8f6f4 v[114:117], v[8:15], v[232:239], v[114:117], v200, v201 op_sel_hi:[0,0,0]
	v_mfma_scale_f32_16x16x128_f8f6f4 v[104:107], v[0:7], v[240:247], v[104:107], v200, v201 op_sel_hi:[0,0,0]
	v_mfma_scale_f32_16x16x128_f8f6f4 v[96:99], v[8:15], v[240:247], v[96:99], v200, v201 op_sel_hi:[0,0,0]
	s_setprio 0
	s_barrier
	s_add_i32 s30, s55, s14
	v_lshl_add_u64 v[180:181], s[74:75], 0, v[164:165]
	s_mov_b32 m0, s30
	ds_read_b128 v[224:227], v169 offset:16384
	ds_read_b128 v[228:231], v169 offset:17408
	ds_read_b128 v[232:235], v169 offset:18432
	ds_read_b128 v[236:239], v169 offset:19456
	ds_read_b128 v[240:243], v169 offset:20480
	ds_read_b128 v[244:247], v169 offset:21504
	ds_read_b128 v[206:209], v169 offset:22528
	ds_read_b128 v[210:213], v169 offset:23552
	global_load_lds_dwordx4 v[180:181], off
	s_add_i32 m0, s30, 0x2000
	s_add_u32 s30, s74, 0x20000
	v_lshl_add_u64 v[182:183], s[74:75], 0, v[162:163]
	s_addc_u32 s31, s75, 0
	s_add_i32 s45, s58, s14
	global_load_lds_dwordx4 v[182:183], off
	v_lshl_add_u64 v[184:185], s[30:31], 0, v[164:165]
	s_mov_b32 m0, s45
	v_cndmask_b32_e64 v112, v168, v173, s[40:41]
	global_load_lds_dwordx4 v[184:185], off
	v_lshl_add_u64 v[184:185], s[30:31], 0, v[162:163]
	s_add_i32 m0, s45, 0x2000
	s_nop 0
	global_load_lds_dwordx4 v[184:185], off
	s_mov_b32 m0, s7
	v_lshl_add_u64 v[184:185], s[76:77], 0, v[112:113]
	global_load_lds_dwordx4 v112, s[76:77]
	v_cndmask_b32_e64 v112, v170, v175, s[40:41]
	s_mov_b32 m0, s33
	v_lshl_add_u64 v[186:187], s[76:77], 0, v[112:113]
	global_load_lds_dwordx4 v112, s[76:77]
	s_waitcnt vmcnt(8)
	s_waitcnt lgkmcnt(0)
	s_barrier
	s_setprio 1
	v_mfma_scale_f32_16x16x128_f8f6f4 v[92:95], v[16:23], v[224:231], v[92:95], v200, v201 op_sel_hi:[0,0,0]
	v_mfma_scale_f32_16x16x128_f8f6f4 v[84:87], v[24:31], v[224:231], v[84:87], v200, v201 op_sel_hi:[0,0,0]
	v_mfma_scale_f32_16x16x128_f8f6f4 v[76:79], v[16:23], v[232:239], v[76:79], v200, v201 op_sel_hi:[0,0,0]
	v_mfma_scale_f32_16x16x128_f8f6f4 v[68:71], v[24:31], v[232:239], v[68:71], v200, v201 op_sel_hi:[0,0,0]
	v_mfma_scale_f32_16x16x128_f8f6f4 v[60:63], v[16:23], v[240:247], v[60:63], v200, v201 op_sel_hi:[0,0,0]
	v_mfma_scale_f32_16x16x128_f8f6f4 v[52:55], v[24:31], v[240:247], v[52:55], v200, v201 op_sel_hi:[0,0,0]
	v_mfma_scale_f32_16x16x128_f8f6f4 v[44:47], v[16:23], v[206:213], v[44:47], v200, v201 op_sel_hi:[0,0,0]
	v_mfma_scale_f32_16x16x128_f8f6f4 v[36:39], v[24:31], v[206:213], v[36:39], v200, v201 op_sel_hi:[0,0,0]
	s_setprio 0
	s_setprio 1
	v_mfma_scale_f32_16x16x128_f8f6f4 v[88:91], v[0:7], v[224:231], v[88:91], v200, v201 op_sel_hi:[0,0,0]
	v_mfma_scale_f32_16x16x128_f8f6f4 v[80:83], v[8:15], v[224:231], v[80:83], v200, v201 op_sel_hi:[0,0,0]
	v_mfma_scale_f32_16x16x128_f8f6f4 v[72:75], v[0:7], v[232:239], v[72:75], v200, v201 op_sel_hi:[0,0,0]
	v_mfma_scale_f32_16x16x128_f8f6f4 v[64:67], v[8:15], v[232:239], v[64:67], v200, v201 op_sel_hi:[0,0,0]
	v_mfma_scale_f32_16x16x128_f8f6f4 v[56:59], v[0:7], v[240:247], v[56:59], v200, v201 op_sel_hi:[0,0,0]
	v_mfma_scale_f32_16x16x128_f8f6f4 v[48:51], v[8:15], v[240:247], v[48:51], v200, v201 op_sel_hi:[0,0,0]
	v_mfma_scale_f32_16x16x128_f8f6f4 v[40:43], v[0:7], v[206:213], v[40:43], v200, v201 op_sel_hi:[0,0,0]
	v_mfma_scale_f32_16x16x128_f8f6f4 v[32:35], v[8:15], v[206:213], v[32:35], v200, v201 op_sel_hi:[0,0,0]
	s_setprio 0
	s_barrier
	s_add_i32 s30, 0, 0x18000
	s_add_i32 s45, 0, 0x1c000
	v_add_u32_e32 v12, s30, v193
	v_add_u32_e32 v28, s45, v193
	ds_read_b128 v[0:3], v12
	ds_read_b128 v[4:7], v12 offset:1024
	ds_read_b128 v[8:11], v12 offset:2048
	ds_read_b128 v[12:15], v12 offset:3072
	ds_read_b128 v[16:19], v28
	ds_read_b128 v[20:23], v28 offset:1024
	ds_read_b128 v[24:27], v28 offset:2048
	ds_read_b128 v[28:31], v28 offset:3072
	s_mov_b32 m0, s34
	v_cndmask_b32_e64 v112, v172, v217, s[40:41]
	ds_read_b128 v[206:209], v169 offset:32768
	ds_read_b128 v[210:213], v169 offset:33792
	ds_read_b128 v[224:227], v169 offset:34816
	ds_read_b128 v[228:231], v169 offset:35840
	ds_read_b128 v[232:235], v169 offset:36864
	ds_read_b128 v[236:239], v169 offset:37888
	ds_read_b128 v[240:243], v169 offset:38912
	ds_read_b128 v[244:247], v169 offset:39936
	global_load_lds_dwordx4 v112, s[76:77]
	v_cndmask_b32_e64 v112, v174, v218, s[40:41]
	s_mov_b32 m0, s50
	s_nop 0
	global_load_lds_dwordx4 v112, s[76:77]
	s_waitcnt vmcnt(8)
	s_waitcnt lgkmcnt(0)
	s_barrier
	s_setprio 1
	v_mfma_scale_f32_16x16x128_f8f6f4 v[158:161], v[0:7], v[206:213], v[158:161], v200, v201 op_sel_hi:[0,0,0]
	v_mfma_scale_f32_16x16x128_f8f6f4 v[150:153], v[8:15], v[206:213], v[150:153], v200, v201 op_sel_hi:[0,0,0]
	v_mfma_scale_f32_16x16x128_f8f6f4 v[142:145], v[0:7], v[224:231], v[142:145], v200, v201 op_sel_hi:[0,0,0]
	v_mfma_scale_f32_16x16x128_f8f6f4 v[134:137], v[8:15], v[224:231], v[134:137], v200, v201 op_sel_hi:[0,0,0]
	v_mfma_scale_f32_16x16x128_f8f6f4 v[126:129], v[0:7], v[232:239], v[126:129], v200, v201 op_sel_hi:[0,0,0]
	v_mfma_scale_f32_16x16x128_f8f6f4 v[118:121], v[8:15], v[232:239], v[118:121], v200, v201 op_sel_hi:[0,0,0]
	v_mfma_scale_f32_16x16x128_f8f6f4 v[108:111], v[0:7], v[240:247], v[108:111], v200, v201 op_sel_hi:[0,0,0]
	v_mfma_scale_f32_16x16x128_f8f6f4 v[100:103], v[8:15], v[240:247], v[100:103], v200, v201 op_sel_hi:[0,0,0]
	s_setprio 0
	s_setprio 1
	v_mfma_scale_f32_16x16x128_f8f6f4 v[154:157], v[16:23], v[206:213], v[154:157], v200, v201 op_sel_hi:[0,0,0]
	v_mfma_scale_f32_16x16x128_f8f6f4 v[146:149], v[24:31], v[206:213], v[146:149], v200, v201 op_sel_hi:[0,0,0]
	v_mfma_scale_f32_16x16x128_f8f6f4 v[138:141], v[16:23], v[224:231], v[138:141], v200, v201 op_sel_hi:[0,0,0]
	v_mfma_scale_f32_16x16x128_f8f6f4 v[130:133], v[24:31], v[224:231], v[130:133], v200, v201 op_sel_hi:[0,0,0]
	v_mfma_scale_f32_16x16x128_f8f6f4 v[122:125], v[16:23], v[232:239], v[122:125], v200, v201 op_sel_hi:[0,0,0]
	v_mfma_scale_f32_16x16x128_f8f6f4 v[114:117], v[24:31], v[232:239], v[114:117], v200, v201 op_sel_hi:[0,0,0]
	v_mfma_scale_f32_16x16x128_f8f6f4 v[104:107], v[16:23], v[240:247], v[104:107], v200, v201 op_sel_hi:[0,0,0]
	v_mfma_scale_f32_16x16x128_f8f6f4 v[96:99], v[24:31], v[240:247], v[96:99], v200, v201 op_sel_hi:[0,0,0]
	s_setprio 0
	s_barrier
	s_add_i32 s30, s30, s14
	v_lshl_add_u64 v[180:181], v[180:181], 0, s[56:57]
	s_mov_b32 m0, s30
	ds_read_b128 v[206:209], v169 offset:49152
	ds_read_b128 v[210:213], v169 offset:50176
	ds_read_b128 v[224:227], v169 offset:51200
	ds_read_b128 v[228:231], v169 offset:52224
	ds_read_b128 v[232:235], v169 offset:53248
	ds_read_b128 v[236:239], v169 offset:54272
	ds_read_b128 v[240:243], v169 offset:55296
	ds_read_b128 v[244:247], v169 offset:56320
	global_load_lds_dwordx4 v[180:181], off
	s_add_i32 m0, s30, 0x2000
	s_add_u32 s30, s74, 0x20080
	v_lshl_add_u64 v[180:181], v[182:183], 0, s[56:57]
	s_addc_u32 s31, s75, 0
	s_add_i32 s40, s45, s14
	global_load_lds_dwordx4 v[180:181], off
	v_lshl_add_u64 v[180:181], s[30:31], 0, v[164:165]
	s_mov_b32 m0, s40
	s_nop 0
	global_load_lds_dwordx4 v[180:181], off
	v_lshl_add_u64 v[180:181], s[30:31], 0, v[162:163]
	s_add_i32 m0, s40, 0x2000
	s_nop 0
	global_load_lds_dwordx4 v[180:181], off
	v_lshl_add_u64 v[180:181], v[184:185], 0, s[56:57]
	s_mov_b32 m0, s4
	s_nop 0
	global_load_lds_dwordx4 v[180:181], off
	v_lshl_add_u64 v[180:181], v[186:187], 0, s[56:57]
	s_mov_b32 m0, s51
	s_nop 0
	global_load_lds_dwordx4 v[180:181], off
	s_waitcnt vmcnt(8)
	s_waitcnt lgkmcnt(0)
	s_barrier
	s_setprio 1
	v_mfma_scale_f32_16x16x128_f8f6f4 v[92:95], v[0:7], v[206:213], v[92:95], v200, v201 op_sel_hi:[0,0,0]
	v_mfma_scale_f32_16x16x128_f8f6f4 v[84:87], v[8:15], v[206:213], v[84:87], v200, v201 op_sel_hi:[0,0,0]
	v_mfma_scale_f32_16x16x128_f8f6f4 v[76:79], v[0:7], v[224:231], v[76:79], v200, v201 op_sel_hi:[0,0,0]
	v_mfma_scale_f32_16x16x128_f8f6f4 v[68:71], v[8:15], v[224:231], v[68:71], v200, v201 op_sel_hi:[0,0,0]
	v_mfma_scale_f32_16x16x128_f8f6f4 v[60:63], v[0:7], v[232:239], v[60:63], v200, v201 op_sel_hi:[0,0,0]
	v_mfma_scale_f32_16x16x128_f8f6f4 v[52:55], v[8:15], v[232:239], v[52:55], v200, v201 op_sel_hi:[0,0,0]
	v_mfma_scale_f32_16x16x128_f8f6f4 v[44:47], v[0:7], v[240:247], v[44:47], v200, v201 op_sel_hi:[0,0,0]
	v_mfma_scale_f32_16x16x128_f8f6f4 v[36:39], v[8:15], v[240:247], v[36:39], v200, v201 op_sel_hi:[0,0,0]
	s_setprio 0
	s_setprio 1
	v_mfma_scale_f32_16x16x128_f8f6f4 v[88:91], v[16:23], v[206:213], v[88:91], v200, v201 op_sel_hi:[0,0,0]
	v_mfma_scale_f32_16x16x128_f8f6f4 v[80:83], v[24:31], v[206:213], v[80:83], v200, v201 op_sel_hi:[0,0,0]
	v_mfma_scale_f32_16x16x128_f8f6f4 v[72:75], v[16:23], v[224:231], v[72:75], v200, v201 op_sel_hi:[0,0,0]
	v_mfma_scale_f32_16x16x128_f8f6f4 v[64:67], v[24:31], v[224:231], v[64:67], v200, v201 op_sel_hi:[0,0,0]
	v_mfma_scale_f32_16x16x128_f8f6f4 v[56:59], v[16:23], v[232:239], v[56:59], v200, v201 op_sel_hi:[0,0,0]
	v_mfma_scale_f32_16x16x128_f8f6f4 v[48:51], v[24:31], v[232:239], v[48:51], v200, v201 op_sel_hi:[0,0,0]
	v_mfma_scale_f32_16x16x128_f8f6f4 v[40:43], v[16:23], v[240:247], v[40:43], v200, v201 op_sel_hi:[0,0,0]
	v_mfma_scale_f32_16x16x128_f8f6f4 v[32:35], v[24:31], v[240:247], v[32:35], v200, v201 op_sel_hi:[0,0,0]
	s_setprio 0
	s_barrier
	s_add_i32 s49, s49, 2
	s_add_u32 s72, s72, 0x100
	s_addc_u32 s73, s73, 0
	s_cmp_gt_u32 s49, 5
	s_cbranch_scc1 .LBB0_1092

.Lpeel_down:
	s_add_u32 s30, s72, 0xfffe0080
	s_addc_u32 s31, s73, -1
	s_add_i32 s51, 0, 0x10000
	s_cmp_eq_u32 s50, 4
	s_cselect_b32 s77, s27, s31
	s_cselect_b32 s76, s37, s30
	s_cselect_b32 s75, s65, s49
	s_cselect_b32 s74, s64, s47
	s_add_i32 s58, 0, 0x14000
	v_add_u32_e32 v0, s51, v183
	v_add_u32_e32 v12, s58, v183
	ds_read_b128 v[16:19], v0
	ds_read_b128 v[20:23], v0 offset:1024
	ds_read_b128 v[24:27], v0 offset:2048
	ds_read_b128 v[28:31], v0 offset:3072
	ds_read_b128 v[0:3], v12
	ds_read_b128 v[4:7], v12 offset:1024
	ds_read_b128 v[8:11], v12 offset:2048
	ds_read_b128 v[12:15], v12 offset:3072
	v_lshl_add_u64 v[194:195], s[72:73], 0, v[168:169]
	s_add_i32 m0, s7, 0xc000
	ds_read_b128 v[174:177], v184
	ds_read_b128 v[178:181], v184 offset:1024
	ds_read_b128 v[186:189], v184 offset:2048
	ds_read_b128 v[190:193], v184 offset:3072
	ds_read_b128 v[206:209], v184 offset:4096
	ds_read_b128 v[210:213], v184 offset:5120
	ds_read_b128 v[216:219], v184 offset:6144
	ds_read_b128 v[220:223], v184 offset:7168
	global_load_lds_dwordx4 v[194:195], off
	v_lshl_add_u64 v[194:195], s[72:73], 0, v[170:171]
	s_add_i32 m0, s7, 0xe000
	s_nop 0
	global_load_lds_dwordx4 v[194:195], off
	s_waitcnt vmcnt(8)
	s_waitcnt lgkmcnt(0)
	s_barrier
	s_setprio 1
	v_mfma_scale_f32_16x16x128_f8f6f4 v[158:161], v[16:23], v[174:181], 0, v200, v201 op_sel_hi:[0,0,0]
	v_mfma_scale_f32_16x16x128_f8f6f4 v[154:157], v[24:31], v[174:181], 0, v200, v201 op_sel_hi:[0,0,0]
	v_mfma_scale_f32_16x16x128_f8f6f4 v[142:145], v[16:23], v[186:193], 0, v200, v201 op_sel_hi:[0,0,0]
	v_mfma_scale_f32_16x16x128_f8f6f4 v[138:141], v[24:31], v[186:193], 0, v200, v201 op_sel_hi:[0,0,0]
	v_mfma_scale_f32_16x16x128_f8f6f4 v[126:129], v[16:23], v[206:213], 0, v200, v201 op_sel_hi:[0,0,0]
	v_mfma_scale_f32_16x16x128_f8f6f4 v[122:125], v[24:31], v[206:213], 0, v200, v201 op_sel_hi:[0,0,0]
	v_mfma_scale_f32_16x16x128_f8f6f4 v[108:111], v[16:23], v[216:223], 0, v200, v201 op_sel_hi:[0,0,0]
	v_mfma_scale_f32_16x16x128_f8f6f4 v[104:107], v[24:31], v[216:223], 0, v200, v201 op_sel_hi:[0,0,0]
	s_setprio 0
	s_setprio 1
	v_mfma_scale_f32_16x16x128_f8f6f4 v[150:153], v[0:7], v[174:181], 0, v200, v201 op_sel_hi:[0,0,0]
	v_mfma_scale_f32_16x16x128_f8f6f4 v[146:149], v[8:15], v[174:181], 0, v200, v201 op_sel_hi:[0,0,0]
	v_mfma_scale_f32_16x16x128_f8f6f4 v[134:137], v[0:7], v[186:193], 0, v200, v201 op_sel_hi:[0,0,0]
	v_mfma_scale_f32_16x16x128_f8f6f4 v[130:133], v[8:15], v[186:193], 0, v200, v201 op_sel_hi:[0,0,0]
	v_mfma_scale_f32_16x16x128_f8f6f4 v[118:121], v[0:7], v[206:213], 0, v200, v201 op_sel_hi:[0,0,0]
	v_mfma_scale_f32_16x16x128_f8f6f4 v[114:117], v[8:15], v[206:213], 0, v200, v201 op_sel_hi:[0,0,0]
	v_mfma_scale_f32_16x16x128_f8f6f4 v[100:103], v[0:7], v[216:223], 0, v200, v201 op_sel_hi:[0,0,0]
	v_mfma_scale_f32_16x16x128_f8f6f4 v[96:99], v[8:15], v[216:223], 0, v200, v201 op_sel_hi:[0,0,0]
	s_setprio 0
	s_barrier
	s_add_i32 s30, s51, s14
	v_lshl_add_u64 v[174:175], s[74:75], 0, v[112:113]
	s_mov_b32 m0, s30
	ds_read_b128 v[186:189], v184 offset:16384
	ds_read_b128 v[190:193], v184 offset:17408
	ds_read_b128 v[206:209], v184 offset:18432
	ds_read_b128 v[210:213], v184 offset:19456
	ds_read_b128 v[216:219], v184 offset:20480
	ds_read_b128 v[220:223], v184 offset:21504
	ds_read_b128 v[224:227], v184 offset:22528
	ds_read_b128 v[228:231], v184 offset:23552
	global_load_lds_dwordx4 v[174:175], off
	s_add_i32 m0, s30, 0x2000
	s_add_u32 s30, s74, 0x20000
	v_lshl_add_u64 v[176:177], s[74:75], 0, v[162:163]
	s_addc_u32 s31, s75, 0
	s_add_i32 s45, s58, s14
	global_load_lds_dwordx4 v[176:177], off
	v_lshl_add_u64 v[178:179], s[30:31], 0, v[112:113]
	s_mov_b32 m0, s45
	v_lshl_add_u64 v[180:181], s[76:77], 0, v[164:165]
	global_load_lds_dwordx4 v[178:179], off
	v_lshl_add_u64 v[178:179], s[30:31], 0, v[162:163]
	s_add_i32 m0, s45, 0x2000
	s_nop 0
	global_load_lds_dwordx4 v[178:179], off
	v_lshl_add_u64 v[178:179], s[76:77], 0, v[166:167]
	s_mov_b32 m0, s7
	s_nop 0
	global_load_lds_dwordx4 v[178:179], off
	s_mov_b32 m0, s25
	s_nop 0
	global_load_lds_dwordx4 v[180:181], off
	s_waitcnt vmcnt(8)
	s_waitcnt lgkmcnt(0)
	s_barrier
	s_setprio 1
	v_mfma_scale_f32_16x16x128_f8f6f4 v[92:95], v[16:23], v[186:193], 0, v200, v201 op_sel_hi:[0,0,0]
	v_mfma_scale_f32_16x16x128_f8f6f4 v[88:91], v[24:31], v[186:193], 0, v200, v201 op_sel_hi:[0,0,0]
	v_mfma_scale_f32_16x16x128_f8f6f4 v[76:79], v[16:23], v[206:213], 0, v200, v201 op_sel_hi:[0,0,0]
	v_mfma_scale_f32_16x16x128_f8f6f4 v[72:75], v[24:31], v[206:213], 0, v200, v201 op_sel_hi:[0,0,0]
	v_mfma_scale_f32_16x16x128_f8f6f4 v[60:63], v[16:23], v[216:223], 0, v200, v201 op_sel_hi:[0,0,0]
	v_mfma_scale_f32_16x16x128_f8f6f4 v[56:59], v[24:31], v[216:223], 0, v200, v201 op_sel_hi:[0,0,0]
	v_mfma_scale_f32_16x16x128_f8f6f4 v[44:47], v[16:23], v[224:231], 0, v200, v201 op_sel_hi:[0,0,0]
	v_mfma_scale_f32_16x16x128_f8f6f4 v[40:43], v[24:31], v[224:231], 0, v200, v201 op_sel_hi:[0,0,0]
	s_setprio 0
	s_setprio 1
	v_mfma_scale_f32_16x16x128_f8f6f4 v[84:87], v[0:7], v[186:193], 0, v200, v201 op_sel_hi:[0,0,0]
	v_mfma_scale_f32_16x16x128_f8f6f4 v[80:83], v[8:15], v[186:193], 0, v200, v201 op_sel_hi:[0,0,0]
	v_mfma_scale_f32_16x16x128_f8f6f4 v[68:71], v[0:7], v[206:213], 0, v200, v201 op_sel_hi:[0,0,0]
	v_mfma_scale_f32_16x16x128_f8f6f4 v[64:67], v[8:15], v[206:213], 0, v200, v201 op_sel_hi:[0,0,0]
	v_mfma_scale_f32_16x16x128_f8f6f4 v[52:55], v[0:7], v[216:223], 0, v200, v201 op_sel_hi:[0,0,0]
	v_mfma_scale_f32_16x16x128_f8f6f4 v[48:51], v[8:15], v[216:223], 0, v200, v201 op_sel_hi:[0,0,0]
	v_mfma_scale_f32_16x16x128_f8f6f4 v[36:39], v[0:7], v[224:231], 0, v200, v201 op_sel_hi:[0,0,0]
	v_mfma_scale_f32_16x16x128_f8f6f4 v[32:35], v[8:15], v[224:231], 0, v200, v201 op_sel_hi:[0,0,0]
	s_setprio 0
	s_barrier
	s_add_i32 s45, 0, 0x18000
	s_add_i32 s51, 0, 0x1c000
	v_add_u32_e32 v12, s45, v183
	v_add_u32_e32 v28, s51, v183
	ds_read_b128 v[0:3], v12
	ds_read_b128 v[4:7], v12 offset:1024
	ds_read_b128 v[8:11], v12 offset:2048
	ds_read_b128 v[12:15], v12 offset:3072
	ds_read_b128 v[16:19], v28
	ds_read_b128 v[20:23], v28 offset:1024
	ds_read_b128 v[24:27], v28 offset:2048
	ds_read_b128 v[28:31], v28 offset:3072
	s_add_u32 s30, s76, 0x20000
	s_addc_u32 s31, s77, 0
	s_mov_b32 m0, s33
	v_lshl_add_u64 v[194:195], s[30:31], 0, v[166:167]
	ds_read_b128 v[186:189], v184 offset:32768
	ds_read_b128 v[190:193], v184 offset:33792
	ds_read_b128 v[206:209], v184 offset:34816
	ds_read_b128 v[210:213], v184 offset:35840
	ds_read_b128 v[216:219], v184 offset:36864
	ds_read_b128 v[220:223], v184 offset:37888
	ds_read_b128 v[224:227], v184 offset:38912
	ds_read_b128 v[228:231], v184 offset:39936
	global_load_lds_dwordx4 v[194:195], off
	v_lshl_add_u64 v[194:195], s[30:31], 0, v[164:165]
	s_mov_b32 m0, s34
	s_nop 0
	global_load_lds_dwordx4 v[194:195], off
	s_waitcnt vmcnt(8)
	s_waitcnt lgkmcnt(0)
	s_barrier
	s_setprio 1
	v_mfma_scale_f32_16x16x128_f8f6f4 v[158:161], v[0:7], v[186:193], v[158:161], v200, v201 op_sel_hi:[0,0,0]
	v_mfma_scale_f32_16x16x128_f8f6f4 v[154:157], v[8:15], v[186:193], v[154:157], v200, v201 op_sel_hi:[0,0,0]
	v_mfma_scale_f32_16x16x128_f8f6f4 v[142:145], v[0:7], v[206:213], v[142:145], v200, v201 op_sel_hi:[0,0,0]
	v_mfma_scale_f32_16x16x128_f8f6f4 v[138:141], v[8:15], v[206:213], v[138:141], v200, v201 op_sel_hi:[0,0,0]
	v_mfma_scale_f32_16x16x128_f8f6f4 v[126:129], v[0:7], v[216:223], v[126:129], v200, v201 op_sel_hi:[0,0,0]
	v_mfma_scale_f32_16x16x128_f8f6f4 v[122:125], v[8:15], v[216:223], v[122:125], v200, v201 op_sel_hi:[0,0,0]
	v_mfma_scale_f32_16x16x128_f8f6f4 v[108:111], v[0:7], v[224:231], v[108:111], v200, v201 op_sel_hi:[0,0,0]
	v_mfma_scale_f32_16x16x128_f8f6f4 v[104:107], v[8:15], v[224:231], v[104:107], v200, v201 op_sel_hi:[0,0,0]
	s_setprio 0
	s_setprio 1
	v_mfma_scale_f32_16x16x128_f8f6f4 v[150:153], v[16:23], v[186:193], v[150:153], v200, v201 op_sel_hi:[0,0,0]
	v_mfma_scale_f32_16x16x128_f8f6f4 v[146:149], v[24:31], v[186:193], v[146:149], v200, v201 op_sel_hi:[0,0,0]
	v_mfma_scale_f32_16x16x128_f8f6f4 v[134:137], v[16:23], v[206:213], v[134:137], v200, v201 op_sel_hi:[0,0,0]
	v_mfma_scale_f32_16x16x128_f8f6f4 v[130:133], v[24:31], v[206:213], v[130:133], v200, v201 op_sel_hi:[0,0,0]
	v_mfma_scale_f32_16x16x128_f8f6f4 v[118:121], v[16:23], v[216:223], v[118:121], v200, v201 op_sel_hi:[0,0,0]
	v_mfma_scale_f32_16x16x128_f8f6f4 v[114:117], v[24:31], v[216:223], v[114:117], v200, v201 op_sel_hi:[0,0,0]
	v_mfma_scale_f32_16x16x128_f8f6f4 v[100:103], v[16:23], v[224:231], v[100:103], v200, v201 op_sel_hi:[0,0,0]
	v_mfma_scale_f32_16x16x128_f8f6f4 v[96:99], v[24:31], v[224:231], v[96:99], v200, v201 op_sel_hi:[0,0,0]
	s_setprio 0
	s_barrier
	s_add_i32 s30, s45, s14
	v_lshl_add_u64 v[174:175], v[174:175], 0, s[56:57]
	s_mov_b32 m0, s30
	ds_read_b128 v[186:189], v184 offset:49152
	ds_read_b128 v[190:193], v184 offset:50176
	ds_read_b128 v[206:209], v184 offset:51200
	ds_read_b128 v[210:213], v184 offset:52224
	ds_read_b128 v[216:219], v184 offset:53248
	ds_read_b128 v[220:223], v184 offset:54272
	ds_read_b128 v[224:227], v184 offset:55296
	ds_read_b128 v[228:231], v184 offset:56320
	global_load_lds_dwordx4 v[174:175], off
	s_add_i32 m0, s30, 0x2000
	s_add_u32 s30, s74, 0x20080
	v_lshl_add_u64 v[174:175], v[176:177], 0, s[56:57]
	s_addc_u32 s31, s75, 0
	s_add_i32 s45, s51, s14
	global_load_lds_dwordx4 v[174:175], off
	v_lshl_add_u64 v[174:175], s[30:31], 0, v[112:113]
	s_mov_b32 m0, s45
	s_nop 0
	global_load_lds_dwordx4 v[174:175], off
	v_lshl_add_u64 v[174:175], s[30:31], 0, v[162:163]
	s_add_i32 m0, s45, 0x2000
	s_nop 0
	global_load_lds_dwordx4 v[174:175], off
	v_lshl_add_u64 v[174:175], v[178:179], 0, s[56:57]
	s_mov_b32 m0, s4
	s_nop 0
	global_load_lds_dwordx4 v[174:175], off
	v_lshl_add_u64 v[174:175], v[180:181], 0, s[56:57]
	s_mov_b32 m0, s54
	s_nop 0
	global_load_lds_dwordx4 v[174:175], off
	s_waitcnt vmcnt(8)
	s_waitcnt lgkmcnt(0)
	s_barrier
	s_setprio 1
	v_mfma_scale_f32_16x16x128_f8f6f4 v[92:95], v[0:7], v[186:193], v[92:95], v200, v201 op_sel_hi:[0,0,0]
	v_mfma_scale_f32_16x16x128_f8f6f4 v[88:91], v[8:15], v[186:193], v[88:91], v200, v201 op_sel_hi:[0,0,0]
	v_mfma_scale_f32_16x16x128_f8f6f4 v[76:79], v[0:7], v[206:213], v[76:79], v200, v201 op_sel_hi:[0,0,0]
	v_mfma_scale_f32_16x16x128_f8f6f4 v[72:75], v[8:15], v[206:213], v[72:75], v200, v201 op_sel_hi:[0,0,0]
	v_mfma_scale_f32_16x16x128_f8f6f4 v[60:63], v[0:7], v[216:223], v[60:63], v200, v201 op_sel_hi:[0,0,0]
	v_mfma_scale_f32_16x16x128_f8f6f4 v[56:59], v[8:15], v[216:223], v[56:59], v200, v201 op_sel_hi:[0,0,0]
	v_mfma_scale_f32_16x16x128_f8f6f4 v[44:47], v[0:7], v[224:231], v[44:47], v200, v201 op_sel_hi:[0,0,0]
	v_mfma_scale_f32_16x16x128_f8f6f4 v[40:43], v[8:15], v[224:231], v[40:43], v200, v201 op_sel_hi:[0,0,0]
	s_setprio 0
	s_setprio 1
	v_mfma_scale_f32_16x16x128_f8f6f4 v[84:87], v[16:23], v[186:193], v[84:87], v200, v201 op_sel_hi:[0,0,0]
	v_mfma_scale_f32_16x16x128_f8f6f4 v[80:83], v[24:31], v[186:193], v[80:83], v200, v201 op_sel_hi:[0,0,0]
	v_mfma_scale_f32_16x16x128_f8f6f4 v[68:71], v[16:23], v[206:213], v[68:71], v200, v201 op_sel_hi:[0,0,0]
	v_mfma_scale_f32_16x16x128_f8f6f4 v[64:67], v[24:31], v[206:213], v[64:67], v200, v201 op_sel_hi:[0,0,0]
	v_mfma_scale_f32_16x16x128_f8f6f4 v[52:55], v[16:23], v[216:223], v[52:55], v200, v201 op_sel_hi:[0,0,0]
	v_mfma_scale_f32_16x16x128_f8f6f4 v[48:51], v[24:31], v[216:223], v[48:51], v200, v201 op_sel_hi:[0,0,0]
	v_mfma_scale_f32_16x16x128_f8f6f4 v[36:39], v[16:23], v[224:231], v[36:39], v200, v201 op_sel_hi:[0,0,0]
	v_mfma_scale_f32_16x16x128_f8f6f4 v[32:35], v[24:31], v[224:231], v[32:35], v200, v201 op_sel_hi:[0,0,0]
	s_setprio 0
	s_barrier
	s_add_i32 s50, s50, 2
	s_add_u32 s72, s72, 0x100
	s_addc_u32 s73, s73, 0
	s_add_u32 s47, s47, 0x100
	s_addc_u32 s49, s49, 0
	s_cmp_gt_u32 s50, 5
.LBB0_1166:
	s_add_u32 s30, s72, 0xfffe0080
	s_addc_u32 s31, s73, -1
	s_add_i32 s51, 0, 0x10000
	s_cmp_eq_u32 s50, 4
	s_cselect_b32 s77, s27, s31
	s_cselect_b32 s76, s37, s30
	s_cselect_b32 s75, s65, s49
	s_cselect_b32 s74, s64, s47
	s_add_i32 s58, 0, 0x14000
	v_add_u32_e32 v0, s51, v183
	v_add_u32_e32 v12, s58, v183
	ds_read_b128 v[16:19], v0
	ds_read_b128 v[20:23], v0 offset:1024
	ds_read_b128 v[24:27], v0 offset:2048
	ds_read_b128 v[28:31], v0 offset:3072
	ds_read_b128 v[0:3], v12
	ds_read_b128 v[4:7], v12 offset:1024
	ds_read_b128 v[8:11], v12 offset:2048
	ds_read_b128 v[12:15], v12 offset:3072
	v_lshl_add_u64 v[194:195], s[72:73], 0, v[168:169]
	s_add_i32 m0, s7, 0xc000
	ds_read_b128 v[174:177], v184
	ds_read_b128 v[178:181], v184 offset:1024
	ds_read_b128 v[186:189], v184 offset:2048
	ds_read_b128 v[190:193], v184 offset:3072
	ds_read_b128 v[206:209], v184 offset:4096
	ds_read_b128 v[210:213], v184 offset:5120
	ds_read_b128 v[216:219], v184 offset:6144
	ds_read_b128 v[220:223], v184 offset:7168
	global_load_lds_dwordx4 v[194:195], off
	v_lshl_add_u64 v[194:195], s[72:73], 0, v[170:171]
	s_add_i32 m0, s7, 0xe000
	s_nop 0
	global_load_lds_dwordx4 v[194:195], off
	s_waitcnt vmcnt(8)
	s_waitcnt lgkmcnt(0)
	s_barrier
	s_setprio 1
	v_mfma_scale_f32_16x16x128_f8f6f4 v[158:161], v[16:23], v[174:181], v[158:161], v200, v201 op_sel_hi:[0,0,0]
	v_mfma_scale_f32_16x16x128_f8f6f4 v[154:157], v[24:31], v[174:181], v[154:157], v200, v201 op_sel_hi:[0,0,0]
	v_mfma_scale_f32_16x16x128_f8f6f4 v[142:145], v[16:23], v[186:193], v[142:145], v200, v201 op_sel_hi:[0,0,0]
	v_mfma_scale_f32_16x16x128_f8f6f4 v[138:141], v[24:31], v[186:193], v[138:141], v200, v201 op_sel_hi:[0,0,0]
	v_mfma_scale_f32_16x16x128_f8f6f4 v[126:129], v[16:23], v[206:213], v[126:129], v200, v201 op_sel_hi:[0,0,0]
	v_mfma_scale_f32_16x16x128_f8f6f4 v[122:125], v[24:31], v[206:213], v[122:125], v200, v201 op_sel_hi:[0,0,0]
	v_mfma_scale_f32_16x16x128_f8f6f4 v[108:111], v[16:23], v[216:223], v[108:111], v200, v201 op_sel_hi:[0,0,0]
	v_mfma_scale_f32_16x16x128_f8f6f4 v[104:107], v[24:31], v[216:223], v[104:107], v200, v201 op_sel_hi:[0,0,0]
	s_setprio 0
	s_setprio 1
	v_mfma_scale_f32_16x16x128_f8f6f4 v[150:153], v[0:7], v[174:181], v[150:153], v200, v201 op_sel_hi:[0,0,0]
	v_mfma_scale_f32_16x16x128_f8f6f4 v[146:149], v[8:15], v[174:181], v[146:149], v200, v201 op_sel_hi:[0,0,0]
	v_mfma_scale_f32_16x16x128_f8f6f4 v[134:137], v[0:7], v[186:193], v[134:137], v200, v201 op_sel_hi:[0,0,0]
	v_mfma_scale_f32_16x16x128_f8f6f4 v[130:133], v[8:15], v[186:193], v[130:133], v200, v201 op_sel_hi:[0,0,0]
	v_mfma_scale_f32_16x16x128_f8f6f4 v[118:121], v[0:7], v[206:213], v[118:121], v200, v201 op_sel_hi:[0,0,0]
	v_mfma_scale_f32_16x16x128_f8f6f4 v[114:117], v[8:15], v[206:213], v[114:117], v200, v201 op_sel_hi:[0,0,0]
	v_mfma_scale_f32_16x16x128_f8f6f4 v[100:103], v[0:7], v[216:223], v[100:103], v200, v201 op_sel_hi:[0,0,0]
	v_mfma_scale_f32_16x16x128_f8f6f4 v[96:99], v[8:15], v[216:223], v[96:99], v200, v201 op_sel_hi:[0,0,0]
	s_setprio 0
	s_barrier
	s_add_i32 s30, s51, s14
	v_lshl_add_u64 v[174:175], s[74:75], 0, v[112:113]
	s_mov_b32 m0, s30
	ds_read_b128 v[186:189], v184 offset:16384
	ds_read_b128 v[190:193], v184 offset:17408
	ds_read_b128 v[206:209], v184 offset:18432
	ds_read_b128 v[210:213], v184 offset:19456
	ds_read_b128 v[216:219], v184 offset:20480
	ds_read_b128 v[220:223], v184 offset:21504
	ds_read_b128 v[224:227], v184 offset:22528
	ds_read_b128 v[228:231], v184 offset:23552
	global_load_lds_dwordx4 v[174:175], off
	s_add_i32 m0, s30, 0x2000
	s_add_u32 s30, s74, 0x20000
	v_lshl_add_u64 v[176:177], s[74:75], 0, v[162:163]
	s_addc_u32 s31, s75, 0
	s_add_i32 s45, s58, s14
	global_load_lds_dwordx4 v[176:177], off
	v_lshl_add_u64 v[178:179], s[30:31], 0, v[112:113]
	s_mov_b32 m0, s45
	v_lshl_add_u64 v[180:181], s[76:77], 0, v[164:165]
	global_load_lds_dwordx4 v[178:179], off
	v_lshl_add_u64 v[178:179], s[30:31], 0, v[162:163]
	s_add_i32 m0, s45, 0x2000
	s_nop 0
	global_load_lds_dwordx4 v[178:179], off
	v_lshl_add_u64 v[178:179], s[76:77], 0, v[166:167]
	s_mov_b32 m0, s7
	s_nop 0
	global_load_lds_dwordx4 v[178:179], off
	s_mov_b32 m0, s25
	s_nop 0
	global_load_lds_dwordx4 v[180:181], off
	s_waitcnt vmcnt(8)
	s_waitcnt lgkmcnt(0)
	s_barrier
	s_setprio 1
	v_mfma_scale_f32_16x16x128_f8f6f4 v[92:95], v[16:23], v[186:193], v[92:95], v200, v201 op_sel_hi:[0,0,0]
	v_mfma_scale_f32_16x16x128_f8f6f4 v[88:91], v[24:31], v[186:193], v[88:91], v200, v201 op_sel_hi:[0,0,0]
	v_mfma_scale_f32_16x16x128_f8f6f4 v[76:79], v[16:23], v[206:213], v[76:79], v200, v201 op_sel_hi:[0,0,0]
	v_mfma_scale_f32_16x16x128_f8f6f4 v[72:75], v[24:31], v[206:213], v[72:75], v200, v201 op_sel_hi:[0,0,0]
	v_mfma_scale_f32_16x16x128_f8f6f4 v[60:63], v[16:23], v[216:223], v[60:63], v200, v201 op_sel_hi:[0,0,0]
	v_mfma_scale_f32_16x16x128_f8f6f4 v[56:59], v[24:31], v[216:223], v[56:59], v200, v201 op_sel_hi:[0,0,0]
	v_mfma_scale_f32_16x16x128_f8f6f4 v[44:47], v[16:23], v[224:231], v[44:47], v200, v201 op_sel_hi:[0,0,0]
	v_mfma_scale_f32_16x16x128_f8f6f4 v[40:43], v[24:31], v[224:231], v[40:43], v200, v201 op_sel_hi:[0,0,0]
	s_setprio 0
	s_setprio 1
	v_mfma_scale_f32_16x16x128_f8f6f4 v[84:87], v[0:7], v[186:193], v[84:87], v200, v201 op_sel_hi:[0,0,0]
	v_mfma_scale_f32_16x16x128_f8f6f4 v[80:83], v[8:15], v[186:193], v[80:83], v200, v201 op_sel_hi:[0,0,0]
	v_mfma_scale_f32_16x16x128_f8f6f4 v[68:71], v[0:7], v[206:213], v[68:71], v200, v201 op_sel_hi:[0,0,0]
	v_mfma_scale_f32_16x16x128_f8f6f4 v[64:67], v[8:15], v[206:213], v[64:67], v200, v201 op_sel_hi:[0,0,0]
	v_mfma_scale_f32_16x16x128_f8f6f4 v[52:55], v[0:7], v[216:223], v[52:55], v200, v201 op_sel_hi:[0,0,0]
	v_mfma_scale_f32_16x16x128_f8f6f4 v[48:51], v[8:15], v[216:223], v[48:51], v200, v201 op_sel_hi:[0,0,0]
	v_mfma_scale_f32_16x16x128_f8f6f4 v[36:39], v[0:7], v[224:231], v[36:39], v200, v201 op_sel_hi:[0,0,0]
	v_mfma_scale_f32_16x16x128_f8f6f4 v[32:35], v[8:15], v[224:231], v[32:35], v200, v201 op_sel_hi:[0,0,0]
	s_setprio 0
	s_barrier
	s_add_i32 s45, 0, 0x18000
	s_add_i32 s51, 0, 0x1c000
	v_add_u32_e32 v12, s45, v183
	v_add_u32_e32 v28, s51, v183
	ds_read_b128 v[0:3], v12
	ds_read_b128 v[4:7], v12 offset:1024
	ds_read_b128 v[8:11], v12 offset:2048
	ds_read_b128 v[12:15], v12 offset:3072
	ds_read_b128 v[16:19], v28
	ds_read_b128 v[20:23], v28 offset:1024
	ds_read_b128 v[24:27], v28 offset:2048
	ds_read_b128 v[28:31], v28 offset:3072
	s_add_u32 s30, s76, 0x20000
	s_addc_u32 s31, s77, 0
	s_mov_b32 m0, s33
	v_lshl_add_u64 v[194:195], s[30:31], 0, v[166:167]
	ds_read_b128 v[186:189], v184 offset:32768
	ds_read_b128 v[190:193], v184 offset:33792
	ds_read_b128 v[206:209], v184 offset:34816
	ds_read_b128 v[210:213], v184 offset:35840
	ds_read_b128 v[216:219], v184 offset:36864
	ds_read_b128 v[220:223], v184 offset:37888
	ds_read_b128 v[224:227], v184 offset:38912
	ds_read_b128 v[228:231], v184 offset:39936
	global_load_lds_dwordx4 v[194:195], off
	v_lshl_add_u64 v[194:195], s[30:31], 0, v[164:165]
	s_mov_b32 m0, s34
	s_nop 0
	global_load_lds_dwordx4 v[194:195], off
	s_waitcnt vmcnt(8)
	s_waitcnt lgkmcnt(0)
	s_barrier
	s_setprio 1
	v_mfma_scale_f32_16x16x128_f8f6f4 v[158:161], v[0:7], v[186:193], v[158:161], v200, v201 op_sel_hi:[0,0,0]
	v_mfma_scale_f32_16x16x128_f8f6f4 v[154:157], v[8:15], v[186:193], v[154:157], v200, v201 op_sel_hi:[0,0,0]
	v_mfma_scale_f32_16x16x128_f8f6f4 v[142:145], v[0:7], v[206:213], v[142:145], v200, v201 op_sel_hi:[0,0,0]
	v_mfma_scale_f32_16x16x128_f8f6f4 v[138:141], v[8:15], v[206:213], v[138:141], v200, v201 op_sel_hi:[0,0,0]
	v_mfma_scale_f32_16x16x128_f8f6f4 v[126:129], v[0:7], v[216:223], v[126:129], v200, v201 op_sel_hi:[0,0,0]
	v_mfma_scale_f32_16x16x128_f8f6f4 v[122:125], v[8:15], v[216:223], v[122:125], v200, v201 op_sel_hi:[0,0,0]
	v_mfma_scale_f32_16x16x128_f8f6f4 v[108:111], v[0:7], v[224:231], v[108:111], v200, v201 op_sel_hi:[0,0,0]
	v_mfma_scale_f32_16x16x128_f8f6f4 v[104:107], v[8:15], v[224:231], v[104:107], v200, v201 op_sel_hi:[0,0,0]
	s_setprio 0
	s_setprio 1
	v_mfma_scale_f32_16x16x128_f8f6f4 v[150:153], v[16:23], v[186:193], v[150:153], v200, v201 op_sel_hi:[0,0,0]
	v_mfma_scale_f32_16x16x128_f8f6f4 v[146:149], v[24:31], v[186:193], v[146:149], v200, v201 op_sel_hi:[0,0,0]
	v_mfma_scale_f32_16x16x128_f8f6f4 v[134:137], v[16:23], v[206:213], v[134:137], v200, v201 op_sel_hi:[0,0,0]
	v_mfma_scale_f32_16x16x128_f8f6f4 v[130:133], v[24:31], v[206:213], v[130:133], v200, v201 op_sel_hi:[0,0,0]
	v_mfma_scale_f32_16x16x128_f8f6f4 v[118:121], v[16:23], v[216:223], v[118:121], v200, v201 op_sel_hi:[0,0,0]
	v_mfma_scale_f32_16x16x128_f8f6f4 v[114:117], v[24:31], v[216:223], v[114:117], v200, v201 op_sel_hi:[0,0,0]
	v_mfma_scale_f32_16x16x128_f8f6f4 v[100:103], v[16:23], v[224:231], v[100:103], v200, v201 op_sel_hi:[0,0,0]
	v_mfma_scale_f32_16x16x128_f8f6f4 v[96:99], v[24:31], v[224:231], v[96:99], v200, v201 op_sel_hi:[0,0,0]
	s_setprio 0
	s_barrier
	s_add_i32 s30, s45, s14
	v_lshl_add_u64 v[174:175], v[174:175], 0, s[56:57]
	s_mov_b32 m0, s30
	ds_read_b128 v[186:189], v184 offset:49152
	ds_read_b128 v[190:193], v184 offset:50176
	ds_read_b128 v[206:209], v184 offset:51200
	ds_read_b128 v[210:213], v184 offset:52224
	ds_read_b128 v[216:219], v184 offset:53248
	ds_read_b128 v[220:223], v184 offset:54272
	ds_read_b128 v[224:227], v184 offset:55296
	ds_read_b128 v[228:231], v184 offset:56320
	global_load_lds_dwordx4 v[174:175], off
	s_add_i32 m0, s30, 0x2000
	s_add_u32 s30, s74, 0x20080
	v_lshl_add_u64 v[174:175], v[176:177], 0, s[56:57]
	s_addc_u32 s31, s75, 0
	s_add_i32 s45, s51, s14
	global_load_lds_dwordx4 v[174:175], off
	v_lshl_add_u64 v[174:175], s[30:31], 0, v[112:113]
	s_mov_b32 m0, s45
	s_nop 0
	global_load_lds_dwordx4 v[174:175], off
	v_lshl_add_u64 v[174:175], s[30:31], 0, v[162:163]
	s_add_i32 m0, s45, 0x2000
	s_nop 0
	global_load_lds_dwordx4 v[174:175], off
	v_lshl_add_u64 v[174:175], v[178:179], 0, s[56:57]
	s_mov_b32 m0, s4
	s_nop 0
	global_load_lds_dwordx4 v[174:175], off
	v_lshl_add_u64 v[174:175], v[180:181], 0, s[56:57]
	s_mov_b32 m0, s54
	s_nop 0
	global_load_lds_dwordx4 v[174:175], off
	s_waitcnt vmcnt(8)
	s_waitcnt lgkmcnt(0)
	s_barrier
	s_setprio 1
	v_mfma_scale_f32_16x16x128_f8f6f4 v[92:95], v[0:7], v[186:193], v[92:95], v200, v201 op_sel_hi:[0,0,0]
	v_mfma_scale_f32_16x16x128_f8f6f4 v[88:91], v[8:15], v[186:193], v[88:91], v200, v201 op_sel_hi:[0,0,0]
	v_mfma_scale_f32_16x16x128_f8f6f4 v[76:79], v[0:7], v[206:213], v[76:79], v200, v201 op_sel_hi:[0,0,0]
	v_mfma_scale_f32_16x16x128_f8f6f4 v[72:75], v[8:15], v[206:213], v[72:75], v200, v201 op_sel_hi:[0,0,0]
	v_mfma_scale_f32_16x16x128_f8f6f4 v[60:63], v[0:7], v[216:223], v[60:63], v200, v201 op_sel_hi:[0,0,0]
	v_mfma_scale_f32_16x16x128_f8f6f4 v[56:59], v[8:15], v[216:223], v[56:59], v200, v201 op_sel_hi:[0,0,0]
	v_mfma_scale_f32_16x16x128_f8f6f4 v[44:47], v[0:7], v[224:231], v[44:47], v200, v201 op_sel_hi:[0,0,0]
	v_mfma_scale_f32_16x16x128_f8f6f4 v[40:43], v[8:15], v[224:231], v[40:43], v200, v201 op_sel_hi:[0,0,0]
	s_setprio 0
	s_setprio 1
	v_mfma_scale_f32_16x16x128_f8f6f4 v[84:87], v[16:23], v[186:193], v[84:87], v200, v201 op_sel_hi:[0,0,0]
	v_mfma_scale_f32_16x16x128_f8f6f4 v[80:83], v[24:31], v[186:193], v[80:83], v200, v201 op_sel_hi:[0,0,0]
	v_mfma_scale_f32_16x16x128_f8f6f4 v[68:71], v[16:23], v[206:213], v[68:71], v200, v201 op_sel_hi:[0,0,0]
	v_mfma_scale_f32_16x16x128_f8f6f4 v[64:67], v[24:31], v[206:213], v[64:67], v200, v201 op_sel_hi:[0,0,0]
	v_mfma_scale_f32_16x16x128_f8f6f4 v[52:55], v[16:23], v[216:223], v[52:55], v200, v201 op_sel_hi:[0,0,0]
	v_mfma_scale_f32_16x16x128_f8f6f4 v[48:51], v[24:31], v[216:223], v[48:51], v200, v201 op_sel_hi:[0,0,0]
	v_mfma_scale_f32_16x16x128_f8f6f4 v[36:39], v[16:23], v[224:231], v[36:39], v200, v201 op_sel_hi:[0,0,0]
	v_mfma_scale_f32_16x16x128_f8f6f4 v[32:35], v[24:31], v[224:231], v[32:35], v200, v201 op_sel_hi:[0,0,0]
	s_setprio 0
	s_barrier
	s_add_i32 s50, s50, 2
	s_add_u32 s72, s72, 0x100
	s_addc_u32 s73, s73, 0
	s_add_u32 s47, s47, 0x100
	s_addc_u32 s49, s49, 0
	s_cmp_gt_u32 s50, 5
	s_cbranch_scc0 .LBB0_1166
	s_and_b64 vcc, exec, s[42:43]
	s_movk_i32 s44, 0xff
	v_readlane_b32 s45, v255, 19
	s_cbranch_vccz .LBB0_1169
	s_barrier
